# v101: v99 (2 VALU per K iteration) + mid-block s_setprio toggles removed
# baseline (speedup 1.0000x reference)
; #define PG8_GIDX(G_, PM_) do { if constexpr (Sched::GATHER) { _Pragma("unroll") for (int h_ = 0; h_ < 2; ++h_) _Pragma("unroll") for (int i_ = 0; i_ < 2; ++i_) { int R_, C_; stage_rc(tid * 16 + i_ * 8192, R_, C_); \
;         const int src_ = S.rowsrc[(PM_) * BM + h_ * HALF + R_]; G_[h_][i_] = (unsigned)(src_ * K + C_) * 2u; } } } while (0)
; #define PG8_STAGE_A(b, h, ptr, NX) do { if constexpr (Sched::GATHER) { unsigned gs_[2]; gs_[0] = ((NX) && last_) ? gN[h][0] : gA[h][0]; gs_[1] = ((NX) && last_) ? gN[h][1] : gA[h][1]; PG8_STAGE(PG8_SA(b, h), ptr, gs_); } \
;         else PG8_STAGE(PG8_SA(b, h), (ptr) + ((h) ? hstep : (size_t)0), voffA); } while (0)
; #define PG8_LDA(dst, b, h) do { _Pragma("unroll") for (int m = 0; m < 4; ++m) _Pragma("unroll") for (int k = 0; k < 2; ++k) dst[m][k] = *(const PG8_LAS bf16x8*)(lds + PG8_SA(b, h) + aoff + m * 2048 + k * 1024); } while (0)
; template <class Epi, class Sched, bool ALIGN_EPI = false, bool SP2 = false>
; __device__ __forceinline__ void gemm_phase(PG8_LAS unsigned char* lds, const Gemm g, const Sched& S, const Epi& E, const bool skip_epi = false) {
;     ...
;         const bool has_next = S.next(ui + 1, nxt);
;         if (has_next) PG8_GIDX(gN, nxt.pm);
;         const char* nA = has_next ? (const char*)g.A + (size_t)nxt.pm * pmstepA + nxt.ko : cA; const char* nB = has_next ? (const char*)g.Bt + (size_t)nxt.pn * tstep + nxt.ko : cB;
;         for (int t = 0; t < nt; t += 2) {
;             const bool last = (t == nt - 2); last_ = last && has_next;
;             const char* a1 = cA + (size_t)(t + 1) * kstep;
;             const char* a2 = last ? nA : cA + (size_t)(t + 2) * kstep; const char* b2 = last ? nB : cB + (size_t)(t + 2) * kstep;
;             const char* a3 = a2 + kstep; const char* b3 = b2 + kstep;
;             if (last && has_next) S.a_ready(nxt);
;             if constexpr (SP2) {
;             PG8_LDB(B0, 0, 0); PG8_LDB(B1, 0, 1); PG8_SCHED; PG8_LDA(At, 0, 0); PG8_STAGE_A(1, 1, a1, false);
;             PG8_WAIT_V(8); PG8_WAIT_L(0); PG8_BAR; PG8_MMA(0, 0, At, B0); PG8_MMA(0, 1, At, B1); PG8_BAR; PG8_SCHED;
;             PG8_LDA(At, 0, 1); PG8_STAGE(PG8_SB(0, 0), b2, voffB); PG8_STAGE(PG8_SB(0, 1), b2 + hstep, voffB); PG8_STAGE_A(0, 0, a2, true);
;             PG8_WAIT_V(8); PG8_WAIT_L(0); PG8_BAR; PG8_MMA(1, 0, At, B0); PG8_MMA(1, 1, At, B1); PG8_BAR; PG8_SCHED;
.LBB0_252:
	s_ashr_i32 s17, s16, 31
	s_lshl_b64 s[18:19], s[16:17], 19
	s_add_u32 s18, s86, s18
	s_addc_u32 s19, s87, s19
	s_and_b64 s[20:21], s[4:5], exec
	s_cselect_b32 s17, s19, s25
	s_cselect_b32 s56, s18, s24
	s_ashr_i32 s15, s14, 31
	s_lshl_b64 s[20:21], s[14:15], 19
	v_readlane_b32 s28, v254, 36
	v_readlane_b32 s29, v254, 37
	s_add_u32 s20, s28, s20
	s_addc_u32 s21, s29, s21
	s_and_b64 s[28:29], s[4:5], exec
	s_cselect_b32 s15, s21, s27
	s_cselect_b32 s57, s20, s26
	s_add_u32 s24, s24, 0x40080
	s_addc_u32 s25, s25, 0
	s_add_u32 s58, s26, 0x100
	s_addc_u32 s59, s27, 0
	s_mov_b32 s60, -2
	s_waitcnt vmcnt(0)
	ds_read_b128 v[148:151], v170
	ds_read_b128 v[152:155], v170 offset:1024
	ds_read_b128 v[156:159], v170 offset:2048
	ds_read_b128 v[160:163], v170 offset:3072
	ds_read_b128 v[176:179], v171
	ds_read_b128 v[180:183], v171 offset:1024
	ds_read_b128 v[184:187], v171 offset:2048
	ds_read_b128 v[188:191], v171 offset:3072
	s_add_u32 s26, s24, 0xfffc0080
	s_addc_u32 s27, s25, -1
	s_cmp_eq_u32 s60, 12
	s_cselect_b32 s29, s17, s27
	s_cselect_b32 s28, s56, s26
	s_cselect_b32 s27, s15, s59
	s_cselect_b32 s26, s57, s58
	s_add_i32 m0, s23, 0xc000
	ds_read_b128 v[192:195], v172
	ds_read_b128 v[196:199], v172 offset:1024
	ds_read_b128 v[200:203], v172 offset:2048
	ds_read_b128 v[204:207], v172 offset:3072
	ds_read_b128 v[208:211], v172 offset:4096
	ds_read_b128 v[212:215], v172 offset:5120
	ds_read_b128 v[216:219], v172 offset:6144
	ds_read_b128 v[220:223], v172 offset:7168
	global_load_lds_dwordx4 v140, s[24:25]
	s_add_i32 m0, s23, 0xe000
	s_nop 0
	global_load_lds_dwordx4 v142, s[24:25]
	s_waitcnt vmcnt(8)
	s_waitcnt lgkmcnt(0)
	s_barrier
	s_setprio 3
	s_waitcnt lgkmcnt(0)
	v_mfma_f32_16x16x32_bf16 v[126:129], v[148:151], v[192:195], 0
	v_mfma_f32_16x16x32_bf16 v[122:125], v[156:159], v[192:195], 0
	v_mfma_f32_16x16x32_bf16 v[114:117], v[148:151], v[200:203], 0
	v_mfma_f32_16x16x32_bf16 v[106:109], v[156:159], v[200:203], 0
	v_mfma_f32_16x16x32_bf16 v[98:101], v[148:151], v[208:211], 0
	v_mfma_f32_16x16x32_bf16 v[90:93], v[156:159], v[208:211], 0
	v_mfma_f32_16x16x32_bf16 v[82:85], v[148:151], v[216:219], 0
	v_mfma_f32_16x16x32_bf16 v[74:77], v[156:159], v[216:219], 0
	v_mfma_f32_16x16x32_bf16 v[126:129], v[152:155], v[196:199], v[126:129]
	v_mfma_f32_16x16x32_bf16 v[122:125], v[160:163], v[196:199], v[122:125]
	v_mfma_f32_16x16x32_bf16 v[114:117], v[152:155], v[204:207], v[114:117]
	v_mfma_f32_16x16x32_bf16 v[106:109], v[160:163], v[204:207], v[106:109]
	v_mfma_f32_16x16x32_bf16 v[98:101], v[152:155], v[212:215], v[98:101]
	v_mfma_f32_16x16x32_bf16 v[90:93], v[160:163], v[212:215], v[90:93]
	v_mfma_f32_16x16x32_bf16 v[82:85], v[152:155], v[220:223], v[82:85]
	v_mfma_f32_16x16x32_bf16 v[74:77], v[160:163], v[220:223], v[74:77]
	v_mfma_f32_16x16x32_bf16 v[118:121], v[176:179], v[192:195], 0
	v_mfma_f32_16x16x32_bf16 v[110:113], v[184:187], v[192:195], 0
	v_mfma_f32_16x16x32_bf16 v[102:105], v[176:179], v[200:203], 0
	v_mfma_f32_16x16x32_bf16 v[94:97], v[184:187], v[200:203], 0
	v_mfma_f32_16x16x32_bf16 v[86:89], v[176:179], v[208:211], 0
	v_mfma_f32_16x16x32_bf16 v[78:81], v[184:187], v[208:211], 0
	v_mfma_f32_16x16x32_bf16 v[70:73], v[176:179], v[216:219], 0
	v_mfma_f32_16x16x32_bf16 v[66:69], v[184:187], v[216:219], 0
	v_mfma_f32_16x16x32_bf16 v[118:121], v[180:183], v[196:199], v[118:121]
	v_mfma_f32_16x16x32_bf16 v[110:113], v[188:191], v[196:199], v[110:113]
	v_mfma_f32_16x16x32_bf16 v[102:105], v[180:183], v[204:207], v[102:105]
	v_mfma_f32_16x16x32_bf16 v[94:97], v[188:191], v[204:207], v[94:97]
	v_mfma_f32_16x16x32_bf16 v[86:89], v[180:183], v[212:215], v[86:89]
	v_mfma_f32_16x16x32_bf16 v[78:81], v[188:191], v[212:215], v[78:81]
	v_mfma_f32_16x16x32_bf16 v[70:73], v[180:183], v[220:223], v[70:73]
	v_mfma_f32_16x16x32_bf16 v[66:69], v[188:191], v[220:223], v[66:69]
	s_setprio 0
	s_barrier
	s_add_i32 s61, s46, s2
	s_mov_b32 m0, s61
	ds_read_b128 v[192:195], v172 offset:16384
	ds_read_b128 v[196:199], v172 offset:17408
	ds_read_b128 v[200:203], v172 offset:18432
	ds_read_b128 v[204:207], v172 offset:19456
	ds_read_b128 v[208:211], v172 offset:20480
	ds_read_b128 v[212:215], v172 offset:21504
	ds_read_b128 v[216:219], v172 offset:22528
	ds_read_b128 v[220:223], v172 offset:23552
	global_load_lds_dwordx4 v134, s[26:27]
	s_add_i32 m0, s61, 0x2000
	s_add_u32 s62, s26, 0x40000
	s_addc_u32 s63, s27, 0
	s_add_i32 s61, s47, s2
	global_load_lds_dwordx4 v130, s[26:27]
	s_mov_b32 m0, s61
	s_mov_b64 s[98:99], s[28:29]
	global_load_lds_dwordx4 v134, s[62:63]
	s_add_i32 m0, s61, 0x2000
	s_nop 0
	global_load_lds_dwordx4 v130, s[62:63]
	s_mov_b32 m0, s23
	s_nop 0
	global_load_lds_dwordx4 v136, s[28:29]
	s_mov_b32 m0, s31
	s_nop 0
	global_load_lds_dwordx4 v132, s[28:29]
	s_waitcnt vmcnt(8)
	s_waitcnt lgkmcnt(0)
	s_barrier
; #define PG8_STAGE_A(b, h, ptr, NX) do { if constexpr (Sched::GATHER) { unsigned gs_[2]; gs_[0] = ((NX) && last_) ? gN[h][0] : gA[h][0]; gs_[1] = ((NX) && last_) ? gN[h][1] : gA[h][1]; PG8_STAGE(PG8_SA(b, h), ptr, gs_); } \
;         else PG8_STAGE(PG8_SA(b, h), (ptr) + ((h) ? hstep : (size_t)0), voffA); } while (0)
; #define PG8_LDA(dst, b, h) do { _Pragma("unroll") for (int m = 0; m < 4; ++m) _Pragma("unroll") for (int k = 0; k < 2; ++k) dst[m][k] = *(const PG8_LAS bf16x8*)(lds + PG8_SA(b, h) + aoff + m * 2048 + k * 1024); } while (0)
; #define PG8_LDB(dst, b, h) do { _Pragma("unroll") for (int n = 0; n < 2; ++n) _Pragma("unroll") for (int k = 0; k < 2; ++k) dst[n][k] = *(const PG8_LAS bf16x8*)(lds + PG8_SB(b, h) + boff + n * 2048 + k * 1024); } while (0)
; #define PG8_MMA(ai, bj, At, Bt) do { __builtin_amdgcn_s_setprio(1); _Pragma("unroll") for (int m = 0; m < 4; ++m) _Pragma("unroll") for (int n = 0; n < 2; ++n) _Pragma("unroll") for (int k = 0; k < 2; ++k) \
;         acc[ai][bj][m][n] = __builtin_amdgcn_mfma_f32_16x16x32_bf16(Bt[n][k], At[m][k], acc[ai][bj][m][n], 0, 0, 0); __builtin_amdgcn_s_setprio(0); } while (0)
; #define PG8_WAIT_V(n) asm volatile("s_waitcnt vmcnt(" #n ")" ::: "memory")
; #define PG8_WAIT_L(n) asm volatile("s_waitcnt lgkmcnt(" #n ")" ::: "memory")
; #define PG8_BAR __builtin_amdgcn_s_barrier()
; #define PG8_SCHED __builtin_amdgcn_sched_barrier(0)
; template <class Epi, class Sched, bool ALIGN_EPI = false, bool SP2 = false>
; __device__ __forceinline__ void gemm_phase(PG8_LAS unsigned char* lds, const Gemm g, const Sched& S, const Epi& E, const bool skip_epi = false) {
;     ...
;             PG8_WAIT_V(8); PG8_WAIT_L(0); PG8_BAR; PG8_MMA(1, 0, At, B0); PG8_MMA(1, 1, At, B1); PG8_BAR; PG8_SCHED;
;             PG8_LDB(B0, 1, 0); PG8_LDB(B1, 1, 1); PG8_SCHED; PG8_LDA(At, 1, 0); PG8_STAGE_A(0, 1, a2, true);
;             PG8_WAIT_V(8); PG8_WAIT_L(0); PG8_BAR; PG8_MMA(0, 0, At, B0); PG8_MMA(0, 1, At, B1); PG8_BAR; PG8_SCHED;
	s_setprio 3
	s_waitcnt lgkmcnt(0)
	v_mfma_f32_16x16x32_bf16 v[62:65], v[148:151], v[192:195], 0
	v_mfma_f32_16x16x32_bf16 v[58:61], v[156:159], v[192:195], 0
	v_mfma_f32_16x16x32_bf16 v[50:53], v[148:151], v[200:203], 0
	v_mfma_f32_16x16x32_bf16 v[42:45], v[156:159], v[200:203], 0
	v_mfma_f32_16x16x32_bf16 v[34:37], v[148:151], v[208:211], 0
	v_mfma_f32_16x16x32_bf16 v[26:29], v[156:159], v[208:211], 0
	v_mfma_f32_16x16x32_bf16 v[18:21], v[148:151], v[216:219], 0
	v_mfma_f32_16x16x32_bf16 v[10:13], v[156:159], v[216:219], 0
	v_mfma_f32_16x16x32_bf16 v[62:65], v[152:155], v[196:199], v[62:65]
	v_mfma_f32_16x16x32_bf16 v[58:61], v[160:163], v[196:199], v[58:61]
	v_mfma_f32_16x16x32_bf16 v[50:53], v[152:155], v[204:207], v[50:53]
	v_mfma_f32_16x16x32_bf16 v[42:45], v[160:163], v[204:207], v[42:45]
	v_mfma_f32_16x16x32_bf16 v[34:37], v[152:155], v[212:215], v[34:37]
	v_mfma_f32_16x16x32_bf16 v[26:29], v[160:163], v[212:215], v[26:29]
	v_mfma_f32_16x16x32_bf16 v[18:21], v[152:155], v[220:223], v[18:21]
	v_mfma_f32_16x16x32_bf16 v[10:13], v[160:163], v[220:223], v[10:13]
	v_mfma_f32_16x16x32_bf16 v[54:57], v[176:179], v[192:195], 0
	v_mfma_f32_16x16x32_bf16 v[46:49], v[184:187], v[192:195], 0
	v_mfma_f32_16x16x32_bf16 v[38:41], v[176:179], v[200:203], 0
	v_mfma_f32_16x16x32_bf16 v[30:33], v[184:187], v[200:203], 0
	v_mfma_f32_16x16x32_bf16 v[22:25], v[176:179], v[208:211], 0
	v_mfma_f32_16x16x32_bf16 v[14:17], v[184:187], v[208:211], 0
	v_mfma_f32_16x16x32_bf16 v[6:9], v[176:179], v[216:219], 0
	v_mfma_f32_16x16x32_bf16 v[2:5], v[184:187], v[216:219], 0
	v_mfma_f32_16x16x32_bf16 v[54:57], v[180:183], v[196:199], v[54:57]
	v_mfma_f32_16x16x32_bf16 v[46:49], v[188:191], v[196:199], v[46:49]
	v_mfma_f32_16x16x32_bf16 v[38:41], v[180:183], v[204:207], v[38:41]
	v_mfma_f32_16x16x32_bf16 v[30:33], v[188:191], v[204:207], v[30:33]
	v_mfma_f32_16x16x32_bf16 v[22:25], v[180:183], v[212:215], v[22:25]
	v_mfma_f32_16x16x32_bf16 v[14:17], v[188:191], v[212:215], v[14:17]
	v_mfma_f32_16x16x32_bf16 v[6:9], v[180:183], v[220:223], v[6:9]
	v_mfma_f32_16x16x32_bf16 v[2:5], v[188:191], v[220:223], v[2:5]
	s_setprio 0
	s_barrier
	s_add_i32 s61, 0, 0x18000
	s_add_i32 s62, 0, 0x1c000
	v_add_u32_e32 v160, s61, v1
	v_add_u32_e32 v188, s62, v1
	ds_read_b128 v[148:151], v160
	ds_read_b128 v[152:155], v160 offset:1024
	ds_read_b128 v[156:159], v160 offset:2048
	ds_read_b128 v[160:163], v160 offset:3072
	ds_read_b128 v[176:179], v188
	ds_read_b128 v[180:183], v188 offset:1024
	ds_read_b128 v[184:187], v188 offset:2048
	ds_read_b128 v[188:191], v188 offset:3072
	s_add_u32 s28, s28, 0x40000
	s_addc_u32 s29, s29, 0
	s_mov_b32 m0, s34
	ds_read_b128 v[192:195], v172 offset:32768
	ds_read_b128 v[196:199], v172 offset:33792
	ds_read_b128 v[200:203], v172 offset:34816
	ds_read_b128 v[204:207], v172 offset:35840
	ds_read_b128 v[208:211], v172 offset:36864
	ds_read_b128 v[212:215], v172 offset:37888
	ds_read_b128 v[216:219], v172 offset:38912
	ds_read_b128 v[220:223], v172 offset:39936
	global_load_lds_dwordx4 v136, s[28:29]
	s_mov_b32 m0, s35
	s_nop 0
	global_load_lds_dwordx4 v132, s[28:29]
	s_waitcnt vmcnt(8)
	s_waitcnt lgkmcnt(0)
	s_barrier
	s_setprio 3
	s_waitcnt lgkmcnt(0)
	v_mfma_f32_16x16x32_bf16 v[126:129], v[148:151], v[192:195], v[126:129]
	v_mfma_f32_16x16x32_bf16 v[122:125], v[156:159], v[192:195], v[122:125]
	v_mfma_f32_16x16x32_bf16 v[114:117], v[148:151], v[200:203], v[114:117]
	v_mfma_f32_16x16x32_bf16 v[106:109], v[156:159], v[200:203], v[106:109]
	v_mfma_f32_16x16x32_bf16 v[98:101], v[148:151], v[208:211], v[98:101]
	v_mfma_f32_16x16x32_bf16 v[90:93], v[156:159], v[208:211], v[90:93]
	v_mfma_f32_16x16x32_bf16 v[82:85], v[148:151], v[216:219], v[82:85]
	v_mfma_f32_16x16x32_bf16 v[74:77], v[156:159], v[216:219], v[74:77]
	v_mfma_f32_16x16x32_bf16 v[126:129], v[152:155], v[196:199], v[126:129]
	v_mfma_f32_16x16x32_bf16 v[122:125], v[160:163], v[196:199], v[122:125]
	v_mfma_f32_16x16x32_bf16 v[114:117], v[152:155], v[204:207], v[114:117]
	v_mfma_f32_16x16x32_bf16 v[106:109], v[160:163], v[204:207], v[106:109]
	v_mfma_f32_16x16x32_bf16 v[98:101], v[152:155], v[212:215], v[98:101]
	v_mfma_f32_16x16x32_bf16 v[90:93], v[160:163], v[212:215], v[90:93]
	v_mfma_f32_16x16x32_bf16 v[82:85], v[152:155], v[220:223], v[82:85]
	v_mfma_f32_16x16x32_bf16 v[74:77], v[160:163], v[220:223], v[74:77]
	v_mfma_f32_16x16x32_bf16 v[118:121], v[176:179], v[192:195], v[118:121]
	v_mfma_f32_16x16x32_bf16 v[110:113], v[184:187], v[192:195], v[110:113]
	v_mfma_f32_16x16x32_bf16 v[102:105], v[176:179], v[200:203], v[102:105]
	v_mfma_f32_16x16x32_bf16 v[94:97], v[184:187], v[200:203], v[94:97]
	v_mfma_f32_16x16x32_bf16 v[86:89], v[176:179], v[208:211], v[86:89]
	v_mfma_f32_16x16x32_bf16 v[78:81], v[184:187], v[208:211], v[78:81]
	v_mfma_f32_16x16x32_bf16 v[70:73], v[176:179], v[216:219], v[70:73]
	v_mfma_f32_16x16x32_bf16 v[66:69], v[184:187], v[216:219], v[66:69]
	v_mfma_f32_16x16x32_bf16 v[118:121], v[180:183], v[196:199], v[118:121]
	v_mfma_f32_16x16x32_bf16 v[110:113], v[188:191], v[196:199], v[110:113]
	v_mfma_f32_16x16x32_bf16 v[102:105], v[180:183], v[204:207], v[102:105]
	v_mfma_f32_16x16x32_bf16 v[94:97], v[188:191], v[204:207], v[94:97]
	v_mfma_f32_16x16x32_bf16 v[86:89], v[180:183], v[212:215], v[86:89]
	v_mfma_f32_16x16x32_bf16 v[78:81], v[188:191], v[212:215], v[78:81]
	v_mfma_f32_16x16x32_bf16 v[70:73], v[180:183], v[220:223], v[70:73]
	v_mfma_f32_16x16x32_bf16 v[66:69], v[188:191], v[220:223], v[66:69]
	s_setprio 0
	s_barrier
; #define PG8_STAGE_A(b, h, ptr, NX) do { if constexpr (Sched::GATHER) { unsigned gs_[2]; gs_[0] = ((NX) && last_) ? gN[h][0] : gA[h][0]; gs_[1] = ((NX) && last_) ? gN[h][1] : gA[h][1]; PG8_STAGE(PG8_SA(b, h), ptr, gs_); } \
;         else PG8_STAGE(PG8_SA(b, h), (ptr) + ((h) ? hstep : (size_t)0), voffA); } while (0)
; #define PG8_STAGE(bufoff, gbase, voff) do { _Pragma("unroll") for (int _i = 0; _i < 2; ++_i) \
;         __builtin_amdgcn_global_load_lds((const unsigned*)((const char*)(gbase) + (voff)[_i]), (PG8_LAS unsigned*)(lds + (bufoff) + ldsw + _i * 8192), 16, 0, 0); } while (0)
; #define PG8_LDA(dst, b, h) do { _Pragma("unroll") for (int m = 0; m < 4; ++m) _Pragma("unroll") for (int k = 0; k < 2; ++k) dst[m][k] = *(const PG8_LAS bf16x8*)(lds + PG8_SA(b, h) + aoff + m * 2048 + k * 1024); } while (0)
; #define PG8_LDB(dst, b, h) do { _Pragma("unroll") for (int n = 0; n < 2; ++n) _Pragma("unroll") for (int k = 0; k < 2; ++k) dst[n][k] = *(const PG8_LAS bf16x8*)(lds + PG8_SB(b, h) + boff + n * 2048 + k * 1024); } while (0)
; #define PG8_WAIT_V(n) asm volatile("s_waitcnt vmcnt(" #n ")" ::: "memory")
; #define PG8_WAIT_L(n) asm volatile("s_waitcnt lgkmcnt(" #n ")" ::: "memory")
; template <class Epi, class Sched, bool ALIGN_EPI = false, bool SP2 = false>
; __device__ __forceinline__ void gemm_phase(PG8_LAS unsigned char* lds, const Gemm g, const Sched& S, const Epi& E, const bool skip_epi = false) {
;     ...
;         for (int t = 0; t < nt; t += 2) {
;             const bool last = (t == nt - 2); last_ = last && has_next;
;             const char* a1 = cA + (size_t)(t + 1) * kstep;
;             const char* a2 = last ? nA : cA + (size_t)(t + 2) * kstep; const char* b2 = last ? nB : cB + (size_t)(t + 2) * kstep;
;             const char* a3 = a2 + kstep; const char* b3 = b2 + kstep;
;             if (last && has_next) S.a_ready(nxt);
;             if constexpr (SP2) {
;             PG8_LDB(B0, 0, 0); PG8_LDB(B1, 0, 1); PG8_SCHED; PG8_LDA(At, 0, 0); PG8_STAGE_A(1, 1, a1, false);
;             PG8_WAIT_V(8); PG8_WAIT_L(0); PG8_BAR; PG8_MMA(0, 0, At, B0); PG8_MMA(0, 1, At, B1); PG8_BAR; PG8_SCHED;
;     ...
;             PG8_LDA(At, 1, 1); PG8_STAGE(PG8_SB(1, 0), b3, voffB); PG8_STAGE(PG8_SB(1, 1), b3 + hstep, voffB); PG8_STAGE_A(1, 0, a3, true);
;             PG8_WAIT_V(8); PG8_WAIT_L(0); PG8_BAR; PG8_MMA(1, 0, At, B0); PG8_MMA(1, 1, At, B1); PG8_BAR; PG8_SCHED;
	s_add_i32 s28, s61, s2
	s_add_i32 m0, s28, 0xffffff80
	ds_read_b128 v[192:195], v172 offset:49152
	ds_read_b128 v[196:199], v172 offset:50176
	ds_read_b128 v[200:203], v172 offset:51200
	ds_read_b128 v[204:207], v172 offset:52224
	ds_read_b128 v[208:211], v172 offset:53248
	ds_read_b128 v[212:215], v172 offset:54272
	ds_read_b128 v[216:219], v172 offset:55296
	ds_read_b128 v[220:223], v172 offset:56320
	global_load_lds_dwordx4 v134, s[26:27] offset:128
	s_add_i32 m0, s28, 0x1f80
	s_add_i32 s28, s62, s2
	global_load_lds_dwordx4 v130, s[26:27] offset:128
	s_add_u32 s26, s26, 0x40080
	s_addc_u32 s27, s27, 0
	s_mov_b32 m0, s28
	s_nop 0
	global_load_lds_dwordx4 v134, s[26:27]
	s_add_i32 m0, s28, 0x2000
	s_nop 0
	global_load_lds_dwordx4 v130, s[26:27]
	s_add_i32 m0, s37, 0xffffff80
	s_nop 0
	global_load_lds_dwordx4 v136, s[98:99] offset:128
	s_add_i32 m0, s38, 0xffffff80
	s_nop 0
	global_load_lds_dwordx4 v132, s[98:99] offset:128
	s_waitcnt vmcnt(8)
	s_waitcnt lgkmcnt(0)
	s_barrier
	s_setprio 3
	s_waitcnt lgkmcnt(0)
	v_mfma_f32_16x16x32_bf16 v[62:65], v[148:151], v[192:195], v[62:65]
	v_mfma_f32_16x16x32_bf16 v[58:61], v[156:159], v[192:195], v[58:61]
	v_mfma_f32_16x16x32_bf16 v[50:53], v[148:151], v[200:203], v[50:53]
	v_mfma_f32_16x16x32_bf16 v[42:45], v[156:159], v[200:203], v[42:45]
	v_mfma_f32_16x16x32_bf16 v[34:37], v[148:151], v[208:211], v[34:37]
	v_mfma_f32_16x16x32_bf16 v[26:29], v[156:159], v[208:211], v[26:29]
	v_mfma_f32_16x16x32_bf16 v[18:21], v[148:151], v[216:219], v[18:21]
	v_mfma_f32_16x16x32_bf16 v[10:13], v[156:159], v[216:219], v[10:13]
	v_mfma_f32_16x16x32_bf16 v[62:65], v[152:155], v[196:199], v[62:65]
	v_mfma_f32_16x16x32_bf16 v[58:61], v[160:163], v[196:199], v[58:61]
	v_mfma_f32_16x16x32_bf16 v[50:53], v[152:155], v[204:207], v[50:53]
	v_mfma_f32_16x16x32_bf16 v[42:45], v[160:163], v[204:207], v[42:45]
	v_mfma_f32_16x16x32_bf16 v[34:37], v[152:155], v[212:215], v[34:37]
	v_mfma_f32_16x16x32_bf16 v[26:29], v[160:163], v[212:215], v[26:29]
	v_mfma_f32_16x16x32_bf16 v[18:21], v[152:155], v[220:223], v[18:21]
	v_mfma_f32_16x16x32_bf16 v[10:13], v[160:163], v[220:223], v[10:13]
	v_mfma_f32_16x16x32_bf16 v[54:57], v[176:179], v[192:195], v[54:57]
	v_mfma_f32_16x16x32_bf16 v[46:49], v[184:187], v[192:195], v[46:49]
	v_mfma_f32_16x16x32_bf16 v[38:41], v[176:179], v[200:203], v[38:41]
	v_mfma_f32_16x16x32_bf16 v[30:33], v[184:187], v[200:203], v[30:33]
	v_mfma_f32_16x16x32_bf16 v[22:25], v[176:179], v[208:211], v[22:25]
	v_mfma_f32_16x16x32_bf16 v[14:17], v[184:187], v[208:211], v[14:17]
	v_mfma_f32_16x16x32_bf16 v[6:9], v[176:179], v[216:219], v[6:9]
	v_mfma_f32_16x16x32_bf16 v[2:5], v[184:187], v[216:219], v[2:5]
	v_mfma_f32_16x16x32_bf16 v[54:57], v[180:183], v[196:199], v[54:57]
	v_mfma_f32_16x16x32_bf16 v[46:49], v[188:191], v[196:199], v[46:49]
	v_mfma_f32_16x16x32_bf16 v[38:41], v[180:183], v[204:207], v[38:41]
	v_mfma_f32_16x16x32_bf16 v[30:33], v[188:191], v[204:207], v[30:33]
	v_mfma_f32_16x16x32_bf16 v[22:25], v[180:183], v[212:215], v[22:25]
	v_mfma_f32_16x16x32_bf16 v[14:17], v[188:191], v[212:215], v[14:17]
	v_mfma_f32_16x16x32_bf16 v[6:9], v[180:183], v[220:223], v[6:9]
	v_mfma_f32_16x16x32_bf16 v[2:5], v[188:191], v[220:223], v[2:5]
	s_setprio 0
	s_barrier
	s_add_i32 s60, s60, 2
	s_add_u32 s24, s24, 0x100
	s_addc_u32 s25, s25, 0
	s_add_u32 s58, s58, 0x100
	s_addc_u32 s59, s59, 0
	s_cmp_gt_u32 s60, 13
.LBB0_253:
	ds_read_b128 v[148:151], v170
	ds_read_b128 v[152:155], v170 offset:1024
	ds_read_b128 v[156:159], v170 offset:2048
	ds_read_b128 v[160:163], v170 offset:3072
	ds_read_b128 v[176:179], v171
	ds_read_b128 v[180:183], v171 offset:1024
	ds_read_b128 v[184:187], v171 offset:2048
	ds_read_b128 v[188:191], v171 offset:3072
	s_add_u32 s26, s24, 0xfffc0080
	s_addc_u32 s27, s25, -1
	s_cmp_eq_u32 s60, 12
	s_cselect_b32 s29, s17, s27
	s_cselect_b32 s28, s56, s26
	s_cselect_b32 s27, s15, s59
	s_cselect_b32 s26, s57, s58
	s_add_i32 m0, s23, 0xc000
	ds_read_b128 v[192:195], v172
	ds_read_b128 v[196:199], v172 offset:1024
	ds_read_b128 v[200:203], v172 offset:2048
	ds_read_b128 v[204:207], v172 offset:3072
	ds_read_b128 v[208:211], v172 offset:4096
	ds_read_b128 v[212:215], v172 offset:5120
	ds_read_b128 v[216:219], v172 offset:6144
	ds_read_b128 v[220:223], v172 offset:7168
	global_load_lds_dwordx4 v140, s[24:25]
	s_add_i32 m0, s23, 0xe000
	s_nop 0
	global_load_lds_dwordx4 v142, s[24:25]
	s_waitcnt vmcnt(8)
	s_waitcnt lgkmcnt(0)
	s_barrier
	s_setprio 3
	s_waitcnt lgkmcnt(0)
	v_mfma_f32_16x16x32_bf16 v[126:129], v[148:151], v[192:195], v[126:129]
	v_mfma_f32_16x16x32_bf16 v[122:125], v[156:159], v[192:195], v[122:125]
	v_mfma_f32_16x16x32_bf16 v[114:117], v[148:151], v[200:203], v[114:117]
	v_mfma_f32_16x16x32_bf16 v[106:109], v[156:159], v[200:203], v[106:109]
	v_mfma_f32_16x16x32_bf16 v[98:101], v[148:151], v[208:211], v[98:101]
	v_mfma_f32_16x16x32_bf16 v[90:93], v[156:159], v[208:211], v[90:93]
	v_mfma_f32_16x16x32_bf16 v[82:85], v[148:151], v[216:219], v[82:85]
	v_mfma_f32_16x16x32_bf16 v[74:77], v[156:159], v[216:219], v[74:77]
	v_mfma_f32_16x16x32_bf16 v[126:129], v[152:155], v[196:199], v[126:129]
	v_mfma_f32_16x16x32_bf16 v[122:125], v[160:163], v[196:199], v[122:125]
	v_mfma_f32_16x16x32_bf16 v[114:117], v[152:155], v[204:207], v[114:117]
	v_mfma_f32_16x16x32_bf16 v[106:109], v[160:163], v[204:207], v[106:109]
	v_mfma_f32_16x16x32_bf16 v[98:101], v[152:155], v[212:215], v[98:101]
	v_mfma_f32_16x16x32_bf16 v[90:93], v[160:163], v[212:215], v[90:93]
	v_mfma_f32_16x16x32_bf16 v[82:85], v[152:155], v[220:223], v[82:85]
	v_mfma_f32_16x16x32_bf16 v[74:77], v[160:163], v[220:223], v[74:77]
	v_mfma_f32_16x16x32_bf16 v[118:121], v[176:179], v[192:195], v[118:121]
	v_mfma_f32_16x16x32_bf16 v[110:113], v[184:187], v[192:195], v[110:113]
	v_mfma_f32_16x16x32_bf16 v[102:105], v[176:179], v[200:203], v[102:105]
	v_mfma_f32_16x16x32_bf16 v[94:97], v[184:187], v[200:203], v[94:97]
	v_mfma_f32_16x16x32_bf16 v[86:89], v[176:179], v[208:211], v[86:89]
	v_mfma_f32_16x16x32_bf16 v[78:81], v[184:187], v[208:211], v[78:81]
	v_mfma_f32_16x16x32_bf16 v[70:73], v[176:179], v[216:219], v[70:73]
	v_mfma_f32_16x16x32_bf16 v[66:69], v[184:187], v[216:219], v[66:69]
	v_mfma_f32_16x16x32_bf16 v[118:121], v[180:183], v[196:199], v[118:121]
	v_mfma_f32_16x16x32_bf16 v[110:113], v[188:191], v[196:199], v[110:113]
	v_mfma_f32_16x16x32_bf16 v[102:105], v[180:183], v[204:207], v[102:105]
	v_mfma_f32_16x16x32_bf16 v[94:97], v[188:191], v[204:207], v[94:97]
	v_mfma_f32_16x16x32_bf16 v[86:89], v[180:183], v[212:215], v[86:89]
	v_mfma_f32_16x16x32_bf16 v[78:81], v[188:191], v[212:215], v[78:81]
	v_mfma_f32_16x16x32_bf16 v[70:73], v[180:183], v[220:223], v[70:73]
	v_mfma_f32_16x16x32_bf16 v[66:69], v[188:191], v[220:223], v[66:69]
	s_setprio 0
	s_barrier
; #define PG8_STAGE_A(b, h, ptr, NX) do { if constexpr (Sched::GATHER) { unsigned gs_[2]; gs_[0] = ((NX) && last_) ? gN[h][0] : gA[h][0]; gs_[1] = ((NX) && last_) ? gN[h][1] : gA[h][1]; PG8_STAGE(PG8_SA(b, h), ptr, gs_); } \
;         else PG8_STAGE(PG8_SA(b, h), (ptr) + ((h) ? hstep : (size_t)0), voffA); } while (0)
; #define PG8_STAGE(bufoff, gbase, voff) do { _Pragma("unroll") for (int _i = 0; _i < 2; ++_i) \
;         __builtin_amdgcn_global_load_lds((const unsigned*)((const char*)(gbase) + (voff)[_i]), (PG8_LAS unsigned*)(lds + (bufoff) + ldsw + _i * 8192), 16, 0, 0); } while (0)
; #define PG8_LDA(dst, b, h) do { _Pragma("unroll") for (int m = 0; m < 4; ++m) _Pragma("unroll") for (int k = 0; k < 2; ++k) dst[m][k] = *(const PG8_LAS bf16x8*)(lds + PG8_SA(b, h) + aoff + m * 2048 + k * 1024); } while (0)
; #define PG8_LDB(dst, b, h) do { _Pragma("unroll") for (int n = 0; n < 2; ++n) _Pragma("unroll") for (int k = 0; k < 2; ++k) dst[n][k] = *(const PG8_LAS bf16x8*)(lds + PG8_SB(b, h) + boff + n * 2048 + k * 1024); } while (0)
; #define PG8_MMA(ai, bj, At, Bt) do { __builtin_amdgcn_s_setprio(1); _Pragma("unroll") for (int m = 0; m < 4; ++m) _Pragma("unroll") for (int n = 0; n < 2; ++n) _Pragma("unroll") for (int k = 0; k < 2; ++k) \
;         acc[ai][bj][m][n] = __builtin_amdgcn_mfma_f32_16x16x32_bf16(Bt[n][k], At[m][k], acc[ai][bj][m][n], 0, 0, 0); __builtin_amdgcn_s_setprio(0); } while (0)
; #define PG8_WAIT_V(n) asm volatile("s_waitcnt vmcnt(" #n ")" ::: "memory")
; #define PG8_WAIT_L(n) asm volatile("s_waitcnt lgkmcnt(" #n ")" ::: "memory")
; #define PG8_BAR __builtin_amdgcn_s_barrier()
; #define PG8_SCHED __builtin_amdgcn_sched_barrier(0)
; template <class Epi, class Sched, bool ALIGN_EPI = false, bool SP2 = false>
; __device__ __forceinline__ void gemm_phase(PG8_LAS unsigned char* lds, const Gemm g, const Sched& S, const Epi& E, const bool skip_epi = false) {
;     ...
;             PG8_LDA(At, 0, 1); PG8_STAGE(PG8_SB(0, 0), b2, voffB); PG8_STAGE(PG8_SB(0, 1), b2 + hstep, voffB); PG8_STAGE_A(0, 0, a2, true);
;             PG8_WAIT_V(8); PG8_WAIT_L(0); PG8_BAR; PG8_MMA(1, 0, At, B0); PG8_MMA(1, 1, At, B1); PG8_BAR; PG8_SCHED;
;             PG8_LDB(B0, 1, 0); PG8_LDB(B1, 1, 1); PG8_SCHED; PG8_LDA(At, 1, 0); PG8_STAGE_A(0, 1, a2, true);
;             PG8_WAIT_V(8); PG8_WAIT_L(0); PG8_BAR; PG8_MMA(0, 0, At, B0); PG8_MMA(0, 1, At, B1); PG8_BAR; PG8_SCHED;
	s_add_i32 s61, s46, s2
	s_mov_b32 m0, s61
	ds_read_b128 v[192:195], v172 offset:16384
	ds_read_b128 v[196:199], v172 offset:17408
	ds_read_b128 v[200:203], v172 offset:18432
	ds_read_b128 v[204:207], v172 offset:19456
	ds_read_b128 v[208:211], v172 offset:20480
	ds_read_b128 v[212:215], v172 offset:21504
	ds_read_b128 v[216:219], v172 offset:22528
	ds_read_b128 v[220:223], v172 offset:23552
	global_load_lds_dwordx4 v134, s[26:27]
	s_add_i32 m0, s61, 0x2000
	s_add_u32 s62, s26, 0x40000
	s_addc_u32 s63, s27, 0
	s_add_i32 s61, s47, s2
	global_load_lds_dwordx4 v130, s[26:27]
	s_mov_b32 m0, s61
	s_mov_b64 s[98:99], s[28:29]
	global_load_lds_dwordx4 v134, s[62:63]
	s_add_i32 m0, s61, 0x2000
	s_nop 0
	global_load_lds_dwordx4 v130, s[62:63]
	s_mov_b32 m0, s23
	s_nop 0
	global_load_lds_dwordx4 v136, s[28:29]
	s_mov_b32 m0, s31
	s_nop 0
	global_load_lds_dwordx4 v132, s[28:29]
	s_waitcnt vmcnt(8)
	s_waitcnt lgkmcnt(0)
	s_barrier
	s_setprio 3
	s_waitcnt lgkmcnt(0)
	v_mfma_f32_16x16x32_bf16 v[62:65], v[148:151], v[192:195], v[62:65]
	v_mfma_f32_16x16x32_bf16 v[58:61], v[156:159], v[192:195], v[58:61]
	v_mfma_f32_16x16x32_bf16 v[50:53], v[148:151], v[200:203], v[50:53]
	v_mfma_f32_16x16x32_bf16 v[42:45], v[156:159], v[200:203], v[42:45]
	v_mfma_f32_16x16x32_bf16 v[34:37], v[148:151], v[208:211], v[34:37]
	v_mfma_f32_16x16x32_bf16 v[26:29], v[156:159], v[208:211], v[26:29]
	v_mfma_f32_16x16x32_bf16 v[18:21], v[148:151], v[216:219], v[18:21]
	v_mfma_f32_16x16x32_bf16 v[10:13], v[156:159], v[216:219], v[10:13]
	v_mfma_f32_16x16x32_bf16 v[62:65], v[152:155], v[196:199], v[62:65]
	v_mfma_f32_16x16x32_bf16 v[58:61], v[160:163], v[196:199], v[58:61]
	v_mfma_f32_16x16x32_bf16 v[50:53], v[152:155], v[204:207], v[50:53]
	v_mfma_f32_16x16x32_bf16 v[42:45], v[160:163], v[204:207], v[42:45]
	v_mfma_f32_16x16x32_bf16 v[34:37], v[152:155], v[212:215], v[34:37]
	v_mfma_f32_16x16x32_bf16 v[26:29], v[160:163], v[212:215], v[26:29]
	v_mfma_f32_16x16x32_bf16 v[18:21], v[152:155], v[220:223], v[18:21]
	v_mfma_f32_16x16x32_bf16 v[10:13], v[160:163], v[220:223], v[10:13]
	v_mfma_f32_16x16x32_bf16 v[54:57], v[176:179], v[192:195], v[54:57]
	v_mfma_f32_16x16x32_bf16 v[46:49], v[184:187], v[192:195], v[46:49]
	v_mfma_f32_16x16x32_bf16 v[38:41], v[176:179], v[200:203], v[38:41]
	v_mfma_f32_16x16x32_bf16 v[30:33], v[184:187], v[200:203], v[30:33]
	v_mfma_f32_16x16x32_bf16 v[22:25], v[176:179], v[208:211], v[22:25]
	v_mfma_f32_16x16x32_bf16 v[14:17], v[184:187], v[208:211], v[14:17]
	v_mfma_f32_16x16x32_bf16 v[6:9], v[176:179], v[216:219], v[6:9]
	v_mfma_f32_16x16x32_bf16 v[2:5], v[184:187], v[216:219], v[2:5]
	v_mfma_f32_16x16x32_bf16 v[54:57], v[180:183], v[196:199], v[54:57]
	v_mfma_f32_16x16x32_bf16 v[46:49], v[188:191], v[196:199], v[46:49]
	v_mfma_f32_16x16x32_bf16 v[38:41], v[180:183], v[204:207], v[38:41]
	v_mfma_f32_16x16x32_bf16 v[30:33], v[188:191], v[204:207], v[30:33]
	v_mfma_f32_16x16x32_bf16 v[22:25], v[180:183], v[212:215], v[22:25]
	v_mfma_f32_16x16x32_bf16 v[14:17], v[188:191], v[212:215], v[14:17]
	v_mfma_f32_16x16x32_bf16 v[6:9], v[180:183], v[220:223], v[6:9]
	v_mfma_f32_16x16x32_bf16 v[2:5], v[188:191], v[220:223], v[2:5]
	s_setprio 0
	s_barrier
	s_add_i32 s61, 0, 0x18000
	s_add_i32 s62, 0, 0x1c000
	v_add_u32_e32 v160, s61, v1
	v_add_u32_e32 v188, s62, v1
	ds_read_b128 v[148:151], v160
	ds_read_b128 v[152:155], v160 offset:1024
	ds_read_b128 v[156:159], v160 offset:2048
	ds_read_b128 v[160:163], v160 offset:3072
	ds_read_b128 v[176:179], v188
	ds_read_b128 v[180:183], v188 offset:1024
	ds_read_b128 v[184:187], v188 offset:2048
	ds_read_b128 v[188:191], v188 offset:3072
	s_add_u32 s28, s28, 0x40000
	s_addc_u32 s29, s29, 0
	s_mov_b32 m0, s34
	ds_read_b128 v[192:195], v172 offset:32768
	ds_read_b128 v[196:199], v172 offset:33792
	ds_read_b128 v[200:203], v172 offset:34816
	ds_read_b128 v[204:207], v172 offset:35840
	ds_read_b128 v[208:211], v172 offset:36864
	ds_read_b128 v[212:215], v172 offset:37888
	ds_read_b128 v[216:219], v172 offset:38912
	ds_read_b128 v[220:223], v172 offset:39936
	global_load_lds_dwordx4 v136, s[28:29]
	s_mov_b32 m0, s35
	s_nop 0
	global_load_lds_dwordx4 v132, s[28:29]
	s_waitcnt vmcnt(8)
	s_waitcnt lgkmcnt(0)
	s_barrier
; #define PG8_STAGE_A(b, h, ptr, NX) do { if constexpr (Sched::GATHER) { unsigned gs_[2]; gs_[0] = ((NX) && last_) ? gN[h][0] : gA[h][0]; gs_[1] = ((NX) && last_) ? gN[h][1] : gA[h][1]; PG8_STAGE(PG8_SA(b, h), ptr, gs_); } \
;         else PG8_STAGE(PG8_SA(b, h), (ptr) + ((h) ? hstep : (size_t)0), voffA); } while (0)
; #define PG8_STAGE(bufoff, gbase, voff) do { _Pragma("unroll") for (int _i = 0; _i < 2; ++_i) \
;         __builtin_amdgcn_global_load_lds((const unsigned*)((const char*)(gbase) + (voff)[_i]), (PG8_LAS unsigned*)(lds + (bufoff) + ldsw + _i * 8192), 16, 0, 0); } while (0)
; #define PG8_LDA(dst, b, h) do { _Pragma("unroll") for (int m = 0; m < 4; ++m) _Pragma("unroll") for (int k = 0; k < 2; ++k) dst[m][k] = *(const PG8_LAS bf16x8*)(lds + PG8_SA(b, h) + aoff + m * 2048 + k * 1024); } while (0)
; #define PG8_MMA(ai, bj, At, Bt) do { __builtin_amdgcn_s_setprio(1); _Pragma("unroll") for (int m = 0; m < 4; ++m) _Pragma("unroll") for (int n = 0; n < 2; ++n) _Pragma("unroll") for (int k = 0; k < 2; ++k) \
;         acc[ai][bj][m][n] = __builtin_amdgcn_mfma_f32_16x16x32_bf16(Bt[n][k], At[m][k], acc[ai][bj][m][n], 0, 0, 0); __builtin_amdgcn_s_setprio(0); } while (0)
; #define PG8_WAIT_V(n) asm volatile("s_waitcnt vmcnt(" #n ")" ::: "memory")
; #define PG8_BAR __builtin_amdgcn_s_barrier()
; __device__ __forceinline__ void rstd8(const float* SS, int rowb, int lane, float (&rs)[2][4]) {
;     f32x4 p[2][4];
; #pragma unroll
;     for (int ai = 0; ai < 2; ++ai)
; #pragma unroll
;         for (int m = 0; m < 4; ++m) p[ai][m] = *(const f32x4*)(SS + (size_t)(rowb + HALF * ai + 16 * m + (lane >> 2)) * 16 + 4 * (lane & 3));
;     asm volatile("" : "+v"(p[0][0]), "+v"(p[0][1]), "+v"(p[0][2]), "+v"(p[0][3]), "+v"(p[1][0]), "+v"(p[1][1]), "+v"(p[1][2]), "+v"(p[1][3]));
; template <class Epi, class Sched, bool ALIGN_EPI = false, bool SP2 = false>
; __device__ __forceinline__ void gemm_phase(PG8_LAS unsigned char* lds, const Gemm g, const Sched& S, const Epi& E, const bool skip_epi = false) {
;     ...
;             PG8_WAIT_V(8); PG8_WAIT_L(0); PG8_BAR; PG8_MMA(0, 0, At, B0); PG8_MMA(0, 1, At, B1); PG8_BAR; PG8_SCHED;
;             PG8_LDA(At, 1, 1); PG8_STAGE(PG8_SB(1, 0), b3, voffB); PG8_STAGE(PG8_SB(1, 1), b3 + hstep, voffB); PG8_STAGE_A(1, 0, a3, true);
;             PG8_WAIT_V(8); PG8_WAIT_L(0); PG8_BAR; PG8_MMA(1, 0, At, B0); PG8_MMA(1, 1, At, B1); PG8_BAR; PG8_SCHED;
	s_setprio 3
	s_waitcnt lgkmcnt(0)
	v_mfma_f32_16x16x32_bf16 v[126:129], v[148:151], v[192:195], v[126:129]
	v_mfma_f32_16x16x32_bf16 v[122:125], v[156:159], v[192:195], v[122:125]
	v_mfma_f32_16x16x32_bf16 v[114:117], v[148:151], v[200:203], v[114:117]
	v_mfma_f32_16x16x32_bf16 v[106:109], v[156:159], v[200:203], v[106:109]
	v_mfma_f32_16x16x32_bf16 v[98:101], v[148:151], v[208:211], v[98:101]
	v_mfma_f32_16x16x32_bf16 v[90:93], v[156:159], v[208:211], v[90:93]
	v_mfma_f32_16x16x32_bf16 v[82:85], v[148:151], v[216:219], v[82:85]
	v_mfma_f32_16x16x32_bf16 v[74:77], v[156:159], v[216:219], v[74:77]
	v_mfma_f32_16x16x32_bf16 v[126:129], v[152:155], v[196:199], v[126:129]
	v_mfma_f32_16x16x32_bf16 v[122:125], v[160:163], v[196:199], v[122:125]
	v_mfma_f32_16x16x32_bf16 v[114:117], v[152:155], v[204:207], v[114:117]
	v_mfma_f32_16x16x32_bf16 v[106:109], v[160:163], v[204:207], v[106:109]
	v_mfma_f32_16x16x32_bf16 v[98:101], v[152:155], v[212:215], v[98:101]
	v_mfma_f32_16x16x32_bf16 v[90:93], v[160:163], v[212:215], v[90:93]
	v_mfma_f32_16x16x32_bf16 v[82:85], v[152:155], v[220:223], v[82:85]
	v_mfma_f32_16x16x32_bf16 v[74:77], v[160:163], v[220:223], v[74:77]
	v_mfma_f32_16x16x32_bf16 v[118:121], v[176:179], v[192:195], v[118:121]
	v_mfma_f32_16x16x32_bf16 v[110:113], v[184:187], v[192:195], v[110:113]
	v_mfma_f32_16x16x32_bf16 v[102:105], v[176:179], v[200:203], v[102:105]
	v_mfma_f32_16x16x32_bf16 v[94:97], v[184:187], v[200:203], v[94:97]
	v_mfma_f32_16x16x32_bf16 v[86:89], v[176:179], v[208:211], v[86:89]
	v_mfma_f32_16x16x32_bf16 v[78:81], v[184:187], v[208:211], v[78:81]
	v_mfma_f32_16x16x32_bf16 v[70:73], v[176:179], v[216:219], v[70:73]
	v_mfma_f32_16x16x32_bf16 v[66:69], v[184:187], v[216:219], v[66:69]
	v_mfma_f32_16x16x32_bf16 v[118:121], v[180:183], v[196:199], v[118:121]
	v_mfma_f32_16x16x32_bf16 v[110:113], v[188:191], v[196:199], v[110:113]
	v_mfma_f32_16x16x32_bf16 v[102:105], v[180:183], v[204:207], v[102:105]
	v_mfma_f32_16x16x32_bf16 v[94:97], v[188:191], v[204:207], v[94:97]
	v_mfma_f32_16x16x32_bf16 v[86:89], v[180:183], v[212:215], v[86:89]
	v_mfma_f32_16x16x32_bf16 v[78:81], v[188:191], v[212:215], v[78:81]
	v_mfma_f32_16x16x32_bf16 v[70:73], v[180:183], v[220:223], v[70:73]
	v_mfma_f32_16x16x32_bf16 v[66:69], v[188:191], v[220:223], v[66:69]
	s_setprio 0
	s_barrier
	s_add_i32 s28, s61, s2
	s_add_i32 m0, s28, 0xffffff80
	ds_read_b128 v[192:195], v172 offset:49152
	ds_read_b128 v[196:199], v172 offset:50176
	ds_read_b128 v[200:203], v172 offset:51200
	ds_read_b128 v[204:207], v172 offset:52224
	ds_read_b128 v[208:211], v172 offset:53248
	ds_read_b128 v[212:215], v172 offset:54272
	ds_read_b128 v[216:219], v172 offset:55296
	ds_read_b128 v[220:223], v172 offset:56320
	global_load_lds_dwordx4 v134, s[26:27] offset:128
	s_add_i32 m0, s28, 0x1f80
	s_add_i32 s28, s62, s2
	global_load_lds_dwordx4 v130, s[26:27] offset:128
	s_add_u32 s26, s26, 0x40080
	s_addc_u32 s27, s27, 0
	s_mov_b32 m0, s28
	s_nop 0
	global_load_lds_dwordx4 v134, s[26:27]
	s_add_i32 m0, s28, 0x2000
	s_nop 0
	global_load_lds_dwordx4 v130, s[26:27]
	s_add_i32 m0, s37, 0xffffff80
	s_nop 0
	global_load_lds_dwordx4 v136, s[98:99] offset:128
	s_add_i32 m0, s38, 0xffffff80
	s_nop 0
	global_load_lds_dwordx4 v132, s[98:99] offset:128
	s_waitcnt vmcnt(8)
	s_waitcnt lgkmcnt(0)
	s_barrier
	s_setprio 3
	s_waitcnt lgkmcnt(0)
	v_mfma_f32_16x16x32_bf16 v[62:65], v[148:151], v[192:195], v[62:65]
	v_mfma_f32_16x16x32_bf16 v[58:61], v[156:159], v[192:195], v[58:61]
	v_mfma_f32_16x16x32_bf16 v[50:53], v[148:151], v[200:203], v[50:53]
	v_mfma_f32_16x16x32_bf16 v[42:45], v[156:159], v[200:203], v[42:45]
	v_mfma_f32_16x16x32_bf16 v[34:37], v[148:151], v[208:211], v[34:37]
	v_mfma_f32_16x16x32_bf16 v[26:29], v[156:159], v[208:211], v[26:29]
	v_mfma_f32_16x16x32_bf16 v[18:21], v[148:151], v[216:219], v[18:21]
	v_mfma_f32_16x16x32_bf16 v[10:13], v[156:159], v[216:219], v[10:13]
	v_mfma_f32_16x16x32_bf16 v[62:65], v[152:155], v[196:199], v[62:65]
	v_mfma_f32_16x16x32_bf16 v[58:61], v[160:163], v[196:199], v[58:61]
	v_mfma_f32_16x16x32_bf16 v[50:53], v[152:155], v[204:207], v[50:53]
	v_mfma_f32_16x16x32_bf16 v[42:45], v[160:163], v[204:207], v[42:45]
	v_mfma_f32_16x16x32_bf16 v[34:37], v[152:155], v[212:215], v[34:37]
	v_mfma_f32_16x16x32_bf16 v[26:29], v[160:163], v[212:215], v[26:29]
	v_mfma_f32_16x16x32_bf16 v[18:21], v[152:155], v[220:223], v[18:21]
	v_mfma_f32_16x16x32_bf16 v[10:13], v[160:163], v[220:223], v[10:13]
	v_mfma_f32_16x16x32_bf16 v[54:57], v[176:179], v[192:195], v[54:57]
	v_mfma_f32_16x16x32_bf16 v[46:49], v[184:187], v[192:195], v[46:49]
	v_mfma_f32_16x16x32_bf16 v[38:41], v[176:179], v[200:203], v[38:41]
	v_mfma_f32_16x16x32_bf16 v[30:33], v[184:187], v[200:203], v[30:33]
	v_mfma_f32_16x16x32_bf16 v[22:25], v[176:179], v[208:211], v[22:25]
	v_mfma_f32_16x16x32_bf16 v[14:17], v[184:187], v[208:211], v[14:17]
	v_mfma_f32_16x16x32_bf16 v[6:9], v[176:179], v[216:219], v[6:9]
	v_mfma_f32_16x16x32_bf16 v[2:5], v[184:187], v[216:219], v[2:5]
	v_mfma_f32_16x16x32_bf16 v[54:57], v[180:183], v[196:199], v[54:57]
	v_mfma_f32_16x16x32_bf16 v[46:49], v[188:191], v[196:199], v[46:49]
	v_mfma_f32_16x16x32_bf16 v[38:41], v[180:183], v[204:207], v[38:41]
	v_mfma_f32_16x16x32_bf16 v[30:33], v[188:191], v[204:207], v[30:33]
	v_mfma_f32_16x16x32_bf16 v[22:25], v[180:183], v[212:215], v[22:25]
	v_mfma_f32_16x16x32_bf16 v[14:17], v[188:191], v[212:215], v[14:17]
	v_mfma_f32_16x16x32_bf16 v[6:9], v[180:183], v[220:223], v[6:9]
	v_mfma_f32_16x16x32_bf16 v[2:5], v[188:191], v[220:223], v[2:5]
	s_setprio 0
	s_barrier
	s_add_i32 s60, s60, 2
	s_add_u32 s24, s24, 0x100
	s_addc_u32 s25, s25, 0
	s_add_u32 s58, s58, 0x100
	s_addc_u32 s59, s59, 0
	s_cmp_gt_u32 s60, 13
	s_cbranch_scc0 .LBB0_253
	v_lshl_add_u32 v164, s22, 8, v167
	v_ashrrev_i32_e32 v165, 31, v164
	v_lshlrev_b64 v[148:149], 6, v[164:165]
	v_lshl_add_u64 v[148:149], v[138:139], 0, v[148:149]
	v_add_co_u32_e32 v150, vcc, 0x2000, v148
	v_addc_co_u32_e32 v151, vcc, 0, v149, vcc
	global_load_dwordx4 v[176:179], v[148:149], off
	global_load_dwordx4 v[180:183], v[148:149], off offset:1024
	global_load_dwordx4 v[184:187], v[148:149], off offset:2048
	global_load_dwordx4 v[188:191], v[148:149], off offset:3072
	global_load_dwordx4 v[192:195], v[150:151], off
	global_load_dwordx4 v[196:199], v[150:151], off offset:1024
	global_load_dwordx4 v[200:203], v[150:151], off offset:2048
	global_load_dwordx4 v[204:207], v[150:151], off offset:3072
	s_and_b64 vcc, exec, s[12:13]
	s_cbranch_vccz .LBB0_256
	s_barrier

; #define PG8_GIDX(G_, PM_) do { if constexpr (Sched::GATHER) { _Pragma("unroll") for (int h_ = 0; h_ < 2; ++h_) _Pragma("unroll") for (int i_ = 0; i_ < 2; ++i_) { int R_, C_; stage_rc(tid * 16 + i_ * 8192, R_, C_); \
;         const int src_ = S.rowsrc[(PM_) * BM + h_ * HALF + R_]; G_[h_][i_] = (unsigned)(src_ * K + C_) * 2u; } } } while (0)
; #define PG8_STAGE_A(b, h, ptr, NX) do { if constexpr (Sched::GATHER) { unsigned gs_[2]; gs_[0] = ((NX) && last_) ? gN[h][0] : gA[h][0]; gs_[1] = ((NX) && last_) ? gN[h][1] : gA[h][1]; PG8_STAGE(PG8_SA(b, h), ptr, gs_); } \
;         else PG8_STAGE(PG8_SA(b, h), (ptr) + ((h) ? hstep : (size_t)0), voffA); } while (0)
; #define PG8_LDA(dst, b, h) do { _Pragma("unroll") for (int m = 0; m < 4; ++m) _Pragma("unroll") for (int k = 0; k < 2; ++k) dst[m][k] = *(const PG8_LAS bf16x8*)(lds + PG8_SA(b, h) + aoff + m * 2048 + k * 1024); } while (0)
; template <class Epi, class Sched, bool ALIGN_EPI = false, bool SP2 = false>
; __device__ __forceinline__ void gemm_phase(PG8_LAS unsigned char* lds, const Gemm g, const Sched& S, const Epi& E, const bool skip_epi = false) {
;     ...
;         const bool has_next = S.next(ui + 1, nxt);
;         if (has_next) PG8_GIDX(gN, nxt.pm);
;         const char* nA = has_next ? (const char*)g.A + (size_t)nxt.pm * pmstepA + nxt.ko : cA; const char* nB = has_next ? (const char*)g.Bt + (size_t)nxt.pn * tstep + nxt.ko : cB;
;         for (int t = 0; t < nt; t += 2) {
;             const bool last = (t == nt - 2); last_ = last && has_next;
;             const char* a1 = cA + (size_t)(t + 1) * kstep;
;             const char* a2 = last ? nA : cA + (size_t)(t + 2) * kstep; const char* b2 = last ? nB : cB + (size_t)(t + 2) * kstep;
;             const char* a3 = a2 + kstep; const char* b3 = b2 + kstep;
;             if (last && has_next) S.a_ready(nxt);
;             if constexpr (SP2) {
;             PG8_LDB(B0, 0, 0); PG8_LDB(B1, 0, 1); PG8_SCHED; PG8_LDA(At, 0, 0); PG8_STAGE_A(1, 1, a1, false);
;             PG8_WAIT_V(8); PG8_WAIT_L(0); PG8_BAR; PG8_MMA(0, 0, At, B0); PG8_MMA(0, 1, At, B1); PG8_BAR; PG8_SCHED;
;             PG8_LDA(At, 0, 1); PG8_STAGE(PG8_SB(0, 0), b2, voffB); PG8_STAGE(PG8_SB(0, 1), b2 + hstep, voffB); PG8_STAGE_A(0, 0, a2, true);
;             PG8_WAIT_V(8); PG8_WAIT_L(0); PG8_BAR; PG8_MMA(1, 0, At, B0); PG8_MMA(1, 1, At, B1); PG8_BAR; PG8_SCHED;
.LBB0_633:
	s_ashr_i32 s19, s18, 31
	s_lshl_b64 s[20:21], s[18:19], 19
	s_add_u32 s20, s46, s20
	s_addc_u32 s21, s47, s21
	s_and_b64 s[22:23], s[6:7], exec
	s_cselect_b32 s19, s21, s27
	s_cselect_b32 s25, s20, s26
	s_ashr_i32 s17, s16, 31
	s_lshl_b64 s[22:23], s[16:17], 19
	v_readlane_b32 s17, v254, 40
	s_add_u32 s22, s17, s22
	v_readlane_b32 s17, v254, 41
	s_addc_u32 s23, s17, s23
	s_and_b64 s[30:31], s[6:7], exec
	s_cselect_b32 s17, s23, s29
	s_cselect_b32 s60, s22, s28
	s_add_u32 s26, s26, 0x40080
	s_addc_u32 s27, s27, 0
	s_add_u32 s61, s28, 0x100
	s_addc_u32 s62, s29, 0
	s_mov_b32 s63, -2
	s_waitcnt lgkmcnt(0)
	ds_read_b128 v[98:101], v234
	ds_read_b128 v[110:113], v234 offset:1024
	ds_read_b128 v[122:125], v234 offset:2048
	ds_read_b128 v[126:129], v234 offset:3072
	ds_read_b128 v[138:141], v235
	ds_read_b128 v[142:145], v235 offset:1024
	ds_read_b128 v[146:149], v235 offset:2048
	ds_read_b128 v[150:153], v235 offset:3072
	s_add_u32 s28, s26, 0xfffc0080
	s_addc_u32 s29, s27, -1
	s_cmp_eq_u32 s63, 12
	s_cselect_b32 s31, s19, s29
	s_cselect_b32 s30, s25, s28
	s_cselect_b32 s29, s17, s62
	s_cselect_b32 s28, s60, s61
	s_add_i32 m0, s3, 0xc000
	ds_read_b128 v[154:157], v236
	ds_read_b128 v[166:169], v236 offset:1024
	ds_read_b128 v[170:173], v236 offset:2048
	ds_read_b128 v[174:177], v236 offset:3072
	ds_read_b128 v[178:181], v236 offset:4096
	ds_read_b128 v[182:185], v236 offset:5120
	ds_read_b128 v[186:189], v236 offset:6144
	ds_read_b128 v[206:209], v236 offset:7168
	global_load_lds_dwordx4 v198, s[26:27]
	s_add_i32 m0, s3, 0xe000
	s_nop 0
	global_load_lds_dwordx4 v200, s[26:27]
	s_waitcnt vmcnt(8)
	s_waitcnt lgkmcnt(0)
	s_barrier
	s_setprio 3
	s_waitcnt lgkmcnt(0)
	v_mfma_f32_16x16x32_bf16 v[162:165], v[98:101], v[154:157], 0
	v_mfma_f32_16x16x32_bf16 v[158:161], v[122:125], v[154:157], 0
	v_mfma_f32_16x16x32_bf16 v[118:121], v[98:101], v[170:173], 0
	v_mfma_f32_16x16x32_bf16 v[114:117], v[122:125], v[170:173], 0
	v_mfma_f32_16x16x32_bf16 v[94:97], v[98:101], v[178:181], 0
	v_mfma_f32_16x16x32_bf16 v[90:93], v[122:125], v[178:181], 0
	v_mfma_f32_16x16x32_bf16 v[78:81], v[98:101], v[186:189], 0
	v_mfma_f32_16x16x32_bf16 v[74:77], v[122:125], v[186:189], 0
	v_mfma_f32_16x16x32_bf16 v[162:165], v[110:113], v[166:169], v[162:165]
	v_mfma_f32_16x16x32_bf16 v[158:161], v[126:129], v[166:169], v[158:161]
	v_mfma_f32_16x16x32_bf16 v[118:121], v[110:113], v[174:177], v[118:121]
	v_mfma_f32_16x16x32_bf16 v[114:117], v[126:129], v[174:177], v[114:117]
	v_mfma_f32_16x16x32_bf16 v[94:97], v[110:113], v[182:185], v[94:97]
	v_mfma_f32_16x16x32_bf16 v[90:93], v[126:129], v[182:185], v[90:93]
	v_mfma_f32_16x16x32_bf16 v[78:81], v[110:113], v[206:209], v[78:81]
	v_mfma_f32_16x16x32_bf16 v[74:77], v[126:129], v[206:209], v[74:77]
	v_mfma_f32_16x16x32_bf16 v[134:137], v[138:141], v[154:157], 0
	v_mfma_f32_16x16x32_bf16 v[130:133], v[146:149], v[154:157], 0
	v_mfma_f32_16x16x32_bf16 v[106:109], v[138:141], v[170:173], 0
	v_mfma_f32_16x16x32_bf16 v[102:105], v[146:149], v[170:173], 0
	v_mfma_f32_16x16x32_bf16 v[86:89], v[138:141], v[178:181], 0
	v_mfma_f32_16x16x32_bf16 v[82:85], v[146:149], v[178:181], 0
	v_mfma_f32_16x16x32_bf16 v[70:73], v[138:141], v[186:189], 0
	v_mfma_f32_16x16x32_bf16 v[66:69], v[146:149], v[186:189], 0
	v_mfma_f32_16x16x32_bf16 v[134:137], v[142:145], v[166:169], v[134:137]
	v_mfma_f32_16x16x32_bf16 v[130:133], v[150:153], v[166:169], v[130:133]
	v_mfma_f32_16x16x32_bf16 v[106:109], v[142:145], v[174:177], v[106:109]
	v_mfma_f32_16x16x32_bf16 v[102:105], v[150:153], v[174:177], v[102:105]
	v_mfma_f32_16x16x32_bf16 v[86:89], v[142:145], v[182:185], v[86:89]
	v_mfma_f32_16x16x32_bf16 v[82:85], v[150:153], v[182:185], v[82:85]
	v_mfma_f32_16x16x32_bf16 v[70:73], v[142:145], v[206:209], v[70:73]
	v_mfma_f32_16x16x32_bf16 v[66:69], v[150:153], v[206:209], v[66:69]
	s_setprio 0
	s_barrier
	s_add_i32 s64, s57, s2
	s_mov_b32 m0, s64
	ds_read_b128 v[154:157], v236 offset:16384
	ds_read_b128 v[166:169], v236 offset:17408
	ds_read_b128 v[170:173], v236 offset:18432
	ds_read_b128 v[174:177], v236 offset:19456
	ds_read_b128 v[178:181], v236 offset:20480
	ds_read_b128 v[182:185], v236 offset:21504
	ds_read_b128 v[186:189], v236 offset:22528
	ds_read_b128 v[206:209], v236 offset:23552
	global_load_lds_dwordx4 v192, s[28:29]
	s_add_i32 m0, s64, 0x2000
	s_add_u32 s64, s28, 0x40000
	s_addc_u32 s65, s29, 0
	s_add_i32 s66, s58, s2
	global_load_lds_dwordx4 v196, s[28:29]
	s_mov_b32 m0, s66
	s_mov_b64 s[98:99], s[30:31]
	global_load_lds_dwordx4 v192, s[64:65]
	s_add_i32 m0, s66, 0x2000
	s_nop 0
	global_load_lds_dwordx4 v196, s[64:65]
	s_mov_b32 m0, s3
	s_nop 0
	global_load_lds_dwordx4 v190, s[30:31]
	s_mov_b32 m0, s34
	s_nop 0
	global_load_lds_dwordx4 v194, s[30:31]
	s_waitcnt vmcnt(8)
	s_waitcnt lgkmcnt(0)
	s_barrier
; #define PG8_STAGE_A(b, h, ptr, NX) do { if constexpr (Sched::GATHER) { unsigned gs_[2]; gs_[0] = ((NX) && last_) ? gN[h][0] : gA[h][0]; gs_[1] = ((NX) && last_) ? gN[h][1] : gA[h][1]; PG8_STAGE(PG8_SA(b, h), ptr, gs_); } \
;         else PG8_STAGE(PG8_SA(b, h), (ptr) + ((h) ? hstep : (size_t)0), voffA); } while (0)
; #define PG8_LDA(dst, b, h) do { _Pragma("unroll") for (int m = 0; m < 4; ++m) _Pragma("unroll") for (int k = 0; k < 2; ++k) dst[m][k] = *(const PG8_LAS bf16x8*)(lds + PG8_SA(b, h) + aoff + m * 2048 + k * 1024); } while (0)
; #define PG8_LDB(dst, b, h) do { _Pragma("unroll") for (int n = 0; n < 2; ++n) _Pragma("unroll") for (int k = 0; k < 2; ++k) dst[n][k] = *(const PG8_LAS bf16x8*)(lds + PG8_SB(b, h) + boff + n * 2048 + k * 1024); } while (0)
; #define PG8_MMA(ai, bj, At, Bt) do { __builtin_amdgcn_s_setprio(1); _Pragma("unroll") for (int m = 0; m < 4; ++m) _Pragma("unroll") for (int n = 0; n < 2; ++n) _Pragma("unroll") for (int k = 0; k < 2; ++k) \
;         acc[ai][bj][m][n] = __builtin_amdgcn_mfma_f32_16x16x32_bf16(Bt[n][k], At[m][k], acc[ai][bj][m][n], 0, 0, 0); __builtin_amdgcn_s_setprio(0); } while (0)
; #define PG8_WAIT_V(n) asm volatile("s_waitcnt vmcnt(" #n ")" ::: "memory")
; #define PG8_WAIT_L(n) asm volatile("s_waitcnt lgkmcnt(" #n ")" ::: "memory")
; #define PG8_BAR __builtin_amdgcn_s_barrier()
; #define PG8_SCHED __builtin_amdgcn_sched_barrier(0)
; template <class Epi, class Sched, bool ALIGN_EPI = false, bool SP2 = false>
; __device__ __forceinline__ void gemm_phase(PG8_LAS unsigned char* lds, const Gemm g, const Sched& S, const Epi& E, const bool skip_epi = false) {
;     ...
;             PG8_WAIT_V(8); PG8_WAIT_L(0); PG8_BAR; PG8_MMA(1, 0, At, B0); PG8_MMA(1, 1, At, B1); PG8_BAR; PG8_SCHED;
;             PG8_LDB(B0, 1, 0); PG8_LDB(B1, 1, 1); PG8_SCHED; PG8_LDA(At, 1, 0); PG8_STAGE_A(0, 1, a2, true);
;             PG8_WAIT_V(8); PG8_WAIT_L(0); PG8_BAR; PG8_MMA(0, 0, At, B0); PG8_MMA(0, 1, At, B1); PG8_BAR; PG8_SCHED;
	s_setprio 3
	s_waitcnt lgkmcnt(0)
	v_mfma_f32_16x16x32_bf16 v[62:65], v[98:101], v[154:157], 0
	v_mfma_f32_16x16x32_bf16 v[58:61], v[122:125], v[154:157], 0
	v_mfma_f32_16x16x32_bf16 v[46:49], v[98:101], v[170:173], 0
	v_mfma_f32_16x16x32_bf16 v[42:45], v[122:125], v[170:173], 0
	v_mfma_f32_16x16x32_bf16 v[30:33], v[98:101], v[178:181], 0
	v_mfma_f32_16x16x32_bf16 v[26:29], v[122:125], v[178:181], 0
	v_mfma_f32_16x16x32_bf16 v[14:17], v[98:101], v[186:189], 0
	v_mfma_f32_16x16x32_bf16 v[10:13], v[122:125], v[186:189], 0
	v_mfma_f32_16x16x32_bf16 v[62:65], v[110:113], v[166:169], v[62:65]
	v_mfma_f32_16x16x32_bf16 v[58:61], v[126:129], v[166:169], v[58:61]
	v_mfma_f32_16x16x32_bf16 v[46:49], v[110:113], v[174:177], v[46:49]
	v_mfma_f32_16x16x32_bf16 v[42:45], v[126:129], v[174:177], v[42:45]
	v_mfma_f32_16x16x32_bf16 v[30:33], v[110:113], v[182:185], v[30:33]
	v_mfma_f32_16x16x32_bf16 v[26:29], v[126:129], v[182:185], v[26:29]
	v_mfma_f32_16x16x32_bf16 v[14:17], v[110:113], v[206:209], v[14:17]
	v_mfma_f32_16x16x32_bf16 v[10:13], v[126:129], v[206:209], v[10:13]
	v_mfma_f32_16x16x32_bf16 v[54:57], v[138:141], v[154:157], 0
	v_mfma_f32_16x16x32_bf16 v[50:53], v[146:149], v[154:157], 0
	v_mfma_f32_16x16x32_bf16 v[38:41], v[138:141], v[170:173], 0
	v_mfma_f32_16x16x32_bf16 v[34:37], v[146:149], v[170:173], 0
	v_mfma_f32_16x16x32_bf16 v[22:25], v[138:141], v[178:181], 0
	v_mfma_f32_16x16x32_bf16 v[18:21], v[146:149], v[178:181], 0
	v_mfma_f32_16x16x32_bf16 v[6:9], v[138:141], v[186:189], 0
	v_mfma_f32_16x16x32_bf16 v[2:5], v[146:149], v[186:189], 0
	v_mfma_f32_16x16x32_bf16 v[54:57], v[142:145], v[166:169], v[54:57]
	v_mfma_f32_16x16x32_bf16 v[50:53], v[150:153], v[166:169], v[50:53]
	v_mfma_f32_16x16x32_bf16 v[38:41], v[142:145], v[174:177], v[38:41]
	v_mfma_f32_16x16x32_bf16 v[34:37], v[150:153], v[174:177], v[34:37]
	v_mfma_f32_16x16x32_bf16 v[22:25], v[142:145], v[182:185], v[22:25]
	v_mfma_f32_16x16x32_bf16 v[18:21], v[150:153], v[182:185], v[18:21]
	v_mfma_f32_16x16x32_bf16 v[6:9], v[142:145], v[206:209], v[6:9]
	v_mfma_f32_16x16x32_bf16 v[2:5], v[150:153], v[206:209], v[2:5]
	s_setprio 0
	s_barrier
	s_add_i32 s64, 0, 0x18000
	s_add_i32 s65, 0, 0x1c000
	v_add_u32_e32 v126, s64, v229
	v_add_u32_e32 v150, s65, v229
	ds_read_b128 v[98:101], v126
	ds_read_b128 v[110:113], v126 offset:1024
	ds_read_b128 v[122:125], v126 offset:2048
	ds_read_b128 v[126:129], v126 offset:3072
	ds_read_b128 v[138:141], v150
	ds_read_b128 v[142:145], v150 offset:1024
	ds_read_b128 v[146:149], v150 offset:2048
	ds_read_b128 v[150:153], v150 offset:3072
	s_add_u32 s30, s30, 0x40000
	s_addc_u32 s31, s31, 0
	s_mov_b32 m0, s35
	ds_read_b128 v[154:157], v236 offset:32768
	ds_read_b128 v[166:169], v236 offset:33792
	ds_read_b128 v[170:173], v236 offset:34816
	ds_read_b128 v[174:177], v236 offset:35840
	ds_read_b128 v[178:181], v236 offset:36864
	ds_read_b128 v[182:185], v236 offset:37888
	ds_read_b128 v[186:189], v236 offset:38912
	ds_read_b128 v[206:209], v236 offset:39936
	global_load_lds_dwordx4 v190, s[30:31]
	s_mov_b32 m0, s36
	s_nop 0
	global_load_lds_dwordx4 v194, s[30:31]
	s_waitcnt vmcnt(8)
	s_waitcnt lgkmcnt(0)
	s_barrier
	s_setprio 3
	s_waitcnt lgkmcnt(0)
	v_mfma_f32_16x16x32_bf16 v[162:165], v[98:101], v[154:157], v[162:165]
	v_mfma_f32_16x16x32_bf16 v[158:161], v[122:125], v[154:157], v[158:161]
	v_mfma_f32_16x16x32_bf16 v[118:121], v[98:101], v[170:173], v[118:121]
	v_mfma_f32_16x16x32_bf16 v[114:117], v[122:125], v[170:173], v[114:117]
	v_mfma_f32_16x16x32_bf16 v[94:97], v[98:101], v[178:181], v[94:97]
	v_mfma_f32_16x16x32_bf16 v[90:93], v[122:125], v[178:181], v[90:93]
	v_mfma_f32_16x16x32_bf16 v[78:81], v[98:101], v[186:189], v[78:81]
	v_mfma_f32_16x16x32_bf16 v[74:77], v[122:125], v[186:189], v[74:77]
	v_mfma_f32_16x16x32_bf16 v[162:165], v[110:113], v[166:169], v[162:165]
	v_mfma_f32_16x16x32_bf16 v[158:161], v[126:129], v[166:169], v[158:161]
	v_mfma_f32_16x16x32_bf16 v[118:121], v[110:113], v[174:177], v[118:121]
	v_mfma_f32_16x16x32_bf16 v[114:117], v[126:129], v[174:177], v[114:117]
	v_mfma_f32_16x16x32_bf16 v[94:97], v[110:113], v[182:185], v[94:97]
	v_mfma_f32_16x16x32_bf16 v[90:93], v[126:129], v[182:185], v[90:93]
	v_mfma_f32_16x16x32_bf16 v[78:81], v[110:113], v[206:209], v[78:81]
	v_mfma_f32_16x16x32_bf16 v[74:77], v[126:129], v[206:209], v[74:77]
	v_mfma_f32_16x16x32_bf16 v[134:137], v[138:141], v[154:157], v[134:137]
	v_mfma_f32_16x16x32_bf16 v[130:133], v[146:149], v[154:157], v[130:133]
	v_mfma_f32_16x16x32_bf16 v[106:109], v[138:141], v[170:173], v[106:109]
	v_mfma_f32_16x16x32_bf16 v[102:105], v[146:149], v[170:173], v[102:105]
	v_mfma_f32_16x16x32_bf16 v[86:89], v[138:141], v[178:181], v[86:89]
	v_mfma_f32_16x16x32_bf16 v[82:85], v[146:149], v[178:181], v[82:85]
	v_mfma_f32_16x16x32_bf16 v[70:73], v[138:141], v[186:189], v[70:73]
	v_mfma_f32_16x16x32_bf16 v[66:69], v[146:149], v[186:189], v[66:69]
	v_mfma_f32_16x16x32_bf16 v[134:137], v[142:145], v[166:169], v[134:137]
	v_mfma_f32_16x16x32_bf16 v[130:133], v[150:153], v[166:169], v[130:133]
	v_mfma_f32_16x16x32_bf16 v[106:109], v[142:145], v[174:177], v[106:109]
	v_mfma_f32_16x16x32_bf16 v[102:105], v[150:153], v[174:177], v[102:105]
	v_mfma_f32_16x16x32_bf16 v[86:89], v[142:145], v[182:185], v[86:89]
	v_mfma_f32_16x16x32_bf16 v[82:85], v[150:153], v[182:185], v[82:85]
	v_mfma_f32_16x16x32_bf16 v[70:73], v[142:145], v[206:209], v[70:73]
	v_mfma_f32_16x16x32_bf16 v[66:69], v[150:153], v[206:209], v[66:69]
	s_setprio 0
	s_barrier
; #define PG8_STAGE_A(b, h, ptr, NX) do { if constexpr (Sched::GATHER) { unsigned gs_[2]; gs_[0] = ((NX) && last_) ? gN[h][0] : gA[h][0]; gs_[1] = ((NX) && last_) ? gN[h][1] : gA[h][1]; PG8_STAGE(PG8_SA(b, h), ptr, gs_); } \
;         else PG8_STAGE(PG8_SA(b, h), (ptr) + ((h) ? hstep : (size_t)0), voffA); } while (0)
; #define PG8_STAGE(bufoff, gbase, voff) do { _Pragma("unroll") for (int _i = 0; _i < 2; ++_i) \
;         __builtin_amdgcn_global_load_lds((const unsigned*)((const char*)(gbase) + (voff)[_i]), (PG8_LAS unsigned*)(lds + (bufoff) + ldsw + _i * 8192), 16, 0, 0); } while (0)
; #define PG8_LDA(dst, b, h) do { _Pragma("unroll") for (int m = 0; m < 4; ++m) _Pragma("unroll") for (int k = 0; k < 2; ++k) dst[m][k] = *(const PG8_LAS bf16x8*)(lds + PG8_SA(b, h) + aoff + m * 2048 + k * 1024); } while (0)
; #define PG8_LDB(dst, b, h) do { _Pragma("unroll") for (int n = 0; n < 2; ++n) _Pragma("unroll") for (int k = 0; k < 2; ++k) dst[n][k] = *(const PG8_LAS bf16x8*)(lds + PG8_SB(b, h) + boff + n * 2048 + k * 1024); } while (0)
; #define PG8_WAIT_V(n) asm volatile("s_waitcnt vmcnt(" #n ")" ::: "memory")
; #define PG8_WAIT_L(n) asm volatile("s_waitcnt lgkmcnt(" #n ")" ::: "memory")
; template <class Epi, class Sched, bool ALIGN_EPI = false, bool SP2 = false>
; __device__ __forceinline__ void gemm_phase(PG8_LAS unsigned char* lds, const Gemm g, const Sched& S, const Epi& E, const bool skip_epi = false) {
;     ...
;         for (int t = 0; t < nt; t += 2) {
;             const bool last = (t == nt - 2); last_ = last && has_next;
;             const char* a1 = cA + (size_t)(t + 1) * kstep;
;             const char* a2 = last ? nA : cA + (size_t)(t + 2) * kstep; const char* b2 = last ? nB : cB + (size_t)(t + 2) * kstep;
;             const char* a3 = a2 + kstep; const char* b3 = b2 + kstep;
;             if (last && has_next) S.a_ready(nxt);
;             if constexpr (SP2) {
;             PG8_LDB(B0, 0, 0); PG8_LDB(B1, 0, 1); PG8_SCHED; PG8_LDA(At, 0, 0); PG8_STAGE_A(1, 1, a1, false);
;             PG8_WAIT_V(8); PG8_WAIT_L(0); PG8_BAR; PG8_MMA(0, 0, At, B0); PG8_MMA(0, 1, At, B1); PG8_BAR; PG8_SCHED;
;     ...
;             PG8_LDA(At, 1, 1); PG8_STAGE(PG8_SB(1, 0), b3, voffB); PG8_STAGE(PG8_SB(1, 1), b3 + hstep, voffB); PG8_STAGE_A(1, 0, a3, true);
;             PG8_WAIT_V(8); PG8_WAIT_L(0); PG8_BAR; PG8_MMA(1, 0, At, B0); PG8_MMA(1, 1, At, B1); PG8_BAR; PG8_SCHED;
	s_add_i32 s30, s64, s2
	s_add_i32 m0, s30, 0xffffff80
	ds_read_b128 v[154:157], v236 offset:49152
	ds_read_b128 v[166:169], v236 offset:50176
	ds_read_b128 v[170:173], v236 offset:51200
	ds_read_b128 v[174:177], v236 offset:52224
	ds_read_b128 v[178:181], v236 offset:53248
	ds_read_b128 v[182:185], v236 offset:54272
	ds_read_b128 v[186:189], v236 offset:55296
	ds_read_b128 v[206:209], v236 offset:56320
	global_load_lds_dwordx4 v192, s[28:29] offset:128
	s_add_i32 m0, s30, 0x1f80
	s_add_i32 s30, s65, s2
	global_load_lds_dwordx4 v196, s[28:29] offset:128
	s_add_u32 s28, s28, 0x40080
	s_addc_u32 s29, s29, 0
	s_mov_b32 m0, s30
	s_nop 0
	global_load_lds_dwordx4 v192, s[28:29]
	s_add_i32 m0, s30, 0x2000
	s_nop 0
	global_load_lds_dwordx4 v196, s[28:29]
	s_add_i32 m0, s39, 0xffffff80
	s_nop 0
	global_load_lds_dwordx4 v190, s[98:99] offset:128
	s_add_i32 m0, s48, 0xffffff80
	s_nop 0
	global_load_lds_dwordx4 v194, s[98:99] offset:128
	s_waitcnt vmcnt(8)
	s_waitcnt lgkmcnt(0)
	s_barrier
	s_setprio 3
	s_waitcnt lgkmcnt(0)
	v_mfma_f32_16x16x32_bf16 v[62:65], v[98:101], v[154:157], v[62:65]
	v_mfma_f32_16x16x32_bf16 v[58:61], v[122:125], v[154:157], v[58:61]
	v_mfma_f32_16x16x32_bf16 v[46:49], v[98:101], v[170:173], v[46:49]
	v_mfma_f32_16x16x32_bf16 v[42:45], v[122:125], v[170:173], v[42:45]
	v_mfma_f32_16x16x32_bf16 v[30:33], v[98:101], v[178:181], v[30:33]
	v_mfma_f32_16x16x32_bf16 v[26:29], v[122:125], v[178:181], v[26:29]
	v_mfma_f32_16x16x32_bf16 v[14:17], v[98:101], v[186:189], v[14:17]
	v_mfma_f32_16x16x32_bf16 v[10:13], v[122:125], v[186:189], v[10:13]
	v_mfma_f32_16x16x32_bf16 v[62:65], v[110:113], v[166:169], v[62:65]
	v_mfma_f32_16x16x32_bf16 v[58:61], v[126:129], v[166:169], v[58:61]
	v_mfma_f32_16x16x32_bf16 v[46:49], v[110:113], v[174:177], v[46:49]
	v_mfma_f32_16x16x32_bf16 v[42:45], v[126:129], v[174:177], v[42:45]
	v_mfma_f32_16x16x32_bf16 v[30:33], v[110:113], v[182:185], v[30:33]
	v_mfma_f32_16x16x32_bf16 v[26:29], v[126:129], v[182:185], v[26:29]
	v_mfma_f32_16x16x32_bf16 v[14:17], v[110:113], v[206:209], v[14:17]
	v_mfma_f32_16x16x32_bf16 v[10:13], v[126:129], v[206:209], v[10:13]
	v_mfma_f32_16x16x32_bf16 v[54:57], v[138:141], v[154:157], v[54:57]
	v_mfma_f32_16x16x32_bf16 v[50:53], v[146:149], v[154:157], v[50:53]
	v_mfma_f32_16x16x32_bf16 v[38:41], v[138:141], v[170:173], v[38:41]
	v_mfma_f32_16x16x32_bf16 v[34:37], v[146:149], v[170:173], v[34:37]
	v_mfma_f32_16x16x32_bf16 v[22:25], v[138:141], v[178:181], v[22:25]
	v_mfma_f32_16x16x32_bf16 v[18:21], v[146:149], v[178:181], v[18:21]
	v_mfma_f32_16x16x32_bf16 v[6:9], v[138:141], v[186:189], v[6:9]
	v_mfma_f32_16x16x32_bf16 v[2:5], v[146:149], v[186:189], v[2:5]
	v_mfma_f32_16x16x32_bf16 v[54:57], v[142:145], v[166:169], v[54:57]
	v_mfma_f32_16x16x32_bf16 v[50:53], v[150:153], v[166:169], v[50:53]
	v_mfma_f32_16x16x32_bf16 v[38:41], v[142:145], v[174:177], v[38:41]
	v_mfma_f32_16x16x32_bf16 v[34:37], v[150:153], v[174:177], v[34:37]
	v_mfma_f32_16x16x32_bf16 v[22:25], v[142:145], v[182:185], v[22:25]
	v_mfma_f32_16x16x32_bf16 v[18:21], v[150:153], v[182:185], v[18:21]
	v_mfma_f32_16x16x32_bf16 v[6:9], v[142:145], v[206:209], v[6:9]
	v_mfma_f32_16x16x32_bf16 v[2:5], v[150:153], v[206:209], v[2:5]
	s_setprio 0
	s_barrier
	s_add_i32 s63, s63, 2
	s_add_u32 s26, s26, 0x100
	s_addc_u32 s27, s27, 0
	s_add_u32 s61, s61, 0x100
	s_addc_u32 s62, s62, 0
	s_cmp_gt_u32 s63, 13
.LBB0_634:
	ds_read_b128 v[98:101], v234
	ds_read_b128 v[110:113], v234 offset:1024
	ds_read_b128 v[122:125], v234 offset:2048
	ds_read_b128 v[126:129], v234 offset:3072
	ds_read_b128 v[138:141], v235
	ds_read_b128 v[142:145], v235 offset:1024
	ds_read_b128 v[146:149], v235 offset:2048
	ds_read_b128 v[150:153], v235 offset:3072
	s_add_u32 s28, s26, 0xfffc0080
	s_addc_u32 s29, s27, -1
	s_cmp_eq_u32 s63, 12
	s_cselect_b32 s31, s19, s29
	s_cselect_b32 s30, s25, s28
	s_cselect_b32 s29, s17, s62
	s_cselect_b32 s28, s60, s61
	s_add_i32 m0, s3, 0xc000
	ds_read_b128 v[154:157], v236
	ds_read_b128 v[166:169], v236 offset:1024
	ds_read_b128 v[170:173], v236 offset:2048
	ds_read_b128 v[174:177], v236 offset:3072
	ds_read_b128 v[178:181], v236 offset:4096
	ds_read_b128 v[182:185], v236 offset:5120
	ds_read_b128 v[186:189], v236 offset:6144
	ds_read_b128 v[206:209], v236 offset:7168
	global_load_lds_dwordx4 v198, s[26:27]
	s_add_i32 m0, s3, 0xe000
	s_nop 0
	global_load_lds_dwordx4 v200, s[26:27]
	s_waitcnt vmcnt(8)
	s_waitcnt lgkmcnt(0)
	s_barrier
	s_setprio 3
	s_waitcnt lgkmcnt(0)
	v_mfma_f32_16x16x32_bf16 v[162:165], v[98:101], v[154:157], v[162:165]
	v_mfma_f32_16x16x32_bf16 v[158:161], v[122:125], v[154:157], v[158:161]
	v_mfma_f32_16x16x32_bf16 v[118:121], v[98:101], v[170:173], v[118:121]
	v_mfma_f32_16x16x32_bf16 v[114:117], v[122:125], v[170:173], v[114:117]
	v_mfma_f32_16x16x32_bf16 v[94:97], v[98:101], v[178:181], v[94:97]
	v_mfma_f32_16x16x32_bf16 v[90:93], v[122:125], v[178:181], v[90:93]
	v_mfma_f32_16x16x32_bf16 v[78:81], v[98:101], v[186:189], v[78:81]
	v_mfma_f32_16x16x32_bf16 v[74:77], v[122:125], v[186:189], v[74:77]
	v_mfma_f32_16x16x32_bf16 v[162:165], v[110:113], v[166:169], v[162:165]
	v_mfma_f32_16x16x32_bf16 v[158:161], v[126:129], v[166:169], v[158:161]
	v_mfma_f32_16x16x32_bf16 v[118:121], v[110:113], v[174:177], v[118:121]
	v_mfma_f32_16x16x32_bf16 v[114:117], v[126:129], v[174:177], v[114:117]
	v_mfma_f32_16x16x32_bf16 v[94:97], v[110:113], v[182:185], v[94:97]
	v_mfma_f32_16x16x32_bf16 v[90:93], v[126:129], v[182:185], v[90:93]
	v_mfma_f32_16x16x32_bf16 v[78:81], v[110:113], v[206:209], v[78:81]
	v_mfma_f32_16x16x32_bf16 v[74:77], v[126:129], v[206:209], v[74:77]
	v_mfma_f32_16x16x32_bf16 v[134:137], v[138:141], v[154:157], v[134:137]
	v_mfma_f32_16x16x32_bf16 v[130:133], v[146:149], v[154:157], v[130:133]
	v_mfma_f32_16x16x32_bf16 v[106:109], v[138:141], v[170:173], v[106:109]
	v_mfma_f32_16x16x32_bf16 v[102:105], v[146:149], v[170:173], v[102:105]
	v_mfma_f32_16x16x32_bf16 v[86:89], v[138:141], v[178:181], v[86:89]
	v_mfma_f32_16x16x32_bf16 v[82:85], v[146:149], v[178:181], v[82:85]
	v_mfma_f32_16x16x32_bf16 v[70:73], v[138:141], v[186:189], v[70:73]
	v_mfma_f32_16x16x32_bf16 v[66:69], v[146:149], v[186:189], v[66:69]
	v_mfma_f32_16x16x32_bf16 v[134:137], v[142:145], v[166:169], v[134:137]
	v_mfma_f32_16x16x32_bf16 v[130:133], v[150:153], v[166:169], v[130:133]
	v_mfma_f32_16x16x32_bf16 v[106:109], v[142:145], v[174:177], v[106:109]
	v_mfma_f32_16x16x32_bf16 v[102:105], v[150:153], v[174:177], v[102:105]
	v_mfma_f32_16x16x32_bf16 v[86:89], v[142:145], v[182:185], v[86:89]
	v_mfma_f32_16x16x32_bf16 v[82:85], v[150:153], v[182:185], v[82:85]
	v_mfma_f32_16x16x32_bf16 v[70:73], v[142:145], v[206:209], v[70:73]
	v_mfma_f32_16x16x32_bf16 v[66:69], v[150:153], v[206:209], v[66:69]
	s_setprio 0
	s_barrier
; #define PG8_STAGE_A(b, h, ptr, NX) do { if constexpr (Sched::GATHER) { unsigned gs_[2]; gs_[0] = ((NX) && last_) ? gN[h][0] : gA[h][0]; gs_[1] = ((NX) && last_) ? gN[h][1] : gA[h][1]; PG8_STAGE(PG8_SA(b, h), ptr, gs_); } \
;         else PG8_STAGE(PG8_SA(b, h), (ptr) + ((h) ? hstep : (size_t)0), voffA); } while (0)
; #define PG8_STAGE(bufoff, gbase, voff) do { _Pragma("unroll") for (int _i = 0; _i < 2; ++_i) \
;         __builtin_amdgcn_global_load_lds((const unsigned*)((const char*)(gbase) + (voff)[_i]), (PG8_LAS unsigned*)(lds + (bufoff) + ldsw + _i * 8192), 16, 0, 0); } while (0)
; #define PG8_LDA(dst, b, h) do { _Pragma("unroll") for (int m = 0; m < 4; ++m) _Pragma("unroll") for (int k = 0; k < 2; ++k) dst[m][k] = *(const PG8_LAS bf16x8*)(lds + PG8_SA(b, h) + aoff + m * 2048 + k * 1024); } while (0)
; #define PG8_LDB(dst, b, h) do { _Pragma("unroll") for (int n = 0; n < 2; ++n) _Pragma("unroll") for (int k = 0; k < 2; ++k) dst[n][k] = *(const PG8_LAS bf16x8*)(lds + PG8_SB(b, h) + boff + n * 2048 + k * 1024); } while (0)
; #define PG8_MMA(ai, bj, At, Bt) do { __builtin_amdgcn_s_setprio(1); _Pragma("unroll") for (int m = 0; m < 4; ++m) _Pragma("unroll") for (int n = 0; n < 2; ++n) _Pragma("unroll") for (int k = 0; k < 2; ++k) \
;         acc[ai][bj][m][n] = __builtin_amdgcn_mfma_f32_16x16x32_bf16(Bt[n][k], At[m][k], acc[ai][bj][m][n], 0, 0, 0); __builtin_amdgcn_s_setprio(0); } while (0)
; #define PG8_WAIT_V(n) asm volatile("s_waitcnt vmcnt(" #n ")" ::: "memory")
; #define PG8_WAIT_L(n) asm volatile("s_waitcnt lgkmcnt(" #n ")" ::: "memory")
; #define PG8_BAR __builtin_amdgcn_s_barrier()
; #define PG8_SCHED __builtin_amdgcn_sched_barrier(0)
; template <class Epi, class Sched, bool ALIGN_EPI = false, bool SP2 = false>
; __device__ __forceinline__ void gemm_phase(PG8_LAS unsigned char* lds, const Gemm g, const Sched& S, const Epi& E, const bool skip_epi = false) {
;     ...
;             PG8_LDA(At, 0, 1); PG8_STAGE(PG8_SB(0, 0), b2, voffB); PG8_STAGE(PG8_SB(0, 1), b2 + hstep, voffB); PG8_STAGE_A(0, 0, a2, true);
;             PG8_WAIT_V(8); PG8_WAIT_L(0); PG8_BAR; PG8_MMA(1, 0, At, B0); PG8_MMA(1, 1, At, B1); PG8_BAR; PG8_SCHED;
;             PG8_LDB(B0, 1, 0); PG8_LDB(B1, 1, 1); PG8_SCHED; PG8_LDA(At, 1, 0); PG8_STAGE_A(0, 1, a2, true);
;             PG8_WAIT_V(8); PG8_WAIT_L(0); PG8_BAR; PG8_MMA(0, 0, At, B0); PG8_MMA(0, 1, At, B1); PG8_BAR; PG8_SCHED;
	s_add_i32 s64, s57, s2
	s_mov_b32 m0, s64
	ds_read_b128 v[154:157], v236 offset:16384
	ds_read_b128 v[166:169], v236 offset:17408
	ds_read_b128 v[170:173], v236 offset:18432
	ds_read_b128 v[174:177], v236 offset:19456
	ds_read_b128 v[178:181], v236 offset:20480
	ds_read_b128 v[182:185], v236 offset:21504
	ds_read_b128 v[186:189], v236 offset:22528
	ds_read_b128 v[206:209], v236 offset:23552
	global_load_lds_dwordx4 v192, s[28:29]
	s_add_i32 m0, s64, 0x2000
	s_add_u32 s64, s28, 0x40000
	s_addc_u32 s65, s29, 0
	s_add_i32 s66, s58, s2
	global_load_lds_dwordx4 v196, s[28:29]
	s_mov_b32 m0, s66
	s_mov_b64 s[98:99], s[30:31]
	global_load_lds_dwordx4 v192, s[64:65]
	s_add_i32 m0, s66, 0x2000
	s_nop 0
	global_load_lds_dwordx4 v196, s[64:65]
	s_mov_b32 m0, s3
	s_nop 0
	global_load_lds_dwordx4 v190, s[30:31]
	s_mov_b32 m0, s34
	s_nop 0
	global_load_lds_dwordx4 v194, s[30:31]
	s_waitcnt vmcnt(8)
	s_waitcnt lgkmcnt(0)
	s_barrier
	s_setprio 3
	s_waitcnt lgkmcnt(0)
	v_mfma_f32_16x16x32_bf16 v[62:65], v[98:101], v[154:157], v[62:65]
	v_mfma_f32_16x16x32_bf16 v[58:61], v[122:125], v[154:157], v[58:61]
	v_mfma_f32_16x16x32_bf16 v[46:49], v[98:101], v[170:173], v[46:49]
	v_mfma_f32_16x16x32_bf16 v[42:45], v[122:125], v[170:173], v[42:45]
	v_mfma_f32_16x16x32_bf16 v[30:33], v[98:101], v[178:181], v[30:33]
	v_mfma_f32_16x16x32_bf16 v[26:29], v[122:125], v[178:181], v[26:29]
	v_mfma_f32_16x16x32_bf16 v[14:17], v[98:101], v[186:189], v[14:17]
	v_mfma_f32_16x16x32_bf16 v[10:13], v[122:125], v[186:189], v[10:13]
	v_mfma_f32_16x16x32_bf16 v[62:65], v[110:113], v[166:169], v[62:65]
	v_mfma_f32_16x16x32_bf16 v[58:61], v[126:129], v[166:169], v[58:61]
	v_mfma_f32_16x16x32_bf16 v[46:49], v[110:113], v[174:177], v[46:49]
	v_mfma_f32_16x16x32_bf16 v[42:45], v[126:129], v[174:177], v[42:45]
	v_mfma_f32_16x16x32_bf16 v[30:33], v[110:113], v[182:185], v[30:33]
	v_mfma_f32_16x16x32_bf16 v[26:29], v[126:129], v[182:185], v[26:29]
	v_mfma_f32_16x16x32_bf16 v[14:17], v[110:113], v[206:209], v[14:17]
	v_mfma_f32_16x16x32_bf16 v[10:13], v[126:129], v[206:209], v[10:13]
	v_mfma_f32_16x16x32_bf16 v[54:57], v[138:141], v[154:157], v[54:57]
	v_mfma_f32_16x16x32_bf16 v[50:53], v[146:149], v[154:157], v[50:53]
	v_mfma_f32_16x16x32_bf16 v[38:41], v[138:141], v[170:173], v[38:41]
	v_mfma_f32_16x16x32_bf16 v[34:37], v[146:149], v[170:173], v[34:37]
	v_mfma_f32_16x16x32_bf16 v[22:25], v[138:141], v[178:181], v[22:25]
	v_mfma_f32_16x16x32_bf16 v[18:21], v[146:149], v[178:181], v[18:21]
	v_mfma_f32_16x16x32_bf16 v[6:9], v[138:141], v[186:189], v[6:9]
	v_mfma_f32_16x16x32_bf16 v[2:5], v[146:149], v[186:189], v[2:5]
	v_mfma_f32_16x16x32_bf16 v[54:57], v[142:145], v[166:169], v[54:57]
	v_mfma_f32_16x16x32_bf16 v[50:53], v[150:153], v[166:169], v[50:53]
	v_mfma_f32_16x16x32_bf16 v[38:41], v[142:145], v[174:177], v[38:41]
	v_mfma_f32_16x16x32_bf16 v[34:37], v[150:153], v[174:177], v[34:37]
	v_mfma_f32_16x16x32_bf16 v[22:25], v[142:145], v[182:185], v[22:25]
	v_mfma_f32_16x16x32_bf16 v[18:21], v[150:153], v[182:185], v[18:21]
	v_mfma_f32_16x16x32_bf16 v[6:9], v[142:145], v[206:209], v[6:9]
	v_mfma_f32_16x16x32_bf16 v[2:5], v[150:153], v[206:209], v[2:5]
	s_setprio 0
	s_barrier
	s_add_i32 s64, 0, 0x18000
	s_add_i32 s65, 0, 0x1c000
	v_add_u32_e32 v126, s64, v229
	v_add_u32_e32 v150, s65, v229
	ds_read_b128 v[98:101], v126
	ds_read_b128 v[110:113], v126 offset:1024
	ds_read_b128 v[122:125], v126 offset:2048
	ds_read_b128 v[126:129], v126 offset:3072
	ds_read_b128 v[138:141], v150
	ds_read_b128 v[142:145], v150 offset:1024
	ds_read_b128 v[146:149], v150 offset:2048
	ds_read_b128 v[150:153], v150 offset:3072
	s_add_u32 s30, s30, 0x40000
	s_addc_u32 s31, s31, 0
	s_mov_b32 m0, s35
	ds_read_b128 v[154:157], v236 offset:32768
	ds_read_b128 v[166:169], v236 offset:33792
	ds_read_b128 v[170:173], v236 offset:34816
	ds_read_b128 v[174:177], v236 offset:35840
	ds_read_b128 v[178:181], v236 offset:36864
	ds_read_b128 v[182:185], v236 offset:37888
	ds_read_b128 v[186:189], v236 offset:38912
	ds_read_b128 v[206:209], v236 offset:39936
	global_load_lds_dwordx4 v190, s[30:31]
	s_mov_b32 m0, s36
	s_nop 0
	global_load_lds_dwordx4 v194, s[30:31]
	s_waitcnt vmcnt(8)
	s_waitcnt lgkmcnt(0)
	s_barrier
; #define PG8_STAGE_A(b, h, ptr, NX) do { if constexpr (Sched::GATHER) { unsigned gs_[2]; gs_[0] = ((NX) && last_) ? gN[h][0] : gA[h][0]; gs_[1] = ((NX) && last_) ? gN[h][1] : gA[h][1]; PG8_STAGE(PG8_SA(b, h), ptr, gs_); } \
;         else PG8_STAGE(PG8_SA(b, h), (ptr) + ((h) ? hstep : (size_t)0), voffA); } while (0)
; #define PG8_STAGE(bufoff, gbase, voff) do { _Pragma("unroll") for (int _i = 0; _i < 2; ++_i) \
;         __builtin_amdgcn_global_load_lds((const unsigned*)((const char*)(gbase) + (voff)[_i]), (PG8_LAS unsigned*)(lds + (bufoff) + ldsw + _i * 8192), 16, 0, 0); } while (0)
; #define PG8_LDA(dst, b, h) do { _Pragma("unroll") for (int m = 0; m < 4; ++m) _Pragma("unroll") for (int k = 0; k < 2; ++k) dst[m][k] = *(const PG8_LAS bf16x8*)(lds + PG8_SA(b, h) + aoff + m * 2048 + k * 1024); } while (0)
; #define PG8_MMA(ai, bj, At, Bt) do { __builtin_amdgcn_s_setprio(1); _Pragma("unroll") for (int m = 0; m < 4; ++m) _Pragma("unroll") for (int n = 0; n < 2; ++n) _Pragma("unroll") for (int k = 0; k < 2; ++k) \
;         acc[ai][bj][m][n] = __builtin_amdgcn_mfma_f32_16x16x32_bf16(Bt[n][k], At[m][k], acc[ai][bj][m][n], 0, 0, 0); __builtin_amdgcn_s_setprio(0); } while (0)
; #define PG8_WAIT_V(n) asm volatile("s_waitcnt vmcnt(" #n ")" ::: "memory")
; #define PG8_WAIT_L(n) asm volatile("s_waitcnt lgkmcnt(" #n ")" ::: "memory")
; #define PG8_BAR __builtin_amdgcn_s_barrier()
; #define PG8_SCHED __builtin_amdgcn_sched_barrier(0)
; template <class Epi, class Sched, bool ALIGN_EPI = false, bool SP2 = false>
; __device__ __forceinline__ void gemm_phase(PG8_LAS unsigned char* lds, const Gemm g, const Sched& S, const Epi& E, const bool skip_epi = false) {
;     ...
;             PG8_WAIT_V(8); PG8_WAIT_L(0); PG8_BAR; PG8_MMA(0, 0, At, B0); PG8_MMA(0, 1, At, B1); PG8_BAR; PG8_SCHED;
;             PG8_LDA(At, 1, 1); PG8_STAGE(PG8_SB(1, 0), b3, voffB); PG8_STAGE(PG8_SB(1, 1), b3 + hstep, voffB); PG8_STAGE_A(1, 0, a3, true);
;             PG8_WAIT_V(8); PG8_WAIT_L(0); PG8_BAR; PG8_MMA(1, 0, At, B0); PG8_MMA(1, 1, At, B1); PG8_BAR; PG8_SCHED;
;     ...
;         if constexpr (ALIGN_EPI) { if (wr == 0) PG8_BAR; }
;         if constexpr (!Epi::AFTER_DRAIN) { if (!skip_epi) E(acc, cur, wr, wc, fr, fq); S.done(cur); }
;         if (!has_next) break;
	s_setprio 3
	s_waitcnt lgkmcnt(0)
	v_mfma_f32_16x16x32_bf16 v[162:165], v[98:101], v[154:157], v[162:165]
	v_mfma_f32_16x16x32_bf16 v[158:161], v[122:125], v[154:157], v[158:161]
	v_mfma_f32_16x16x32_bf16 v[118:121], v[98:101], v[170:173], v[118:121]
	v_mfma_f32_16x16x32_bf16 v[114:117], v[122:125], v[170:173], v[114:117]
	v_mfma_f32_16x16x32_bf16 v[94:97], v[98:101], v[178:181], v[94:97]
	v_mfma_f32_16x16x32_bf16 v[90:93], v[122:125], v[178:181], v[90:93]
	v_mfma_f32_16x16x32_bf16 v[78:81], v[98:101], v[186:189], v[78:81]
	v_mfma_f32_16x16x32_bf16 v[74:77], v[122:125], v[186:189], v[74:77]
	v_mfma_f32_16x16x32_bf16 v[162:165], v[110:113], v[166:169], v[162:165]
	v_mfma_f32_16x16x32_bf16 v[158:161], v[126:129], v[166:169], v[158:161]
	v_mfma_f32_16x16x32_bf16 v[118:121], v[110:113], v[174:177], v[118:121]
	v_mfma_f32_16x16x32_bf16 v[114:117], v[126:129], v[174:177], v[114:117]
	v_mfma_f32_16x16x32_bf16 v[94:97], v[110:113], v[182:185], v[94:97]
	v_mfma_f32_16x16x32_bf16 v[90:93], v[126:129], v[182:185], v[90:93]
	v_mfma_f32_16x16x32_bf16 v[78:81], v[110:113], v[206:209], v[78:81]
	v_mfma_f32_16x16x32_bf16 v[74:77], v[126:129], v[206:209], v[74:77]
	v_mfma_f32_16x16x32_bf16 v[134:137], v[138:141], v[154:157], v[134:137]
	v_mfma_f32_16x16x32_bf16 v[130:133], v[146:149], v[154:157], v[130:133]
	v_mfma_f32_16x16x32_bf16 v[106:109], v[138:141], v[170:173], v[106:109]
	v_mfma_f32_16x16x32_bf16 v[102:105], v[146:149], v[170:173], v[102:105]
	v_mfma_f32_16x16x32_bf16 v[86:89], v[138:141], v[178:181], v[86:89]
	v_mfma_f32_16x16x32_bf16 v[82:85], v[146:149], v[178:181], v[82:85]
	v_mfma_f32_16x16x32_bf16 v[70:73], v[138:141], v[186:189], v[70:73]
	v_mfma_f32_16x16x32_bf16 v[66:69], v[146:149], v[186:189], v[66:69]
	v_mfma_f32_16x16x32_bf16 v[134:137], v[142:145], v[166:169], v[134:137]
	v_mfma_f32_16x16x32_bf16 v[130:133], v[150:153], v[166:169], v[130:133]
	v_mfma_f32_16x16x32_bf16 v[106:109], v[142:145], v[174:177], v[106:109]
	v_mfma_f32_16x16x32_bf16 v[102:105], v[150:153], v[174:177], v[102:105]
	v_mfma_f32_16x16x32_bf16 v[86:89], v[142:145], v[182:185], v[86:89]
	v_mfma_f32_16x16x32_bf16 v[82:85], v[150:153], v[182:185], v[82:85]
	v_mfma_f32_16x16x32_bf16 v[70:73], v[142:145], v[206:209], v[70:73]
	v_mfma_f32_16x16x32_bf16 v[66:69], v[150:153], v[206:209], v[66:69]
	s_setprio 0
	s_barrier
	s_add_i32 s30, s64, s2
	s_add_i32 m0, s30, 0xffffff80
	ds_read_b128 v[154:157], v236 offset:49152
	ds_read_b128 v[166:169], v236 offset:50176
	ds_read_b128 v[170:173], v236 offset:51200
	ds_read_b128 v[174:177], v236 offset:52224
	ds_read_b128 v[178:181], v236 offset:53248
	ds_read_b128 v[182:185], v236 offset:54272
	ds_read_b128 v[186:189], v236 offset:55296
	ds_read_b128 v[206:209], v236 offset:56320
	global_load_lds_dwordx4 v192, s[28:29] offset:128
	s_add_i32 m0, s30, 0x1f80
	s_add_i32 s30, s65, s2
	global_load_lds_dwordx4 v196, s[28:29] offset:128
	s_add_u32 s28, s28, 0x40080
	s_addc_u32 s29, s29, 0
	s_mov_b32 m0, s30
	s_nop 0
	global_load_lds_dwordx4 v192, s[28:29]
	s_add_i32 m0, s30, 0x2000
	s_nop 0
	global_load_lds_dwordx4 v196, s[28:29]
	s_add_i32 m0, s39, 0xffffff80
	s_nop 0
	global_load_lds_dwordx4 v190, s[98:99] offset:128
	s_add_i32 m0, s48, 0xffffff80
	s_nop 0
	global_load_lds_dwordx4 v194, s[98:99] offset:128
	s_waitcnt vmcnt(8)
	s_waitcnt lgkmcnt(0)
	s_barrier
	s_setprio 3
	s_waitcnt lgkmcnt(0)
	v_mfma_f32_16x16x32_bf16 v[62:65], v[98:101], v[154:157], v[62:65]
	v_mfma_f32_16x16x32_bf16 v[58:61], v[122:125], v[154:157], v[58:61]
	v_mfma_f32_16x16x32_bf16 v[46:49], v[98:101], v[170:173], v[46:49]
	v_mfma_f32_16x16x32_bf16 v[42:45], v[122:125], v[170:173], v[42:45]
	v_mfma_f32_16x16x32_bf16 v[30:33], v[98:101], v[178:181], v[30:33]
	v_mfma_f32_16x16x32_bf16 v[26:29], v[122:125], v[178:181], v[26:29]
	v_mfma_f32_16x16x32_bf16 v[14:17], v[98:101], v[186:189], v[14:17]
	v_mfma_f32_16x16x32_bf16 v[10:13], v[122:125], v[186:189], v[10:13]
	v_mfma_f32_16x16x32_bf16 v[62:65], v[110:113], v[166:169], v[62:65]
	v_mfma_f32_16x16x32_bf16 v[58:61], v[126:129], v[166:169], v[58:61]
	v_mfma_f32_16x16x32_bf16 v[46:49], v[110:113], v[174:177], v[46:49]
	v_mfma_f32_16x16x32_bf16 v[42:45], v[126:129], v[174:177], v[42:45]
	v_mfma_f32_16x16x32_bf16 v[30:33], v[110:113], v[182:185], v[30:33]
	v_mfma_f32_16x16x32_bf16 v[26:29], v[126:129], v[182:185], v[26:29]
	v_mfma_f32_16x16x32_bf16 v[14:17], v[110:113], v[206:209], v[14:17]
	v_mfma_f32_16x16x32_bf16 v[10:13], v[126:129], v[206:209], v[10:13]
	v_mfma_f32_16x16x32_bf16 v[54:57], v[138:141], v[154:157], v[54:57]
	v_mfma_f32_16x16x32_bf16 v[50:53], v[146:149], v[154:157], v[50:53]
	v_mfma_f32_16x16x32_bf16 v[38:41], v[138:141], v[170:173], v[38:41]
	v_mfma_f32_16x16x32_bf16 v[34:37], v[146:149], v[170:173], v[34:37]
	v_mfma_f32_16x16x32_bf16 v[22:25], v[138:141], v[178:181], v[22:25]
	v_mfma_f32_16x16x32_bf16 v[18:21], v[146:149], v[178:181], v[18:21]
	v_mfma_f32_16x16x32_bf16 v[6:9], v[138:141], v[186:189], v[6:9]
	v_mfma_f32_16x16x32_bf16 v[2:5], v[146:149], v[186:189], v[2:5]
	v_mfma_f32_16x16x32_bf16 v[54:57], v[142:145], v[166:169], v[54:57]
	v_mfma_f32_16x16x32_bf16 v[50:53], v[150:153], v[166:169], v[50:53]
	v_mfma_f32_16x16x32_bf16 v[38:41], v[142:145], v[174:177], v[38:41]
	v_mfma_f32_16x16x32_bf16 v[34:37], v[150:153], v[174:177], v[34:37]
	v_mfma_f32_16x16x32_bf16 v[22:25], v[142:145], v[182:185], v[22:25]
	v_mfma_f32_16x16x32_bf16 v[18:21], v[150:153], v[182:185], v[18:21]
	v_mfma_f32_16x16x32_bf16 v[6:9], v[142:145], v[206:209], v[6:9]
	v_mfma_f32_16x16x32_bf16 v[2:5], v[150:153], v[206:209], v[2:5]
	s_setprio 0
	s_barrier
	s_add_i32 s63, s63, 2
	s_add_u32 s26, s26, 0x100
	s_addc_u32 s27, s27, 0
	s_add_u32 s61, s61, 0x100
	s_addc_u32 s62, s62, 0
	s_cmp_gt_u32 s63, 13
	s_cbranch_scc0 .LBB0_634
	s_and_b64 vcc, exec, s[14:15]
	s_cbranch_vccz .LBB0_637
	s_barrier

; #define PG8_GIDX(G_, PM_) do { if constexpr (Sched::GATHER) { _Pragma("unroll") for (int h_ = 0; h_ < 2; ++h_) _Pragma("unroll") for (int i_ = 0; i_ < 2; ++i_) { int R_, C_; stage_rc(tid * 16 + i_ * 8192, R_, C_); \
;         const int src_ = S.rowsrc[(PM_) * BM + h_ * HALF + R_]; G_[h_][i_] = (unsigned)(src_ * K + C_) * 2u; } } } while (0)
; #define PG8_STAGE_A(b, h, ptr, NX) do { if constexpr (Sched::GATHER) { unsigned gs_[2]; gs_[0] = ((NX) && last_) ? gN[h][0] : gA[h][0]; gs_[1] = ((NX) && last_) ? gN[h][1] : gA[h][1]; PG8_STAGE(PG8_SA(b, h), ptr, gs_); } \
;         else PG8_STAGE(PG8_SA(b, h), (ptr) + ((h) ? hstep : (size_t)0), voffA); } while (0)
; #define PG8_LDA(dst, b, h) do { _Pragma("unroll") for (int m = 0; m < 4; ++m) _Pragma("unroll") for (int k = 0; k < 2; ++k) dst[m][k] = *(const PG8_LAS bf16x8*)(lds + PG8_SA(b, h) + aoff + m * 2048 + k * 1024); } while (0)
; template <class Epi, class Sched, bool ALIGN_EPI = false, bool SP2 = false>
; __device__ __forceinline__ void gemm_phase(PG8_LAS unsigned char* lds, const Gemm g, const Sched& S, const Epi& E, const bool skip_epi = false) {
;     ...
;         const bool has_next = S.next(ui + 1, nxt);
;         if (has_next) PG8_GIDX(gN, nxt.pm);
;         const char* nA = has_next ? (const char*)g.A + (size_t)nxt.pm * pmstepA + nxt.ko : cA; const char* nB = has_next ? (const char*)g.Bt + (size_t)nxt.pn * tstep + nxt.ko : cB;
;         for (int t = 0; t < nt; t += 2) {
;             const bool last = (t == nt - 2); last_ = last && has_next;
;             const char* a1 = cA + (size_t)(t + 1) * kstep;
;             const char* a2 = last ? nA : cA + (size_t)(t + 2) * kstep; const char* b2 = last ? nB : cB + (size_t)(t + 2) * kstep;
;             const char* a3 = a2 + kstep; const char* b3 = b2 + kstep;
;             if (last && has_next) S.a_ready(nxt);
;             if constexpr (SP2) {
;             PG8_LDB(B0, 0, 0); PG8_LDB(B1, 0, 1); PG8_SCHED; PG8_LDA(At, 0, 0); PG8_STAGE_A(1, 1, a1, false);
;             PG8_WAIT_V(8); PG8_WAIT_L(0); PG8_BAR; PG8_MMA(0, 0, At, B0); PG8_MMA(0, 1, At, B1); PG8_BAR; PG8_SCHED;
;             PG8_LDA(At, 0, 1); PG8_STAGE(PG8_SB(0, 0), b2, voffB); PG8_STAGE(PG8_SB(0, 1), b2 + hstep, voffB); PG8_STAGE_A(0, 0, a2, true);
;             PG8_WAIT_V(8); PG8_WAIT_L(0); PG8_BAR; PG8_MMA(1, 0, At, B0); PG8_MMA(1, 1, At, B1); PG8_BAR; PG8_SCHED;
.LBB0_720:
	s_ashr_i32 s15, s14, 31
	s_lshl_b64 s[16:17], s[14:15], 19
	s_add_u32 s16, s86, s16
	s_addc_u32 s17, s87, s17
	s_and_b64 s[18:19], s[4:5], exec
	s_cselect_b32 s15, s17, s23
	s_cselect_b32 s56, s16, s22
	s_ashr_i32 s13, s12, 31
	s_lshl_b64 s[18:19], s[12:13], 19
	v_readlane_b32 s26, v254, 15
	v_readlane_b32 s27, v254, 16
	s_add_u32 s18, s26, s18
	s_addc_u32 s19, s27, s19
	s_and_b64 s[26:27], s[4:5], exec
	s_cselect_b32 s13, s19, s25
	s_cselect_b32 s57, s18, s24
	s_add_u32 s22, s22, 0x40080
	s_addc_u32 s23, s23, 0
	s_add_u32 s58, s24, 0x100
	s_addc_u32 s59, s25, 0
	s_mov_b32 s60, -2
	s_waitcnt vmcnt(0)
	v_lshl_add_u32 v130, s20, 8, v175
	v_ashrrev_i32_e32 v131, 31, v130
	v_lshlrev_b64 v[130:131], 6, v[130:131]
	v_lshl_add_u64 v[130:131], v[150:151], 0, v[130:131]
	global_load_dwordx4 v[238:241], v[130:131], off
	global_load_dwordx4 v[242:245], v[130:131], off offset:1024
	global_load_dwordx4 v[246:249], v[130:131], off offset:2048
	global_load_dwordx4 v[250:253], v[130:131], off offset:3072
	ds_read_b128 v[130:133], v187
	ds_read_b128 v[134:137], v187 offset:1024
	ds_read_b128 v[138:141], v187 offset:2048
	ds_read_b128 v[160:163], v187 offset:3072
	ds_read_b128 v[164:167], v188
	ds_read_b128 v[182:185], v188 offset:1024
	ds_read_b128 v[192:195], v188 offset:2048
	ds_read_b128 v[196:199], v188 offset:3072
	s_add_u32 s24, s22, 0xfffc0080
	s_addc_u32 s25, s23, -1
	s_cmp_eq_u32 s60, 12
	s_cselect_b32 s27, s15, s25
	s_cselect_b32 s26, s56, s24
	s_cselect_b32 s25, s13, s59
	s_cselect_b32 s24, s57, s58
	s_add_i32 m0, s29, 0xc000
	ds_read_b128 v[200:203], v189
	ds_read_b128 v[204:207], v189 offset:1024
	ds_read_b128 v[208:211], v189 offset:2048
	ds_read_b128 v[212:215], v189 offset:3072
	ds_read_b128 v[216:219], v189 offset:4096
	ds_read_b128 v[220:223], v189 offset:5120
	ds_read_b128 v[224:227], v189 offset:6144
	ds_read_b128 v[230:233], v189 offset:7168
	global_load_lds_dwordx4 v152, s[22:23]
	s_add_i32 m0, s29, 0xe000
	s_nop 0
	global_load_lds_dwordx4 v154, s[22:23]
	s_waitcnt vmcnt(8)
	s_waitcnt lgkmcnt(0)
	s_barrier
	s_setprio 3
	s_waitcnt lgkmcnt(0)
	v_mfma_f32_16x16x32_bf16 v[126:129], v[130:133], v[200:203], 0
	v_mfma_f32_16x16x32_bf16 v[122:125], v[138:141], v[200:203], 0
	v_mfma_f32_16x16x32_bf16 v[110:113], v[130:133], v[208:211], 0
	v_mfma_f32_16x16x32_bf16 v[106:109], v[138:141], v[208:211], 0
	v_mfma_f32_16x16x32_bf16 v[94:97], v[130:133], v[216:219], 0
	v_mfma_f32_16x16x32_bf16 v[90:93], v[138:141], v[216:219], 0
	v_mfma_f32_16x16x32_bf16 v[78:81], v[130:133], v[224:227], 0
	v_mfma_f32_16x16x32_bf16 v[74:77], v[138:141], v[224:227], 0
	v_mfma_f32_16x16x32_bf16 v[126:129], v[134:137], v[204:207], v[126:129]
	v_mfma_f32_16x16x32_bf16 v[122:125], v[160:163], v[204:207], v[122:125]
	v_mfma_f32_16x16x32_bf16 v[110:113], v[134:137], v[212:215], v[110:113]
	v_mfma_f32_16x16x32_bf16 v[106:109], v[160:163], v[212:215], v[106:109]
	v_mfma_f32_16x16x32_bf16 v[94:97], v[134:137], v[220:223], v[94:97]
	v_mfma_f32_16x16x32_bf16 v[90:93], v[160:163], v[220:223], v[90:93]
	v_mfma_f32_16x16x32_bf16 v[78:81], v[134:137], v[230:233], v[78:81]
	v_mfma_f32_16x16x32_bf16 v[74:77], v[160:163], v[230:233], v[74:77]
	v_mfma_f32_16x16x32_bf16 v[118:121], v[164:167], v[200:203], 0
	v_mfma_f32_16x16x32_bf16 v[114:117], v[192:195], v[200:203], 0
	v_mfma_f32_16x16x32_bf16 v[102:105], v[164:167], v[208:211], 0
	v_mfma_f32_16x16x32_bf16 v[98:101], v[192:195], v[208:211], 0
	v_mfma_f32_16x16x32_bf16 v[86:89], v[164:167], v[216:219], 0
	v_mfma_f32_16x16x32_bf16 v[82:85], v[192:195], v[216:219], 0
	v_mfma_f32_16x16x32_bf16 v[70:73], v[164:167], v[224:227], 0
	v_mfma_f32_16x16x32_bf16 v[66:69], v[192:195], v[224:227], 0
	v_mfma_f32_16x16x32_bf16 v[118:121], v[182:185], v[204:207], v[118:121]
	v_mfma_f32_16x16x32_bf16 v[114:117], v[196:199], v[204:207], v[114:117]
	v_mfma_f32_16x16x32_bf16 v[102:105], v[182:185], v[212:215], v[102:105]
	v_mfma_f32_16x16x32_bf16 v[98:101], v[196:199], v[212:215], v[98:101]
	v_mfma_f32_16x16x32_bf16 v[86:89], v[182:185], v[220:223], v[86:89]
	v_mfma_f32_16x16x32_bf16 v[82:85], v[196:199], v[220:223], v[82:85]
	v_mfma_f32_16x16x32_bf16 v[70:73], v[182:185], v[230:233], v[70:73]
	v_mfma_f32_16x16x32_bf16 v[66:69], v[196:199], v[230:233], v[66:69]
	s_setprio 0
	s_barrier
	s_add_i32 s61, s39, s2
	s_mov_b32 m0, s61
	ds_read_b128 v[200:203], v189 offset:16384
	ds_read_b128 v[204:207], v189 offset:17408
	ds_read_b128 v[208:211], v189 offset:18432
	ds_read_b128 v[212:215], v189 offset:19456
	ds_read_b128 v[216:219], v189 offset:20480
	ds_read_b128 v[220:223], v189 offset:21504
	ds_read_b128 v[224:227], v189 offset:22528
	ds_read_b128 v[230:233], v189 offset:23552
	global_load_lds_dwordx4 v146, s[24:25]
	s_add_i32 m0, s61, 0x2000
	s_add_u32 s62, s24, 0x40000
	s_addc_u32 s63, s25, 0
	s_add_i32 s61, s48, s2
	global_load_lds_dwordx4 v142, s[24:25]
	s_mov_b32 m0, s61
	s_mov_b64 s[98:99], s[26:27]
	global_load_lds_dwordx4 v146, s[62:63]
	s_add_i32 m0, s61, 0x2000
	s_nop 0
	global_load_lds_dwordx4 v142, s[62:63]
	s_mov_b32 m0, s29
	s_nop 0
	global_load_lds_dwordx4 v148, s[26:27]
	s_mov_b32 m0, s30
	s_nop 0
	global_load_lds_dwordx4 v144, s[26:27]
	s_waitcnt vmcnt(8)
	s_waitcnt lgkmcnt(0)
	s_barrier
; #define PG8_STAGE_A(b, h, ptr, NX) do { if constexpr (Sched::GATHER) { unsigned gs_[2]; gs_[0] = ((NX) && last_) ? gN[h][0] : gA[h][0]; gs_[1] = ((NX) && last_) ? gN[h][1] : gA[h][1]; PG8_STAGE(PG8_SA(b, h), ptr, gs_); } \
;         else PG8_STAGE(PG8_SA(b, h), (ptr) + ((h) ? hstep : (size_t)0), voffA); } while (0)
; #define PG8_LDA(dst, b, h) do { _Pragma("unroll") for (int m = 0; m < 4; ++m) _Pragma("unroll") for (int k = 0; k < 2; ++k) dst[m][k] = *(const PG8_LAS bf16x8*)(lds + PG8_SA(b, h) + aoff + m * 2048 + k * 1024); } while (0)
; #define PG8_LDB(dst, b, h) do { _Pragma("unroll") for (int n = 0; n < 2; ++n) _Pragma("unroll") for (int k = 0; k < 2; ++k) dst[n][k] = *(const PG8_LAS bf16x8*)(lds + PG8_SB(b, h) + boff + n * 2048 + k * 1024); } while (0)
; #define PG8_MMA(ai, bj, At, Bt) do { __builtin_amdgcn_s_setprio(1); _Pragma("unroll") for (int m = 0; m < 4; ++m) _Pragma("unroll") for (int n = 0; n < 2; ++n) _Pragma("unroll") for (int k = 0; k < 2; ++k) \
;         acc[ai][bj][m][n] = __builtin_amdgcn_mfma_f32_16x16x32_bf16(Bt[n][k], At[m][k], acc[ai][bj][m][n], 0, 0, 0); __builtin_amdgcn_s_setprio(0); } while (0)
; #define PG8_WAIT_V(n) asm volatile("s_waitcnt vmcnt(" #n ")" ::: "memory")
; #define PG8_WAIT_L(n) asm volatile("s_waitcnt lgkmcnt(" #n ")" ::: "memory")
; #define PG8_BAR __builtin_amdgcn_s_barrier()
; #define PG8_SCHED __builtin_amdgcn_sched_barrier(0)
; template <class Epi, class Sched, bool ALIGN_EPI = false, bool SP2 = false>
; __device__ __forceinline__ void gemm_phase(PG8_LAS unsigned char* lds, const Gemm g, const Sched& S, const Epi& E, const bool skip_epi = false) {
;     ...
;             PG8_WAIT_V(8); PG8_WAIT_L(0); PG8_BAR; PG8_MMA(1, 0, At, B0); PG8_MMA(1, 1, At, B1); PG8_BAR; PG8_SCHED;
;             PG8_LDB(B0, 1, 0); PG8_LDB(B1, 1, 1); PG8_SCHED; PG8_LDA(At, 1, 0); PG8_STAGE_A(0, 1, a2, true);
;             PG8_WAIT_V(8); PG8_WAIT_L(0); PG8_BAR; PG8_MMA(0, 0, At, B0); PG8_MMA(0, 1, At, B1); PG8_BAR; PG8_SCHED;
	s_setprio 3
	s_waitcnt lgkmcnt(0)
	v_mfma_f32_16x16x32_bf16 v[62:65], v[130:133], v[200:203], 0
	v_mfma_f32_16x16x32_bf16 v[58:61], v[138:141], v[200:203], 0
	v_mfma_f32_16x16x32_bf16 v[46:49], v[130:133], v[208:211], 0
	v_mfma_f32_16x16x32_bf16 v[42:45], v[138:141], v[208:211], 0
	v_mfma_f32_16x16x32_bf16 v[30:33], v[130:133], v[216:219], 0
	v_mfma_f32_16x16x32_bf16 v[26:29], v[138:141], v[216:219], 0
	v_mfma_f32_16x16x32_bf16 v[14:17], v[130:133], v[224:227], 0
	v_mfma_f32_16x16x32_bf16 v[10:13], v[138:141], v[224:227], 0
	v_mfma_f32_16x16x32_bf16 v[62:65], v[134:137], v[204:207], v[62:65]
	v_mfma_f32_16x16x32_bf16 v[58:61], v[160:163], v[204:207], v[58:61]
	v_mfma_f32_16x16x32_bf16 v[46:49], v[134:137], v[212:215], v[46:49]
	v_mfma_f32_16x16x32_bf16 v[42:45], v[160:163], v[212:215], v[42:45]
	v_mfma_f32_16x16x32_bf16 v[30:33], v[134:137], v[220:223], v[30:33]
	v_mfma_f32_16x16x32_bf16 v[26:29], v[160:163], v[220:223], v[26:29]
	v_mfma_f32_16x16x32_bf16 v[14:17], v[134:137], v[230:233], v[14:17]
	v_mfma_f32_16x16x32_bf16 v[10:13], v[160:163], v[230:233], v[10:13]
	v_mfma_f32_16x16x32_bf16 v[54:57], v[164:167], v[200:203], 0
	v_mfma_f32_16x16x32_bf16 v[50:53], v[192:195], v[200:203], 0
	v_mfma_f32_16x16x32_bf16 v[38:41], v[164:167], v[208:211], 0
	v_mfma_f32_16x16x32_bf16 v[34:37], v[192:195], v[208:211], 0
	v_mfma_f32_16x16x32_bf16 v[22:25], v[164:167], v[216:219], 0
	v_mfma_f32_16x16x32_bf16 v[18:21], v[192:195], v[216:219], 0
	v_mfma_f32_16x16x32_bf16 v[6:9], v[164:167], v[224:227], 0
	v_mfma_f32_16x16x32_bf16 v[2:5], v[192:195], v[224:227], 0
	v_mfma_f32_16x16x32_bf16 v[54:57], v[182:185], v[204:207], v[54:57]
	v_mfma_f32_16x16x32_bf16 v[50:53], v[196:199], v[204:207], v[50:53]
	v_mfma_f32_16x16x32_bf16 v[38:41], v[182:185], v[212:215], v[38:41]
	v_mfma_f32_16x16x32_bf16 v[34:37], v[196:199], v[212:215], v[34:37]
	v_mfma_f32_16x16x32_bf16 v[22:25], v[182:185], v[220:223], v[22:25]
	v_mfma_f32_16x16x32_bf16 v[18:21], v[196:199], v[220:223], v[18:21]
	v_mfma_f32_16x16x32_bf16 v[6:9], v[182:185], v[230:233], v[6:9]
	v_mfma_f32_16x16x32_bf16 v[2:5], v[196:199], v[230:233], v[2:5]
	s_setprio 0
	s_barrier
	s_add_i32 s61, 0, 0x18000
	s_add_i32 s62, 0, 0x1c000
	v_add_u32_e32 v160, s61, v1
	v_add_u32_e32 v170, s62, v1
	ds_read_b128 v[130:133], v160
	ds_read_b128 v[134:137], v160 offset:1024
	ds_read_b128 v[138:141], v160 offset:2048
	ds_read_b128 v[160:163], v160 offset:3072
	ds_read_b128 v[164:167], v170
	ds_read_b128 v[182:185], v170 offset:1024
	ds_read_b128 v[192:195], v170 offset:2048
	ds_read_b128 v[196:199], v170 offset:3072
	s_add_u32 s26, s26, 0x40000
	s_addc_u32 s27, s27, 0
	s_mov_b32 m0, s31
	ds_read_b128 v[200:203], v189 offset:32768
	ds_read_b128 v[204:207], v189 offset:33792
	ds_read_b128 v[208:211], v189 offset:34816
	ds_read_b128 v[212:215], v189 offset:35840
	ds_read_b128 v[216:219], v189 offset:36864
	ds_read_b128 v[220:223], v189 offset:37888
	ds_read_b128 v[224:227], v189 offset:38912
	ds_read_b128 v[230:233], v189 offset:39936
	global_load_lds_dwordx4 v148, s[26:27]
	s_mov_b32 m0, s34
	s_nop 0
	global_load_lds_dwordx4 v144, s[26:27]
	s_waitcnt vmcnt(8)
	s_waitcnt lgkmcnt(0)
	s_barrier
	s_setprio 3
	s_waitcnt lgkmcnt(0)
	v_mfma_f32_16x16x32_bf16 v[126:129], v[130:133], v[200:203], v[126:129]
	v_mfma_f32_16x16x32_bf16 v[122:125], v[138:141], v[200:203], v[122:125]
	v_mfma_f32_16x16x32_bf16 v[110:113], v[130:133], v[208:211], v[110:113]
	v_mfma_f32_16x16x32_bf16 v[106:109], v[138:141], v[208:211], v[106:109]
	v_mfma_f32_16x16x32_bf16 v[94:97], v[130:133], v[216:219], v[94:97]
	v_mfma_f32_16x16x32_bf16 v[90:93], v[138:141], v[216:219], v[90:93]
	v_mfma_f32_16x16x32_bf16 v[78:81], v[130:133], v[224:227], v[78:81]
	v_mfma_f32_16x16x32_bf16 v[74:77], v[138:141], v[224:227], v[74:77]
	v_mfma_f32_16x16x32_bf16 v[126:129], v[134:137], v[204:207], v[126:129]
	v_mfma_f32_16x16x32_bf16 v[122:125], v[160:163], v[204:207], v[122:125]
	v_mfma_f32_16x16x32_bf16 v[110:113], v[134:137], v[212:215], v[110:113]
	v_mfma_f32_16x16x32_bf16 v[106:109], v[160:163], v[212:215], v[106:109]
	v_mfma_f32_16x16x32_bf16 v[94:97], v[134:137], v[220:223], v[94:97]
	v_mfma_f32_16x16x32_bf16 v[90:93], v[160:163], v[220:223], v[90:93]
	v_mfma_f32_16x16x32_bf16 v[78:81], v[134:137], v[230:233], v[78:81]
	v_mfma_f32_16x16x32_bf16 v[74:77], v[160:163], v[230:233], v[74:77]
	v_mfma_f32_16x16x32_bf16 v[118:121], v[164:167], v[200:203], v[118:121]
	v_mfma_f32_16x16x32_bf16 v[114:117], v[192:195], v[200:203], v[114:117]
	v_mfma_f32_16x16x32_bf16 v[102:105], v[164:167], v[208:211], v[102:105]
	v_mfma_f32_16x16x32_bf16 v[98:101], v[192:195], v[208:211], v[98:101]
	v_mfma_f32_16x16x32_bf16 v[86:89], v[164:167], v[216:219], v[86:89]
	v_mfma_f32_16x16x32_bf16 v[82:85], v[192:195], v[216:219], v[82:85]
	v_mfma_f32_16x16x32_bf16 v[70:73], v[164:167], v[224:227], v[70:73]
	v_mfma_f32_16x16x32_bf16 v[66:69], v[192:195], v[224:227], v[66:69]
	v_mfma_f32_16x16x32_bf16 v[118:121], v[182:185], v[204:207], v[118:121]
	v_mfma_f32_16x16x32_bf16 v[114:117], v[196:199], v[204:207], v[114:117]
	v_mfma_f32_16x16x32_bf16 v[102:105], v[182:185], v[212:215], v[102:105]
	v_mfma_f32_16x16x32_bf16 v[98:101], v[196:199], v[212:215], v[98:101]
	v_mfma_f32_16x16x32_bf16 v[86:89], v[182:185], v[220:223], v[86:89]
	v_mfma_f32_16x16x32_bf16 v[82:85], v[196:199], v[220:223], v[82:85]
	v_mfma_f32_16x16x32_bf16 v[70:73], v[182:185], v[230:233], v[70:73]
	v_mfma_f32_16x16x32_bf16 v[66:69], v[196:199], v[230:233], v[66:69]
	s_setprio 0
	s_barrier
; #define PG8_STAGE_A(b, h, ptr, NX) do { if constexpr (Sched::GATHER) { unsigned gs_[2]; gs_[0] = ((NX) && last_) ? gN[h][0] : gA[h][0]; gs_[1] = ((NX) && last_) ? gN[h][1] : gA[h][1]; PG8_STAGE(PG8_SA(b, h), ptr, gs_); } \
;         else PG8_STAGE(PG8_SA(b, h), (ptr) + ((h) ? hstep : (size_t)0), voffA); } while (0)
; #define PG8_STAGE(bufoff, gbase, voff) do { _Pragma("unroll") for (int _i = 0; _i < 2; ++_i) \
;         __builtin_amdgcn_global_load_lds((const unsigned*)((const char*)(gbase) + (voff)[_i]), (PG8_LAS unsigned*)(lds + (bufoff) + ldsw + _i * 8192), 16, 0, 0); } while (0)
; #define PG8_LDA(dst, b, h) do { _Pragma("unroll") for (int m = 0; m < 4; ++m) _Pragma("unroll") for (int k = 0; k < 2; ++k) dst[m][k] = *(const PG8_LAS bf16x8*)(lds + PG8_SA(b, h) + aoff + m * 2048 + k * 1024); } while (0)
; #define PG8_LDB(dst, b, h) do { _Pragma("unroll") for (int n = 0; n < 2; ++n) _Pragma("unroll") for (int k = 0; k < 2; ++k) dst[n][k] = *(const PG8_LAS bf16x8*)(lds + PG8_SB(b, h) + boff + n * 2048 + k * 1024); } while (0)
; #define PG8_WAIT_V(n) asm volatile("s_waitcnt vmcnt(" #n ")" ::: "memory")
; #define PG8_WAIT_L(n) asm volatile("s_waitcnt lgkmcnt(" #n ")" ::: "memory")
; template <class Epi, class Sched, bool ALIGN_EPI = false, bool SP2 = false>
; __device__ __forceinline__ void gemm_phase(PG8_LAS unsigned char* lds, const Gemm g, const Sched& S, const Epi& E, const bool skip_epi = false) {
;     ...
;         for (int t = 0; t < nt; t += 2) {
;             const bool last = (t == nt - 2); last_ = last && has_next;
;             const char* a1 = cA + (size_t)(t + 1) * kstep;
;             const char* a2 = last ? nA : cA + (size_t)(t + 2) * kstep; const char* b2 = last ? nB : cB + (size_t)(t + 2) * kstep;
;             const char* a3 = a2 + kstep; const char* b3 = b2 + kstep;
;             if (last && has_next) S.a_ready(nxt);
;             if constexpr (SP2) {
;             PG8_LDB(B0, 0, 0); PG8_LDB(B1, 0, 1); PG8_SCHED; PG8_LDA(At, 0, 0); PG8_STAGE_A(1, 1, a1, false);
;             PG8_WAIT_V(8); PG8_WAIT_L(0); PG8_BAR; PG8_MMA(0, 0, At, B0); PG8_MMA(0, 1, At, B1); PG8_BAR; PG8_SCHED;
;     ...
;             PG8_LDA(At, 1, 1); PG8_STAGE(PG8_SB(1, 0), b3, voffB); PG8_STAGE(PG8_SB(1, 1), b3 + hstep, voffB); PG8_STAGE_A(1, 0, a3, true);
;             PG8_WAIT_V(8); PG8_WAIT_L(0); PG8_BAR; PG8_MMA(1, 0, At, B0); PG8_MMA(1, 1, At, B1); PG8_BAR; PG8_SCHED;
	s_add_i32 s26, s61, s2
	s_add_i32 m0, s26, 0xffffff80
	ds_read_b128 v[200:203], v189 offset:49152
	ds_read_b128 v[204:207], v189 offset:50176
	ds_read_b128 v[208:211], v189 offset:51200
	ds_read_b128 v[212:215], v189 offset:52224
	ds_read_b128 v[216:219], v189 offset:53248
	ds_read_b128 v[220:223], v189 offset:54272
	ds_read_b128 v[224:227], v189 offset:55296
	ds_read_b128 v[230:233], v189 offset:56320
	global_load_lds_dwordx4 v146, s[24:25] offset:128
	s_add_i32 m0, s26, 0x1f80
	s_add_i32 s26, s62, s2
	global_load_lds_dwordx4 v142, s[24:25] offset:128
	s_add_u32 s24, s24, 0x40080
	s_addc_u32 s25, s25, 0
	s_mov_b32 m0, s26
	s_nop 0
	global_load_lds_dwordx4 v146, s[24:25]
	s_add_i32 m0, s26, 0x2000
	s_nop 0
	global_load_lds_dwordx4 v142, s[24:25]
	s_add_i32 m0, s36, 0xffffff80
	s_nop 0
	global_load_lds_dwordx4 v148, s[98:99] offset:128
	s_add_i32 m0, s37, 0xffffff80
	s_nop 0
	global_load_lds_dwordx4 v144, s[98:99] offset:128
	s_waitcnt vmcnt(8)
	s_waitcnt lgkmcnt(0)
	s_barrier
	s_setprio 3
	s_waitcnt lgkmcnt(0)
	v_mfma_f32_16x16x32_bf16 v[62:65], v[130:133], v[200:203], v[62:65]
	v_mfma_f32_16x16x32_bf16 v[58:61], v[138:141], v[200:203], v[58:61]
	v_mfma_f32_16x16x32_bf16 v[46:49], v[130:133], v[208:211], v[46:49]
	v_mfma_f32_16x16x32_bf16 v[42:45], v[138:141], v[208:211], v[42:45]
	v_mfma_f32_16x16x32_bf16 v[30:33], v[130:133], v[216:219], v[30:33]
	v_mfma_f32_16x16x32_bf16 v[26:29], v[138:141], v[216:219], v[26:29]
	v_mfma_f32_16x16x32_bf16 v[14:17], v[130:133], v[224:227], v[14:17]
	v_mfma_f32_16x16x32_bf16 v[10:13], v[138:141], v[224:227], v[10:13]
	v_mfma_f32_16x16x32_bf16 v[62:65], v[134:137], v[204:207], v[62:65]
	v_mfma_f32_16x16x32_bf16 v[58:61], v[160:163], v[204:207], v[58:61]
	v_mfma_f32_16x16x32_bf16 v[46:49], v[134:137], v[212:215], v[46:49]
	v_mfma_f32_16x16x32_bf16 v[42:45], v[160:163], v[212:215], v[42:45]
	v_mfma_f32_16x16x32_bf16 v[30:33], v[134:137], v[220:223], v[30:33]
	v_mfma_f32_16x16x32_bf16 v[26:29], v[160:163], v[220:223], v[26:29]
	v_mfma_f32_16x16x32_bf16 v[14:17], v[134:137], v[230:233], v[14:17]
	v_mfma_f32_16x16x32_bf16 v[10:13], v[160:163], v[230:233], v[10:13]
	v_mfma_f32_16x16x32_bf16 v[54:57], v[164:167], v[200:203], v[54:57]
	v_mfma_f32_16x16x32_bf16 v[50:53], v[192:195], v[200:203], v[50:53]
	v_mfma_f32_16x16x32_bf16 v[38:41], v[164:167], v[208:211], v[38:41]
	v_mfma_f32_16x16x32_bf16 v[34:37], v[192:195], v[208:211], v[34:37]
	v_mfma_f32_16x16x32_bf16 v[22:25], v[164:167], v[216:219], v[22:25]
	v_mfma_f32_16x16x32_bf16 v[18:21], v[192:195], v[216:219], v[18:21]
	v_mfma_f32_16x16x32_bf16 v[6:9], v[164:167], v[224:227], v[6:9]
	v_mfma_f32_16x16x32_bf16 v[2:5], v[192:195], v[224:227], v[2:5]
	v_mfma_f32_16x16x32_bf16 v[54:57], v[182:185], v[204:207], v[54:57]
	v_mfma_f32_16x16x32_bf16 v[50:53], v[196:199], v[204:207], v[50:53]
	v_mfma_f32_16x16x32_bf16 v[38:41], v[182:185], v[212:215], v[38:41]
	v_mfma_f32_16x16x32_bf16 v[34:37], v[196:199], v[212:215], v[34:37]
	v_mfma_f32_16x16x32_bf16 v[22:25], v[182:185], v[220:223], v[22:25]
	v_mfma_f32_16x16x32_bf16 v[18:21], v[196:199], v[220:223], v[18:21]
	v_mfma_f32_16x16x32_bf16 v[6:9], v[182:185], v[230:233], v[6:9]
	v_mfma_f32_16x16x32_bf16 v[2:5], v[196:199], v[230:233], v[2:5]
	s_setprio 0
	s_barrier
	s_add_i32 s60, s60, 2
	s_add_u32 s22, s22, 0x100
	s_addc_u32 s23, s23, 0
	s_add_u32 s58, s58, 0x100
	s_addc_u32 s59, s59, 0
	s_cmp_gt_u32 s60, 13
.LBB0_721:
	ds_read_b128 v[130:133], v187
	ds_read_b128 v[134:137], v187 offset:1024
	ds_read_b128 v[138:141], v187 offset:2048
	ds_read_b128 v[160:163], v187 offset:3072
	ds_read_b128 v[164:167], v188
	ds_read_b128 v[182:185], v188 offset:1024
	ds_read_b128 v[192:195], v188 offset:2048
	ds_read_b128 v[196:199], v188 offset:3072
	s_add_u32 s24, s22, 0xfffc0080
	s_addc_u32 s25, s23, -1
	s_cmp_eq_u32 s60, 12
	s_cselect_b32 s27, s15, s25
	s_cselect_b32 s26, s56, s24
	s_cselect_b32 s25, s13, s59
	s_cselect_b32 s24, s57, s58
	s_add_i32 m0, s29, 0xc000
	ds_read_b128 v[200:203], v189
	ds_read_b128 v[204:207], v189 offset:1024
	ds_read_b128 v[208:211], v189 offset:2048
	ds_read_b128 v[212:215], v189 offset:3072
	ds_read_b128 v[216:219], v189 offset:4096
	ds_read_b128 v[220:223], v189 offset:5120
	ds_read_b128 v[224:227], v189 offset:6144
	ds_read_b128 v[230:233], v189 offset:7168
	global_load_lds_dwordx4 v152, s[22:23]
	s_add_i32 m0, s29, 0xe000
	s_nop 0
	global_load_lds_dwordx4 v154, s[22:23]
	s_waitcnt vmcnt(8)
	s_waitcnt lgkmcnt(0)
	s_barrier
	s_setprio 3
	s_waitcnt lgkmcnt(0)
	v_mfma_f32_16x16x32_bf16 v[126:129], v[130:133], v[200:203], v[126:129]
	v_mfma_f32_16x16x32_bf16 v[122:125], v[138:141], v[200:203], v[122:125]
	v_mfma_f32_16x16x32_bf16 v[110:113], v[130:133], v[208:211], v[110:113]
	v_mfma_f32_16x16x32_bf16 v[106:109], v[138:141], v[208:211], v[106:109]
	v_mfma_f32_16x16x32_bf16 v[94:97], v[130:133], v[216:219], v[94:97]
	v_mfma_f32_16x16x32_bf16 v[90:93], v[138:141], v[216:219], v[90:93]
	v_mfma_f32_16x16x32_bf16 v[78:81], v[130:133], v[224:227], v[78:81]
	v_mfma_f32_16x16x32_bf16 v[74:77], v[138:141], v[224:227], v[74:77]
	v_mfma_f32_16x16x32_bf16 v[126:129], v[134:137], v[204:207], v[126:129]
	v_mfma_f32_16x16x32_bf16 v[122:125], v[160:163], v[204:207], v[122:125]
	v_mfma_f32_16x16x32_bf16 v[110:113], v[134:137], v[212:215], v[110:113]
	v_mfma_f32_16x16x32_bf16 v[106:109], v[160:163], v[212:215], v[106:109]
	v_mfma_f32_16x16x32_bf16 v[94:97], v[134:137], v[220:223], v[94:97]
	v_mfma_f32_16x16x32_bf16 v[90:93], v[160:163], v[220:223], v[90:93]
	v_mfma_f32_16x16x32_bf16 v[78:81], v[134:137], v[230:233], v[78:81]
	v_mfma_f32_16x16x32_bf16 v[74:77], v[160:163], v[230:233], v[74:77]
	v_mfma_f32_16x16x32_bf16 v[118:121], v[164:167], v[200:203], v[118:121]
	v_mfma_f32_16x16x32_bf16 v[114:117], v[192:195], v[200:203], v[114:117]
	v_mfma_f32_16x16x32_bf16 v[102:105], v[164:167], v[208:211], v[102:105]
	v_mfma_f32_16x16x32_bf16 v[98:101], v[192:195], v[208:211], v[98:101]
	v_mfma_f32_16x16x32_bf16 v[86:89], v[164:167], v[216:219], v[86:89]
	v_mfma_f32_16x16x32_bf16 v[82:85], v[192:195], v[216:219], v[82:85]
	v_mfma_f32_16x16x32_bf16 v[70:73], v[164:167], v[224:227], v[70:73]
	v_mfma_f32_16x16x32_bf16 v[66:69], v[192:195], v[224:227], v[66:69]
	v_mfma_f32_16x16x32_bf16 v[118:121], v[182:185], v[204:207], v[118:121]
	v_mfma_f32_16x16x32_bf16 v[114:117], v[196:199], v[204:207], v[114:117]
	v_mfma_f32_16x16x32_bf16 v[102:105], v[182:185], v[212:215], v[102:105]
	v_mfma_f32_16x16x32_bf16 v[98:101], v[196:199], v[212:215], v[98:101]
	v_mfma_f32_16x16x32_bf16 v[86:89], v[182:185], v[220:223], v[86:89]
	v_mfma_f32_16x16x32_bf16 v[82:85], v[196:199], v[220:223], v[82:85]
	v_mfma_f32_16x16x32_bf16 v[70:73], v[182:185], v[230:233], v[70:73]
	v_mfma_f32_16x16x32_bf16 v[66:69], v[196:199], v[230:233], v[66:69]
	s_setprio 0
	s_barrier
; #define PG8_STAGE_A(b, h, ptr, NX) do { if constexpr (Sched::GATHER) { unsigned gs_[2]; gs_[0] = ((NX) && last_) ? gN[h][0] : gA[h][0]; gs_[1] = ((NX) && last_) ? gN[h][1] : gA[h][1]; PG8_STAGE(PG8_SA(b, h), ptr, gs_); } \
;         else PG8_STAGE(PG8_SA(b, h), (ptr) + ((h) ? hstep : (size_t)0), voffA); } while (0)
; #define PG8_STAGE(bufoff, gbase, voff) do { _Pragma("unroll") for (int _i = 0; _i < 2; ++_i) \
;         __builtin_amdgcn_global_load_lds((const unsigned*)((const char*)(gbase) + (voff)[_i]), (PG8_LAS unsigned*)(lds + (bufoff) + ldsw + _i * 8192), 16, 0, 0); } while (0)
; #define PG8_LDA(dst, b, h) do { _Pragma("unroll") for (int m = 0; m < 4; ++m) _Pragma("unroll") for (int k = 0; k < 2; ++k) dst[m][k] = *(const PG8_LAS bf16x8*)(lds + PG8_SA(b, h) + aoff + m * 2048 + k * 1024); } while (0)
; #define PG8_LDB(dst, b, h) do { _Pragma("unroll") for (int n = 0; n < 2; ++n) _Pragma("unroll") for (int k = 0; k < 2; ++k) dst[n][k] = *(const PG8_LAS bf16x8*)(lds + PG8_SB(b, h) + boff + n * 2048 + k * 1024); } while (0)
; #define PG8_MMA(ai, bj, At, Bt) do { __builtin_amdgcn_s_setprio(1); _Pragma("unroll") for (int m = 0; m < 4; ++m) _Pragma("unroll") for (int n = 0; n < 2; ++n) _Pragma("unroll") for (int k = 0; k < 2; ++k) \
;         acc[ai][bj][m][n] = __builtin_amdgcn_mfma_f32_16x16x32_bf16(Bt[n][k], At[m][k], acc[ai][bj][m][n], 0, 0, 0); __builtin_amdgcn_s_setprio(0); } while (0)
; #define PG8_WAIT_V(n) asm volatile("s_waitcnt vmcnt(" #n ")" ::: "memory")
; #define PG8_WAIT_L(n) asm volatile("s_waitcnt lgkmcnt(" #n ")" ::: "memory")
; #define PG8_BAR __builtin_amdgcn_s_barrier()
; #define PG8_SCHED __builtin_amdgcn_sched_barrier(0)
; template <class Epi, class Sched, bool ALIGN_EPI = false, bool SP2 = false>
; __device__ __forceinline__ void gemm_phase(PG8_LAS unsigned char* lds, const Gemm g, const Sched& S, const Epi& E, const bool skip_epi = false) {
;     ...
;             PG8_LDA(At, 0, 1); PG8_STAGE(PG8_SB(0, 0), b2, voffB); PG8_STAGE(PG8_SB(0, 1), b2 + hstep, voffB); PG8_STAGE_A(0, 0, a2, true);
;             PG8_WAIT_V(8); PG8_WAIT_L(0); PG8_BAR; PG8_MMA(1, 0, At, B0); PG8_MMA(1, 1, At, B1); PG8_BAR; PG8_SCHED;
;             PG8_LDB(B0, 1, 0); PG8_LDB(B1, 1, 1); PG8_SCHED; PG8_LDA(At, 1, 0); PG8_STAGE_A(0, 1, a2, true);
;             PG8_WAIT_V(8); PG8_WAIT_L(0); PG8_BAR; PG8_MMA(0, 0, At, B0); PG8_MMA(0, 1, At, B1); PG8_BAR; PG8_SCHED;
	s_add_i32 s61, s39, s2
	s_mov_b32 m0, s61
	ds_read_b128 v[200:203], v189 offset:16384
	ds_read_b128 v[204:207], v189 offset:17408
	ds_read_b128 v[208:211], v189 offset:18432
	ds_read_b128 v[212:215], v189 offset:19456
	ds_read_b128 v[216:219], v189 offset:20480
	ds_read_b128 v[220:223], v189 offset:21504
	ds_read_b128 v[224:227], v189 offset:22528
	ds_read_b128 v[230:233], v189 offset:23552
	global_load_lds_dwordx4 v146, s[24:25]
	s_add_i32 m0, s61, 0x2000
	s_add_u32 s62, s24, 0x40000
	s_addc_u32 s63, s25, 0
	s_add_i32 s61, s48, s2
	global_load_lds_dwordx4 v142, s[24:25]
	s_mov_b32 m0, s61
	s_mov_b64 s[98:99], s[26:27]
	global_load_lds_dwordx4 v146, s[62:63]
	s_add_i32 m0, s61, 0x2000
	s_nop 0
	global_load_lds_dwordx4 v142, s[62:63]
	s_mov_b32 m0, s29
	s_nop 0
	global_load_lds_dwordx4 v148, s[26:27]
	s_mov_b32 m0, s30
	s_nop 0
	global_load_lds_dwordx4 v144, s[26:27]
	s_waitcnt vmcnt(8)
	s_waitcnt lgkmcnt(0)
	s_barrier
	s_setprio 3
	s_waitcnt lgkmcnt(0)
	v_mfma_f32_16x16x32_bf16 v[62:65], v[130:133], v[200:203], v[62:65]
	v_mfma_f32_16x16x32_bf16 v[58:61], v[138:141], v[200:203], v[58:61]
	v_mfma_f32_16x16x32_bf16 v[46:49], v[130:133], v[208:211], v[46:49]
	v_mfma_f32_16x16x32_bf16 v[42:45], v[138:141], v[208:211], v[42:45]
	v_mfma_f32_16x16x32_bf16 v[30:33], v[130:133], v[216:219], v[30:33]
	v_mfma_f32_16x16x32_bf16 v[26:29], v[138:141], v[216:219], v[26:29]
	v_mfma_f32_16x16x32_bf16 v[14:17], v[130:133], v[224:227], v[14:17]
	v_mfma_f32_16x16x32_bf16 v[10:13], v[138:141], v[224:227], v[10:13]
	v_mfma_f32_16x16x32_bf16 v[62:65], v[134:137], v[204:207], v[62:65]
	v_mfma_f32_16x16x32_bf16 v[58:61], v[160:163], v[204:207], v[58:61]
	v_mfma_f32_16x16x32_bf16 v[46:49], v[134:137], v[212:215], v[46:49]
	v_mfma_f32_16x16x32_bf16 v[42:45], v[160:163], v[212:215], v[42:45]
	v_mfma_f32_16x16x32_bf16 v[30:33], v[134:137], v[220:223], v[30:33]
	v_mfma_f32_16x16x32_bf16 v[26:29], v[160:163], v[220:223], v[26:29]
	v_mfma_f32_16x16x32_bf16 v[14:17], v[134:137], v[230:233], v[14:17]
	v_mfma_f32_16x16x32_bf16 v[10:13], v[160:163], v[230:233], v[10:13]
	v_mfma_f32_16x16x32_bf16 v[54:57], v[164:167], v[200:203], v[54:57]
	v_mfma_f32_16x16x32_bf16 v[50:53], v[192:195], v[200:203], v[50:53]
	v_mfma_f32_16x16x32_bf16 v[38:41], v[164:167], v[208:211], v[38:41]
	v_mfma_f32_16x16x32_bf16 v[34:37], v[192:195], v[208:211], v[34:37]
	v_mfma_f32_16x16x32_bf16 v[22:25], v[164:167], v[216:219], v[22:25]
	v_mfma_f32_16x16x32_bf16 v[18:21], v[192:195], v[216:219], v[18:21]
	v_mfma_f32_16x16x32_bf16 v[6:9], v[164:167], v[224:227], v[6:9]
	v_mfma_f32_16x16x32_bf16 v[2:5], v[192:195], v[224:227], v[2:5]
	v_mfma_f32_16x16x32_bf16 v[54:57], v[182:185], v[204:207], v[54:57]
	v_mfma_f32_16x16x32_bf16 v[50:53], v[196:199], v[204:207], v[50:53]
	v_mfma_f32_16x16x32_bf16 v[38:41], v[182:185], v[212:215], v[38:41]
	v_mfma_f32_16x16x32_bf16 v[34:37], v[196:199], v[212:215], v[34:37]
	v_mfma_f32_16x16x32_bf16 v[22:25], v[182:185], v[220:223], v[22:25]
	v_mfma_f32_16x16x32_bf16 v[18:21], v[196:199], v[220:223], v[18:21]
	v_mfma_f32_16x16x32_bf16 v[6:9], v[182:185], v[230:233], v[6:9]
	v_mfma_f32_16x16x32_bf16 v[2:5], v[196:199], v[230:233], v[2:5]
	s_setprio 0
	s_barrier
	s_add_i32 s61, 0, 0x18000
	s_add_i32 s62, 0, 0x1c000
	v_add_u32_e32 v160, s61, v1
	v_add_u32_e32 v170, s62, v1
	ds_read_b128 v[130:133], v160
	ds_read_b128 v[134:137], v160 offset:1024
	ds_read_b128 v[138:141], v160 offset:2048
	ds_read_b128 v[160:163], v160 offset:3072
	ds_read_b128 v[164:167], v170
	ds_read_b128 v[182:185], v170 offset:1024
	ds_read_b128 v[192:195], v170 offset:2048
	ds_read_b128 v[196:199], v170 offset:3072
	s_add_u32 s26, s26, 0x40000
	s_addc_u32 s27, s27, 0
	s_mov_b32 m0, s31
	ds_read_b128 v[200:203], v189 offset:32768
	ds_read_b128 v[204:207], v189 offset:33792
	ds_read_b128 v[208:211], v189 offset:34816
	ds_read_b128 v[212:215], v189 offset:35840
	ds_read_b128 v[216:219], v189 offset:36864
	ds_read_b128 v[220:223], v189 offset:37888
	ds_read_b128 v[224:227], v189 offset:38912
	ds_read_b128 v[230:233], v189 offset:39936
	global_load_lds_dwordx4 v148, s[26:27]
	s_mov_b32 m0, s34
	s_nop 0
	global_load_lds_dwordx4 v144, s[26:27]
	s_waitcnt vmcnt(8)
	s_waitcnt lgkmcnt(0)
	s_barrier
; #define PG8_STAGE_A(b, h, ptr, NX) do { if constexpr (Sched::GATHER) { unsigned gs_[2]; gs_[0] = ((NX) && last_) ? gN[h][0] : gA[h][0]; gs_[1] = ((NX) && last_) ? gN[h][1] : gA[h][1]; PG8_STAGE(PG8_SA(b, h), ptr, gs_); } \
;         else PG8_STAGE(PG8_SA(b, h), (ptr) + ((h) ? hstep : (size_t)0), voffA); } while (0)
; #define PG8_STAGE(bufoff, gbase, voff) do { _Pragma("unroll") for (int _i = 0; _i < 2; ++_i) \
;         __builtin_amdgcn_global_load_lds((const unsigned*)((const char*)(gbase) + (voff)[_i]), (PG8_LAS unsigned*)(lds + (bufoff) + ldsw + _i * 8192), 16, 0, 0); } while (0)
; #define PG8_LDA(dst, b, h) do { _Pragma("unroll") for (int m = 0; m < 4; ++m) _Pragma("unroll") for (int k = 0; k < 2; ++k) dst[m][k] = *(const PG8_LAS bf16x8*)(lds + PG8_SA(b, h) + aoff + m * 2048 + k * 1024); } while (0)
; #define PG8_MMA(ai, bj, At, Bt) do { __builtin_amdgcn_s_setprio(1); _Pragma("unroll") for (int m = 0; m < 4; ++m) _Pragma("unroll") for (int n = 0; n < 2; ++n) _Pragma("unroll") for (int k = 0; k < 2; ++k) \
;         acc[ai][bj][m][n] = __builtin_amdgcn_mfma_f32_16x16x32_bf16(Bt[n][k], At[m][k], acc[ai][bj][m][n], 0, 0, 0); __builtin_amdgcn_s_setprio(0); } while (0)
; #define PG8_WAIT_V(n) asm volatile("s_waitcnt vmcnt(" #n ")" ::: "memory")
; #define PG8_WAIT_L(n) asm volatile("s_waitcnt lgkmcnt(" #n ")" ::: "memory")
; #define PG8_BAR __builtin_amdgcn_s_barrier()
; #define PG8_SCHED __builtin_amdgcn_sched_barrier(0)
; template <class Epi, class Sched, bool ALIGN_EPI = false, bool SP2 = false>
; __device__ __forceinline__ void gemm_phase(PG8_LAS unsigned char* lds, const Gemm g, const Sched& S, const Epi& E, const bool skip_epi = false) {
;     ...
;             PG8_WAIT_V(8); PG8_WAIT_L(0); PG8_BAR; PG8_MMA(0, 0, At, B0); PG8_MMA(0, 1, At, B1); PG8_BAR; PG8_SCHED;
;             PG8_LDA(At, 1, 1); PG8_STAGE(PG8_SB(1, 0), b3, voffB); PG8_STAGE(PG8_SB(1, 1), b3 + hstep, voffB); PG8_STAGE_A(1, 0, a3, true);
;             PG8_WAIT_V(8); PG8_WAIT_L(0); PG8_BAR; PG8_MMA(1, 0, At, B0); PG8_MMA(1, 1, At, B1); PG8_BAR; PG8_SCHED;
;     ...
;         if constexpr (ALIGN_EPI) { if (wr == 0) PG8_BAR; }
;         if constexpr (!Epi::AFTER_DRAIN) { if (!skip_epi) E(acc, cur, wr, wc, fr, fq); S.done(cur); }
;         if (!has_next) break;
	s_setprio 3
	s_waitcnt lgkmcnt(0)
	v_mfma_f32_16x16x32_bf16 v[126:129], v[130:133], v[200:203], v[126:129]
	v_mfma_f32_16x16x32_bf16 v[122:125], v[138:141], v[200:203], v[122:125]
	v_mfma_f32_16x16x32_bf16 v[110:113], v[130:133], v[208:211], v[110:113]
	v_mfma_f32_16x16x32_bf16 v[106:109], v[138:141], v[208:211], v[106:109]
	v_mfma_f32_16x16x32_bf16 v[94:97], v[130:133], v[216:219], v[94:97]
	v_mfma_f32_16x16x32_bf16 v[90:93], v[138:141], v[216:219], v[90:93]
	v_mfma_f32_16x16x32_bf16 v[78:81], v[130:133], v[224:227], v[78:81]
	v_mfma_f32_16x16x32_bf16 v[74:77], v[138:141], v[224:227], v[74:77]
	v_mfma_f32_16x16x32_bf16 v[126:129], v[134:137], v[204:207], v[126:129]
	v_mfma_f32_16x16x32_bf16 v[122:125], v[160:163], v[204:207], v[122:125]
	v_mfma_f32_16x16x32_bf16 v[110:113], v[134:137], v[212:215], v[110:113]
	v_mfma_f32_16x16x32_bf16 v[106:109], v[160:163], v[212:215], v[106:109]
	v_mfma_f32_16x16x32_bf16 v[94:97], v[134:137], v[220:223], v[94:97]
	v_mfma_f32_16x16x32_bf16 v[90:93], v[160:163], v[220:223], v[90:93]
	v_mfma_f32_16x16x32_bf16 v[78:81], v[134:137], v[230:233], v[78:81]
	v_mfma_f32_16x16x32_bf16 v[74:77], v[160:163], v[230:233], v[74:77]
	v_mfma_f32_16x16x32_bf16 v[118:121], v[164:167], v[200:203], v[118:121]
	v_mfma_f32_16x16x32_bf16 v[114:117], v[192:195], v[200:203], v[114:117]
	v_mfma_f32_16x16x32_bf16 v[102:105], v[164:167], v[208:211], v[102:105]
	v_mfma_f32_16x16x32_bf16 v[98:101], v[192:195], v[208:211], v[98:101]
	v_mfma_f32_16x16x32_bf16 v[86:89], v[164:167], v[216:219], v[86:89]
	v_mfma_f32_16x16x32_bf16 v[82:85], v[192:195], v[216:219], v[82:85]
	v_mfma_f32_16x16x32_bf16 v[70:73], v[164:167], v[224:227], v[70:73]
	v_mfma_f32_16x16x32_bf16 v[66:69], v[192:195], v[224:227], v[66:69]
	v_mfma_f32_16x16x32_bf16 v[118:121], v[182:185], v[204:207], v[118:121]
	v_mfma_f32_16x16x32_bf16 v[114:117], v[196:199], v[204:207], v[114:117]
	v_mfma_f32_16x16x32_bf16 v[102:105], v[182:185], v[212:215], v[102:105]
	v_mfma_f32_16x16x32_bf16 v[98:101], v[196:199], v[212:215], v[98:101]
	v_mfma_f32_16x16x32_bf16 v[86:89], v[182:185], v[220:223], v[86:89]
	v_mfma_f32_16x16x32_bf16 v[82:85], v[196:199], v[220:223], v[82:85]
	v_mfma_f32_16x16x32_bf16 v[70:73], v[182:185], v[230:233], v[70:73]
	v_mfma_f32_16x16x32_bf16 v[66:69], v[196:199], v[230:233], v[66:69]
	s_setprio 0
	s_barrier
	s_add_i32 s26, s61, s2
	s_add_i32 m0, s26, 0xffffff80
	ds_read_b128 v[200:203], v189 offset:49152
	ds_read_b128 v[204:207], v189 offset:50176
	ds_read_b128 v[208:211], v189 offset:51200
	ds_read_b128 v[212:215], v189 offset:52224
	ds_read_b128 v[216:219], v189 offset:53248
	ds_read_b128 v[220:223], v189 offset:54272
	ds_read_b128 v[224:227], v189 offset:55296
	ds_read_b128 v[230:233], v189 offset:56320
	global_load_lds_dwordx4 v146, s[24:25] offset:128
	s_add_i32 m0, s26, 0x1f80
	s_add_i32 s26, s62, s2
	global_load_lds_dwordx4 v142, s[24:25] offset:128
	s_add_u32 s24, s24, 0x40080
	s_addc_u32 s25, s25, 0
	s_mov_b32 m0, s26
	s_nop 0
	global_load_lds_dwordx4 v146, s[24:25]
	s_add_i32 m0, s26, 0x2000
	s_nop 0
	global_load_lds_dwordx4 v142, s[24:25]
	s_add_i32 m0, s36, 0xffffff80
	s_nop 0
	global_load_lds_dwordx4 v148, s[98:99] offset:128
	s_add_i32 m0, s37, 0xffffff80
	s_nop 0
	global_load_lds_dwordx4 v144, s[98:99] offset:128
	s_waitcnt vmcnt(8)
	s_waitcnt lgkmcnt(0)
	s_barrier
	s_setprio 3
	s_waitcnt lgkmcnt(0)
	v_mfma_f32_16x16x32_bf16 v[62:65], v[130:133], v[200:203], v[62:65]
	v_mfma_f32_16x16x32_bf16 v[58:61], v[138:141], v[200:203], v[58:61]
	v_mfma_f32_16x16x32_bf16 v[46:49], v[130:133], v[208:211], v[46:49]
	v_mfma_f32_16x16x32_bf16 v[42:45], v[138:141], v[208:211], v[42:45]
	v_mfma_f32_16x16x32_bf16 v[30:33], v[130:133], v[216:219], v[30:33]
	v_mfma_f32_16x16x32_bf16 v[26:29], v[138:141], v[216:219], v[26:29]
	v_mfma_f32_16x16x32_bf16 v[14:17], v[130:133], v[224:227], v[14:17]
	v_mfma_f32_16x16x32_bf16 v[10:13], v[138:141], v[224:227], v[10:13]
	v_mfma_f32_16x16x32_bf16 v[62:65], v[134:137], v[204:207], v[62:65]
	v_mfma_f32_16x16x32_bf16 v[58:61], v[160:163], v[204:207], v[58:61]
	v_mfma_f32_16x16x32_bf16 v[46:49], v[134:137], v[212:215], v[46:49]
	v_mfma_f32_16x16x32_bf16 v[42:45], v[160:163], v[212:215], v[42:45]
	v_mfma_f32_16x16x32_bf16 v[30:33], v[134:137], v[220:223], v[30:33]
	v_mfma_f32_16x16x32_bf16 v[26:29], v[160:163], v[220:223], v[26:29]
	v_mfma_f32_16x16x32_bf16 v[14:17], v[134:137], v[230:233], v[14:17]
	v_mfma_f32_16x16x32_bf16 v[10:13], v[160:163], v[230:233], v[10:13]
	v_mfma_f32_16x16x32_bf16 v[54:57], v[164:167], v[200:203], v[54:57]
	v_mfma_f32_16x16x32_bf16 v[50:53], v[192:195], v[200:203], v[50:53]
	v_mfma_f32_16x16x32_bf16 v[38:41], v[164:167], v[208:211], v[38:41]
	v_mfma_f32_16x16x32_bf16 v[34:37], v[192:195], v[208:211], v[34:37]
	v_mfma_f32_16x16x32_bf16 v[22:25], v[164:167], v[216:219], v[22:25]
	v_mfma_f32_16x16x32_bf16 v[18:21], v[192:195], v[216:219], v[18:21]
	v_mfma_f32_16x16x32_bf16 v[6:9], v[164:167], v[224:227], v[6:9]
	v_mfma_f32_16x16x32_bf16 v[2:5], v[192:195], v[224:227], v[2:5]
	v_mfma_f32_16x16x32_bf16 v[54:57], v[182:185], v[204:207], v[54:57]
	v_mfma_f32_16x16x32_bf16 v[50:53], v[196:199], v[204:207], v[50:53]
	v_mfma_f32_16x16x32_bf16 v[38:41], v[182:185], v[212:215], v[38:41]
	v_mfma_f32_16x16x32_bf16 v[34:37], v[196:199], v[212:215], v[34:37]
	v_mfma_f32_16x16x32_bf16 v[22:25], v[182:185], v[220:223], v[22:25]
	v_mfma_f32_16x16x32_bf16 v[18:21], v[196:199], v[220:223], v[18:21]
	v_mfma_f32_16x16x32_bf16 v[6:9], v[182:185], v[230:233], v[6:9]
	v_mfma_f32_16x16x32_bf16 v[2:5], v[196:199], v[230:233], v[2:5]
	s_setprio 0
	s_barrier
	s_add_i32 s60, s60, 2
	s_add_u32 s22, s22, 0x100
	s_addc_u32 s23, s23, 0
	s_add_u32 s58, s58, 0x100
	s_addc_u32 s59, s59, 0
	s_cmp_gt_u32 s60, 13
	s_cbranch_scc0 .LBB0_721
	s_and_b64 vcc, exec, s[10:11]
	s_cbranch_vccz .LBB0_724
	s_barrier

; #define PG8_STAGE_A(b, h, ptr, NX) do { if constexpr (Sched::GATHER) { unsigned gs_[2]; gs_[0] = ((NX) && last_) ? gN[h][0] : gA[h][0]; gs_[1] = ((NX) && last_) ? gN[h][1] : gA[h][1]; PG8_STAGE(PG8_SA(b, h), ptr, gs_); } \
;         else PG8_STAGE(PG8_SA(b, h), (ptr) + ((h) ? hstep : (size_t)0), voffA); } while (0)
; #define PG8_STAGE(bufoff, gbase, voff) do { _Pragma("unroll") for (int _i = 0; _i < 2; ++_i) \
;         __builtin_amdgcn_global_load_lds((const unsigned*)((const char*)(gbase) + (voff)[_i]), (PG8_LAS unsigned*)(lds + (bufoff) + ldsw + _i * 8192), 16, 0, 0); } while (0)
; #define PG8_LDA(dst, b, h) do { _Pragma("unroll") for (int m = 0; m < 4; ++m) _Pragma("unroll") for (int k = 0; k < 2; ++k) dst[m][k] = *(const PG8_LAS bf16x8*)(lds + PG8_SA(b, h) + aoff + m * 2048 + k * 1024); } while (0)
; #define PG8_LDB(dst, b, h) do { _Pragma("unroll") for (int n = 0; n < 2; ++n) _Pragma("unroll") for (int k = 0; k < 2; ++k) dst[n][k] = *(const PG8_LAS bf16x8*)(lds + PG8_SB(b, h) + boff + n * 2048 + k * 1024); } while (0)
; #define PG8_WAIT_V(n) asm volatile("s_waitcnt vmcnt(" #n ")" ::: "memory")
; #define PG8_WAIT_L(n) asm volatile("s_waitcnt lgkmcnt(" #n ")" ::: "memory")
; template <class Epi, class Sched, bool ALIGN_EPI = false, bool SP2 = false>
; __device__ __forceinline__ void gemm_phase(PG8_LAS unsigned char* lds, const Gemm g, const Sched& S, const Epi& E, const bool skip_epi = false) {
;     ...
;         for (int t = 0; t < nt; t += 2) {
;             const bool last = (t == nt - 2); last_ = last && has_next;
;             const char* a1 = cA + (size_t)(t + 1) * kstep;
;             const char* a2 = last ? nA : cA + (size_t)(t + 2) * kstep; const char* b2 = last ? nB : cB + (size_t)(t + 2) * kstep;
;             const char* a3 = a2 + kstep; const char* b3 = b2 + kstep;
;             if (last && has_next) S.a_ready(nxt);
;             if constexpr (SP2) {
;             PG8_LDB(B0, 0, 0); PG8_LDB(B1, 0, 1); PG8_SCHED; PG8_LDA(At, 0, 0); PG8_STAGE_A(1, 1, a1, false);
;             PG8_WAIT_V(8); PG8_WAIT_L(0); PG8_BAR; PG8_MMA(0, 0, At, B0); PG8_MMA(0, 1, At, B1); PG8_BAR; PG8_SCHED;
;             PG8_LDA(At, 0, 1); PG8_STAGE(PG8_SB(0, 0), b2, voffB); PG8_STAGE(PG8_SB(0, 1), b2 + hstep, voffB); PG8_STAGE_A(0, 0, a2, true);
;             PG8_WAIT_V(8); PG8_WAIT_L(0); PG8_BAR; PG8_MMA(1, 0, At, B0); PG8_MMA(1, 1, At, B1); PG8_BAR; PG8_SCHED;
.LBB0_856:
	s_add_u32 s55, s22, 0x100
	s_addc_u32 s56, s23, 0
	s_mov_b32 s57, -2
	s_waitcnt vmcnt(0)
	s_waitcnt lgkmcnt(0)
	ds_read_b128 v[98:101], v234
	ds_read_b128 v[110:113], v234 offset:1024
	ds_read_b128 v[122:125], v234 offset:2048
	ds_read_b128 v[126:129], v234 offset:3072
	ds_read_b128 v[138:141], v235
	ds_read_b128 v[142:145], v235 offset:1024
	ds_read_b128 v[146:149], v235 offset:2048
	ds_read_b128 v[150:153], v235 offset:3072
	s_add_u32 s22, s20, 0x100
	s_addc_u32 s23, s21, 0
	s_cmp_eq_u32 s57, 40
	s_cselect_b32 s27, s9, s23
	s_cselect_b32 s26, s8, s22
	s_cselect_b32 s25, s19, s56
	s_cselect_b32 s24, s18, s55
	v_lshl_add_u64 v[210:211], s[20:21], 0, v[198:199]
	s_add_i32 m0, s3, 0xc000
	ds_read_b128 v[154:157], v236
	ds_read_b128 v[166:169], v236 offset:1024
	ds_read_b128 v[170:173], v236 offset:2048
	ds_read_b128 v[174:177], v236 offset:3072
	ds_read_b128 v[178:181], v236 offset:4096
	ds_read_b128 v[182:185], v236 offset:5120
	ds_read_b128 v[186:189], v236 offset:6144
	ds_read_b128 v[206:209], v236 offset:7168
	global_load_lds_dwordx4 v[210:211], off
	v_lshl_add_u64 v[210:211], s[20:21], 0, v[200:201]
	s_add_i32 m0, s3, 0xe000
	s_nop 0
	global_load_lds_dwordx4 v[210:211], off
	s_waitcnt vmcnt(8)
	s_waitcnt lgkmcnt(0)
	s_barrier
	s_setprio 3
	s_waitcnt lgkmcnt(0)
	v_mfma_f32_16x16x32_bf16 v[162:165], v[98:101], v[154:157], 0
	v_mfma_f32_16x16x32_bf16 v[158:161], v[122:125], v[154:157], 0
	v_mfma_f32_16x16x32_bf16 v[118:121], v[98:101], v[170:173], 0
	v_mfma_f32_16x16x32_bf16 v[114:117], v[122:125], v[170:173], 0
	v_mfma_f32_16x16x32_bf16 v[94:97], v[98:101], v[178:181], 0
	v_mfma_f32_16x16x32_bf16 v[90:93], v[122:125], v[178:181], 0
	v_mfma_f32_16x16x32_bf16 v[78:81], v[98:101], v[186:189], 0
	v_mfma_f32_16x16x32_bf16 v[74:77], v[122:125], v[186:189], 0
	v_mfma_f32_16x16x32_bf16 v[162:165], v[110:113], v[166:169], v[162:165]
	v_mfma_f32_16x16x32_bf16 v[158:161], v[126:129], v[166:169], v[158:161]
	v_mfma_f32_16x16x32_bf16 v[118:121], v[110:113], v[174:177], v[118:121]
	v_mfma_f32_16x16x32_bf16 v[114:117], v[126:129], v[174:177], v[114:117]
	v_mfma_f32_16x16x32_bf16 v[94:97], v[110:113], v[182:185], v[94:97]
	v_mfma_f32_16x16x32_bf16 v[90:93], v[126:129], v[182:185], v[90:93]
	v_mfma_f32_16x16x32_bf16 v[78:81], v[110:113], v[206:209], v[78:81]
	v_mfma_f32_16x16x32_bf16 v[74:77], v[126:129], v[206:209], v[74:77]
	v_mfma_f32_16x16x32_bf16 v[134:137], v[138:141], v[154:157], 0
	v_mfma_f32_16x16x32_bf16 v[130:133], v[146:149], v[154:157], 0
	v_mfma_f32_16x16x32_bf16 v[106:109], v[138:141], v[170:173], 0
	v_mfma_f32_16x16x32_bf16 v[102:105], v[146:149], v[170:173], 0
	v_mfma_f32_16x16x32_bf16 v[86:89], v[138:141], v[178:181], 0
	v_mfma_f32_16x16x32_bf16 v[82:85], v[146:149], v[178:181], 0
	v_mfma_f32_16x16x32_bf16 v[70:73], v[138:141], v[186:189], 0
	v_mfma_f32_16x16x32_bf16 v[66:69], v[146:149], v[186:189], 0
	v_mfma_f32_16x16x32_bf16 v[134:137], v[142:145], v[166:169], v[134:137]
	v_mfma_f32_16x16x32_bf16 v[130:133], v[150:153], v[166:169], v[130:133]
	v_mfma_f32_16x16x32_bf16 v[106:109], v[142:145], v[174:177], v[106:109]
	v_mfma_f32_16x16x32_bf16 v[102:105], v[150:153], v[174:177], v[102:105]
	v_mfma_f32_16x16x32_bf16 v[86:89], v[142:145], v[182:185], v[86:89]
	v_mfma_f32_16x16x32_bf16 v[82:85], v[150:153], v[182:185], v[82:85]
	v_mfma_f32_16x16x32_bf16 v[70:73], v[142:145], v[206:209], v[70:73]
	v_mfma_f32_16x16x32_bf16 v[66:69], v[150:153], v[206:209], v[66:69]
	s_setprio 0
	s_barrier
	s_add_i32 s20, s39, s2
	s_mov_b64 s[98:99], s[24:25]
	s_mov_b32 m0, s20
	ds_read_b128 v[154:157], v236 offset:16384
	ds_read_b128 v[166:169], v236 offset:17408
	ds_read_b128 v[170:173], v236 offset:18432
	ds_read_b128 v[174:177], v236 offset:19456
	ds_read_b128 v[178:181], v236 offset:20480
	ds_read_b128 v[182:185], v236 offset:21504
	ds_read_b128 v[186:189], v236 offset:22528
	ds_read_b128 v[206:209], v236 offset:23552
	global_load_lds_dwordx4 v192, s[24:25]
	s_add_i32 m0, s20, 0x2000
	s_add_u32 s20, s24, 0xb0000
	s_addc_u32 s21, s25, 0
	s_add_i32 s58, s48, s2
	global_load_lds_dwordx4 v196, s[24:25]
	s_mov_b32 m0, s58
	s_nop 0
	global_load_lds_dwordx4 v192, s[20:21]
	s_add_i32 m0, s58, 0x2000
	s_nop 0
	global_load_lds_dwordx4 v196, s[20:21]
	s_mov_b32 m0, s3
	s_nop 0
	global_load_lds_dwordx4 v190, s[26:27]
	s_mov_b32 m0, s28
	s_nop 0
	global_load_lds_dwordx4 v194, s[26:27]
	s_waitcnt vmcnt(8)
	s_waitcnt lgkmcnt(0)
	s_barrier
	s_setprio 3
	s_waitcnt lgkmcnt(0)
	v_mfma_f32_16x16x32_bf16 v[62:65], v[98:101], v[154:157], 0
	v_mfma_f32_16x16x32_bf16 v[58:61], v[122:125], v[154:157], 0
	v_mfma_f32_16x16x32_bf16 v[46:49], v[98:101], v[170:173], 0
	v_mfma_f32_16x16x32_bf16 v[42:45], v[122:125], v[170:173], 0
	v_mfma_f32_16x16x32_bf16 v[30:33], v[98:101], v[178:181], 0
	v_mfma_f32_16x16x32_bf16 v[26:29], v[122:125], v[178:181], 0
	v_mfma_f32_16x16x32_bf16 v[14:17], v[98:101], v[186:189], 0
	v_mfma_f32_16x16x32_bf16 v[10:13], v[122:125], v[186:189], 0
	v_mfma_f32_16x16x32_bf16 v[62:65], v[110:113], v[166:169], v[62:65]
	v_mfma_f32_16x16x32_bf16 v[58:61], v[126:129], v[166:169], v[58:61]
	v_mfma_f32_16x16x32_bf16 v[46:49], v[110:113], v[174:177], v[46:49]
	v_mfma_f32_16x16x32_bf16 v[42:45], v[126:129], v[174:177], v[42:45]
	v_mfma_f32_16x16x32_bf16 v[30:33], v[110:113], v[182:185], v[30:33]
	v_mfma_f32_16x16x32_bf16 v[26:29], v[126:129], v[182:185], v[26:29]
	v_mfma_f32_16x16x32_bf16 v[14:17], v[110:113], v[206:209], v[14:17]
	v_mfma_f32_16x16x32_bf16 v[10:13], v[126:129], v[206:209], v[10:13]
	v_mfma_f32_16x16x32_bf16 v[54:57], v[138:141], v[154:157], 0
	v_mfma_f32_16x16x32_bf16 v[50:53], v[146:149], v[154:157], 0
	v_mfma_f32_16x16x32_bf16 v[38:41], v[138:141], v[170:173], 0
	v_mfma_f32_16x16x32_bf16 v[34:37], v[146:149], v[170:173], 0
	v_mfma_f32_16x16x32_bf16 v[22:25], v[138:141], v[178:181], 0
	v_mfma_f32_16x16x32_bf16 v[18:21], v[146:149], v[178:181], 0
	v_mfma_f32_16x16x32_bf16 v[6:9], v[138:141], v[186:189], 0
	v_mfma_f32_16x16x32_bf16 v[2:5], v[146:149], v[186:189], 0
	v_mfma_f32_16x16x32_bf16 v[54:57], v[142:145], v[166:169], v[54:57]
	v_mfma_f32_16x16x32_bf16 v[50:53], v[150:153], v[166:169], v[50:53]
	v_mfma_f32_16x16x32_bf16 v[38:41], v[142:145], v[174:177], v[38:41]
	v_mfma_f32_16x16x32_bf16 v[34:37], v[150:153], v[174:177], v[34:37]
	v_mfma_f32_16x16x32_bf16 v[22:25], v[142:145], v[182:185], v[22:25]
	v_mfma_f32_16x16x32_bf16 v[18:21], v[150:153], v[182:185], v[18:21]
	v_mfma_f32_16x16x32_bf16 v[6:9], v[142:145], v[206:209], v[6:9]
	v_mfma_f32_16x16x32_bf16 v[2:5], v[150:153], v[206:209], v[2:5]
	s_setprio 0
	s_barrier
; #define PG8_STAGE_A(b, h, ptr, NX) do { if constexpr (Sched::GATHER) { unsigned gs_[2]; gs_[0] = ((NX) && last_) ? gN[h][0] : gA[h][0]; gs_[1] = ((NX) && last_) ? gN[h][1] : gA[h][1]; PG8_STAGE(PG8_SA(b, h), ptr, gs_); } \
;         else PG8_STAGE(PG8_SA(b, h), (ptr) + ((h) ? hstep : (size_t)0), voffA); } while (0)
; #define PG8_STAGE(bufoff, gbase, voff) do { _Pragma("unroll") for (int _i = 0; _i < 2; ++_i) \
;         __builtin_amdgcn_global_load_lds((const unsigned*)((const char*)(gbase) + (voff)[_i]), (PG8_LAS unsigned*)(lds + (bufoff) + ldsw + _i * 8192), 16, 0, 0); } while (0)
; #define PG8_LDA(dst, b, h) do { _Pragma("unroll") for (int m = 0; m < 4; ++m) _Pragma("unroll") for (int k = 0; k < 2; ++k) dst[m][k] = *(const PG8_LAS bf16x8*)(lds + PG8_SA(b, h) + aoff + m * 2048 + k * 1024); } while (0)
; #define PG8_LDB(dst, b, h) do { _Pragma("unroll") for (int n = 0; n < 2; ++n) _Pragma("unroll") for (int k = 0; k < 2; ++k) dst[n][k] = *(const PG8_LAS bf16x8*)(lds + PG8_SB(b, h) + boff + n * 2048 + k * 1024); } while (0)
; #define PG8_MMA(ai, bj, At, Bt) do { __builtin_amdgcn_s_setprio(1); _Pragma("unroll") for (int m = 0; m < 4; ++m) _Pragma("unroll") for (int n = 0; n < 2; ++n) _Pragma("unroll") for (int k = 0; k < 2; ++k) \
;         acc[ai][bj][m][n] = __builtin_amdgcn_mfma_f32_16x16x32_bf16(Bt[n][k], At[m][k], acc[ai][bj][m][n], 0, 0, 0); __builtin_amdgcn_s_setprio(0); } while (0)
; #define PG8_WAIT_V(n) asm volatile("s_waitcnt vmcnt(" #n ")" ::: "memory")
; #define PG8_WAIT_L(n) asm volatile("s_waitcnt lgkmcnt(" #n ")" ::: "memory")
; #define PG8_BAR __builtin_amdgcn_s_barrier()
; #define PG8_SCHED __builtin_amdgcn_sched_barrier(0)
; template <class Epi, class Sched, bool ALIGN_EPI = false, bool SP2 = false>
; __device__ __forceinline__ void gemm_phase(PG8_LAS unsigned char* lds, const Gemm g, const Sched& S, const Epi& E, const bool skip_epi = false) {
;     ...
;             PG8_LDB(B0, 1, 0); PG8_LDB(B1, 1, 1); PG8_SCHED; PG8_LDA(At, 1, 0); PG8_STAGE_A(0, 1, a2, true);
;             PG8_WAIT_V(8); PG8_WAIT_L(0); PG8_BAR; PG8_MMA(0, 0, At, B0); PG8_MMA(0, 1, At, B1); PG8_BAR; PG8_SCHED;
;             PG8_LDA(At, 1, 1); PG8_STAGE(PG8_SB(1, 0), b3, voffB); PG8_STAGE(PG8_SB(1, 1), b3 + hstep, voffB); PG8_STAGE_A(1, 0, a3, true);
;             PG8_WAIT_V(8); PG8_WAIT_L(0); PG8_BAR; PG8_MMA(1, 0, At, B0); PG8_MMA(1, 1, At, B1); PG8_BAR; PG8_SCHED;
	s_add_i32 s58, 0, 0x18000
	s_add_i32 s59, 0, 0x1c000
	v_add_u32_e32 v126, s58, v229
	v_add_u32_e32 v150, s59, v229
	ds_read_b128 v[98:101], v126
	ds_read_b128 v[110:113], v126 offset:1024
	ds_read_b128 v[122:125], v126 offset:2048
	ds_read_b128 v[126:129], v126 offset:3072
	ds_read_b128 v[138:141], v150
	ds_read_b128 v[142:145], v150 offset:1024
	ds_read_b128 v[146:149], v150 offset:2048
	ds_read_b128 v[150:153], v150 offset:3072
	s_add_u32 s20, s26, 0xb0000
	s_addc_u32 s21, s27, 0
	s_mov_b32 m0, s29
	ds_read_b128 v[154:157], v236 offset:32768
	ds_read_b128 v[166:169], v236 offset:33792
	ds_read_b128 v[170:173], v236 offset:34816
	ds_read_b128 v[174:177], v236 offset:35840
	ds_read_b128 v[178:181], v236 offset:36864
	ds_read_b128 v[182:185], v236 offset:37888
	ds_read_b128 v[186:189], v236 offset:38912
	ds_read_b128 v[206:209], v236 offset:39936
	global_load_lds_dwordx4 v190, s[20:21]
	s_mov_b32 m0, s30
	s_nop 0
	global_load_lds_dwordx4 v194, s[20:21]
	s_waitcnt vmcnt(8)
	s_waitcnt lgkmcnt(0)
	s_barrier
	s_setprio 3
	s_waitcnt lgkmcnt(0)
	v_mfma_f32_16x16x32_bf16 v[162:165], v[98:101], v[154:157], v[162:165]
	v_mfma_f32_16x16x32_bf16 v[158:161], v[122:125], v[154:157], v[158:161]
	v_mfma_f32_16x16x32_bf16 v[118:121], v[98:101], v[170:173], v[118:121]
	v_mfma_f32_16x16x32_bf16 v[114:117], v[122:125], v[170:173], v[114:117]
	v_mfma_f32_16x16x32_bf16 v[94:97], v[98:101], v[178:181], v[94:97]
	v_mfma_f32_16x16x32_bf16 v[90:93], v[122:125], v[178:181], v[90:93]
	v_mfma_f32_16x16x32_bf16 v[78:81], v[98:101], v[186:189], v[78:81]
	v_mfma_f32_16x16x32_bf16 v[74:77], v[122:125], v[186:189], v[74:77]
	v_mfma_f32_16x16x32_bf16 v[162:165], v[110:113], v[166:169], v[162:165]
	v_mfma_f32_16x16x32_bf16 v[158:161], v[126:129], v[166:169], v[158:161]
	v_mfma_f32_16x16x32_bf16 v[118:121], v[110:113], v[174:177], v[118:121]
	v_mfma_f32_16x16x32_bf16 v[114:117], v[126:129], v[174:177], v[114:117]
	v_mfma_f32_16x16x32_bf16 v[94:97], v[110:113], v[182:185], v[94:97]
	v_mfma_f32_16x16x32_bf16 v[90:93], v[126:129], v[182:185], v[90:93]
	v_mfma_f32_16x16x32_bf16 v[78:81], v[110:113], v[206:209], v[78:81]
	v_mfma_f32_16x16x32_bf16 v[74:77], v[126:129], v[206:209], v[74:77]
	v_mfma_f32_16x16x32_bf16 v[134:137], v[138:141], v[154:157], v[134:137]
	v_mfma_f32_16x16x32_bf16 v[130:133], v[146:149], v[154:157], v[130:133]
	v_mfma_f32_16x16x32_bf16 v[106:109], v[138:141], v[170:173], v[106:109]
	v_mfma_f32_16x16x32_bf16 v[102:105], v[146:149], v[170:173], v[102:105]
	v_mfma_f32_16x16x32_bf16 v[86:89], v[138:141], v[178:181], v[86:89]
	v_mfma_f32_16x16x32_bf16 v[82:85], v[146:149], v[178:181], v[82:85]
	v_mfma_f32_16x16x32_bf16 v[70:73], v[138:141], v[186:189], v[70:73]
	v_mfma_f32_16x16x32_bf16 v[66:69], v[146:149], v[186:189], v[66:69]
	v_mfma_f32_16x16x32_bf16 v[134:137], v[142:145], v[166:169], v[134:137]
	v_mfma_f32_16x16x32_bf16 v[130:133], v[150:153], v[166:169], v[130:133]
	v_mfma_f32_16x16x32_bf16 v[106:109], v[142:145], v[174:177], v[106:109]
	v_mfma_f32_16x16x32_bf16 v[102:105], v[150:153], v[174:177], v[102:105]
	v_mfma_f32_16x16x32_bf16 v[86:89], v[142:145], v[182:185], v[86:89]
	v_mfma_f32_16x16x32_bf16 v[82:85], v[150:153], v[182:185], v[82:85]
	v_mfma_f32_16x16x32_bf16 v[70:73], v[142:145], v[206:209], v[70:73]
	v_mfma_f32_16x16x32_bf16 v[66:69], v[150:153], v[206:209], v[66:69]
	s_setprio 0
	s_barrier
	s_add_i32 s20, s58, s2
	s_add_i32 m0, s20, 0xffffff80
	ds_read_b128 v[154:157], v236 offset:49152
	ds_read_b128 v[166:169], v236 offset:50176
	ds_read_b128 v[170:173], v236 offset:51200
	ds_read_b128 v[174:177], v236 offset:52224
	ds_read_b128 v[178:181], v236 offset:53248
	ds_read_b128 v[182:185], v236 offset:54272
	ds_read_b128 v[186:189], v236 offset:55296
	ds_read_b128 v[206:209], v236 offset:56320
	global_load_lds_dwordx4 v192, s[24:25] offset:128
	s_add_i32 m0, s20, 0x1f80
	s_add_u32 s20, s24, 0xb0080
	s_addc_u32 s21, s25, 0
	s_add_i32 s24, s59, s2
	global_load_lds_dwordx4 v196, s[98:99] offset:128
	s_mov_b32 m0, s24
	s_nop 0
	global_load_lds_dwordx4 v192, s[20:21]
	s_add_i32 m0, s24, 0x2000
	s_nop 0
	global_load_lds_dwordx4 v196, s[20:21]
	s_add_i32 m0, s35, 0xffffff80
	s_nop 0
	global_load_lds_dwordx4 v190, s[26:27] offset:128
	s_add_i32 m0, s36, 0xffffff80
	s_nop 0
	global_load_lds_dwordx4 v194, s[26:27] offset:128
	s_waitcnt vmcnt(8)
	s_waitcnt lgkmcnt(0)
	s_barrier
	s_setprio 3
	s_waitcnt lgkmcnt(0)
	v_mfma_f32_16x16x32_bf16 v[62:65], v[98:101], v[154:157], v[62:65]
	v_mfma_f32_16x16x32_bf16 v[58:61], v[122:125], v[154:157], v[58:61]
	v_mfma_f32_16x16x32_bf16 v[46:49], v[98:101], v[170:173], v[46:49]
	v_mfma_f32_16x16x32_bf16 v[42:45], v[122:125], v[170:173], v[42:45]
	v_mfma_f32_16x16x32_bf16 v[30:33], v[98:101], v[178:181], v[30:33]
	v_mfma_f32_16x16x32_bf16 v[26:29], v[122:125], v[178:181], v[26:29]
	v_mfma_f32_16x16x32_bf16 v[14:17], v[98:101], v[186:189], v[14:17]
	v_mfma_f32_16x16x32_bf16 v[10:13], v[122:125], v[186:189], v[10:13]
	v_mfma_f32_16x16x32_bf16 v[62:65], v[110:113], v[166:169], v[62:65]
	v_mfma_f32_16x16x32_bf16 v[58:61], v[126:129], v[166:169], v[58:61]
	v_mfma_f32_16x16x32_bf16 v[46:49], v[110:113], v[174:177], v[46:49]
	v_mfma_f32_16x16x32_bf16 v[42:45], v[126:129], v[174:177], v[42:45]
	v_mfma_f32_16x16x32_bf16 v[30:33], v[110:113], v[182:185], v[30:33]
	v_mfma_f32_16x16x32_bf16 v[26:29], v[126:129], v[182:185], v[26:29]
	v_mfma_f32_16x16x32_bf16 v[14:17], v[110:113], v[206:209], v[14:17]
	v_mfma_f32_16x16x32_bf16 v[10:13], v[126:129], v[206:209], v[10:13]
	v_mfma_f32_16x16x32_bf16 v[54:57], v[138:141], v[154:157], v[54:57]
	v_mfma_f32_16x16x32_bf16 v[50:53], v[146:149], v[154:157], v[50:53]
	v_mfma_f32_16x16x32_bf16 v[38:41], v[138:141], v[170:173], v[38:41]
	v_mfma_f32_16x16x32_bf16 v[34:37], v[146:149], v[170:173], v[34:37]
	v_mfma_f32_16x16x32_bf16 v[22:25], v[138:141], v[178:181], v[22:25]
	v_mfma_f32_16x16x32_bf16 v[18:21], v[146:149], v[178:181], v[18:21]
	v_mfma_f32_16x16x32_bf16 v[6:9], v[138:141], v[186:189], v[6:9]
	v_mfma_f32_16x16x32_bf16 v[2:5], v[146:149], v[186:189], v[2:5]
	v_mfma_f32_16x16x32_bf16 v[54:57], v[142:145], v[166:169], v[54:57]
	v_mfma_f32_16x16x32_bf16 v[50:53], v[150:153], v[166:169], v[50:53]
	v_mfma_f32_16x16x32_bf16 v[38:41], v[142:145], v[174:177], v[38:41]
	v_mfma_f32_16x16x32_bf16 v[34:37], v[150:153], v[174:177], v[34:37]
	v_mfma_f32_16x16x32_bf16 v[22:25], v[142:145], v[182:185], v[22:25]
	v_mfma_f32_16x16x32_bf16 v[18:21], v[150:153], v[182:185], v[18:21]
	v_mfma_f32_16x16x32_bf16 v[6:9], v[142:145], v[206:209], v[6:9]
	v_mfma_f32_16x16x32_bf16 v[2:5], v[150:153], v[206:209], v[2:5]
	s_setprio 0
	s_barrier
	s_add_i32 s57, s57, 2
	s_add_u32 s55, s55, 0x100
	s_addc_u32 s56, s56, 0
	s_cmp_gt_u32 s57, 41
	s_mov_b64 s[20:21], s[22:23]
; #define PG8_STAGE_A(b, h, ptr, NX) do { if constexpr (Sched::GATHER) { unsigned gs_[2]; gs_[0] = ((NX) && last_) ? gN[h][0] : gA[h][0]; gs_[1] = ((NX) && last_) ? gN[h][1] : gA[h][1]; PG8_STAGE(PG8_SA(b, h), ptr, gs_); } \
;         else PG8_STAGE(PG8_SA(b, h), (ptr) + ((h) ? hstep : (size_t)0), voffA); } while (0)
; #define PG8_STAGE(bufoff, gbase, voff) do { _Pragma("unroll") for (int _i = 0; _i < 2; ++_i) \
;         __builtin_amdgcn_global_load_lds((const unsigned*)((const char*)(gbase) + (voff)[_i]), (PG8_LAS unsigned*)(lds + (bufoff) + ldsw + _i * 8192), 16, 0, 0); } while (0)
; #define PG8_LDA(dst, b, h) do { _Pragma("unroll") for (int m = 0; m < 4; ++m) _Pragma("unroll") for (int k = 0; k < 2; ++k) dst[m][k] = *(const PG8_LAS bf16x8*)(lds + PG8_SA(b, h) + aoff + m * 2048 + k * 1024); } while (0)
; #define PG8_LDB(dst, b, h) do { _Pragma("unroll") for (int n = 0; n < 2; ++n) _Pragma("unroll") for (int k = 0; k < 2; ++k) dst[n][k] = *(const PG8_LAS bf16x8*)(lds + PG8_SB(b, h) + boff + n * 2048 + k * 1024); } while (0)
; #define PG8_WAIT_V(n) asm volatile("s_waitcnt vmcnt(" #n ")" ::: "memory")
; #define PG8_WAIT_L(n) asm volatile("s_waitcnt lgkmcnt(" #n ")" ::: "memory")
; template <class Epi, class Sched, bool ALIGN_EPI = false, bool SP2 = false>
; __device__ __forceinline__ void gemm_phase(PG8_LAS unsigned char* lds, const Gemm g, const Sched& S, const Epi& E, const bool skip_epi = false) {
;     ...
;         for (int t = 0; t < nt; t += 2) {
;             const bool last = (t == nt - 2); last_ = last && has_next;
;             const char* a1 = cA + (size_t)(t + 1) * kstep;
;             const char* a2 = last ? nA : cA + (size_t)(t + 2) * kstep; const char* b2 = last ? nB : cB + (size_t)(t + 2) * kstep;
;             const char* a3 = a2 + kstep; const char* b3 = b2 + kstep;
;             if (last && has_next) S.a_ready(nxt);
;             if constexpr (SP2) {
;             PG8_LDB(B0, 0, 0); PG8_LDB(B1, 0, 1); PG8_SCHED; PG8_LDA(At, 0, 0); PG8_STAGE_A(1, 1, a1, false);
;             PG8_WAIT_V(8); PG8_WAIT_L(0); PG8_BAR; PG8_MMA(0, 0, At, B0); PG8_MMA(0, 1, At, B1); PG8_BAR; PG8_SCHED;
;             PG8_LDA(At, 0, 1); PG8_STAGE(PG8_SB(0, 0), b2, voffB); PG8_STAGE(PG8_SB(0, 1), b2 + hstep, voffB); PG8_STAGE_A(0, 0, a2, true);
;             PG8_WAIT_V(8); PG8_WAIT_L(0); PG8_BAR; PG8_MMA(1, 0, At, B0); PG8_MMA(1, 1, At, B1); PG8_BAR; PG8_SCHED;
.LBB0_857:
	ds_read_b128 v[98:101], v234
	ds_read_b128 v[110:113], v234 offset:1024
	ds_read_b128 v[122:125], v234 offset:2048
	ds_read_b128 v[126:129], v234 offset:3072
	ds_read_b128 v[138:141], v235
	ds_read_b128 v[142:145], v235 offset:1024
	ds_read_b128 v[146:149], v235 offset:2048
	ds_read_b128 v[150:153], v235 offset:3072
	s_add_u32 s22, s20, 0x100
	s_addc_u32 s23, s21, 0
	s_cmp_eq_u32 s57, 40
	s_cselect_b32 s27, s9, s23
	s_cselect_b32 s26, s8, s22
	s_cselect_b32 s25, s19, s56
	s_cselect_b32 s24, s18, s55
	v_lshl_add_u64 v[210:211], s[20:21], 0, v[198:199]
	s_add_i32 m0, s3, 0xc000
	ds_read_b128 v[154:157], v236
	ds_read_b128 v[166:169], v236 offset:1024
	ds_read_b128 v[170:173], v236 offset:2048
	ds_read_b128 v[174:177], v236 offset:3072
	ds_read_b128 v[178:181], v236 offset:4096
	ds_read_b128 v[182:185], v236 offset:5120
	ds_read_b128 v[186:189], v236 offset:6144
	ds_read_b128 v[206:209], v236 offset:7168
	global_load_lds_dwordx4 v[210:211], off
	v_lshl_add_u64 v[210:211], s[20:21], 0, v[200:201]
	s_add_i32 m0, s3, 0xe000
	s_nop 0
	global_load_lds_dwordx4 v[210:211], off
	s_waitcnt vmcnt(8)
	s_waitcnt lgkmcnt(0)
	s_barrier
	s_setprio 3
	s_waitcnt lgkmcnt(0)
	v_mfma_f32_16x16x32_bf16 v[162:165], v[98:101], v[154:157], v[162:165]
	v_mfma_f32_16x16x32_bf16 v[158:161], v[122:125], v[154:157], v[158:161]
	v_mfma_f32_16x16x32_bf16 v[118:121], v[98:101], v[170:173], v[118:121]
	v_mfma_f32_16x16x32_bf16 v[114:117], v[122:125], v[170:173], v[114:117]
	v_mfma_f32_16x16x32_bf16 v[94:97], v[98:101], v[178:181], v[94:97]
	v_mfma_f32_16x16x32_bf16 v[90:93], v[122:125], v[178:181], v[90:93]
	v_mfma_f32_16x16x32_bf16 v[78:81], v[98:101], v[186:189], v[78:81]
	v_mfma_f32_16x16x32_bf16 v[74:77], v[122:125], v[186:189], v[74:77]
	v_mfma_f32_16x16x32_bf16 v[162:165], v[110:113], v[166:169], v[162:165]
	v_mfma_f32_16x16x32_bf16 v[158:161], v[126:129], v[166:169], v[158:161]
	v_mfma_f32_16x16x32_bf16 v[118:121], v[110:113], v[174:177], v[118:121]
	v_mfma_f32_16x16x32_bf16 v[114:117], v[126:129], v[174:177], v[114:117]
	v_mfma_f32_16x16x32_bf16 v[94:97], v[110:113], v[182:185], v[94:97]
	v_mfma_f32_16x16x32_bf16 v[90:93], v[126:129], v[182:185], v[90:93]
	v_mfma_f32_16x16x32_bf16 v[78:81], v[110:113], v[206:209], v[78:81]
	v_mfma_f32_16x16x32_bf16 v[74:77], v[126:129], v[206:209], v[74:77]
	v_mfma_f32_16x16x32_bf16 v[134:137], v[138:141], v[154:157], v[134:137]
	v_mfma_f32_16x16x32_bf16 v[130:133], v[146:149], v[154:157], v[130:133]
	v_mfma_f32_16x16x32_bf16 v[106:109], v[138:141], v[170:173], v[106:109]
	v_mfma_f32_16x16x32_bf16 v[102:105], v[146:149], v[170:173], v[102:105]
	v_mfma_f32_16x16x32_bf16 v[86:89], v[138:141], v[178:181], v[86:89]
	v_mfma_f32_16x16x32_bf16 v[82:85], v[146:149], v[178:181], v[82:85]
	v_mfma_f32_16x16x32_bf16 v[70:73], v[138:141], v[186:189], v[70:73]
	v_mfma_f32_16x16x32_bf16 v[66:69], v[146:149], v[186:189], v[66:69]
	v_mfma_f32_16x16x32_bf16 v[134:137], v[142:145], v[166:169], v[134:137]
	v_mfma_f32_16x16x32_bf16 v[130:133], v[150:153], v[166:169], v[130:133]
	v_mfma_f32_16x16x32_bf16 v[106:109], v[142:145], v[174:177], v[106:109]
	v_mfma_f32_16x16x32_bf16 v[102:105], v[150:153], v[174:177], v[102:105]
	v_mfma_f32_16x16x32_bf16 v[86:89], v[142:145], v[182:185], v[86:89]
	v_mfma_f32_16x16x32_bf16 v[82:85], v[150:153], v[182:185], v[82:85]
	v_mfma_f32_16x16x32_bf16 v[70:73], v[142:145], v[206:209], v[70:73]
	v_mfma_f32_16x16x32_bf16 v[66:69], v[150:153], v[206:209], v[66:69]
	s_setprio 0
	s_barrier
	s_add_i32 s20, s39, s2
	s_mov_b64 s[98:99], s[24:25]
	s_mov_b32 m0, s20
	ds_read_b128 v[154:157], v236 offset:16384
	ds_read_b128 v[166:169], v236 offset:17408
	ds_read_b128 v[170:173], v236 offset:18432
	ds_read_b128 v[174:177], v236 offset:19456
	ds_read_b128 v[178:181], v236 offset:20480
	ds_read_b128 v[182:185], v236 offset:21504
	ds_read_b128 v[186:189], v236 offset:22528
	ds_read_b128 v[206:209], v236 offset:23552
	global_load_lds_dwordx4 v192, s[24:25]
	s_add_i32 m0, s20, 0x2000
	s_add_u32 s20, s24, 0xb0000
	s_addc_u32 s21, s25, 0
	s_add_i32 s58, s48, s2
	global_load_lds_dwordx4 v196, s[24:25]
	s_mov_b32 m0, s58
	s_nop 0
	global_load_lds_dwordx4 v192, s[20:21]
	s_add_i32 m0, s58, 0x2000
	s_nop 0
	global_load_lds_dwordx4 v196, s[20:21]
	s_mov_b32 m0, s3
	s_nop 0
	global_load_lds_dwordx4 v190, s[26:27]
	s_mov_b32 m0, s28
	s_nop 0
	global_load_lds_dwordx4 v194, s[26:27]
	s_waitcnt vmcnt(8)
	s_waitcnt lgkmcnt(0)
	s_barrier
	s_setprio 3
	s_waitcnt lgkmcnt(0)
	v_mfma_f32_16x16x32_bf16 v[62:65], v[98:101], v[154:157], v[62:65]
	v_mfma_f32_16x16x32_bf16 v[58:61], v[122:125], v[154:157], v[58:61]
	v_mfma_f32_16x16x32_bf16 v[46:49], v[98:101], v[170:173], v[46:49]
	v_mfma_f32_16x16x32_bf16 v[42:45], v[122:125], v[170:173], v[42:45]
	v_mfma_f32_16x16x32_bf16 v[30:33], v[98:101], v[178:181], v[30:33]
	v_mfma_f32_16x16x32_bf16 v[26:29], v[122:125], v[178:181], v[26:29]
	v_mfma_f32_16x16x32_bf16 v[14:17], v[98:101], v[186:189], v[14:17]
	v_mfma_f32_16x16x32_bf16 v[10:13], v[122:125], v[186:189], v[10:13]
	v_mfma_f32_16x16x32_bf16 v[62:65], v[110:113], v[166:169], v[62:65]
	v_mfma_f32_16x16x32_bf16 v[58:61], v[126:129], v[166:169], v[58:61]
	v_mfma_f32_16x16x32_bf16 v[46:49], v[110:113], v[174:177], v[46:49]
	v_mfma_f32_16x16x32_bf16 v[42:45], v[126:129], v[174:177], v[42:45]
	v_mfma_f32_16x16x32_bf16 v[30:33], v[110:113], v[182:185], v[30:33]
	v_mfma_f32_16x16x32_bf16 v[26:29], v[126:129], v[182:185], v[26:29]
	v_mfma_f32_16x16x32_bf16 v[14:17], v[110:113], v[206:209], v[14:17]
	v_mfma_f32_16x16x32_bf16 v[10:13], v[126:129], v[206:209], v[10:13]
	v_mfma_f32_16x16x32_bf16 v[54:57], v[138:141], v[154:157], v[54:57]
	v_mfma_f32_16x16x32_bf16 v[50:53], v[146:149], v[154:157], v[50:53]
	v_mfma_f32_16x16x32_bf16 v[38:41], v[138:141], v[170:173], v[38:41]
	v_mfma_f32_16x16x32_bf16 v[34:37], v[146:149], v[170:173], v[34:37]
	v_mfma_f32_16x16x32_bf16 v[22:25], v[138:141], v[178:181], v[22:25]
	v_mfma_f32_16x16x32_bf16 v[18:21], v[146:149], v[178:181], v[18:21]
	v_mfma_f32_16x16x32_bf16 v[6:9], v[138:141], v[186:189], v[6:9]
	v_mfma_f32_16x16x32_bf16 v[2:5], v[146:149], v[186:189], v[2:5]
	v_mfma_f32_16x16x32_bf16 v[54:57], v[142:145], v[166:169], v[54:57]
	v_mfma_f32_16x16x32_bf16 v[50:53], v[150:153], v[166:169], v[50:53]
	v_mfma_f32_16x16x32_bf16 v[38:41], v[142:145], v[174:177], v[38:41]
	v_mfma_f32_16x16x32_bf16 v[34:37], v[150:153], v[174:177], v[34:37]
	v_mfma_f32_16x16x32_bf16 v[22:25], v[142:145], v[182:185], v[22:25]
	v_mfma_f32_16x16x32_bf16 v[18:21], v[150:153], v[182:185], v[18:21]
	v_mfma_f32_16x16x32_bf16 v[6:9], v[142:145], v[206:209], v[6:9]
	v_mfma_f32_16x16x32_bf16 v[2:5], v[150:153], v[206:209], v[2:5]
	s_setprio 0
	s_barrier
; #define PG8_STAGE_A(b, h, ptr, NX) do { if constexpr (Sched::GATHER) { unsigned gs_[2]; gs_[0] = ((NX) && last_) ? gN[h][0] : gA[h][0]; gs_[1] = ((NX) && last_) ? gN[h][1] : gA[h][1]; PG8_STAGE(PG8_SA(b, h), ptr, gs_); } \
;         else PG8_STAGE(PG8_SA(b, h), (ptr) + ((h) ? hstep : (size_t)0), voffA); } while (0)
; #define PG8_STAGE(bufoff, gbase, voff) do { _Pragma("unroll") for (int _i = 0; _i < 2; ++_i) \
;         __builtin_amdgcn_global_load_lds((const unsigned*)((const char*)(gbase) + (voff)[_i]), (PG8_LAS unsigned*)(lds + (bufoff) + ldsw + _i * 8192), 16, 0, 0); } while (0)
; #define PG8_LDA(dst, b, h) do { _Pragma("unroll") for (int m = 0; m < 4; ++m) _Pragma("unroll") for (int k = 0; k < 2; ++k) dst[m][k] = *(const PG8_LAS bf16x8*)(lds + PG8_SA(b, h) + aoff + m * 2048 + k * 1024); } while (0)
; #define PG8_LDB(dst, b, h) do { _Pragma("unroll") for (int n = 0; n < 2; ++n) _Pragma("unroll") for (int k = 0; k < 2; ++k) dst[n][k] = *(const PG8_LAS bf16x8*)(lds + PG8_SB(b, h) + boff + n * 2048 + k * 1024); } while (0)
; #define PG8_MMA(ai, bj, At, Bt) do { __builtin_amdgcn_s_setprio(1); _Pragma("unroll") for (int m = 0; m < 4; ++m) _Pragma("unroll") for (int n = 0; n < 2; ++n) _Pragma("unroll") for (int k = 0; k < 2; ++k) \
;         acc[ai][bj][m][n] = __builtin_amdgcn_mfma_f32_16x16x32_bf16(Bt[n][k], At[m][k], acc[ai][bj][m][n], 0, 0, 0); __builtin_amdgcn_s_setprio(0); } while (0)
; #define PG8_WAIT_V(n) asm volatile("s_waitcnt vmcnt(" #n ")" ::: "memory")
; #define PG8_WAIT_L(n) asm volatile("s_waitcnt lgkmcnt(" #n ")" ::: "memory")
; #define PG8_BAR __builtin_amdgcn_s_barrier()
; #define PG8_SCHED __builtin_amdgcn_sched_barrier(0)
; template <class Epi, class Sched, bool ALIGN_EPI = false, bool SP2 = false>
; __device__ __forceinline__ void gemm_phase(PG8_LAS unsigned char* lds, const Gemm g, const Sched& S, const Epi& E, const bool skip_epi = false) {
;     ...
;             PG8_LDB(B0, 1, 0); PG8_LDB(B1, 1, 1); PG8_SCHED; PG8_LDA(At, 1, 0); PG8_STAGE_A(0, 1, a2, true);
;             PG8_WAIT_V(8); PG8_WAIT_L(0); PG8_BAR; PG8_MMA(0, 0, At, B0); PG8_MMA(0, 1, At, B1); PG8_BAR; PG8_SCHED;
;             PG8_LDA(At, 1, 1); PG8_STAGE(PG8_SB(1, 0), b3, voffB); PG8_STAGE(PG8_SB(1, 1), b3 + hstep, voffB); PG8_STAGE_A(1, 0, a3, true);
;             PG8_WAIT_V(8); PG8_WAIT_L(0); PG8_BAR; PG8_MMA(1, 0, At, B0); PG8_MMA(1, 1, At, B1); PG8_BAR; PG8_SCHED;
	s_add_i32 s58, 0, 0x18000
	s_add_i32 s59, 0, 0x1c000
	v_add_u32_e32 v126, s58, v229
	v_add_u32_e32 v150, s59, v229
	ds_read_b128 v[98:101], v126
	ds_read_b128 v[110:113], v126 offset:1024
	ds_read_b128 v[122:125], v126 offset:2048
	ds_read_b128 v[126:129], v126 offset:3072
	ds_read_b128 v[138:141], v150
	ds_read_b128 v[142:145], v150 offset:1024
	ds_read_b128 v[146:149], v150 offset:2048
	ds_read_b128 v[150:153], v150 offset:3072
	s_add_u32 s20, s26, 0xb0000
	s_addc_u32 s21, s27, 0
	s_mov_b32 m0, s29
	ds_read_b128 v[154:157], v236 offset:32768
	ds_read_b128 v[166:169], v236 offset:33792
	ds_read_b128 v[170:173], v236 offset:34816
	ds_read_b128 v[174:177], v236 offset:35840
	ds_read_b128 v[178:181], v236 offset:36864
	ds_read_b128 v[182:185], v236 offset:37888
	ds_read_b128 v[186:189], v236 offset:38912
	ds_read_b128 v[206:209], v236 offset:39936
	global_load_lds_dwordx4 v190, s[20:21]
	s_mov_b32 m0, s30
	s_nop 0
	global_load_lds_dwordx4 v194, s[20:21]
	s_waitcnt vmcnt(8)
	s_waitcnt lgkmcnt(0)
	s_barrier
	s_setprio 3
	s_waitcnt lgkmcnt(0)
	v_mfma_f32_16x16x32_bf16 v[162:165], v[98:101], v[154:157], v[162:165]
	v_mfma_f32_16x16x32_bf16 v[158:161], v[122:125], v[154:157], v[158:161]
	v_mfma_f32_16x16x32_bf16 v[118:121], v[98:101], v[170:173], v[118:121]
	v_mfma_f32_16x16x32_bf16 v[114:117], v[122:125], v[170:173], v[114:117]
	v_mfma_f32_16x16x32_bf16 v[94:97], v[98:101], v[178:181], v[94:97]
	v_mfma_f32_16x16x32_bf16 v[90:93], v[122:125], v[178:181], v[90:93]
	v_mfma_f32_16x16x32_bf16 v[78:81], v[98:101], v[186:189], v[78:81]
	v_mfma_f32_16x16x32_bf16 v[74:77], v[122:125], v[186:189], v[74:77]
	v_mfma_f32_16x16x32_bf16 v[162:165], v[110:113], v[166:169], v[162:165]
	v_mfma_f32_16x16x32_bf16 v[158:161], v[126:129], v[166:169], v[158:161]
	v_mfma_f32_16x16x32_bf16 v[118:121], v[110:113], v[174:177], v[118:121]
	v_mfma_f32_16x16x32_bf16 v[114:117], v[126:129], v[174:177], v[114:117]
	v_mfma_f32_16x16x32_bf16 v[94:97], v[110:113], v[182:185], v[94:97]
	v_mfma_f32_16x16x32_bf16 v[90:93], v[126:129], v[182:185], v[90:93]
	v_mfma_f32_16x16x32_bf16 v[78:81], v[110:113], v[206:209], v[78:81]
	v_mfma_f32_16x16x32_bf16 v[74:77], v[126:129], v[206:209], v[74:77]
	v_mfma_f32_16x16x32_bf16 v[134:137], v[138:141], v[154:157], v[134:137]
	v_mfma_f32_16x16x32_bf16 v[130:133], v[146:149], v[154:157], v[130:133]
	v_mfma_f32_16x16x32_bf16 v[106:109], v[138:141], v[170:173], v[106:109]
	v_mfma_f32_16x16x32_bf16 v[102:105], v[146:149], v[170:173], v[102:105]
	v_mfma_f32_16x16x32_bf16 v[86:89], v[138:141], v[178:181], v[86:89]
	v_mfma_f32_16x16x32_bf16 v[82:85], v[146:149], v[178:181], v[82:85]
	v_mfma_f32_16x16x32_bf16 v[70:73], v[138:141], v[186:189], v[70:73]
	v_mfma_f32_16x16x32_bf16 v[66:69], v[146:149], v[186:189], v[66:69]
	v_mfma_f32_16x16x32_bf16 v[134:137], v[142:145], v[166:169], v[134:137]
	v_mfma_f32_16x16x32_bf16 v[130:133], v[150:153], v[166:169], v[130:133]
	v_mfma_f32_16x16x32_bf16 v[106:109], v[142:145], v[174:177], v[106:109]
	v_mfma_f32_16x16x32_bf16 v[102:105], v[150:153], v[174:177], v[102:105]
	v_mfma_f32_16x16x32_bf16 v[86:89], v[142:145], v[182:185], v[86:89]
	v_mfma_f32_16x16x32_bf16 v[82:85], v[150:153], v[182:185], v[82:85]
	v_mfma_f32_16x16x32_bf16 v[70:73], v[142:145], v[206:209], v[70:73]
	v_mfma_f32_16x16x32_bf16 v[66:69], v[150:153], v[206:209], v[66:69]
	s_setprio 0
	s_barrier
	s_add_i32 s20, s58, s2
	s_add_i32 m0, s20, 0xffffff80
	ds_read_b128 v[154:157], v236 offset:49152
	ds_read_b128 v[166:169], v236 offset:50176
	ds_read_b128 v[170:173], v236 offset:51200
	ds_read_b128 v[174:177], v236 offset:52224
	ds_read_b128 v[178:181], v236 offset:53248
	ds_read_b128 v[182:185], v236 offset:54272
	ds_read_b128 v[186:189], v236 offset:55296
	ds_read_b128 v[206:209], v236 offset:56320
	global_load_lds_dwordx4 v192, s[24:25] offset:128
	s_add_i32 m0, s20, 0x1f80
	s_add_u32 s20, s24, 0xb0080
	s_addc_u32 s21, s25, 0
	s_add_i32 s24, s59, s2
	global_load_lds_dwordx4 v196, s[98:99] offset:128
	s_mov_b32 m0, s24
	s_nop 0
	global_load_lds_dwordx4 v192, s[20:21]
	s_add_i32 m0, s24, 0x2000
	s_nop 0
	global_load_lds_dwordx4 v196, s[20:21]
	s_add_i32 m0, s35, 0xffffff80
	s_nop 0
	global_load_lds_dwordx4 v190, s[26:27] offset:128
	s_add_i32 m0, s36, 0xffffff80
	s_nop 0
	global_load_lds_dwordx4 v194, s[26:27] offset:128
	s_waitcnt vmcnt(8)
	s_waitcnt lgkmcnt(0)
	s_barrier
	s_setprio 3
	s_waitcnt lgkmcnt(0)
	v_mfma_f32_16x16x32_bf16 v[62:65], v[98:101], v[154:157], v[62:65]
	v_mfma_f32_16x16x32_bf16 v[58:61], v[122:125], v[154:157], v[58:61]
	v_mfma_f32_16x16x32_bf16 v[46:49], v[98:101], v[170:173], v[46:49]
	v_mfma_f32_16x16x32_bf16 v[42:45], v[122:125], v[170:173], v[42:45]
	v_mfma_f32_16x16x32_bf16 v[30:33], v[98:101], v[178:181], v[30:33]
	v_mfma_f32_16x16x32_bf16 v[26:29], v[122:125], v[178:181], v[26:29]
	v_mfma_f32_16x16x32_bf16 v[14:17], v[98:101], v[186:189], v[14:17]
	v_mfma_f32_16x16x32_bf16 v[10:13], v[122:125], v[186:189], v[10:13]
	v_mfma_f32_16x16x32_bf16 v[62:65], v[110:113], v[166:169], v[62:65]
	v_mfma_f32_16x16x32_bf16 v[58:61], v[126:129], v[166:169], v[58:61]
	v_mfma_f32_16x16x32_bf16 v[46:49], v[110:113], v[174:177], v[46:49]
	v_mfma_f32_16x16x32_bf16 v[42:45], v[126:129], v[174:177], v[42:45]
	v_mfma_f32_16x16x32_bf16 v[30:33], v[110:113], v[182:185], v[30:33]
	v_mfma_f32_16x16x32_bf16 v[26:29], v[126:129], v[182:185], v[26:29]
	v_mfma_f32_16x16x32_bf16 v[14:17], v[110:113], v[206:209], v[14:17]
	v_mfma_f32_16x16x32_bf16 v[10:13], v[126:129], v[206:209], v[10:13]
	v_mfma_f32_16x16x32_bf16 v[54:57], v[138:141], v[154:157], v[54:57]
	v_mfma_f32_16x16x32_bf16 v[50:53], v[146:149], v[154:157], v[50:53]
	v_mfma_f32_16x16x32_bf16 v[38:41], v[138:141], v[170:173], v[38:41]
	v_mfma_f32_16x16x32_bf16 v[34:37], v[146:149], v[170:173], v[34:37]
	v_mfma_f32_16x16x32_bf16 v[22:25], v[138:141], v[178:181], v[22:25]
	v_mfma_f32_16x16x32_bf16 v[18:21], v[146:149], v[178:181], v[18:21]
	v_mfma_f32_16x16x32_bf16 v[6:9], v[138:141], v[186:189], v[6:9]
	v_mfma_f32_16x16x32_bf16 v[2:5], v[146:149], v[186:189], v[2:5]
	v_mfma_f32_16x16x32_bf16 v[54:57], v[142:145], v[166:169], v[54:57]
	v_mfma_f32_16x16x32_bf16 v[50:53], v[150:153], v[166:169], v[50:53]
	v_mfma_f32_16x16x32_bf16 v[38:41], v[142:145], v[174:177], v[38:41]
	v_mfma_f32_16x16x32_bf16 v[34:37], v[150:153], v[174:177], v[34:37]
	v_mfma_f32_16x16x32_bf16 v[22:25], v[142:145], v[182:185], v[22:25]
	v_mfma_f32_16x16x32_bf16 v[18:21], v[150:153], v[182:185], v[18:21]
	v_mfma_f32_16x16x32_bf16 v[6:9], v[142:145], v[206:209], v[6:9]
	v_mfma_f32_16x16x32_bf16 v[2:5], v[150:153], v[206:209], v[2:5]
	s_setprio 0
	s_barrier
	s_add_i32 s57, s57, 2
	s_add_u32 s55, s55, 0x100
	s_addc_u32 s56, s56, 0
	s_cmp_gt_u32 s57, 41
	s_mov_b64 s[20:21], s[22:23]
	s_cbranch_scc0 .LBB0_857
	s_and_b64 vcc, exec, s[16:17]
	s_cbranch_vccz .LBB0_860
	s_barrier

; #define PG8_GIDX(G_, PM_) do { if constexpr (Sched::GATHER) { _Pragma("unroll") for (int h_ = 0; h_ < 2; ++h_) _Pragma("unroll") for (int i_ = 0; i_ < 2; ++i_) { int R_, C_; stage_rc(tid * 16 + i_ * 8192, R_, C_); \
;         const int src_ = S.rowsrc[(PM_) * BM + h_ * HALF + R_]; G_[h_][i_] = (unsigned)(src_ * K + C_) * 2u; } } } while (0)
; #define PG8_STAGE_A(b, h, ptr, NX) do { if constexpr (Sched::GATHER) { unsigned gs_[2]; gs_[0] = ((NX) && last_) ? gN[h][0] : gA[h][0]; gs_[1] = ((NX) && last_) ? gN[h][1] : gA[h][1]; PG8_STAGE(PG8_SA(b, h), ptr, gs_); } \
;         else PG8_STAGE(PG8_SA(b, h), (ptr) + ((h) ? hstep : (size_t)0), voffA); } while (0)
; #define PG8_LDA(dst, b, h) do { _Pragma("unroll") for (int m = 0; m < 4; ++m) _Pragma("unroll") for (int k = 0; k < 2; ++k) dst[m][k] = *(const PG8_LAS bf16x8*)(lds + PG8_SA(b, h) + aoff + m * 2048 + k * 1024); } while (0)
; template <class Epi, class Sched, bool ALIGN_EPI = false, bool SP2 = false>
; __device__ __forceinline__ void gemm_phase(PG8_LAS unsigned char* lds, const Gemm g, const Sched& S, const Epi& E, const bool skip_epi = false) {
;     ...
;         const bool has_next = S.next(ui + 1, nxt);
;         if (has_next) PG8_GIDX(gN, nxt.pm);
;         const char* nA = has_next ? (const char*)g.A + (size_t)nxt.pm * pmstepA + nxt.ko : cA; const char* nB = has_next ? (const char*)g.Bt + (size_t)nxt.pn * tstep + nxt.ko : cB;
;         for (int t = 0; t < nt; t += 2) {
;             const bool last = (t == nt - 2); last_ = last && has_next;
;             const char* a1 = cA + (size_t)(t + 1) * kstep;
;             const char* a2 = last ? nA : cA + (size_t)(t + 2) * kstep; const char* b2 = last ? nB : cB + (size_t)(t + 2) * kstep;
;             const char* a3 = a2 + kstep; const char* b3 = b2 + kstep;
;             if (last && has_next) S.a_ready(nxt);
;             if constexpr (SP2) {
;             PG8_LDB(B0, 0, 0); PG8_LDB(B1, 0, 1); PG8_SCHED; PG8_LDA(At, 0, 0); PG8_STAGE_A(1, 1, a1, false);
;             PG8_WAIT_V(8); PG8_WAIT_L(0); PG8_BAR; PG8_MMA(0, 0, At, B0); PG8_MMA(0, 1, At, B1); PG8_BAR; PG8_SCHED;
;             PG8_LDA(At, 0, 1); PG8_STAGE(PG8_SB(0, 0), b2, voffB); PG8_STAGE(PG8_SB(0, 1), b2 + hstep, voffB); PG8_STAGE_A(0, 0, a2, true);
;             PG8_WAIT_V(8); PG8_WAIT_L(0); PG8_BAR; PG8_MMA(1, 0, At, B0); PG8_MMA(1, 1, At, B1); PG8_BAR; PG8_SCHED;
.LBB0_943:
	s_ashr_i32 s15, s14, 31
	s_lshl_b64 s[16:17], s[14:15], 19
	s_add_u32 s16, s86, s16
	s_addc_u32 s17, s87, s17
	s_and_b64 s[18:19], s[4:5], exec
	s_cselect_b32 s15, s17, s23
	s_cselect_b32 s54, s16, s22
	s_ashr_i32 s13, s12, 31
	s_lshl_b64 s[18:19], s[12:13], 19
	s_add_u32 s18, s2, s18
	s_addc_u32 s19, s3, s19
	s_and_b64 s[26:27], s[4:5], exec
	s_cselect_b32 s13, s19, s25
	s_cselect_b32 s55, s18, s24
	s_add_u32 s22, s22, 0x40080
	s_addc_u32 s23, s23, 0
	s_add_u32 s56, s24, 0x100
	s_addc_u32 s57, s25, 0
	s_mov_b32 s58, -2
	s_waitcnt vmcnt(0)
	ds_read_b128 v[148:151], v170
	ds_read_b128 v[152:155], v170 offset:1024
	ds_read_b128 v[156:159], v170 offset:2048
	ds_read_b128 v[160:163], v170 offset:3072
	ds_read_b128 v[176:179], v171
	ds_read_b128 v[180:183], v171 offset:1024
	ds_read_b128 v[184:187], v171 offset:2048
	ds_read_b128 v[188:191], v171 offset:3072
	s_add_u32 s24, s22, 0xfffc0080
	s_addc_u32 s25, s23, -1
	s_cmp_eq_u32 s58, 12
	s_cselect_b32 s27, s15, s25
	s_cselect_b32 s26, s54, s24
	s_cselect_b32 s25, s13, s57
	s_cselect_b32 s24, s55, s56
	s_add_i32 m0, s21, 0xc000
	ds_read_b128 v[192:195], v172
	ds_read_b128 v[196:199], v172 offset:1024
	ds_read_b128 v[200:203], v172 offset:2048
	ds_read_b128 v[204:207], v172 offset:3072
	ds_read_b128 v[208:211], v172 offset:4096
	ds_read_b128 v[212:215], v172 offset:5120
	ds_read_b128 v[216:219], v172 offset:6144
	ds_read_b128 v[220:223], v172 offset:7168
	global_load_lds_dwordx4 v140, s[22:23]
	s_add_i32 m0, s21, 0xe000
	s_nop 0
	global_load_lds_dwordx4 v142, s[22:23]
	s_waitcnt vmcnt(8)
	s_waitcnt lgkmcnt(0)
	s_barrier
	s_setprio 3
	s_waitcnt lgkmcnt(0)
	v_mfma_f32_16x16x32_bf16 v[126:129], v[148:151], v[192:195], 0
	v_mfma_f32_16x16x32_bf16 v[122:125], v[156:159], v[192:195], 0
	v_mfma_f32_16x16x32_bf16 v[114:117], v[148:151], v[200:203], 0
	v_mfma_f32_16x16x32_bf16 v[106:109], v[156:159], v[200:203], 0
	v_mfma_f32_16x16x32_bf16 v[98:101], v[148:151], v[208:211], 0
	v_mfma_f32_16x16x32_bf16 v[90:93], v[156:159], v[208:211], 0
	v_mfma_f32_16x16x32_bf16 v[82:85], v[148:151], v[216:219], 0
	v_mfma_f32_16x16x32_bf16 v[74:77], v[156:159], v[216:219], 0
	v_mfma_f32_16x16x32_bf16 v[126:129], v[152:155], v[196:199], v[126:129]
	v_mfma_f32_16x16x32_bf16 v[122:125], v[160:163], v[196:199], v[122:125]
	v_mfma_f32_16x16x32_bf16 v[114:117], v[152:155], v[204:207], v[114:117]
	v_mfma_f32_16x16x32_bf16 v[106:109], v[160:163], v[204:207], v[106:109]
	v_mfma_f32_16x16x32_bf16 v[98:101], v[152:155], v[212:215], v[98:101]
	v_mfma_f32_16x16x32_bf16 v[90:93], v[160:163], v[212:215], v[90:93]
	v_mfma_f32_16x16x32_bf16 v[82:85], v[152:155], v[220:223], v[82:85]
	v_mfma_f32_16x16x32_bf16 v[74:77], v[160:163], v[220:223], v[74:77]
	v_mfma_f32_16x16x32_bf16 v[118:121], v[176:179], v[192:195], 0
	v_mfma_f32_16x16x32_bf16 v[110:113], v[184:187], v[192:195], 0
	v_mfma_f32_16x16x32_bf16 v[102:105], v[176:179], v[200:203], 0
	v_mfma_f32_16x16x32_bf16 v[94:97], v[184:187], v[200:203], 0
	v_mfma_f32_16x16x32_bf16 v[86:89], v[176:179], v[208:211], 0
	v_mfma_f32_16x16x32_bf16 v[78:81], v[184:187], v[208:211], 0
	v_mfma_f32_16x16x32_bf16 v[70:73], v[176:179], v[216:219], 0
	v_mfma_f32_16x16x32_bf16 v[66:69], v[184:187], v[216:219], 0
	v_mfma_f32_16x16x32_bf16 v[118:121], v[180:183], v[196:199], v[118:121]
	v_mfma_f32_16x16x32_bf16 v[110:113], v[188:191], v[196:199], v[110:113]
	v_mfma_f32_16x16x32_bf16 v[102:105], v[180:183], v[204:207], v[102:105]
	v_mfma_f32_16x16x32_bf16 v[94:97], v[188:191], v[204:207], v[94:97]
	v_mfma_f32_16x16x32_bf16 v[86:89], v[180:183], v[212:215], v[86:89]
	v_mfma_f32_16x16x32_bf16 v[78:81], v[188:191], v[212:215], v[78:81]
	v_mfma_f32_16x16x32_bf16 v[70:73], v[180:183], v[220:223], v[70:73]
	v_mfma_f32_16x16x32_bf16 v[66:69], v[188:191], v[220:223], v[66:69]
	s_setprio 0
	s_barrier
	s_add_i32 s59, s48, s28
	s_mov_b32 m0, s59
	ds_read_b128 v[192:195], v172 offset:16384
	ds_read_b128 v[196:199], v172 offset:17408
	ds_read_b128 v[200:203], v172 offset:18432
	ds_read_b128 v[204:207], v172 offset:19456
	ds_read_b128 v[208:211], v172 offset:20480
	ds_read_b128 v[212:215], v172 offset:21504
	ds_read_b128 v[216:219], v172 offset:22528
	ds_read_b128 v[220:223], v172 offset:23552
	global_load_lds_dwordx4 v134, s[24:25]
	s_add_i32 m0, s59, 0x2000
	s_add_u32 s60, s24, 0x40000
	s_addc_u32 s61, s25, 0
	s_add_i32 s59, s49, s28
	global_load_lds_dwordx4 v130, s[24:25]
	s_mov_b32 m0, s59
	s_mov_b64 s[98:99], s[26:27]
	global_load_lds_dwordx4 v134, s[60:61]
	s_add_i32 m0, s59, 0x2000
	s_nop 0
	global_load_lds_dwordx4 v130, s[60:61]
	s_mov_b32 m0, s21
	s_nop 0
	global_load_lds_dwordx4 v136, s[26:27]
	s_mov_b32 m0, s31
	s_nop 0
	global_load_lds_dwordx4 v132, s[26:27]
	s_waitcnt vmcnt(8)
	s_waitcnt lgkmcnt(0)
	s_barrier
; #define PG8_STAGE_A(b, h, ptr, NX) do { if constexpr (Sched::GATHER) { unsigned gs_[2]; gs_[0] = ((NX) && last_) ? gN[h][0] : gA[h][0]; gs_[1] = ((NX) && last_) ? gN[h][1] : gA[h][1]; PG8_STAGE(PG8_SA(b, h), ptr, gs_); } \
;         else PG8_STAGE(PG8_SA(b, h), (ptr) + ((h) ? hstep : (size_t)0), voffA); } while (0)
; #define PG8_STAGE(bufoff, gbase, voff) do { _Pragma("unroll") for (int _i = 0; _i < 2; ++_i) \
;         __builtin_amdgcn_global_load_lds((const unsigned*)((const char*)(gbase) + (voff)[_i]), (PG8_LAS unsigned*)(lds + (bufoff) + ldsw + _i * 8192), 16, 0, 0); } while (0)
; #define PG8_LDA(dst, b, h) do { _Pragma("unroll") for (int m = 0; m < 4; ++m) _Pragma("unroll") for (int k = 0; k < 2; ++k) dst[m][k] = *(const PG8_LAS bf16x8*)(lds + PG8_SA(b, h) + aoff + m * 2048 + k * 1024); } while (0)
; #define PG8_LDB(dst, b, h) do { _Pragma("unroll") for (int n = 0; n < 2; ++n) _Pragma("unroll") for (int k = 0; k < 2; ++k) dst[n][k] = *(const PG8_LAS bf16x8*)(lds + PG8_SB(b, h) + boff + n * 2048 + k * 1024); } while (0)
; #define PG8_WAIT_V(n) asm volatile("s_waitcnt vmcnt(" #n ")" ::: "memory")
; #define PG8_BAR __builtin_amdgcn_s_barrier()
; template <class Epi, class Sched, bool ALIGN_EPI = false, bool SP2 = false>
; __device__ __forceinline__ void gemm_phase(PG8_LAS unsigned char* lds, const Gemm g, const Sched& S, const Epi& E, const bool skip_epi = false) {
;     ...
;             PG8_LDB(B0, 0, 0); PG8_LDB(B1, 0, 1); PG8_SCHED; PG8_LDA(At, 0, 0); PG8_STAGE_A(1, 1, a1, false);
;             PG8_WAIT_V(8); PG8_WAIT_L(0); PG8_BAR; PG8_MMA(0, 0, At, B0); PG8_MMA(0, 1, At, B1); PG8_BAR; PG8_SCHED;
;             PG8_LDA(At, 0, 1); PG8_STAGE(PG8_SB(0, 0), b2, voffB); PG8_STAGE(PG8_SB(0, 1), b2 + hstep, voffB); PG8_STAGE_A(0, 0, a2, true);
;             PG8_WAIT_V(8); PG8_WAIT_L(0); PG8_BAR; PG8_MMA(1, 0, At, B0); PG8_MMA(1, 1, At, B1); PG8_BAR; PG8_SCHED;
;             PG8_LDB(B0, 1, 0); PG8_LDB(B1, 1, 1); PG8_SCHED; PG8_LDA(At, 1, 0); PG8_STAGE_A(0, 1, a2, true);
;             PG8_WAIT_V(8); PG8_WAIT_L(0); PG8_BAR; PG8_MMA(0, 0, At, B0); PG8_MMA(0, 1, At, B1); PG8_BAR; PG8_SCHED;
;             PG8_LDA(At, 1, 1); PG8_STAGE(PG8_SB(1, 0), b3, voffB); PG8_STAGE(PG8_SB(1, 1), b3 + hstep, voffB); PG8_STAGE_A(1, 0, a3, true);
;             PG8_WAIT_V(8); PG8_WAIT_L(0); PG8_BAR; PG8_MMA(1, 0, At, B0); PG8_MMA(1, 1, At, B1); PG8_BAR; PG8_SCHED;
	s_setprio 3
	s_waitcnt lgkmcnt(0)
	v_mfma_f32_16x16x32_bf16 v[62:65], v[148:151], v[192:195], 0
	v_mfma_f32_16x16x32_bf16 v[58:61], v[156:159], v[192:195], 0
	v_mfma_f32_16x16x32_bf16 v[50:53], v[148:151], v[200:203], 0
	v_mfma_f32_16x16x32_bf16 v[42:45], v[156:159], v[200:203], 0
	v_mfma_f32_16x16x32_bf16 v[34:37], v[148:151], v[208:211], 0
	v_mfma_f32_16x16x32_bf16 v[26:29], v[156:159], v[208:211], 0
	v_mfma_f32_16x16x32_bf16 v[18:21], v[148:151], v[216:219], 0
	v_mfma_f32_16x16x32_bf16 v[10:13], v[156:159], v[216:219], 0
	v_mfma_f32_16x16x32_bf16 v[62:65], v[152:155], v[196:199], v[62:65]
	v_mfma_f32_16x16x32_bf16 v[58:61], v[160:163], v[196:199], v[58:61]
	v_mfma_f32_16x16x32_bf16 v[50:53], v[152:155], v[204:207], v[50:53]
	v_mfma_f32_16x16x32_bf16 v[42:45], v[160:163], v[204:207], v[42:45]
	v_mfma_f32_16x16x32_bf16 v[34:37], v[152:155], v[212:215], v[34:37]
	v_mfma_f32_16x16x32_bf16 v[26:29], v[160:163], v[212:215], v[26:29]
	v_mfma_f32_16x16x32_bf16 v[18:21], v[152:155], v[220:223], v[18:21]
	v_mfma_f32_16x16x32_bf16 v[10:13], v[160:163], v[220:223], v[10:13]
	v_mfma_f32_16x16x32_bf16 v[54:57], v[176:179], v[192:195], 0
	v_mfma_f32_16x16x32_bf16 v[46:49], v[184:187], v[192:195], 0
	v_mfma_f32_16x16x32_bf16 v[38:41], v[176:179], v[200:203], 0
	v_mfma_f32_16x16x32_bf16 v[30:33], v[184:187], v[200:203], 0
	v_mfma_f32_16x16x32_bf16 v[22:25], v[176:179], v[208:211], 0
	v_mfma_f32_16x16x32_bf16 v[14:17], v[184:187], v[208:211], 0
	v_mfma_f32_16x16x32_bf16 v[6:9], v[176:179], v[216:219], 0
	v_mfma_f32_16x16x32_bf16 v[2:5], v[184:187], v[216:219], 0
	v_mfma_f32_16x16x32_bf16 v[54:57], v[180:183], v[196:199], v[54:57]
	v_mfma_f32_16x16x32_bf16 v[46:49], v[188:191], v[196:199], v[46:49]
	v_mfma_f32_16x16x32_bf16 v[38:41], v[180:183], v[204:207], v[38:41]
	v_mfma_f32_16x16x32_bf16 v[30:33], v[188:191], v[204:207], v[30:33]
	v_mfma_f32_16x16x32_bf16 v[22:25], v[180:183], v[212:215], v[22:25]
	v_mfma_f32_16x16x32_bf16 v[14:17], v[188:191], v[212:215], v[14:17]
	v_mfma_f32_16x16x32_bf16 v[6:9], v[180:183], v[220:223], v[6:9]
	v_mfma_f32_16x16x32_bf16 v[2:5], v[188:191], v[220:223], v[2:5]
	s_setprio 0
	s_barrier
	s_add_i32 s59, 0, 0x18000
	s_add_i32 s60, 0, 0x1c000
	v_add_u32_e32 v160, s59, v1
	v_add_u32_e32 v188, s60, v1
	ds_read_b128 v[148:151], v160
	ds_read_b128 v[152:155], v160 offset:1024
	ds_read_b128 v[156:159], v160 offset:2048
	ds_read_b128 v[160:163], v160 offset:3072
	ds_read_b128 v[176:179], v188
	ds_read_b128 v[180:183], v188 offset:1024
	ds_read_b128 v[184:187], v188 offset:2048
	ds_read_b128 v[188:191], v188 offset:3072
	s_add_u32 s26, s26, 0x40000
	s_addc_u32 s27, s27, 0
	s_mov_b32 m0, s34
	ds_read_b128 v[192:195], v172 offset:32768
	ds_read_b128 v[196:199], v172 offset:33792
	ds_read_b128 v[200:203], v172 offset:34816
	ds_read_b128 v[204:207], v172 offset:35840
	ds_read_b128 v[208:211], v172 offset:36864
	ds_read_b128 v[212:215], v172 offset:37888
	ds_read_b128 v[216:219], v172 offset:38912
	ds_read_b128 v[220:223], v172 offset:39936
	global_load_lds_dwordx4 v136, s[26:27]
	s_mov_b32 m0, s35
	s_nop 0
	global_load_lds_dwordx4 v132, s[26:27]
	s_waitcnt vmcnt(8)
	s_waitcnt lgkmcnt(0)
	s_barrier
	s_setprio 3
	s_waitcnt lgkmcnt(0)
	v_mfma_f32_16x16x32_bf16 v[126:129], v[148:151], v[192:195], v[126:129]
	v_mfma_f32_16x16x32_bf16 v[122:125], v[156:159], v[192:195], v[122:125]
	v_mfma_f32_16x16x32_bf16 v[114:117], v[148:151], v[200:203], v[114:117]
	v_mfma_f32_16x16x32_bf16 v[106:109], v[156:159], v[200:203], v[106:109]
	v_mfma_f32_16x16x32_bf16 v[98:101], v[148:151], v[208:211], v[98:101]
	v_mfma_f32_16x16x32_bf16 v[90:93], v[156:159], v[208:211], v[90:93]
	v_mfma_f32_16x16x32_bf16 v[82:85], v[148:151], v[216:219], v[82:85]
	v_mfma_f32_16x16x32_bf16 v[74:77], v[156:159], v[216:219], v[74:77]
	v_mfma_f32_16x16x32_bf16 v[126:129], v[152:155], v[196:199], v[126:129]
	v_mfma_f32_16x16x32_bf16 v[122:125], v[160:163], v[196:199], v[122:125]
	v_mfma_f32_16x16x32_bf16 v[114:117], v[152:155], v[204:207], v[114:117]
	v_mfma_f32_16x16x32_bf16 v[106:109], v[160:163], v[204:207], v[106:109]
	v_mfma_f32_16x16x32_bf16 v[98:101], v[152:155], v[212:215], v[98:101]
	v_mfma_f32_16x16x32_bf16 v[90:93], v[160:163], v[212:215], v[90:93]
	v_mfma_f32_16x16x32_bf16 v[82:85], v[152:155], v[220:223], v[82:85]
	v_mfma_f32_16x16x32_bf16 v[74:77], v[160:163], v[220:223], v[74:77]
	v_mfma_f32_16x16x32_bf16 v[118:121], v[176:179], v[192:195], v[118:121]
	v_mfma_f32_16x16x32_bf16 v[110:113], v[184:187], v[192:195], v[110:113]
	v_mfma_f32_16x16x32_bf16 v[102:105], v[176:179], v[200:203], v[102:105]
	v_mfma_f32_16x16x32_bf16 v[94:97], v[184:187], v[200:203], v[94:97]
	v_mfma_f32_16x16x32_bf16 v[86:89], v[176:179], v[208:211], v[86:89]
	v_mfma_f32_16x16x32_bf16 v[78:81], v[184:187], v[208:211], v[78:81]
	v_mfma_f32_16x16x32_bf16 v[70:73], v[176:179], v[216:219], v[70:73]
	v_mfma_f32_16x16x32_bf16 v[66:69], v[184:187], v[216:219], v[66:69]
	v_mfma_f32_16x16x32_bf16 v[118:121], v[180:183], v[196:199], v[118:121]
	v_mfma_f32_16x16x32_bf16 v[110:113], v[188:191], v[196:199], v[110:113]
	v_mfma_f32_16x16x32_bf16 v[102:105], v[180:183], v[204:207], v[102:105]
	v_mfma_f32_16x16x32_bf16 v[94:97], v[188:191], v[204:207], v[94:97]
	v_mfma_f32_16x16x32_bf16 v[86:89], v[180:183], v[212:215], v[86:89]
	v_mfma_f32_16x16x32_bf16 v[78:81], v[188:191], v[212:215], v[78:81]
	v_mfma_f32_16x16x32_bf16 v[70:73], v[180:183], v[220:223], v[70:73]
	v_mfma_f32_16x16x32_bf16 v[66:69], v[188:191], v[220:223], v[66:69]
	s_setprio 0
	s_barrier
; #define PG8_STAGE_A(b, h, ptr, NX) do { if constexpr (Sched::GATHER) { unsigned gs_[2]; gs_[0] = ((NX) && last_) ? gN[h][0] : gA[h][0]; gs_[1] = ((NX) && last_) ? gN[h][1] : gA[h][1]; PG8_STAGE(PG8_SA(b, h), ptr, gs_); } \
;         else PG8_STAGE(PG8_SA(b, h), (ptr) + ((h) ? hstep : (size_t)0), voffA); } while (0)
; #define PG8_STAGE(bufoff, gbase, voff) do { _Pragma("unroll") for (int _i = 0; _i < 2; ++_i) \
;         __builtin_amdgcn_global_load_lds((const unsigned*)((const char*)(gbase) + (voff)[_i]), (PG8_LAS unsigned*)(lds + (bufoff) + ldsw + _i * 8192), 16, 0, 0); } while (0)
; #define PG8_LDA(dst, b, h) do { _Pragma("unroll") for (int m = 0; m < 4; ++m) _Pragma("unroll") for (int k = 0; k < 2; ++k) dst[m][k] = *(const PG8_LAS bf16x8*)(lds + PG8_SA(b, h) + aoff + m * 2048 + k * 1024); } while (0)
; #define PG8_LDB(dst, b, h) do { _Pragma("unroll") for (int n = 0; n < 2; ++n) _Pragma("unroll") for (int k = 0; k < 2; ++k) dst[n][k] = *(const PG8_LAS bf16x8*)(lds + PG8_SB(b, h) + boff + n * 2048 + k * 1024); } while (0)
; #define PG8_MMA(ai, bj, At, Bt) do { __builtin_amdgcn_s_setprio(1); _Pragma("unroll") for (int m = 0; m < 4; ++m) _Pragma("unroll") for (int n = 0; n < 2; ++n) _Pragma("unroll") for (int k = 0; k < 2; ++k) \
;         acc[ai][bj][m][n] = __builtin_amdgcn_mfma_f32_16x16x32_bf16(Bt[n][k], At[m][k], acc[ai][bj][m][n], 0, 0, 0); __builtin_amdgcn_s_setprio(0); } while (0)
; #define PG8_WAIT_V(n) asm volatile("s_waitcnt vmcnt(" #n ")" ::: "memory")
; #define PG8_WAIT_L(n) asm volatile("s_waitcnt lgkmcnt(" #n ")" ::: "memory")
; #define PG8_BAR __builtin_amdgcn_s_barrier()
; #define PG8_SCHED __builtin_amdgcn_sched_barrier(0)
; template <class Epi, class Sched, bool ALIGN_EPI = false, bool SP2 = false>
; __device__ __forceinline__ void gemm_phase(PG8_LAS unsigned char* lds, const Gemm g, const Sched& S, const Epi& E, const bool skip_epi = false) {
;     ...
;             PG8_LDB(B0, 0, 0); PG8_LDB(B1, 0, 1); PG8_SCHED; PG8_LDA(At, 0, 0); PG8_STAGE_A(1, 1, a1, false);
;             PG8_WAIT_V(8); PG8_WAIT_L(0); PG8_BAR; PG8_MMA(0, 0, At, B0); PG8_MMA(0, 1, At, B1); PG8_BAR; PG8_SCHED;
;     ...
;             PG8_LDA(At, 1, 1); PG8_STAGE(PG8_SB(1, 0), b3, voffB); PG8_STAGE(PG8_SB(1, 1), b3 + hstep, voffB); PG8_STAGE_A(1, 0, a3, true);
;             PG8_WAIT_V(8); PG8_WAIT_L(0); PG8_BAR; PG8_MMA(1, 0, At, B0); PG8_MMA(1, 1, At, B1); PG8_BAR; PG8_SCHED;
	s_add_i32 s26, s59, s28
	s_add_i32 m0, s26, 0xffffff80
	ds_read_b128 v[192:195], v172 offset:49152
	ds_read_b128 v[196:199], v172 offset:50176
	ds_read_b128 v[200:203], v172 offset:51200
	ds_read_b128 v[204:207], v172 offset:52224
	ds_read_b128 v[208:211], v172 offset:53248
	ds_read_b128 v[212:215], v172 offset:54272
	ds_read_b128 v[216:219], v172 offset:55296
	ds_read_b128 v[220:223], v172 offset:56320
	global_load_lds_dwordx4 v134, s[24:25] offset:128
	s_add_i32 m0, s26, 0x1f80
	s_add_i32 s26, s60, s28
	global_load_lds_dwordx4 v130, s[24:25] offset:128
	s_add_u32 s24, s24, 0x40080
	s_addc_u32 s25, s25, 0
	s_mov_b32 m0, s26
	s_nop 0
	global_load_lds_dwordx4 v134, s[24:25]
	s_add_i32 m0, s26, 0x2000
	s_nop 0
	global_load_lds_dwordx4 v130, s[24:25]
	s_add_i32 m0, s37, 0xffffff80
	s_nop 0
	global_load_lds_dwordx4 v136, s[98:99] offset:128
	s_add_i32 m0, s38, 0xffffff80
	s_nop 0
	global_load_lds_dwordx4 v132, s[98:99] offset:128
	s_waitcnt vmcnt(8)
	s_waitcnt lgkmcnt(0)
	s_barrier
	s_setprio 3
	s_waitcnt lgkmcnt(0)
	v_mfma_f32_16x16x32_bf16 v[62:65], v[148:151], v[192:195], v[62:65]
	v_mfma_f32_16x16x32_bf16 v[58:61], v[156:159], v[192:195], v[58:61]
	v_mfma_f32_16x16x32_bf16 v[50:53], v[148:151], v[200:203], v[50:53]
	v_mfma_f32_16x16x32_bf16 v[42:45], v[156:159], v[200:203], v[42:45]
	v_mfma_f32_16x16x32_bf16 v[34:37], v[148:151], v[208:211], v[34:37]
	v_mfma_f32_16x16x32_bf16 v[26:29], v[156:159], v[208:211], v[26:29]
	v_mfma_f32_16x16x32_bf16 v[18:21], v[148:151], v[216:219], v[18:21]
	v_mfma_f32_16x16x32_bf16 v[10:13], v[156:159], v[216:219], v[10:13]
	v_mfma_f32_16x16x32_bf16 v[62:65], v[152:155], v[196:199], v[62:65]
	v_mfma_f32_16x16x32_bf16 v[58:61], v[160:163], v[196:199], v[58:61]
	v_mfma_f32_16x16x32_bf16 v[50:53], v[152:155], v[204:207], v[50:53]
	v_mfma_f32_16x16x32_bf16 v[42:45], v[160:163], v[204:207], v[42:45]
	v_mfma_f32_16x16x32_bf16 v[34:37], v[152:155], v[212:215], v[34:37]
	v_mfma_f32_16x16x32_bf16 v[26:29], v[160:163], v[212:215], v[26:29]
	v_mfma_f32_16x16x32_bf16 v[18:21], v[152:155], v[220:223], v[18:21]
	v_mfma_f32_16x16x32_bf16 v[10:13], v[160:163], v[220:223], v[10:13]
	v_mfma_f32_16x16x32_bf16 v[54:57], v[176:179], v[192:195], v[54:57]
	v_mfma_f32_16x16x32_bf16 v[46:49], v[184:187], v[192:195], v[46:49]
	v_mfma_f32_16x16x32_bf16 v[38:41], v[176:179], v[200:203], v[38:41]
	v_mfma_f32_16x16x32_bf16 v[30:33], v[184:187], v[200:203], v[30:33]
	v_mfma_f32_16x16x32_bf16 v[22:25], v[176:179], v[208:211], v[22:25]
	v_mfma_f32_16x16x32_bf16 v[14:17], v[184:187], v[208:211], v[14:17]
	v_mfma_f32_16x16x32_bf16 v[6:9], v[176:179], v[216:219], v[6:9]
	v_mfma_f32_16x16x32_bf16 v[2:5], v[184:187], v[216:219], v[2:5]
	v_mfma_f32_16x16x32_bf16 v[54:57], v[180:183], v[196:199], v[54:57]
	v_mfma_f32_16x16x32_bf16 v[46:49], v[188:191], v[196:199], v[46:49]
	v_mfma_f32_16x16x32_bf16 v[38:41], v[180:183], v[204:207], v[38:41]
	v_mfma_f32_16x16x32_bf16 v[30:33], v[188:191], v[204:207], v[30:33]
	v_mfma_f32_16x16x32_bf16 v[22:25], v[180:183], v[212:215], v[22:25]
	v_mfma_f32_16x16x32_bf16 v[14:17], v[188:191], v[212:215], v[14:17]
	v_mfma_f32_16x16x32_bf16 v[6:9], v[180:183], v[220:223], v[6:9]
	v_mfma_f32_16x16x32_bf16 v[2:5], v[188:191], v[220:223], v[2:5]
	s_setprio 0
	s_barrier
	s_add_i32 s58, s58, 2
	s_add_u32 s22, s22, 0x100
	s_addc_u32 s23, s23, 0
	s_add_u32 s56, s56, 0x100
	s_addc_u32 s57, s57, 0
	s_cmp_gt_u32 s58, 13
.LBB0_944:
	ds_read_b128 v[148:151], v170
	ds_read_b128 v[152:155], v170 offset:1024
	ds_read_b128 v[156:159], v170 offset:2048
	ds_read_b128 v[160:163], v170 offset:3072
	ds_read_b128 v[176:179], v171
	ds_read_b128 v[180:183], v171 offset:1024
	ds_read_b128 v[184:187], v171 offset:2048
	ds_read_b128 v[188:191], v171 offset:3072
	s_add_u32 s24, s22, 0xfffc0080
	s_addc_u32 s25, s23, -1
	s_cmp_eq_u32 s58, 12
	s_cselect_b32 s27, s15, s25
	s_cselect_b32 s26, s54, s24
	s_cselect_b32 s25, s13, s57
	s_cselect_b32 s24, s55, s56
	s_add_i32 m0, s21, 0xc000
	ds_read_b128 v[192:195], v172
	ds_read_b128 v[196:199], v172 offset:1024
	ds_read_b128 v[200:203], v172 offset:2048
	ds_read_b128 v[204:207], v172 offset:3072
	ds_read_b128 v[208:211], v172 offset:4096
	ds_read_b128 v[212:215], v172 offset:5120
	ds_read_b128 v[216:219], v172 offset:6144
	ds_read_b128 v[220:223], v172 offset:7168
	global_load_lds_dwordx4 v140, s[22:23]
	s_add_i32 m0, s21, 0xe000
	s_nop 0
	global_load_lds_dwordx4 v142, s[22:23]
	s_waitcnt vmcnt(8)
	s_waitcnt lgkmcnt(0)
	s_barrier
	s_setprio 3
	s_waitcnt lgkmcnt(0)
	v_mfma_f32_16x16x32_bf16 v[126:129], v[148:151], v[192:195], v[126:129]
	v_mfma_f32_16x16x32_bf16 v[122:125], v[156:159], v[192:195], v[122:125]
	v_mfma_f32_16x16x32_bf16 v[114:117], v[148:151], v[200:203], v[114:117]
	v_mfma_f32_16x16x32_bf16 v[106:109], v[156:159], v[200:203], v[106:109]
	v_mfma_f32_16x16x32_bf16 v[98:101], v[148:151], v[208:211], v[98:101]
	v_mfma_f32_16x16x32_bf16 v[90:93], v[156:159], v[208:211], v[90:93]
	v_mfma_f32_16x16x32_bf16 v[82:85], v[148:151], v[216:219], v[82:85]
	v_mfma_f32_16x16x32_bf16 v[74:77], v[156:159], v[216:219], v[74:77]
	v_mfma_f32_16x16x32_bf16 v[126:129], v[152:155], v[196:199], v[126:129]
	v_mfma_f32_16x16x32_bf16 v[122:125], v[160:163], v[196:199], v[122:125]
	v_mfma_f32_16x16x32_bf16 v[114:117], v[152:155], v[204:207], v[114:117]
	v_mfma_f32_16x16x32_bf16 v[106:109], v[160:163], v[204:207], v[106:109]
	v_mfma_f32_16x16x32_bf16 v[98:101], v[152:155], v[212:215], v[98:101]
	v_mfma_f32_16x16x32_bf16 v[90:93], v[160:163], v[212:215], v[90:93]
	v_mfma_f32_16x16x32_bf16 v[82:85], v[152:155], v[220:223], v[82:85]
	v_mfma_f32_16x16x32_bf16 v[74:77], v[160:163], v[220:223], v[74:77]
	v_mfma_f32_16x16x32_bf16 v[118:121], v[176:179], v[192:195], v[118:121]
	v_mfma_f32_16x16x32_bf16 v[110:113], v[184:187], v[192:195], v[110:113]
	v_mfma_f32_16x16x32_bf16 v[102:105], v[176:179], v[200:203], v[102:105]
	v_mfma_f32_16x16x32_bf16 v[94:97], v[184:187], v[200:203], v[94:97]
	v_mfma_f32_16x16x32_bf16 v[86:89], v[176:179], v[208:211], v[86:89]
	v_mfma_f32_16x16x32_bf16 v[78:81], v[184:187], v[208:211], v[78:81]
	v_mfma_f32_16x16x32_bf16 v[70:73], v[176:179], v[216:219], v[70:73]
	v_mfma_f32_16x16x32_bf16 v[66:69], v[184:187], v[216:219], v[66:69]
	v_mfma_f32_16x16x32_bf16 v[118:121], v[180:183], v[196:199], v[118:121]
	v_mfma_f32_16x16x32_bf16 v[110:113], v[188:191], v[196:199], v[110:113]
	v_mfma_f32_16x16x32_bf16 v[102:105], v[180:183], v[204:207], v[102:105]
	v_mfma_f32_16x16x32_bf16 v[94:97], v[188:191], v[204:207], v[94:97]
	v_mfma_f32_16x16x32_bf16 v[86:89], v[180:183], v[212:215], v[86:89]
	v_mfma_f32_16x16x32_bf16 v[78:81], v[188:191], v[212:215], v[78:81]
	v_mfma_f32_16x16x32_bf16 v[70:73], v[180:183], v[220:223], v[70:73]
	v_mfma_f32_16x16x32_bf16 v[66:69], v[188:191], v[220:223], v[66:69]
	s_setprio 0
	s_barrier
; #define PG8_STAGE_A(b, h, ptr, NX) do { if constexpr (Sched::GATHER) { unsigned gs_[2]; gs_[0] = ((NX) && last_) ? gN[h][0] : gA[h][0]; gs_[1] = ((NX) && last_) ? gN[h][1] : gA[h][1]; PG8_STAGE(PG8_SA(b, h), ptr, gs_); } \
;         else PG8_STAGE(PG8_SA(b, h), (ptr) + ((h) ? hstep : (size_t)0), voffA); } while (0)
; #define PG8_STAGE(bufoff, gbase, voff) do { _Pragma("unroll") for (int _i = 0; _i < 2; ++_i) \
;         __builtin_amdgcn_global_load_lds((const unsigned*)((const char*)(gbase) + (voff)[_i]), (PG8_LAS unsigned*)(lds + (bufoff) + ldsw + _i * 8192), 16, 0, 0); } while (0)
; #define PG8_LDA(dst, b, h) do { _Pragma("unroll") for (int m = 0; m < 4; ++m) _Pragma("unroll") for (int k = 0; k < 2; ++k) dst[m][k] = *(const PG8_LAS bf16x8*)(lds + PG8_SA(b, h) + aoff + m * 2048 + k * 1024); } while (0)
; #define PG8_LDB(dst, b, h) do { _Pragma("unroll") for (int n = 0; n < 2; ++n) _Pragma("unroll") for (int k = 0; k < 2; ++k) dst[n][k] = *(const PG8_LAS bf16x8*)(lds + PG8_SB(b, h) + boff + n * 2048 + k * 1024); } while (0)
; #define PG8_MMA(ai, bj, At, Bt) do { __builtin_amdgcn_s_setprio(1); _Pragma("unroll") for (int m = 0; m < 4; ++m) _Pragma("unroll") for (int n = 0; n < 2; ++n) _Pragma("unroll") for (int k = 0; k < 2; ++k) \
;         acc[ai][bj][m][n] = __builtin_amdgcn_mfma_f32_16x16x32_bf16(Bt[n][k], At[m][k], acc[ai][bj][m][n], 0, 0, 0); __builtin_amdgcn_s_setprio(0); } while (0)
; #define PG8_WAIT_V(n) asm volatile("s_waitcnt vmcnt(" #n ")" ::: "memory")
; #define PG8_WAIT_L(n) asm volatile("s_waitcnt lgkmcnt(" #n ")" ::: "memory")
; #define PG8_BAR __builtin_amdgcn_s_barrier()
; #define PG8_SCHED __builtin_amdgcn_sched_barrier(0)
; template <class Epi, class Sched, bool ALIGN_EPI = false, bool SP2 = false>
; __device__ __forceinline__ void gemm_phase(PG8_LAS unsigned char* lds, const Gemm g, const Sched& S, const Epi& E, const bool skip_epi = false) {
;     ...
;             PG8_LDA(At, 0, 1); PG8_STAGE(PG8_SB(0, 0), b2, voffB); PG8_STAGE(PG8_SB(0, 1), b2 + hstep, voffB); PG8_STAGE_A(0, 0, a2, true);
;             PG8_WAIT_V(8); PG8_WAIT_L(0); PG8_BAR; PG8_MMA(1, 0, At, B0); PG8_MMA(1, 1, At, B1); PG8_BAR; PG8_SCHED;
;             PG8_LDB(B0, 1, 0); PG8_LDB(B1, 1, 1); PG8_SCHED; PG8_LDA(At, 1, 0); PG8_STAGE_A(0, 1, a2, true);
;             PG8_WAIT_V(8); PG8_WAIT_L(0); PG8_BAR; PG8_MMA(0, 0, At, B0); PG8_MMA(0, 1, At, B1); PG8_BAR; PG8_SCHED;
	s_add_i32 s59, s48, s28
	s_mov_b32 m0, s59
	ds_read_b128 v[192:195], v172 offset:16384
	ds_read_b128 v[196:199], v172 offset:17408
	ds_read_b128 v[200:203], v172 offset:18432
	ds_read_b128 v[204:207], v172 offset:19456
	ds_read_b128 v[208:211], v172 offset:20480
	ds_read_b128 v[212:215], v172 offset:21504
	ds_read_b128 v[216:219], v172 offset:22528
	ds_read_b128 v[220:223], v172 offset:23552
	global_load_lds_dwordx4 v134, s[24:25]
	s_add_i32 m0, s59, 0x2000
	s_add_u32 s60, s24, 0x40000
	s_addc_u32 s61, s25, 0
	s_add_i32 s59, s49, s28
	global_load_lds_dwordx4 v130, s[24:25]
	s_mov_b32 m0, s59
	s_mov_b64 s[98:99], s[26:27]
	global_load_lds_dwordx4 v134, s[60:61]
	s_add_i32 m0, s59, 0x2000
	s_nop 0
	global_load_lds_dwordx4 v130, s[60:61]
	s_mov_b32 m0, s21
	s_nop 0
	global_load_lds_dwordx4 v136, s[26:27]
	s_mov_b32 m0, s31
	s_nop 0
	global_load_lds_dwordx4 v132, s[26:27]
	s_waitcnt vmcnt(8)
	s_waitcnt lgkmcnt(0)
	s_barrier
	s_setprio 3
	s_waitcnt lgkmcnt(0)
	v_mfma_f32_16x16x32_bf16 v[62:65], v[148:151], v[192:195], v[62:65]
	v_mfma_f32_16x16x32_bf16 v[58:61], v[156:159], v[192:195], v[58:61]
	v_mfma_f32_16x16x32_bf16 v[50:53], v[148:151], v[200:203], v[50:53]
	v_mfma_f32_16x16x32_bf16 v[42:45], v[156:159], v[200:203], v[42:45]
	v_mfma_f32_16x16x32_bf16 v[34:37], v[148:151], v[208:211], v[34:37]
	v_mfma_f32_16x16x32_bf16 v[26:29], v[156:159], v[208:211], v[26:29]
	v_mfma_f32_16x16x32_bf16 v[18:21], v[148:151], v[216:219], v[18:21]
	v_mfma_f32_16x16x32_bf16 v[10:13], v[156:159], v[216:219], v[10:13]
	v_mfma_f32_16x16x32_bf16 v[62:65], v[152:155], v[196:199], v[62:65]
	v_mfma_f32_16x16x32_bf16 v[58:61], v[160:163], v[196:199], v[58:61]
	v_mfma_f32_16x16x32_bf16 v[50:53], v[152:155], v[204:207], v[50:53]
	v_mfma_f32_16x16x32_bf16 v[42:45], v[160:163], v[204:207], v[42:45]
	v_mfma_f32_16x16x32_bf16 v[34:37], v[152:155], v[212:215], v[34:37]
	v_mfma_f32_16x16x32_bf16 v[26:29], v[160:163], v[212:215], v[26:29]
	v_mfma_f32_16x16x32_bf16 v[18:21], v[152:155], v[220:223], v[18:21]
	v_mfma_f32_16x16x32_bf16 v[10:13], v[160:163], v[220:223], v[10:13]
	v_mfma_f32_16x16x32_bf16 v[54:57], v[176:179], v[192:195], v[54:57]
	v_mfma_f32_16x16x32_bf16 v[46:49], v[184:187], v[192:195], v[46:49]
	v_mfma_f32_16x16x32_bf16 v[38:41], v[176:179], v[200:203], v[38:41]
	v_mfma_f32_16x16x32_bf16 v[30:33], v[184:187], v[200:203], v[30:33]
	v_mfma_f32_16x16x32_bf16 v[22:25], v[176:179], v[208:211], v[22:25]
	v_mfma_f32_16x16x32_bf16 v[14:17], v[184:187], v[208:211], v[14:17]
	v_mfma_f32_16x16x32_bf16 v[6:9], v[176:179], v[216:219], v[6:9]
	v_mfma_f32_16x16x32_bf16 v[2:5], v[184:187], v[216:219], v[2:5]
	v_mfma_f32_16x16x32_bf16 v[54:57], v[180:183], v[196:199], v[54:57]
	v_mfma_f32_16x16x32_bf16 v[46:49], v[188:191], v[196:199], v[46:49]
	v_mfma_f32_16x16x32_bf16 v[38:41], v[180:183], v[204:207], v[38:41]
	v_mfma_f32_16x16x32_bf16 v[30:33], v[188:191], v[204:207], v[30:33]
	v_mfma_f32_16x16x32_bf16 v[22:25], v[180:183], v[212:215], v[22:25]
	v_mfma_f32_16x16x32_bf16 v[14:17], v[188:191], v[212:215], v[14:17]
	v_mfma_f32_16x16x32_bf16 v[6:9], v[180:183], v[220:223], v[6:9]
	v_mfma_f32_16x16x32_bf16 v[2:5], v[188:191], v[220:223], v[2:5]
	s_setprio 0
	s_barrier
	s_add_i32 s59, 0, 0x18000
	s_add_i32 s60, 0, 0x1c000
	v_add_u32_e32 v160, s59, v1
	v_add_u32_e32 v188, s60, v1
	ds_read_b128 v[148:151], v160
	ds_read_b128 v[152:155], v160 offset:1024
	ds_read_b128 v[156:159], v160 offset:2048
	ds_read_b128 v[160:163], v160 offset:3072
	ds_read_b128 v[176:179], v188
	ds_read_b128 v[180:183], v188 offset:1024
	ds_read_b128 v[184:187], v188 offset:2048
	ds_read_b128 v[188:191], v188 offset:3072
	s_add_u32 s26, s26, 0x40000
	s_addc_u32 s27, s27, 0
	s_mov_b32 m0, s34
	ds_read_b128 v[192:195], v172 offset:32768
	ds_read_b128 v[196:199], v172 offset:33792
	ds_read_b128 v[200:203], v172 offset:34816
	ds_read_b128 v[204:207], v172 offset:35840
	ds_read_b128 v[208:211], v172 offset:36864
	ds_read_b128 v[212:215], v172 offset:37888
	ds_read_b128 v[216:219], v172 offset:38912
	ds_read_b128 v[220:223], v172 offset:39936
	global_load_lds_dwordx4 v136, s[26:27]
	s_mov_b32 m0, s35
	s_nop 0
	global_load_lds_dwordx4 v132, s[26:27]
	s_waitcnt vmcnt(8)
	s_waitcnt lgkmcnt(0)
	s_barrier
; #define PG8_STAGE_A(b, h, ptr, NX) do { if constexpr (Sched::GATHER) { unsigned gs_[2]; gs_[0] = ((NX) && last_) ? gN[h][0] : gA[h][0]; gs_[1] = ((NX) && last_) ? gN[h][1] : gA[h][1]; PG8_STAGE(PG8_SA(b, h), ptr, gs_); } \
;         else PG8_STAGE(PG8_SA(b, h), (ptr) + ((h) ? hstep : (size_t)0), voffA); } while (0)
; #define PG8_STAGE(bufoff, gbase, voff) do { _Pragma("unroll") for (int _i = 0; _i < 2; ++_i) \
;         __builtin_amdgcn_global_load_lds((const unsigned*)((const char*)(gbase) + (voff)[_i]), (PG8_LAS unsigned*)(lds + (bufoff) + ldsw + _i * 8192), 16, 0, 0); } while (0)
; #define PG8_LDA(dst, b, h) do { _Pragma("unroll") for (int m = 0; m < 4; ++m) _Pragma("unroll") for (int k = 0; k < 2; ++k) dst[m][k] = *(const PG8_LAS bf16x8*)(lds + PG8_SA(b, h) + aoff + m * 2048 + k * 1024); } while (0)
; #define PG8_MMA(ai, bj, At, Bt) do { __builtin_amdgcn_s_setprio(1); _Pragma("unroll") for (int m = 0; m < 4; ++m) _Pragma("unroll") for (int n = 0; n < 2; ++n) _Pragma("unroll") for (int k = 0; k < 2; ++k) \
;         acc[ai][bj][m][n] = __builtin_amdgcn_mfma_f32_16x16x32_bf16(Bt[n][k], At[m][k], acc[ai][bj][m][n], 0, 0, 0); __builtin_amdgcn_s_setprio(0); } while (0)
; #define PG8_WAIT_V(n) asm volatile("s_waitcnt vmcnt(" #n ")" ::: "memory")
; #define PG8_WAIT_L(n) asm volatile("s_waitcnt lgkmcnt(" #n ")" ::: "memory")
; #define PG8_BAR __builtin_amdgcn_s_barrier()
; #define PG8_SCHED __builtin_amdgcn_sched_barrier(0)
; __device__ __forceinline__ void rstd8(const float* SS, int rowb, int lane, float (&rs)[2][4]) {
;     ...
;         for (int m = 0; m < 4; ++m) p[ai][m] = *(const f32x4*)(SS + (size_t)(rowb + HALF * ai + 16 * m + (lane >> 2)) * 16 + 4 * (lane & 3));
; template <class Epi, class Sched, bool ALIGN_EPI = false, bool SP2 = false>
; __device__ __forceinline__ void gemm_phase(PG8_LAS unsigned char* lds, const Gemm g, const Sched& S, const Epi& E, const bool skip_epi = false) {
;     ...
;             PG8_WAIT_V(8); PG8_WAIT_L(0); PG8_BAR; PG8_MMA(0, 0, At, B0); PG8_MMA(0, 1, At, B1); PG8_BAR; PG8_SCHED;
;             PG8_LDA(At, 1, 1); PG8_STAGE(PG8_SB(1, 0), b3, voffB); PG8_STAGE(PG8_SB(1, 1), b3 + hstep, voffB); PG8_STAGE_A(1, 0, a3, true);
;             PG8_WAIT_V(8); PG8_WAIT_L(0); PG8_BAR; PG8_MMA(1, 0, At, B0); PG8_MMA(1, 1, At, B1); PG8_BAR; PG8_SCHED;
	s_setprio 3
	s_waitcnt lgkmcnt(0)
	v_mfma_f32_16x16x32_bf16 v[126:129], v[148:151], v[192:195], v[126:129]
	v_mfma_f32_16x16x32_bf16 v[122:125], v[156:159], v[192:195], v[122:125]
	v_mfma_f32_16x16x32_bf16 v[114:117], v[148:151], v[200:203], v[114:117]
	v_mfma_f32_16x16x32_bf16 v[106:109], v[156:159], v[200:203], v[106:109]
	v_mfma_f32_16x16x32_bf16 v[98:101], v[148:151], v[208:211], v[98:101]
	v_mfma_f32_16x16x32_bf16 v[90:93], v[156:159], v[208:211], v[90:93]
	v_mfma_f32_16x16x32_bf16 v[82:85], v[148:151], v[216:219], v[82:85]
	v_mfma_f32_16x16x32_bf16 v[74:77], v[156:159], v[216:219], v[74:77]
	v_mfma_f32_16x16x32_bf16 v[126:129], v[152:155], v[196:199], v[126:129]
	v_mfma_f32_16x16x32_bf16 v[122:125], v[160:163], v[196:199], v[122:125]
	v_mfma_f32_16x16x32_bf16 v[114:117], v[152:155], v[204:207], v[114:117]
	v_mfma_f32_16x16x32_bf16 v[106:109], v[160:163], v[204:207], v[106:109]
	v_mfma_f32_16x16x32_bf16 v[98:101], v[152:155], v[212:215], v[98:101]
	v_mfma_f32_16x16x32_bf16 v[90:93], v[160:163], v[212:215], v[90:93]
	v_mfma_f32_16x16x32_bf16 v[82:85], v[152:155], v[220:223], v[82:85]
	v_mfma_f32_16x16x32_bf16 v[74:77], v[160:163], v[220:223], v[74:77]
	v_mfma_f32_16x16x32_bf16 v[118:121], v[176:179], v[192:195], v[118:121]
	v_mfma_f32_16x16x32_bf16 v[110:113], v[184:187], v[192:195], v[110:113]
	v_mfma_f32_16x16x32_bf16 v[102:105], v[176:179], v[200:203], v[102:105]
	v_mfma_f32_16x16x32_bf16 v[94:97], v[184:187], v[200:203], v[94:97]
	v_mfma_f32_16x16x32_bf16 v[86:89], v[176:179], v[208:211], v[86:89]
	v_mfma_f32_16x16x32_bf16 v[78:81], v[184:187], v[208:211], v[78:81]
	v_mfma_f32_16x16x32_bf16 v[70:73], v[176:179], v[216:219], v[70:73]
	v_mfma_f32_16x16x32_bf16 v[66:69], v[184:187], v[216:219], v[66:69]
	v_mfma_f32_16x16x32_bf16 v[118:121], v[180:183], v[196:199], v[118:121]
	v_mfma_f32_16x16x32_bf16 v[110:113], v[188:191], v[196:199], v[110:113]
	v_mfma_f32_16x16x32_bf16 v[102:105], v[180:183], v[204:207], v[102:105]
	v_mfma_f32_16x16x32_bf16 v[94:97], v[188:191], v[204:207], v[94:97]
	v_mfma_f32_16x16x32_bf16 v[86:89], v[180:183], v[212:215], v[86:89]
	v_mfma_f32_16x16x32_bf16 v[78:81], v[188:191], v[212:215], v[78:81]
	v_mfma_f32_16x16x32_bf16 v[70:73], v[180:183], v[220:223], v[70:73]
	v_mfma_f32_16x16x32_bf16 v[66:69], v[188:191], v[220:223], v[66:69]
	s_setprio 0
	s_barrier
	s_add_i32 s26, s59, s28
	s_add_i32 m0, s26, 0xffffff80
	ds_read_b128 v[192:195], v172 offset:49152
	ds_read_b128 v[196:199], v172 offset:50176
	ds_read_b128 v[200:203], v172 offset:51200
	ds_read_b128 v[204:207], v172 offset:52224
	ds_read_b128 v[208:211], v172 offset:53248
	ds_read_b128 v[212:215], v172 offset:54272
	ds_read_b128 v[216:219], v172 offset:55296
	ds_read_b128 v[220:223], v172 offset:56320
	global_load_lds_dwordx4 v134, s[24:25] offset:128
	s_add_i32 m0, s26, 0x1f80
	s_add_i32 s26, s60, s28
	global_load_lds_dwordx4 v130, s[24:25] offset:128
	s_add_u32 s24, s24, 0x40080
	s_addc_u32 s25, s25, 0
	s_mov_b32 m0, s26
	s_nop 0
	global_load_lds_dwordx4 v134, s[24:25]
	s_add_i32 m0, s26, 0x2000
	s_nop 0
	global_load_lds_dwordx4 v130, s[24:25]
	s_add_i32 m0, s37, 0xffffff80
	s_nop 0
	global_load_lds_dwordx4 v136, s[98:99] offset:128
	s_add_i32 m0, s38, 0xffffff80
	s_nop 0
	global_load_lds_dwordx4 v132, s[98:99] offset:128
	s_waitcnt vmcnt(8)
	s_waitcnt lgkmcnt(0)
	s_barrier
	s_setprio 3
	s_waitcnt lgkmcnt(0)
	v_mfma_f32_16x16x32_bf16 v[62:65], v[148:151], v[192:195], v[62:65]
	v_mfma_f32_16x16x32_bf16 v[58:61], v[156:159], v[192:195], v[58:61]
	v_mfma_f32_16x16x32_bf16 v[50:53], v[148:151], v[200:203], v[50:53]
	v_mfma_f32_16x16x32_bf16 v[42:45], v[156:159], v[200:203], v[42:45]
	v_mfma_f32_16x16x32_bf16 v[34:37], v[148:151], v[208:211], v[34:37]
	v_mfma_f32_16x16x32_bf16 v[26:29], v[156:159], v[208:211], v[26:29]
	v_mfma_f32_16x16x32_bf16 v[18:21], v[148:151], v[216:219], v[18:21]
	v_mfma_f32_16x16x32_bf16 v[10:13], v[156:159], v[216:219], v[10:13]
	v_mfma_f32_16x16x32_bf16 v[62:65], v[152:155], v[196:199], v[62:65]
	v_mfma_f32_16x16x32_bf16 v[58:61], v[160:163], v[196:199], v[58:61]
	v_mfma_f32_16x16x32_bf16 v[50:53], v[152:155], v[204:207], v[50:53]
	v_mfma_f32_16x16x32_bf16 v[42:45], v[160:163], v[204:207], v[42:45]
	v_mfma_f32_16x16x32_bf16 v[34:37], v[152:155], v[212:215], v[34:37]
	v_mfma_f32_16x16x32_bf16 v[26:29], v[160:163], v[212:215], v[26:29]
	v_mfma_f32_16x16x32_bf16 v[18:21], v[152:155], v[220:223], v[18:21]
	v_mfma_f32_16x16x32_bf16 v[10:13], v[160:163], v[220:223], v[10:13]
	v_mfma_f32_16x16x32_bf16 v[54:57], v[176:179], v[192:195], v[54:57]
	v_mfma_f32_16x16x32_bf16 v[46:49], v[184:187], v[192:195], v[46:49]
	v_mfma_f32_16x16x32_bf16 v[38:41], v[176:179], v[200:203], v[38:41]
	v_mfma_f32_16x16x32_bf16 v[30:33], v[184:187], v[200:203], v[30:33]
	v_mfma_f32_16x16x32_bf16 v[22:25], v[176:179], v[208:211], v[22:25]
	v_mfma_f32_16x16x32_bf16 v[14:17], v[184:187], v[208:211], v[14:17]
	v_mfma_f32_16x16x32_bf16 v[6:9], v[176:179], v[216:219], v[6:9]
	v_mfma_f32_16x16x32_bf16 v[2:5], v[184:187], v[216:219], v[2:5]
	v_mfma_f32_16x16x32_bf16 v[54:57], v[180:183], v[196:199], v[54:57]
	v_mfma_f32_16x16x32_bf16 v[46:49], v[188:191], v[196:199], v[46:49]
	v_mfma_f32_16x16x32_bf16 v[38:41], v[180:183], v[204:207], v[38:41]
	v_mfma_f32_16x16x32_bf16 v[30:33], v[188:191], v[204:207], v[30:33]
	v_mfma_f32_16x16x32_bf16 v[22:25], v[180:183], v[212:215], v[22:25]
	v_mfma_f32_16x16x32_bf16 v[14:17], v[188:191], v[212:215], v[14:17]
	v_mfma_f32_16x16x32_bf16 v[6:9], v[180:183], v[220:223], v[6:9]
	v_mfma_f32_16x16x32_bf16 v[2:5], v[188:191], v[220:223], v[2:5]
	s_setprio 0
	s_barrier
	s_add_i32 s58, s58, 2
	s_add_u32 s22, s22, 0x100
	s_addc_u32 s23, s23, 0
	s_add_u32 s56, s56, 0x100
	s_addc_u32 s57, s57, 0
	s_cmp_gt_u32 s58, 13
	s_cbranch_scc0 .LBB0_944
	v_lshl_add_u32 v164, s20, 8, v167
	v_ashrrev_i32_e32 v165, 31, v164
	v_lshlrev_b64 v[148:149], 6, v[164:165]
	v_lshl_add_u64 v[148:149], v[138:139], 0, v[148:149]
	v_add_co_u32_e32 v150, vcc, 0x2000, v148
	v_addc_co_u32_e32 v151, vcc, 0, v149, vcc
	global_load_dwordx4 v[176:179], v[148:149], off
	global_load_dwordx4 v[180:183], v[148:149], off offset:1024
	global_load_dwordx4 v[184:187], v[148:149], off offset:2048
	global_load_dwordx4 v[188:191], v[148:149], off offset:3072
	global_load_dwordx4 v[192:195], v[150:151], off
	global_load_dwordx4 v[196:199], v[150:151], off offset:1024
	global_load_dwordx4 v[200:203], v[150:151], off offset:2048
	global_load_dwordx4 v[204:207], v[150:151], off offset:3072
	s_and_b64 vcc, exec, s[10:11]
	s_cbranch_vccz .LBB0_947
	s_barrier

; #define PG8_STAGE_A(b, h, ptr, NX) do { if constexpr (Sched::GATHER) { unsigned gs_[2]; gs_[0] = ((NX) && last_) ? gN[h][0] : gA[h][0]; gs_[1] = ((NX) && last_) ? gN[h][1] : gA[h][1]; PG8_STAGE(PG8_SA(b, h), ptr, gs_); } \
;         else PG8_STAGE(PG8_SA(b, h), (ptr) + ((h) ? hstep : (size_t)0), voffA); } while (0)
; #define PG8_LDA(dst, b, h) do { _Pragma("unroll") for (int m = 0; m < 4; ++m) _Pragma("unroll") for (int k = 0; k < 2; ++k) dst[m][k] = *(const PG8_LAS bf16x8*)(lds + PG8_SA(b, h) + aoff + m * 2048 + k * 1024); } while (0)
; #define PG8_LDB(dst, b, h) do { _Pragma("unroll") for (int n = 0; n < 2; ++n) _Pragma("unroll") for (int k = 0; k < 2; ++k) dst[n][k] = *(const PG8_LAS bf16x8*)(lds + PG8_SB(b, h) + boff + n * 2048 + k * 1024); } while (0)
; #define PG8_MMA(ai, bj, At, Bt) do { __builtin_amdgcn_s_setprio(1); _Pragma("unroll") for (int m = 0; m < 4; ++m) _Pragma("unroll") for (int n = 0; n < 2; ++n) _Pragma("unroll") for (int k = 0; k < 2; ++k) \
;         acc[ai][bj][m][n] = __builtin_amdgcn_mfma_f32_16x16x32_bf16(Bt[n][k], At[m][k], acc[ai][bj][m][n], 0, 0, 0); __builtin_amdgcn_s_setprio(0); } while (0)
; #define PG8_WAIT_V(n) asm volatile("s_waitcnt vmcnt(" #n ")" ::: "memory")
; #define PG8_WAIT_L(n) asm volatile("s_waitcnt lgkmcnt(" #n ")" ::: "memory")
; #define PG8_BAR __builtin_amdgcn_s_barrier()
; #define PG8_SCHED __builtin_amdgcn_sched_barrier(0)
; template <class Epi, class Sched, bool ALIGN_EPI = false, bool SP2 = false>
; __device__ __forceinline__ void gemm_phase(PG8_LAS unsigned char* lds, const Gemm g, const Sched& S, const Epi& E, const bool skip_epi = false) {
;     ...
;         const char* nA = has_next ? (const char*)g.A + (size_t)nxt.pm * pmstepA + nxt.ko : cA; const char* nB = has_next ? (const char*)g.Bt + (size_t)nxt.pn * tstep + nxt.ko : cB;
;     ...
;             const char* a2 = last ? nA : cA + (size_t)(t + 2) * kstep; const char* b2 = last ? nB : cB + (size_t)(t + 2) * kstep;
;             const char* a3 = a2 + kstep; const char* b3 = b2 + kstep;
;             if (last && has_next) S.a_ready(nxt);
;             if constexpr (SP2) {
;             PG8_LDB(B0, 0, 0); PG8_LDB(B1, 0, 1); PG8_SCHED; PG8_LDA(At, 0, 0); PG8_STAGE_A(1, 1, a1, false);
;             PG8_WAIT_V(8); PG8_WAIT_L(0); PG8_BAR; PG8_MMA(0, 0, At, B0); PG8_MMA(0, 1, At, B1); PG8_BAR; PG8_SCHED;
.LBB0_1323:
	s_ashr_i32 s25, s24, 31
	s_lshl_b64 s[26:27], s[24:25], 19
	s_add_u32 s26, s46, s26
	s_addc_u32 s27, s47, s27
	s_and_b64 s[28:29], s[6:7], exec
	s_cselect_b32 s25, s27, s35
	s_cselect_b32 s31, s26, s34
	s_ashr_i32 s23, s22, 31
	s_lshl_b64 s[28:29], s[22:23], 19
	s_add_u32 s28, s2, s28
	s_addc_u32 s29, s3, s29
	s_and_b64 s[38:39], s[6:7], exec
	s_cselect_b32 s23, s29, s37
	s_cselect_b32 s60, s28, s36
	s_add_u32 s34, s34, 0x40080
	s_addc_u32 s35, s35, 0
	s_add_u32 s61, s36, 0x100
	s_addc_u32 s62, s37, 0
	s_mov_b32 s63, -2
	s_waitcnt vmcnt(0)
	s_waitcnt lgkmcnt(0)
	ds_read_b128 v[98:101], v225
	ds_read_b128 v[110:113], v225 offset:1024
	ds_read_b128 v[122:125], v225 offset:2048
	ds_read_b128 v[130:133], v225 offset:3072
	ds_read_b128 v[146:149], v226
	ds_read_b128 v[150:153], v226 offset:1024
	ds_read_b128 v[154:157], v226 offset:2048
	ds_read_b128 v[158:161], v226 offset:3072
	s_add_u32 s36, s34, 0xfffc0080
	s_addc_u32 s37, s35, -1
	s_cmp_eq_u32 s63, 12
	s_cselect_b32 s39, s25, s37
	s_cselect_b32 s38, s31, s36
	s_cselect_b32 s37, s23, s62
	s_cselect_b32 s36, s60, s61
	s_add_i32 m0, s41, 0xc000
	ds_read_b128 v[162:165], v227
	ds_read_b128 v[166:169], v227 offset:1024
	ds_read_b128 v[170:173], v227 offset:2048
	ds_read_b128 v[174:177], v227 offset:3072
	ds_read_b128 v[178:181], v227 offset:4096
	ds_read_b128 v[182:185], v227 offset:5120
	ds_read_b128 v[202:205], v227 offset:6144
	ds_read_b128 v[206:209], v227 offset:7168
	global_load_lds_dwordx4 v194, s[34:35]
	s_add_i32 m0, s41, 0xe000
	s_nop 0
	global_load_lds_dwordx4 v196, s[34:35]
	s_waitcnt vmcnt(8)
	s_waitcnt lgkmcnt(0)
	s_barrier
	s_setprio 3
	s_waitcnt lgkmcnt(0)
	v_mfma_f32_16x16x32_bf16 v[142:145], v[98:101], v[162:165], 0
	v_mfma_f32_16x16x32_bf16 v[138:141], v[122:125], v[162:165], 0
	v_mfma_f32_16x16x32_bf16 v[118:121], v[98:101], v[170:173], 0
	v_mfma_f32_16x16x32_bf16 v[114:117], v[122:125], v[170:173], 0
	v_mfma_f32_16x16x32_bf16 v[94:97], v[98:101], v[178:181], 0
	v_mfma_f32_16x16x32_bf16 v[90:93], v[122:125], v[178:181], 0
	v_mfma_f32_16x16x32_bf16 v[78:81], v[98:101], v[202:205], 0
	v_mfma_f32_16x16x32_bf16 v[74:77], v[122:125], v[202:205], 0
	v_mfma_f32_16x16x32_bf16 v[142:145], v[110:113], v[166:169], v[142:145]
	v_mfma_f32_16x16x32_bf16 v[138:141], v[130:133], v[166:169], v[138:141]
	v_mfma_f32_16x16x32_bf16 v[118:121], v[110:113], v[174:177], v[118:121]
	v_mfma_f32_16x16x32_bf16 v[114:117], v[130:133], v[174:177], v[114:117]
	v_mfma_f32_16x16x32_bf16 v[94:97], v[110:113], v[182:185], v[94:97]
	v_mfma_f32_16x16x32_bf16 v[90:93], v[130:133], v[182:185], v[90:93]
	v_mfma_f32_16x16x32_bf16 v[78:81], v[110:113], v[206:209], v[78:81]
	v_mfma_f32_16x16x32_bf16 v[74:77], v[130:133], v[206:209], v[74:77]
	v_mfma_f32_16x16x32_bf16 v[134:137], v[146:149], v[162:165], 0
	v_mfma_f32_16x16x32_bf16 v[126:129], v[154:157], v[162:165], 0
	v_mfma_f32_16x16x32_bf16 v[106:109], v[146:149], v[170:173], 0
	v_mfma_f32_16x16x32_bf16 v[102:105], v[154:157], v[170:173], 0
	v_mfma_f32_16x16x32_bf16 v[86:89], v[146:149], v[178:181], 0
	v_mfma_f32_16x16x32_bf16 v[82:85], v[154:157], v[178:181], 0
	v_mfma_f32_16x16x32_bf16 v[70:73], v[146:149], v[202:205], 0
	v_mfma_f32_16x16x32_bf16 v[66:69], v[154:157], v[202:205], 0
	v_mfma_f32_16x16x32_bf16 v[134:137], v[150:153], v[166:169], v[134:137]
	v_mfma_f32_16x16x32_bf16 v[126:129], v[158:161], v[166:169], v[126:129]
	v_mfma_f32_16x16x32_bf16 v[106:109], v[150:153], v[174:177], v[106:109]
	v_mfma_f32_16x16x32_bf16 v[102:105], v[158:161], v[174:177], v[102:105]
	v_mfma_f32_16x16x32_bf16 v[86:89], v[150:153], v[182:185], v[86:89]
	v_mfma_f32_16x16x32_bf16 v[82:85], v[158:161], v[182:185], v[82:85]
	v_mfma_f32_16x16x32_bf16 v[70:73], v[150:153], v[206:209], v[70:73]
	v_mfma_f32_16x16x32_bf16 v[66:69], v[158:161], v[206:209], v[66:69]
	s_setprio 0
	s_barrier
	s_add_i32 s64, s57, s40
	s_mov_b32 m0, s64
	ds_read_b128 v[162:165], v227 offset:16384
	ds_read_b128 v[166:169], v227 offset:17408
	ds_read_b128 v[170:173], v227 offset:18432
	ds_read_b128 v[174:177], v227 offset:19456
	ds_read_b128 v[178:181], v227 offset:20480
	ds_read_b128 v[182:185], v227 offset:21504
	ds_read_b128 v[202:205], v227 offset:22528
	ds_read_b128 v[206:209], v227 offset:23552
	global_load_lds_dwordx4 v188, s[36:37]
	s_add_i32 m0, s64, 0x2000
	s_add_u32 s64, s36, 0x40000
	s_addc_u32 s65, s37, 0
	s_add_i32 s66, s58, s40
	global_load_lds_dwordx4 v192, s[36:37]
	s_mov_b32 m0, s66
	s_mov_b64 s[98:99], s[38:39]
	global_load_lds_dwordx4 v188, s[64:65]
	s_add_i32 m0, s66, 0x2000
	s_nop 0
	global_load_lds_dwordx4 v192, s[64:65]
	s_mov_b32 m0, s41
	s_nop 0
	global_load_lds_dwordx4 v186, s[38:39]
	s_mov_b32 m0, s44
	s_nop 0
	global_load_lds_dwordx4 v190, s[38:39]
	s_waitcnt vmcnt(8)
	s_waitcnt lgkmcnt(0)
	s_barrier
; #define PG8_STAGE_A(b, h, ptr, NX) do { if constexpr (Sched::GATHER) { unsigned gs_[2]; gs_[0] = ((NX) && last_) ? gN[h][0] : gA[h][0]; gs_[1] = ((NX) && last_) ? gN[h][1] : gA[h][1]; PG8_STAGE(PG8_SA(b, h), ptr, gs_); } \
;         else PG8_STAGE(PG8_SA(b, h), (ptr) + ((h) ? hstep : (size_t)0), voffA); } while (0)
; #define PG8_STAGE(bufoff, gbase, voff) do { _Pragma("unroll") for (int _i = 0; _i < 2; ++_i) \
;         __builtin_amdgcn_global_load_lds((const unsigned*)((const char*)(gbase) + (voff)[_i]), (PG8_LAS unsigned*)(lds + (bufoff) + ldsw + _i * 8192), 16, 0, 0); } while (0)
; #define PG8_LDA(dst, b, h) do { _Pragma("unroll") for (int m = 0; m < 4; ++m) _Pragma("unroll") for (int k = 0; k < 2; ++k) dst[m][k] = *(const PG8_LAS bf16x8*)(lds + PG8_SA(b, h) + aoff + m * 2048 + k * 1024); } while (0)
; #define PG8_LDB(dst, b, h) do { _Pragma("unroll") for (int n = 0; n < 2; ++n) _Pragma("unroll") for (int k = 0; k < 2; ++k) dst[n][k] = *(const PG8_LAS bf16x8*)(lds + PG8_SB(b, h) + boff + n * 2048 + k * 1024); } while (0)
; #define PG8_MMA(ai, bj, At, Bt) do { __builtin_amdgcn_s_setprio(1); _Pragma("unroll") for (int m = 0; m < 4; ++m) _Pragma("unroll") for (int n = 0; n < 2; ++n) _Pragma("unroll") for (int k = 0; k < 2; ++k) \
;         acc[ai][bj][m][n] = __builtin_amdgcn_mfma_f32_16x16x32_bf16(Bt[n][k], At[m][k], acc[ai][bj][m][n], 0, 0, 0); __builtin_amdgcn_s_setprio(0); } while (0)
; #define PG8_WAIT_V(n) asm volatile("s_waitcnt vmcnt(" #n ")" ::: "memory")
; #define PG8_WAIT_L(n) asm volatile("s_waitcnt lgkmcnt(" #n ")" ::: "memory")
; #define PG8_BAR __builtin_amdgcn_s_barrier()
; #define PG8_SCHED __builtin_amdgcn_sched_barrier(0)
; template <class Epi, class Sched, bool ALIGN_EPI = false, bool SP2 = false>
; __device__ __forceinline__ void gemm_phase(PG8_LAS unsigned char* lds, const Gemm g, const Sched& S, const Epi& E, const bool skip_epi = false) {
;     ...
;             PG8_LDA(At, 0, 1); PG8_STAGE(PG8_SB(0, 0), b2, voffB); PG8_STAGE(PG8_SB(0, 1), b2 + hstep, voffB); PG8_STAGE_A(0, 0, a2, true);
;             PG8_WAIT_V(8); PG8_WAIT_L(0); PG8_BAR; PG8_MMA(1, 0, At, B0); PG8_MMA(1, 1, At, B1); PG8_BAR; PG8_SCHED;
;             PG8_LDB(B0, 1, 0); PG8_LDB(B1, 1, 1); PG8_SCHED; PG8_LDA(At, 1, 0); PG8_STAGE_A(0, 1, a2, true);
;             PG8_WAIT_V(8); PG8_WAIT_L(0); PG8_BAR; PG8_MMA(0, 0, At, B0); PG8_MMA(0, 1, At, B1); PG8_BAR; PG8_SCHED;
	s_setprio 3
	s_waitcnt lgkmcnt(0)
	v_mfma_f32_16x16x32_bf16 v[62:65], v[98:101], v[162:165], 0
	v_mfma_f32_16x16x32_bf16 v[58:61], v[122:125], v[162:165], 0
	v_mfma_f32_16x16x32_bf16 v[46:49], v[98:101], v[170:173], 0
	v_mfma_f32_16x16x32_bf16 v[42:45], v[122:125], v[170:173], 0
	v_mfma_f32_16x16x32_bf16 v[30:33], v[98:101], v[178:181], 0
	v_mfma_f32_16x16x32_bf16 v[26:29], v[122:125], v[178:181], 0
	v_mfma_f32_16x16x32_bf16 v[14:17], v[98:101], v[202:205], 0
	v_mfma_f32_16x16x32_bf16 v[10:13], v[122:125], v[202:205], 0
	v_mfma_f32_16x16x32_bf16 v[62:65], v[110:113], v[166:169], v[62:65]
	v_mfma_f32_16x16x32_bf16 v[58:61], v[130:133], v[166:169], v[58:61]
	v_mfma_f32_16x16x32_bf16 v[46:49], v[110:113], v[174:177], v[46:49]
	v_mfma_f32_16x16x32_bf16 v[42:45], v[130:133], v[174:177], v[42:45]
	v_mfma_f32_16x16x32_bf16 v[30:33], v[110:113], v[182:185], v[30:33]
	v_mfma_f32_16x16x32_bf16 v[26:29], v[130:133], v[182:185], v[26:29]
	v_mfma_f32_16x16x32_bf16 v[14:17], v[110:113], v[206:209], v[14:17]
	v_mfma_f32_16x16x32_bf16 v[10:13], v[130:133], v[206:209], v[10:13]
	v_mfma_f32_16x16x32_bf16 v[54:57], v[146:149], v[162:165], 0
	v_mfma_f32_16x16x32_bf16 v[50:53], v[154:157], v[162:165], 0
	v_mfma_f32_16x16x32_bf16 v[38:41], v[146:149], v[170:173], 0
	v_mfma_f32_16x16x32_bf16 v[34:37], v[154:157], v[170:173], 0
	v_mfma_f32_16x16x32_bf16 v[22:25], v[146:149], v[178:181], 0
	v_mfma_f32_16x16x32_bf16 v[18:21], v[154:157], v[178:181], 0
	v_mfma_f32_16x16x32_bf16 v[6:9], v[146:149], v[202:205], 0
	v_mfma_f32_16x16x32_bf16 v[2:5], v[154:157], v[202:205], 0
	v_mfma_f32_16x16x32_bf16 v[54:57], v[150:153], v[166:169], v[54:57]
	v_mfma_f32_16x16x32_bf16 v[50:53], v[158:161], v[166:169], v[50:53]
	v_mfma_f32_16x16x32_bf16 v[38:41], v[150:153], v[174:177], v[38:41]
	v_mfma_f32_16x16x32_bf16 v[34:37], v[158:161], v[174:177], v[34:37]
	v_mfma_f32_16x16x32_bf16 v[22:25], v[150:153], v[182:185], v[22:25]
	v_mfma_f32_16x16x32_bf16 v[18:21], v[158:161], v[182:185], v[18:21]
	v_mfma_f32_16x16x32_bf16 v[6:9], v[150:153], v[206:209], v[6:9]
	v_mfma_f32_16x16x32_bf16 v[2:5], v[158:161], v[206:209], v[2:5]
	s_setprio 0
	s_barrier
	s_add_i32 s64, 0, 0x18000
	s_add_i32 s65, 0, 0x1c000
	v_add_u32_e32 v130, s64, v220
	v_add_u32_e32 v158, s65, v220
	ds_read_b128 v[98:101], v130
	ds_read_b128 v[110:113], v130 offset:1024
	ds_read_b128 v[122:125], v130 offset:2048
	ds_read_b128 v[130:133], v130 offset:3072
	ds_read_b128 v[146:149], v158
	ds_read_b128 v[150:153], v158 offset:1024
	ds_read_b128 v[154:157], v158 offset:2048
	ds_read_b128 v[158:161], v158 offset:3072
	s_add_u32 s38, s38, 0x40000
	s_addc_u32 s39, s39, 0
	s_mov_b32 m0, s45
	ds_read_b128 v[162:165], v227 offset:32768
	ds_read_b128 v[166:169], v227 offset:33792
	ds_read_b128 v[170:173], v227 offset:34816
	ds_read_b128 v[174:177], v227 offset:35840
	ds_read_b128 v[178:181], v227 offset:36864
	ds_read_b128 v[182:185], v227 offset:37888
	ds_read_b128 v[202:205], v227 offset:38912
	ds_read_b128 v[206:209], v227 offset:39936
	global_load_lds_dwordx4 v186, s[38:39]
	s_mov_b32 m0, s48
	s_nop 0
	global_load_lds_dwordx4 v190, s[38:39]
	s_waitcnt vmcnt(8)
	s_waitcnt lgkmcnt(0)
	s_barrier
	s_setprio 3
	s_waitcnt lgkmcnt(0)
	v_mfma_f32_16x16x32_bf16 v[142:145], v[98:101], v[162:165], v[142:145]
	v_mfma_f32_16x16x32_bf16 v[138:141], v[122:125], v[162:165], v[138:141]
	v_mfma_f32_16x16x32_bf16 v[118:121], v[98:101], v[170:173], v[118:121]
	v_mfma_f32_16x16x32_bf16 v[114:117], v[122:125], v[170:173], v[114:117]
	v_mfma_f32_16x16x32_bf16 v[94:97], v[98:101], v[178:181], v[94:97]
	v_mfma_f32_16x16x32_bf16 v[90:93], v[122:125], v[178:181], v[90:93]
	v_mfma_f32_16x16x32_bf16 v[78:81], v[98:101], v[202:205], v[78:81]
	v_mfma_f32_16x16x32_bf16 v[74:77], v[122:125], v[202:205], v[74:77]
	v_mfma_f32_16x16x32_bf16 v[142:145], v[110:113], v[166:169], v[142:145]
	v_mfma_f32_16x16x32_bf16 v[138:141], v[130:133], v[166:169], v[138:141]
	v_mfma_f32_16x16x32_bf16 v[118:121], v[110:113], v[174:177], v[118:121]
	v_mfma_f32_16x16x32_bf16 v[114:117], v[130:133], v[174:177], v[114:117]
	v_mfma_f32_16x16x32_bf16 v[94:97], v[110:113], v[182:185], v[94:97]
	v_mfma_f32_16x16x32_bf16 v[90:93], v[130:133], v[182:185], v[90:93]
	v_mfma_f32_16x16x32_bf16 v[78:81], v[110:113], v[206:209], v[78:81]
	v_mfma_f32_16x16x32_bf16 v[74:77], v[130:133], v[206:209], v[74:77]
	v_mfma_f32_16x16x32_bf16 v[134:137], v[146:149], v[162:165], v[134:137]
	v_mfma_f32_16x16x32_bf16 v[126:129], v[154:157], v[162:165], v[126:129]
	v_mfma_f32_16x16x32_bf16 v[106:109], v[146:149], v[170:173], v[106:109]
	v_mfma_f32_16x16x32_bf16 v[102:105], v[154:157], v[170:173], v[102:105]
	v_mfma_f32_16x16x32_bf16 v[86:89], v[146:149], v[178:181], v[86:89]
	v_mfma_f32_16x16x32_bf16 v[82:85], v[154:157], v[178:181], v[82:85]
	v_mfma_f32_16x16x32_bf16 v[70:73], v[146:149], v[202:205], v[70:73]
	v_mfma_f32_16x16x32_bf16 v[66:69], v[154:157], v[202:205], v[66:69]
	v_mfma_f32_16x16x32_bf16 v[134:137], v[150:153], v[166:169], v[134:137]
	v_mfma_f32_16x16x32_bf16 v[126:129], v[158:161], v[166:169], v[126:129]
	v_mfma_f32_16x16x32_bf16 v[106:109], v[150:153], v[174:177], v[106:109]
	v_mfma_f32_16x16x32_bf16 v[102:105], v[158:161], v[174:177], v[102:105]
	v_mfma_f32_16x16x32_bf16 v[86:89], v[150:153], v[182:185], v[86:89]
	v_mfma_f32_16x16x32_bf16 v[82:85], v[158:161], v[182:185], v[82:85]
	v_mfma_f32_16x16x32_bf16 v[70:73], v[150:153], v[206:209], v[70:73]
	v_mfma_f32_16x16x32_bf16 v[66:69], v[158:161], v[206:209], v[66:69]
	s_setprio 0
	s_barrier
; #define PG8_STAGE_A(b, h, ptr, NX) do { if constexpr (Sched::GATHER) { unsigned gs_[2]; gs_[0] = ((NX) && last_) ? gN[h][0] : gA[h][0]; gs_[1] = ((NX) && last_) ? gN[h][1] : gA[h][1]; PG8_STAGE(PG8_SA(b, h), ptr, gs_); } \
;         else PG8_STAGE(PG8_SA(b, h), (ptr) + ((h) ? hstep : (size_t)0), voffA); } while (0)
; #define PG8_STAGE(bufoff, gbase, voff) do { _Pragma("unroll") for (int _i = 0; _i < 2; ++_i) \
;         __builtin_amdgcn_global_load_lds((const unsigned*)((const char*)(gbase) + (voff)[_i]), (PG8_LAS unsigned*)(lds + (bufoff) + ldsw + _i * 8192), 16, 0, 0); } while (0)
; #define PG8_LDA(dst, b, h) do { _Pragma("unroll") for (int m = 0; m < 4; ++m) _Pragma("unroll") for (int k = 0; k < 2; ++k) dst[m][k] = *(const PG8_LAS bf16x8*)(lds + PG8_SA(b, h) + aoff + m * 2048 + k * 1024); } while (0)
; #define PG8_LDB(dst, b, h) do { _Pragma("unroll") for (int n = 0; n < 2; ++n) _Pragma("unroll") for (int k = 0; k < 2; ++k) dst[n][k] = *(const PG8_LAS bf16x8*)(lds + PG8_SB(b, h) + boff + n * 2048 + k * 1024); } while (0)
; #define PG8_MMA(ai, bj, At, Bt) do { __builtin_amdgcn_s_setprio(1); _Pragma("unroll") for (int m = 0; m < 4; ++m) _Pragma("unroll") for (int n = 0; n < 2; ++n) _Pragma("unroll") for (int k = 0; k < 2; ++k) \
;         acc[ai][bj][m][n] = __builtin_amdgcn_mfma_f32_16x16x32_bf16(Bt[n][k], At[m][k], acc[ai][bj][m][n], 0, 0, 0); __builtin_amdgcn_s_setprio(0); } while (0)
; #define PG8_WAIT_V(n) asm volatile("s_waitcnt vmcnt(" #n ")" ::: "memory")
; #define PG8_WAIT_L(n) asm volatile("s_waitcnt lgkmcnt(" #n ")" ::: "memory")
; #define PG8_BAR __builtin_amdgcn_s_barrier()
; #define PG8_SCHED __builtin_amdgcn_sched_barrier(0)
; template <class Epi, class Sched, bool ALIGN_EPI = false, bool SP2 = false>
; __device__ __forceinline__ void gemm_phase(PG8_LAS unsigned char* lds, const Gemm g, const Sched& S, const Epi& E, const bool skip_epi = false) {
;     ...
;             PG8_LDB(B0, 0, 0); PG8_LDB(B1, 0, 1); PG8_SCHED; PG8_LDA(At, 0, 0); PG8_STAGE_A(1, 1, a1, false);
;             PG8_WAIT_V(8); PG8_WAIT_L(0); PG8_BAR; PG8_MMA(0, 0, At, B0); PG8_MMA(0, 1, At, B1); PG8_BAR; PG8_SCHED;
;     ...
;             PG8_LDA(At, 1, 1); PG8_STAGE(PG8_SB(1, 0), b3, voffB); PG8_STAGE(PG8_SB(1, 1), b3 + hstep, voffB); PG8_STAGE_A(1, 0, a3, true);
;             PG8_WAIT_V(8); PG8_WAIT_L(0); PG8_BAR; PG8_MMA(1, 0, At, B0); PG8_MMA(1, 1, At, B1); PG8_BAR; PG8_SCHED;
	s_add_i32 s38, s64, s40
	s_add_i32 m0, s38, 0xffffff80
	ds_read_b128 v[162:165], v227 offset:49152
	ds_read_b128 v[166:169], v227 offset:50176
	ds_read_b128 v[170:173], v227 offset:51200
	ds_read_b128 v[174:177], v227 offset:52224
	ds_read_b128 v[178:181], v227 offset:53248
	ds_read_b128 v[182:185], v227 offset:54272
	ds_read_b128 v[202:205], v227 offset:55296
	ds_read_b128 v[206:209], v227 offset:56320
	global_load_lds_dwordx4 v188, s[36:37] offset:128
	s_add_i32 m0, s38, 0x1f80
	s_add_i32 s38, s65, s40
	global_load_lds_dwordx4 v192, s[36:37] offset:128
	s_add_u32 s36, s36, 0x40080
	s_addc_u32 s37, s37, 0
	s_mov_b32 m0, s38
	s_nop 0
	global_load_lds_dwordx4 v188, s[36:37]
	s_add_i32 m0, s38, 0x2000
	s_nop 0
	global_load_lds_dwordx4 v192, s[36:37]
	s_add_i32 m0, s53, 0xffffff80
	s_nop 0
	global_load_lds_dwordx4 v186, s[98:99] offset:128
	s_add_i32 m0, s54, 0xffffff80
	s_nop 0
	global_load_lds_dwordx4 v190, s[98:99] offset:128
	s_waitcnt vmcnt(8)
	s_waitcnt lgkmcnt(0)
	s_barrier
	s_setprio 3
	s_waitcnt lgkmcnt(0)
	v_mfma_f32_16x16x32_bf16 v[62:65], v[98:101], v[162:165], v[62:65]
	v_mfma_f32_16x16x32_bf16 v[58:61], v[122:125], v[162:165], v[58:61]
	v_mfma_f32_16x16x32_bf16 v[46:49], v[98:101], v[170:173], v[46:49]
	v_mfma_f32_16x16x32_bf16 v[42:45], v[122:125], v[170:173], v[42:45]
	v_mfma_f32_16x16x32_bf16 v[30:33], v[98:101], v[178:181], v[30:33]
	v_mfma_f32_16x16x32_bf16 v[26:29], v[122:125], v[178:181], v[26:29]
	v_mfma_f32_16x16x32_bf16 v[14:17], v[98:101], v[202:205], v[14:17]
	v_mfma_f32_16x16x32_bf16 v[10:13], v[122:125], v[202:205], v[10:13]
	v_mfma_f32_16x16x32_bf16 v[62:65], v[110:113], v[166:169], v[62:65]
	v_mfma_f32_16x16x32_bf16 v[58:61], v[130:133], v[166:169], v[58:61]
	v_mfma_f32_16x16x32_bf16 v[46:49], v[110:113], v[174:177], v[46:49]
	v_mfma_f32_16x16x32_bf16 v[42:45], v[130:133], v[174:177], v[42:45]
	v_mfma_f32_16x16x32_bf16 v[30:33], v[110:113], v[182:185], v[30:33]
	v_mfma_f32_16x16x32_bf16 v[26:29], v[130:133], v[182:185], v[26:29]
	v_mfma_f32_16x16x32_bf16 v[14:17], v[110:113], v[206:209], v[14:17]
	v_mfma_f32_16x16x32_bf16 v[10:13], v[130:133], v[206:209], v[10:13]
	v_mfma_f32_16x16x32_bf16 v[54:57], v[146:149], v[162:165], v[54:57]
	v_mfma_f32_16x16x32_bf16 v[50:53], v[154:157], v[162:165], v[50:53]
	v_mfma_f32_16x16x32_bf16 v[38:41], v[146:149], v[170:173], v[38:41]
	v_mfma_f32_16x16x32_bf16 v[34:37], v[154:157], v[170:173], v[34:37]
	v_mfma_f32_16x16x32_bf16 v[22:25], v[146:149], v[178:181], v[22:25]
	v_mfma_f32_16x16x32_bf16 v[18:21], v[154:157], v[178:181], v[18:21]
	v_mfma_f32_16x16x32_bf16 v[6:9], v[146:149], v[202:205], v[6:9]
	v_mfma_f32_16x16x32_bf16 v[2:5], v[154:157], v[202:205], v[2:5]
	v_mfma_f32_16x16x32_bf16 v[54:57], v[150:153], v[166:169], v[54:57]
	v_mfma_f32_16x16x32_bf16 v[50:53], v[158:161], v[166:169], v[50:53]
	v_mfma_f32_16x16x32_bf16 v[38:41], v[150:153], v[174:177], v[38:41]
	v_mfma_f32_16x16x32_bf16 v[34:37], v[158:161], v[174:177], v[34:37]
	v_mfma_f32_16x16x32_bf16 v[22:25], v[150:153], v[182:185], v[22:25]
	v_mfma_f32_16x16x32_bf16 v[18:21], v[158:161], v[182:185], v[18:21]
	v_mfma_f32_16x16x32_bf16 v[6:9], v[150:153], v[206:209], v[6:9]
	v_mfma_f32_16x16x32_bf16 v[2:5], v[158:161], v[206:209], v[2:5]
	s_setprio 0
	s_barrier
	s_add_i32 s63, s63, 2
	s_add_u32 s34, s34, 0x100
	s_addc_u32 s35, s35, 0
	s_add_u32 s61, s61, 0x100
	s_addc_u32 s62, s62, 0
	s_cmp_gt_u32 s63, 13
.LBB0_1324:
	ds_read_b128 v[98:101], v225
	ds_read_b128 v[110:113], v225 offset:1024
	ds_read_b128 v[122:125], v225 offset:2048
	ds_read_b128 v[130:133], v225 offset:3072
	ds_read_b128 v[146:149], v226
	ds_read_b128 v[150:153], v226 offset:1024
	ds_read_b128 v[154:157], v226 offset:2048
	ds_read_b128 v[158:161], v226 offset:3072
	s_add_u32 s36, s34, 0xfffc0080
	s_addc_u32 s37, s35, -1
	s_cmp_eq_u32 s63, 12
	s_cselect_b32 s39, s25, s37
	s_cselect_b32 s38, s31, s36
	s_cselect_b32 s37, s23, s62
	s_cselect_b32 s36, s60, s61
	s_add_i32 m0, s41, 0xc000
	ds_read_b128 v[162:165], v227
	ds_read_b128 v[166:169], v227 offset:1024
	ds_read_b128 v[170:173], v227 offset:2048
	ds_read_b128 v[174:177], v227 offset:3072
	ds_read_b128 v[178:181], v227 offset:4096
	ds_read_b128 v[182:185], v227 offset:5120
	ds_read_b128 v[202:205], v227 offset:6144
	ds_read_b128 v[206:209], v227 offset:7168
	global_load_lds_dwordx4 v194, s[34:35]
	s_add_i32 m0, s41, 0xe000
	s_nop 0
	global_load_lds_dwordx4 v196, s[34:35]
	s_waitcnt vmcnt(8)
	s_waitcnt lgkmcnt(0)
	s_barrier
	s_setprio 3
	s_waitcnt lgkmcnt(0)
	v_mfma_f32_16x16x32_bf16 v[142:145], v[98:101], v[162:165], v[142:145]
	v_mfma_f32_16x16x32_bf16 v[138:141], v[122:125], v[162:165], v[138:141]
	v_mfma_f32_16x16x32_bf16 v[118:121], v[98:101], v[170:173], v[118:121]
	v_mfma_f32_16x16x32_bf16 v[114:117], v[122:125], v[170:173], v[114:117]
	v_mfma_f32_16x16x32_bf16 v[94:97], v[98:101], v[178:181], v[94:97]
	v_mfma_f32_16x16x32_bf16 v[90:93], v[122:125], v[178:181], v[90:93]
	v_mfma_f32_16x16x32_bf16 v[78:81], v[98:101], v[202:205], v[78:81]
	v_mfma_f32_16x16x32_bf16 v[74:77], v[122:125], v[202:205], v[74:77]
	v_mfma_f32_16x16x32_bf16 v[142:145], v[110:113], v[166:169], v[142:145]
	v_mfma_f32_16x16x32_bf16 v[138:141], v[130:133], v[166:169], v[138:141]
	v_mfma_f32_16x16x32_bf16 v[118:121], v[110:113], v[174:177], v[118:121]
	v_mfma_f32_16x16x32_bf16 v[114:117], v[130:133], v[174:177], v[114:117]
	v_mfma_f32_16x16x32_bf16 v[94:97], v[110:113], v[182:185], v[94:97]
	v_mfma_f32_16x16x32_bf16 v[90:93], v[130:133], v[182:185], v[90:93]
	v_mfma_f32_16x16x32_bf16 v[78:81], v[110:113], v[206:209], v[78:81]
	v_mfma_f32_16x16x32_bf16 v[74:77], v[130:133], v[206:209], v[74:77]
	v_mfma_f32_16x16x32_bf16 v[134:137], v[146:149], v[162:165], v[134:137]
	v_mfma_f32_16x16x32_bf16 v[126:129], v[154:157], v[162:165], v[126:129]
	v_mfma_f32_16x16x32_bf16 v[106:109], v[146:149], v[170:173], v[106:109]
	v_mfma_f32_16x16x32_bf16 v[102:105], v[154:157], v[170:173], v[102:105]
	v_mfma_f32_16x16x32_bf16 v[86:89], v[146:149], v[178:181], v[86:89]
	v_mfma_f32_16x16x32_bf16 v[82:85], v[154:157], v[178:181], v[82:85]
	v_mfma_f32_16x16x32_bf16 v[70:73], v[146:149], v[202:205], v[70:73]
	v_mfma_f32_16x16x32_bf16 v[66:69], v[154:157], v[202:205], v[66:69]
	v_mfma_f32_16x16x32_bf16 v[134:137], v[150:153], v[166:169], v[134:137]
	v_mfma_f32_16x16x32_bf16 v[126:129], v[158:161], v[166:169], v[126:129]
	v_mfma_f32_16x16x32_bf16 v[106:109], v[150:153], v[174:177], v[106:109]
	v_mfma_f32_16x16x32_bf16 v[102:105], v[158:161], v[174:177], v[102:105]
	v_mfma_f32_16x16x32_bf16 v[86:89], v[150:153], v[182:185], v[86:89]
	v_mfma_f32_16x16x32_bf16 v[82:85], v[158:161], v[182:185], v[82:85]
	v_mfma_f32_16x16x32_bf16 v[70:73], v[150:153], v[206:209], v[70:73]
	v_mfma_f32_16x16x32_bf16 v[66:69], v[158:161], v[206:209], v[66:69]
	s_setprio 0
	s_barrier
; #define PG8_STAGE_A(b, h, ptr, NX) do { if constexpr (Sched::GATHER) { unsigned gs_[2]; gs_[0] = ((NX) && last_) ? gN[h][0] : gA[h][0]; gs_[1] = ((NX) && last_) ? gN[h][1] : gA[h][1]; PG8_STAGE(PG8_SA(b, h), ptr, gs_); } \
;         else PG8_STAGE(PG8_SA(b, h), (ptr) + ((h) ? hstep : (size_t)0), voffA); } while (0)
; #define PG8_STAGE(bufoff, gbase, voff) do { _Pragma("unroll") for (int _i = 0; _i < 2; ++_i) \
;         __builtin_amdgcn_global_load_lds((const unsigned*)((const char*)(gbase) + (voff)[_i]), (PG8_LAS unsigned*)(lds + (bufoff) + ldsw + _i * 8192), 16, 0, 0); } while (0)
; #define PG8_LDA(dst, b, h) do { _Pragma("unroll") for (int m = 0; m < 4; ++m) _Pragma("unroll") for (int k = 0; k < 2; ++k) dst[m][k] = *(const PG8_LAS bf16x8*)(lds + PG8_SA(b, h) + aoff + m * 2048 + k * 1024); } while (0)
; #define PG8_LDB(dst, b, h) do { _Pragma("unroll") for (int n = 0; n < 2; ++n) _Pragma("unroll") for (int k = 0; k < 2; ++k) dst[n][k] = *(const PG8_LAS bf16x8*)(lds + PG8_SB(b, h) + boff + n * 2048 + k * 1024); } while (0)
; #define PG8_MMA(ai, bj, At, Bt) do { __builtin_amdgcn_s_setprio(1); _Pragma("unroll") for (int m = 0; m < 4; ++m) _Pragma("unroll") for (int n = 0; n < 2; ++n) _Pragma("unroll") for (int k = 0; k < 2; ++k) \
;         acc[ai][bj][m][n] = __builtin_amdgcn_mfma_f32_16x16x32_bf16(Bt[n][k], At[m][k], acc[ai][bj][m][n], 0, 0, 0); __builtin_amdgcn_s_setprio(0); } while (0)
; #define PG8_WAIT_V(n) asm volatile("s_waitcnt vmcnt(" #n ")" ::: "memory")
; #define PG8_WAIT_L(n) asm volatile("s_waitcnt lgkmcnt(" #n ")" ::: "memory")
; #define PG8_BAR __builtin_amdgcn_s_barrier()
; #define PG8_SCHED __builtin_amdgcn_sched_barrier(0)
; template <class Epi, class Sched, bool ALIGN_EPI = false, bool SP2 = false>
; __device__ __forceinline__ void gemm_phase(PG8_LAS unsigned char* lds, const Gemm g, const Sched& S, const Epi& E, const bool skip_epi = false) {
;     ...
;             PG8_LDA(At, 0, 1); PG8_STAGE(PG8_SB(0, 0), b2, voffB); PG8_STAGE(PG8_SB(0, 1), b2 + hstep, voffB); PG8_STAGE_A(0, 0, a2, true);
;             PG8_WAIT_V(8); PG8_WAIT_L(0); PG8_BAR; PG8_MMA(1, 0, At, B0); PG8_MMA(1, 1, At, B1); PG8_BAR; PG8_SCHED;
;             PG8_LDB(B0, 1, 0); PG8_LDB(B1, 1, 1); PG8_SCHED; PG8_LDA(At, 1, 0); PG8_STAGE_A(0, 1, a2, true);
;             PG8_WAIT_V(8); PG8_WAIT_L(0); PG8_BAR; PG8_MMA(0, 0, At, B0); PG8_MMA(0, 1, At, B1); PG8_BAR; PG8_SCHED;
	s_add_i32 s64, s57, s40
	s_mov_b32 m0, s64
	ds_read_b128 v[162:165], v227 offset:16384
	ds_read_b128 v[166:169], v227 offset:17408
	ds_read_b128 v[170:173], v227 offset:18432
	ds_read_b128 v[174:177], v227 offset:19456
	ds_read_b128 v[178:181], v227 offset:20480
	ds_read_b128 v[182:185], v227 offset:21504
	ds_read_b128 v[202:205], v227 offset:22528
	ds_read_b128 v[206:209], v227 offset:23552
	global_load_lds_dwordx4 v188, s[36:37]
	s_add_i32 m0, s64, 0x2000
	s_add_u32 s64, s36, 0x40000
	s_addc_u32 s65, s37, 0
	s_add_i32 s66, s58, s40
	global_load_lds_dwordx4 v192, s[36:37]
	s_mov_b32 m0, s66
	s_mov_b64 s[98:99], s[38:39]
	global_load_lds_dwordx4 v188, s[64:65]
	s_add_i32 m0, s66, 0x2000
	s_nop 0
	global_load_lds_dwordx4 v192, s[64:65]
	s_mov_b32 m0, s41
	s_nop 0
	global_load_lds_dwordx4 v186, s[38:39]
	s_mov_b32 m0, s44
	s_nop 0
	global_load_lds_dwordx4 v190, s[38:39]
	s_waitcnt vmcnt(8)
	s_waitcnt lgkmcnt(0)
	s_barrier
	s_setprio 3
	s_waitcnt lgkmcnt(0)
	v_mfma_f32_16x16x32_bf16 v[62:65], v[98:101], v[162:165], v[62:65]
	v_mfma_f32_16x16x32_bf16 v[58:61], v[122:125], v[162:165], v[58:61]
	v_mfma_f32_16x16x32_bf16 v[46:49], v[98:101], v[170:173], v[46:49]
	v_mfma_f32_16x16x32_bf16 v[42:45], v[122:125], v[170:173], v[42:45]
	v_mfma_f32_16x16x32_bf16 v[30:33], v[98:101], v[178:181], v[30:33]
	v_mfma_f32_16x16x32_bf16 v[26:29], v[122:125], v[178:181], v[26:29]
	v_mfma_f32_16x16x32_bf16 v[14:17], v[98:101], v[202:205], v[14:17]
	v_mfma_f32_16x16x32_bf16 v[10:13], v[122:125], v[202:205], v[10:13]
	v_mfma_f32_16x16x32_bf16 v[62:65], v[110:113], v[166:169], v[62:65]
	v_mfma_f32_16x16x32_bf16 v[58:61], v[130:133], v[166:169], v[58:61]
	v_mfma_f32_16x16x32_bf16 v[46:49], v[110:113], v[174:177], v[46:49]
	v_mfma_f32_16x16x32_bf16 v[42:45], v[130:133], v[174:177], v[42:45]
	v_mfma_f32_16x16x32_bf16 v[30:33], v[110:113], v[182:185], v[30:33]
	v_mfma_f32_16x16x32_bf16 v[26:29], v[130:133], v[182:185], v[26:29]
	v_mfma_f32_16x16x32_bf16 v[14:17], v[110:113], v[206:209], v[14:17]
	v_mfma_f32_16x16x32_bf16 v[10:13], v[130:133], v[206:209], v[10:13]
	v_mfma_f32_16x16x32_bf16 v[54:57], v[146:149], v[162:165], v[54:57]
	v_mfma_f32_16x16x32_bf16 v[50:53], v[154:157], v[162:165], v[50:53]
	v_mfma_f32_16x16x32_bf16 v[38:41], v[146:149], v[170:173], v[38:41]
	v_mfma_f32_16x16x32_bf16 v[34:37], v[154:157], v[170:173], v[34:37]
	v_mfma_f32_16x16x32_bf16 v[22:25], v[146:149], v[178:181], v[22:25]
	v_mfma_f32_16x16x32_bf16 v[18:21], v[154:157], v[178:181], v[18:21]
	v_mfma_f32_16x16x32_bf16 v[6:9], v[146:149], v[202:205], v[6:9]
	v_mfma_f32_16x16x32_bf16 v[2:5], v[154:157], v[202:205], v[2:5]
	v_mfma_f32_16x16x32_bf16 v[54:57], v[150:153], v[166:169], v[54:57]
	v_mfma_f32_16x16x32_bf16 v[50:53], v[158:161], v[166:169], v[50:53]
	v_mfma_f32_16x16x32_bf16 v[38:41], v[150:153], v[174:177], v[38:41]
	v_mfma_f32_16x16x32_bf16 v[34:37], v[158:161], v[174:177], v[34:37]
	v_mfma_f32_16x16x32_bf16 v[22:25], v[150:153], v[182:185], v[22:25]
	v_mfma_f32_16x16x32_bf16 v[18:21], v[158:161], v[182:185], v[18:21]
	v_mfma_f32_16x16x32_bf16 v[6:9], v[150:153], v[206:209], v[6:9]
	v_mfma_f32_16x16x32_bf16 v[2:5], v[158:161], v[206:209], v[2:5]
	s_setprio 0
	s_barrier
	s_add_i32 s64, 0, 0x18000
	s_add_i32 s65, 0, 0x1c000
	v_add_u32_e32 v130, s64, v220
	v_add_u32_e32 v158, s65, v220
	ds_read_b128 v[98:101], v130
	ds_read_b128 v[110:113], v130 offset:1024
	ds_read_b128 v[122:125], v130 offset:2048
	ds_read_b128 v[130:133], v130 offset:3072
	ds_read_b128 v[146:149], v158
	ds_read_b128 v[150:153], v158 offset:1024
	ds_read_b128 v[154:157], v158 offset:2048
	ds_read_b128 v[158:161], v158 offset:3072
	s_add_u32 s38, s38, 0x40000
	s_addc_u32 s39, s39, 0
	s_mov_b32 m0, s45
	ds_read_b128 v[162:165], v227 offset:32768
	ds_read_b128 v[166:169], v227 offset:33792
	ds_read_b128 v[170:173], v227 offset:34816
	ds_read_b128 v[174:177], v227 offset:35840
	ds_read_b128 v[178:181], v227 offset:36864
	ds_read_b128 v[182:185], v227 offset:37888
	ds_read_b128 v[202:205], v227 offset:38912
	ds_read_b128 v[206:209], v227 offset:39936
	global_load_lds_dwordx4 v186, s[38:39]
	s_mov_b32 m0, s48
	s_nop 0
	global_load_lds_dwordx4 v190, s[38:39]
	s_waitcnt vmcnt(8)
	s_waitcnt lgkmcnt(0)
	s_barrier
; #define PG8_STAGE_A(b, h, ptr, NX) do { if constexpr (Sched::GATHER) { unsigned gs_[2]; gs_[0] = ((NX) && last_) ? gN[h][0] : gA[h][0]; gs_[1] = ((NX) && last_) ? gN[h][1] : gA[h][1]; PG8_STAGE(PG8_SA(b, h), ptr, gs_); } \
;         else PG8_STAGE(PG8_SA(b, h), (ptr) + ((h) ? hstep : (size_t)0), voffA); } while (0)
; #define PG8_STAGE(bufoff, gbase, voff) do { _Pragma("unroll") for (int _i = 0; _i < 2; ++_i) \
;         __builtin_amdgcn_global_load_lds((const unsigned*)((const char*)(gbase) + (voff)[_i]), (PG8_LAS unsigned*)(lds + (bufoff) + ldsw + _i * 8192), 16, 0, 0); } while (0)
; #define PG8_LDA(dst, b, h) do { _Pragma("unroll") for (int m = 0; m < 4; ++m) _Pragma("unroll") for (int k = 0; k < 2; ++k) dst[m][k] = *(const PG8_LAS bf16x8*)(lds + PG8_SA(b, h) + aoff + m * 2048 + k * 1024); } while (0)
; #define PG8_MMA(ai, bj, At, Bt) do { __builtin_amdgcn_s_setprio(1); _Pragma("unroll") for (int m = 0; m < 4; ++m) _Pragma("unroll") for (int n = 0; n < 2; ++n) _Pragma("unroll") for (int k = 0; k < 2; ++k) \
;         acc[ai][bj][m][n] = __builtin_amdgcn_mfma_f32_16x16x32_bf16(Bt[n][k], At[m][k], acc[ai][bj][m][n], 0, 0, 0); __builtin_amdgcn_s_setprio(0); } while (0)
; #define PG8_WAIT_V(n) asm volatile("s_waitcnt vmcnt(" #n ")" ::: "memory")
; #define PG8_WAIT_L(n) asm volatile("s_waitcnt lgkmcnt(" #n ")" ::: "memory")
; #define PG8_BAR __builtin_amdgcn_s_barrier()
; #define PG8_SCHED __builtin_amdgcn_sched_barrier(0)
; template <class Epi, class Sched, bool ALIGN_EPI = false, bool SP2 = false>
; __device__ __forceinline__ void gemm_phase(PG8_LAS unsigned char* lds, const Gemm g, const Sched& S, const Epi& E, const bool skip_epi = false) {
;     ...
;             PG8_WAIT_V(8); PG8_WAIT_L(0); PG8_BAR; PG8_MMA(0, 0, At, B0); PG8_MMA(0, 1, At, B1); PG8_BAR; PG8_SCHED;
;             PG8_LDA(At, 1, 1); PG8_STAGE(PG8_SB(1, 0), b3, voffB); PG8_STAGE(PG8_SB(1, 1), b3 + hstep, voffB); PG8_STAGE_A(1, 0, a3, true);
;             PG8_WAIT_V(8); PG8_WAIT_L(0); PG8_BAR; PG8_MMA(1, 0, At, B0); PG8_MMA(1, 1, At, B1); PG8_BAR; PG8_SCHED;
	s_setprio 3
	s_waitcnt lgkmcnt(0)
	v_mfma_f32_16x16x32_bf16 v[142:145], v[98:101], v[162:165], v[142:145]
	v_mfma_f32_16x16x32_bf16 v[138:141], v[122:125], v[162:165], v[138:141]
	v_mfma_f32_16x16x32_bf16 v[118:121], v[98:101], v[170:173], v[118:121]
	v_mfma_f32_16x16x32_bf16 v[114:117], v[122:125], v[170:173], v[114:117]
	v_mfma_f32_16x16x32_bf16 v[94:97], v[98:101], v[178:181], v[94:97]
	v_mfma_f32_16x16x32_bf16 v[90:93], v[122:125], v[178:181], v[90:93]
	v_mfma_f32_16x16x32_bf16 v[78:81], v[98:101], v[202:205], v[78:81]
	v_mfma_f32_16x16x32_bf16 v[74:77], v[122:125], v[202:205], v[74:77]
	v_mfma_f32_16x16x32_bf16 v[142:145], v[110:113], v[166:169], v[142:145]
	v_mfma_f32_16x16x32_bf16 v[138:141], v[130:133], v[166:169], v[138:141]
	v_mfma_f32_16x16x32_bf16 v[118:121], v[110:113], v[174:177], v[118:121]
	v_mfma_f32_16x16x32_bf16 v[114:117], v[130:133], v[174:177], v[114:117]
	v_mfma_f32_16x16x32_bf16 v[94:97], v[110:113], v[182:185], v[94:97]
	v_mfma_f32_16x16x32_bf16 v[90:93], v[130:133], v[182:185], v[90:93]
	v_mfma_f32_16x16x32_bf16 v[78:81], v[110:113], v[206:209], v[78:81]
	v_mfma_f32_16x16x32_bf16 v[74:77], v[130:133], v[206:209], v[74:77]
	v_mfma_f32_16x16x32_bf16 v[134:137], v[146:149], v[162:165], v[134:137]
	v_mfma_f32_16x16x32_bf16 v[126:129], v[154:157], v[162:165], v[126:129]
	v_mfma_f32_16x16x32_bf16 v[106:109], v[146:149], v[170:173], v[106:109]
	v_mfma_f32_16x16x32_bf16 v[102:105], v[154:157], v[170:173], v[102:105]
	v_mfma_f32_16x16x32_bf16 v[86:89], v[146:149], v[178:181], v[86:89]
	v_mfma_f32_16x16x32_bf16 v[82:85], v[154:157], v[178:181], v[82:85]
	v_mfma_f32_16x16x32_bf16 v[70:73], v[146:149], v[202:205], v[70:73]
	v_mfma_f32_16x16x32_bf16 v[66:69], v[154:157], v[202:205], v[66:69]
	v_mfma_f32_16x16x32_bf16 v[134:137], v[150:153], v[166:169], v[134:137]
	v_mfma_f32_16x16x32_bf16 v[126:129], v[158:161], v[166:169], v[126:129]
	v_mfma_f32_16x16x32_bf16 v[106:109], v[150:153], v[174:177], v[106:109]
	v_mfma_f32_16x16x32_bf16 v[102:105], v[158:161], v[174:177], v[102:105]
	v_mfma_f32_16x16x32_bf16 v[86:89], v[150:153], v[182:185], v[86:89]
	v_mfma_f32_16x16x32_bf16 v[82:85], v[158:161], v[182:185], v[82:85]
	v_mfma_f32_16x16x32_bf16 v[70:73], v[150:153], v[206:209], v[70:73]
	v_mfma_f32_16x16x32_bf16 v[66:69], v[158:161], v[206:209], v[66:69]
	s_setprio 0
	s_barrier
	s_add_i32 s38, s64, s40
	s_add_i32 m0, s38, 0xffffff80
	ds_read_b128 v[162:165], v227 offset:49152
	ds_read_b128 v[166:169], v227 offset:50176
	ds_read_b128 v[170:173], v227 offset:51200
	ds_read_b128 v[174:177], v227 offset:52224
	ds_read_b128 v[178:181], v227 offset:53248
	ds_read_b128 v[182:185], v227 offset:54272
	ds_read_b128 v[202:205], v227 offset:55296
	ds_read_b128 v[206:209], v227 offset:56320
	global_load_lds_dwordx4 v188, s[36:37] offset:128
	s_add_i32 m0, s38, 0x1f80
	s_add_i32 s38, s65, s40
	global_load_lds_dwordx4 v192, s[36:37] offset:128
	s_add_u32 s36, s36, 0x40080
	s_addc_u32 s37, s37, 0
	s_mov_b32 m0, s38
	s_nop 0
	global_load_lds_dwordx4 v188, s[36:37]
	s_add_i32 m0, s38, 0x2000
	s_nop 0
	global_load_lds_dwordx4 v192, s[36:37]
	s_add_i32 m0, s53, 0xffffff80
	s_nop 0
	global_load_lds_dwordx4 v186, s[98:99] offset:128
	s_add_i32 m0, s54, 0xffffff80
	s_nop 0
	global_load_lds_dwordx4 v190, s[98:99] offset:128
	s_waitcnt vmcnt(8)
	s_waitcnt lgkmcnt(0)
	s_barrier
	s_setprio 3
	s_waitcnt lgkmcnt(0)
	v_mfma_f32_16x16x32_bf16 v[62:65], v[98:101], v[162:165], v[62:65]
	v_mfma_f32_16x16x32_bf16 v[58:61], v[122:125], v[162:165], v[58:61]
	v_mfma_f32_16x16x32_bf16 v[46:49], v[98:101], v[170:173], v[46:49]
	v_mfma_f32_16x16x32_bf16 v[42:45], v[122:125], v[170:173], v[42:45]
	v_mfma_f32_16x16x32_bf16 v[30:33], v[98:101], v[178:181], v[30:33]
	v_mfma_f32_16x16x32_bf16 v[26:29], v[122:125], v[178:181], v[26:29]
	v_mfma_f32_16x16x32_bf16 v[14:17], v[98:101], v[202:205], v[14:17]
	v_mfma_f32_16x16x32_bf16 v[10:13], v[122:125], v[202:205], v[10:13]
	v_mfma_f32_16x16x32_bf16 v[62:65], v[110:113], v[166:169], v[62:65]
	v_mfma_f32_16x16x32_bf16 v[58:61], v[130:133], v[166:169], v[58:61]
	v_mfma_f32_16x16x32_bf16 v[46:49], v[110:113], v[174:177], v[46:49]
	v_mfma_f32_16x16x32_bf16 v[42:45], v[130:133], v[174:177], v[42:45]
	v_mfma_f32_16x16x32_bf16 v[30:33], v[110:113], v[182:185], v[30:33]
	v_mfma_f32_16x16x32_bf16 v[26:29], v[130:133], v[182:185], v[26:29]
	v_mfma_f32_16x16x32_bf16 v[14:17], v[110:113], v[206:209], v[14:17]
	v_mfma_f32_16x16x32_bf16 v[10:13], v[130:133], v[206:209], v[10:13]
	v_mfma_f32_16x16x32_bf16 v[54:57], v[146:149], v[162:165], v[54:57]
	v_mfma_f32_16x16x32_bf16 v[50:53], v[154:157], v[162:165], v[50:53]
	v_mfma_f32_16x16x32_bf16 v[38:41], v[146:149], v[170:173], v[38:41]
	v_mfma_f32_16x16x32_bf16 v[34:37], v[154:157], v[170:173], v[34:37]
	v_mfma_f32_16x16x32_bf16 v[22:25], v[146:149], v[178:181], v[22:25]
	v_mfma_f32_16x16x32_bf16 v[18:21], v[154:157], v[178:181], v[18:21]
	v_mfma_f32_16x16x32_bf16 v[6:9], v[146:149], v[202:205], v[6:9]
	v_mfma_f32_16x16x32_bf16 v[2:5], v[154:157], v[202:205], v[2:5]
	v_mfma_f32_16x16x32_bf16 v[54:57], v[150:153], v[166:169], v[54:57]
	v_mfma_f32_16x16x32_bf16 v[50:53], v[158:161], v[166:169], v[50:53]
	v_mfma_f32_16x16x32_bf16 v[38:41], v[150:153], v[174:177], v[38:41]
	v_mfma_f32_16x16x32_bf16 v[34:37], v[158:161], v[174:177], v[34:37]
	v_mfma_f32_16x16x32_bf16 v[22:25], v[150:153], v[182:185], v[22:25]
	v_mfma_f32_16x16x32_bf16 v[18:21], v[158:161], v[182:185], v[18:21]
	v_mfma_f32_16x16x32_bf16 v[6:9], v[150:153], v[206:209], v[6:9]
	v_mfma_f32_16x16x32_bf16 v[2:5], v[158:161], v[206:209], v[2:5]
	s_setprio 0
	s_barrier
	s_add_i32 s63, s63, 2
	s_add_u32 s34, s34, 0x100
	s_addc_u32 s35, s35, 0
	s_add_u32 s61, s61, 0x100
	s_addc_u32 s62, s62, 0
	s_cmp_gt_u32 s63, 13
	s_cbranch_scc0 .LBB0_1324
	s_and_b64 vcc, exec, s[14:15]
	s_cbranch_vccz .LBB0_1327
	s_barrier

; #define PG8_STAGE_A(b, h, ptr, NX) do { if constexpr (Sched::GATHER) { unsigned gs_[2]; gs_[0] = ((NX) && last_) ? gN[h][0] : gA[h][0]; gs_[1] = ((NX) && last_) ? gN[h][1] : gA[h][1]; PG8_STAGE(PG8_SA(b, h), ptr, gs_); } \
;         else PG8_STAGE(PG8_SA(b, h), (ptr) + ((h) ? hstep : (size_t)0), voffA); } while (0)
; #define PG8_LDA(dst, b, h) do { _Pragma("unroll") for (int m = 0; m < 4; ++m) _Pragma("unroll") for (int k = 0; k < 2; ++k) dst[m][k] = *(const PG8_LAS bf16x8*)(lds + PG8_SA(b, h) + aoff + m * 2048 + k * 1024); } while (0)
; #define PG8_LDB(dst, b, h) do { _Pragma("unroll") for (int n = 0; n < 2; ++n) _Pragma("unroll") for (int k = 0; k < 2; ++k) dst[n][k] = *(const PG8_LAS bf16x8*)(lds + PG8_SB(b, h) + boff + n * 2048 + k * 1024); } while (0)
; #define PG8_MMA(ai, bj, At, Bt) do { __builtin_amdgcn_s_setprio(1); _Pragma("unroll") for (int m = 0; m < 4; ++m) _Pragma("unroll") for (int n = 0; n < 2; ++n) _Pragma("unroll") for (int k = 0; k < 2; ++k) \
;         acc[ai][bj][m][n] = __builtin_amdgcn_mfma_f32_16x16x32_bf16(Bt[n][k], At[m][k], acc[ai][bj][m][n], 0, 0, 0); __builtin_amdgcn_s_setprio(0); } while (0)
; #define PG8_WAIT_V(n) asm volatile("s_waitcnt vmcnt(" #n ")" ::: "memory")
; #define PG8_BAR __builtin_amdgcn_s_barrier()
; template <class Epi, class Sched, bool ALIGN_EPI = false, bool SP2 = false>
; __device__ __forceinline__ void gemm_phase(PG8_LAS unsigned char* lds, const Gemm g, const Sched& S, const Epi& E, const bool skip_epi = false) {
;     ...
;         const char* nA = has_next ? (const char*)g.A + (size_t)nxt.pm * pmstepA + nxt.ko : cA; const char* nB = has_next ? (const char*)g.Bt + (size_t)nxt.pn * tstep + nxt.ko : cB;
;         for (int t = 0; t < nt; t += 2) {
;             const bool last = (t == nt - 2); last_ = last && has_next;
;             const char* a1 = cA + (size_t)(t + 1) * kstep;
;             const char* a2 = last ? nA : cA + (size_t)(t + 2) * kstep; const char* b2 = last ? nB : cB + (size_t)(t + 2) * kstep;
;             const char* a3 = a2 + kstep; const char* b3 = b2 + kstep;
;             if (last && has_next) S.a_ready(nxt);
;             if constexpr (SP2) {
;             PG8_LDB(B0, 0, 0); PG8_LDB(B1, 0, 1); PG8_SCHED; PG8_LDA(At, 0, 0); PG8_STAGE_A(1, 1, a1, false);
;             PG8_WAIT_V(8); PG8_WAIT_L(0); PG8_BAR; PG8_MMA(0, 0, At, B0); PG8_MMA(0, 1, At, B1); PG8_BAR; PG8_SCHED;
.Lg5_zero:
.LBB0_1727:
	s_mov_b32 s29, s41
	s_mov_b32 s31, s40
	v_mov_b32_e32 v143, v133
	v_mov_b32_e32 v141, v133
	s_add_u32 s61, s40, 0x100
	v_lshl_add_u64 v[146:147], s[24:25], 0, v[140:141]
	v_lshl_add_u64 v[148:149], s[24:25], 0, v[142:143]
	s_addc_u32 s62, s41, 0
	s_mov_b32 s63, -2
	s_mov_b64 s[40:41], 0
	ds_read_b128 v[166:169], v158
	ds_read_b128 v[170:173], v158 offset:1024
	ds_read_b128 v[174:177], v158 offset:2048
	ds_read_b128 v[178:181], v158 offset:3072
	ds_read_b128 v[182:185], v159
	ds_read_b128 v[186:189], v159 offset:1024
	ds_read_b128 v[190:193], v159 offset:2048
	ds_read_b128 v[194:197], v159 offset:3072
	s_add_u32 s42, s78, s40
	s_addc_u32 s43, s79, s41
	s_add_u32 s44, s42, 0x1aa00100
	s_addc_u32 s45, s43, 0
	s_add_u32 s66, s61, s40
	s_addc_u32 s67, s62, s41
	s_cmpk_eq_i32 s40, 0x700
	s_cselect_b64 s[64:65], -1, 0
	s_and_b64 s[42:43], s[64:65], exec
	s_cselect_b32 s45, s87, s45
	s_cselect_b32 s44, s86, s44
	s_cselect_b32 s42, s31, s66
	s_cselect_b32 s43, s29, s67
	s_and_b64 vcc, s[6:7], s[64:65]
	v_lshl_add_u64 v[226:227], v[148:149], 0, s[40:41]
	s_add_i32 m0, s37, 0xc000
	ds_read_b128 v[198:201], v160
	ds_read_b128 v[202:205], v160 offset:1024
	ds_read_b128 v[206:209], v160 offset:2048
	ds_read_b128 v[210:213], v160 offset:3072
	ds_read_b128 v[214:217], v160 offset:4096
	ds_read_b128 v[218:221], v160 offset:5120
	ds_read_b128 v[222:225], v160 offset:6144
	ds_read_b128 v[230:233], v160 offset:7168
	global_load_lds_dwordx4 v[226:227], off
	v_lshl_add_u64 v[226:227], v[146:147], 0, s[40:41]
	s_add_i32 m0, s37, 0xe000
	s_nop 0
	global_load_lds_dwordx4 v[226:227], off
	s_waitcnt vmcnt(8)
	s_waitcnt lgkmcnt(0)
	s_barrier
	s_setprio 3
	s_waitcnt lgkmcnt(0)
	v_mfma_f32_16x16x32_bf16 v[126:129], v[166:169], v[198:201], 0
	v_mfma_f32_16x16x32_bf16 v[122:125], v[174:177], v[198:201], 0
	v_mfma_f32_16x16x32_bf16 v[110:113], v[166:169], v[206:209], 0
	v_mfma_f32_16x16x32_bf16 v[106:109], v[174:177], v[206:209], 0
	v_mfma_f32_16x16x32_bf16 v[94:97], v[166:169], v[214:217], 0
	v_mfma_f32_16x16x32_bf16 v[90:93], v[174:177], v[214:217], 0
	v_mfma_f32_16x16x32_bf16 v[78:81], v[166:169], v[222:225], 0
	v_mfma_f32_16x16x32_bf16 v[74:77], v[174:177], v[222:225], 0
	v_mfma_f32_16x16x32_bf16 v[126:129], v[170:173], v[202:205], v[126:129]
	v_mfma_f32_16x16x32_bf16 v[122:125], v[178:181], v[202:205], v[122:125]
	v_mfma_f32_16x16x32_bf16 v[110:113], v[170:173], v[210:213], v[110:113]
	v_mfma_f32_16x16x32_bf16 v[106:109], v[178:181], v[210:213], v[106:109]
	v_mfma_f32_16x16x32_bf16 v[94:97], v[170:173], v[218:221], v[94:97]
	v_mfma_f32_16x16x32_bf16 v[90:93], v[178:181], v[218:221], v[90:93]
	v_mfma_f32_16x16x32_bf16 v[78:81], v[170:173], v[230:233], v[78:81]
	v_mfma_f32_16x16x32_bf16 v[74:77], v[178:181], v[230:233], v[74:77]
	v_mfma_f32_16x16x32_bf16 v[118:121], v[182:185], v[198:201], 0
	v_mfma_f32_16x16x32_bf16 v[114:117], v[190:193], v[198:201], 0
	v_mfma_f32_16x16x32_bf16 v[102:105], v[182:185], v[206:209], 0
	v_mfma_f32_16x16x32_bf16 v[98:101], v[190:193], v[206:209], 0
	v_mfma_f32_16x16x32_bf16 v[86:89], v[182:185], v[214:217], 0
	v_mfma_f32_16x16x32_bf16 v[82:85], v[190:193], v[214:217], 0
	v_mfma_f32_16x16x32_bf16 v[70:73], v[182:185], v[222:225], 0
	v_mfma_f32_16x16x32_bf16 v[66:69], v[190:193], v[222:225], 0
	v_mfma_f32_16x16x32_bf16 v[118:121], v[186:189], v[202:205], v[118:121]
	v_mfma_f32_16x16x32_bf16 v[114:117], v[194:197], v[202:205], v[114:117]
	v_mfma_f32_16x16x32_bf16 v[102:105], v[186:189], v[210:213], v[102:105]
	v_mfma_f32_16x16x32_bf16 v[98:101], v[194:197], v[210:213], v[98:101]
	v_mfma_f32_16x16x32_bf16 v[86:89], v[186:189], v[218:221], v[86:89]
	v_mfma_f32_16x16x32_bf16 v[82:85], v[194:197], v[218:221], v[82:85]
	v_mfma_f32_16x16x32_bf16 v[70:73], v[186:189], v[230:233], v[70:73]
	v_mfma_f32_16x16x32_bf16 v[66:69], v[194:197], v[230:233], v[66:69]
	s_setprio 0
	s_barrier
	s_add_i32 s64, s58, s50
	s_mov_b32 m0, s64
	ds_read_b128 v[198:201], v160 offset:16384
	ds_read_b128 v[202:205], v160 offset:17408
	ds_read_b128 v[206:209], v160 offset:18432
	ds_read_b128 v[210:213], v160 offset:19456
	ds_read_b128 v[214:217], v160 offset:20480
	ds_read_b128 v[218:221], v160 offset:21504
	ds_read_b128 v[222:225], v160 offset:22528
	ds_read_b128 v[230:233], v160 offset:23552
	global_load_lds_dwordx4 v134, s[42:43]
	s_add_i32 m0, s64, 0x2000
	s_add_u32 s64, s42, 0x40000
	s_addc_u32 s65, s43, 0
	s_add_i32 s66, s59, s50
	global_load_lds_dwordx4 v136, s[42:43]
	s_mov_b32 m0, s66
	v_cndmask_b32_e32 v132, v130, v164, vcc
	global_load_lds_dwordx4 v134, s[64:65]
	s_add_i32 m0, s66, 0x2000
	v_lshl_add_u64 v[238:239], s[44:45], 0, v[132:133]
	global_load_lds_dwordx4 v136, s[64:65]
	s_mov_b32 m0, s37
	v_cndmask_b32_e32 v236, v144, v163, vcc
	global_load_lds_dwordx4 v132, s[44:45]
	s_mov_b32 m0, s39
	v_mov_b32_e32 v237, v133
	global_load_lds_dwordx4 v236, s[44:45]
	s_waitcnt vmcnt(8)
	s_waitcnt lgkmcnt(0)
	v_lshl_add_u64 v[236:237], s[44:45], 0, v[236:237]
	s_barrier
; #define PG8_STAGE_A(b, h, ptr, NX) do { if constexpr (Sched::GATHER) { unsigned gs_[2]; gs_[0] = ((NX) && last_) ? gN[h][0] : gA[h][0]; gs_[1] = ((NX) && last_) ? gN[h][1] : gA[h][1]; PG8_STAGE(PG8_SA(b, h), ptr, gs_); } \
;         else PG8_STAGE(PG8_SA(b, h), (ptr) + ((h) ? hstep : (size_t)0), voffA); } while (0)
; #define PG8_STAGE(bufoff, gbase, voff) do { _Pragma("unroll") for (int _i = 0; _i < 2; ++_i) \
;         __builtin_amdgcn_global_load_lds((const unsigned*)((const char*)(gbase) + (voff)[_i]), (PG8_LAS unsigned*)(lds + (bufoff) + ldsw + _i * 8192), 16, 0, 0); } while (0)
; #define PG8_LDA(dst, b, h) do { _Pragma("unroll") for (int m = 0; m < 4; ++m) _Pragma("unroll") for (int k = 0; k < 2; ++k) dst[m][k] = *(const PG8_LAS bf16x8*)(lds + PG8_SA(b, h) + aoff + m * 2048 + k * 1024); } while (0)
; #define PG8_LDB(dst, b, h) do { _Pragma("unroll") for (int n = 0; n < 2; ++n) _Pragma("unroll") for (int k = 0; k < 2; ++k) dst[n][k] = *(const PG8_LAS bf16x8*)(lds + PG8_SB(b, h) + boff + n * 2048 + k * 1024); } while (0)
; #define PG8_MMA(ai, bj, At, Bt) do { __builtin_amdgcn_s_setprio(1); _Pragma("unroll") for (int m = 0; m < 4; ++m) _Pragma("unroll") for (int n = 0; n < 2; ++n) _Pragma("unroll") for (int k = 0; k < 2; ++k) \
;         acc[ai][bj][m][n] = __builtin_amdgcn_mfma_f32_16x16x32_bf16(Bt[n][k], At[m][k], acc[ai][bj][m][n], 0, 0, 0); __builtin_amdgcn_s_setprio(0); } while (0)
; #define PG8_WAIT_V(n) asm volatile("s_waitcnt vmcnt(" #n ")" ::: "memory")
; #define PG8_WAIT_L(n) asm volatile("s_waitcnt lgkmcnt(" #n ")" ::: "memory")
; #define PG8_BAR __builtin_amdgcn_s_barrier()
; #define PG8_SCHED __builtin_amdgcn_sched_barrier(0)
; template <class Epi, class Sched, bool ALIGN_EPI = false, bool SP2 = false>
; __device__ __forceinline__ void gemm_phase(PG8_LAS unsigned char* lds, const Gemm g, const Sched& S, const Epi& E, const bool skip_epi = false) {
;     ...
;             PG8_LDA(At, 0, 1); PG8_STAGE(PG8_SB(0, 0), b2, voffB); PG8_STAGE(PG8_SB(0, 1), b2 + hstep, voffB); PG8_STAGE_A(0, 0, a2, true);
;             PG8_WAIT_V(8); PG8_WAIT_L(0); PG8_BAR; PG8_MMA(1, 0, At, B0); PG8_MMA(1, 1, At, B1); PG8_BAR; PG8_SCHED;
;             PG8_LDB(B0, 1, 0); PG8_LDB(B1, 1, 1); PG8_SCHED; PG8_LDA(At, 1, 0); PG8_STAGE_A(0, 1, a2, true);
;             PG8_WAIT_V(8); PG8_WAIT_L(0); PG8_BAR; PG8_MMA(0, 0, At, B0); PG8_MMA(0, 1, At, B1); PG8_BAR; PG8_SCHED;
	s_setprio 3
	s_waitcnt lgkmcnt(0)
	v_mfma_f32_16x16x32_bf16 v[62:65], v[166:169], v[198:201], 0
	v_mfma_f32_16x16x32_bf16 v[58:61], v[174:177], v[198:201], 0
	v_mfma_f32_16x16x32_bf16 v[38:41], v[166:169], v[206:209], 0
	v_mfma_f32_16x16x32_bf16 v[34:37], v[174:177], v[206:209], 0
	v_mfma_f32_16x16x32_bf16 v[22:25], v[166:169], v[214:217], 0
	v_mfma_f32_16x16x32_bf16 v[18:21], v[174:177], v[214:217], 0
	v_mfma_f32_16x16x32_bf16 v[6:9], v[166:169], v[222:225], 0
	v_mfma_f32_16x16x32_bf16 v[2:5], v[174:177], v[222:225], 0
	v_mfma_f32_16x16x32_bf16 v[62:65], v[170:173], v[202:205], v[62:65]
	v_mfma_f32_16x16x32_bf16 v[58:61], v[178:181], v[202:205], v[58:61]
	v_mfma_f32_16x16x32_bf16 v[38:41], v[170:173], v[210:213], v[38:41]
	v_mfma_f32_16x16x32_bf16 v[34:37], v[178:181], v[210:213], v[34:37]
	v_mfma_f32_16x16x32_bf16 v[22:25], v[170:173], v[218:221], v[22:25]
	v_mfma_f32_16x16x32_bf16 v[18:21], v[178:181], v[218:221], v[18:21]
	v_mfma_f32_16x16x32_bf16 v[6:9], v[170:173], v[230:233], v[6:9]
	v_mfma_f32_16x16x32_bf16 v[2:5], v[178:181], v[230:233], v[2:5]
	v_mfma_f32_16x16x32_bf16 v[50:53], v[182:185], v[198:201], 0
	v_mfma_f32_16x16x32_bf16 v[42:45], v[190:193], v[198:201], 0
	v_mfma_f32_16x16x32_bf16 v[54:57], v[182:185], v[206:209], 0
	v_mfma_f32_16x16x32_bf16 v[46:49], v[190:193], v[206:209], 0
	v_mfma_f32_16x16x32_bf16 v[30:33], v[182:185], v[214:217], 0
	v_mfma_f32_16x16x32_bf16 v[26:29], v[190:193], v[214:217], 0
	v_mfma_f32_16x16x32_bf16 v[14:17], v[182:185], v[222:225], 0
	v_mfma_f32_16x16x32_bf16 v[10:13], v[190:193], v[222:225], 0
	v_mfma_f32_16x16x32_bf16 v[50:53], v[186:189], v[202:205], v[50:53]
	v_mfma_f32_16x16x32_bf16 v[42:45], v[194:197], v[202:205], v[42:45]
	v_mfma_f32_16x16x32_bf16 v[54:57], v[186:189], v[210:213], v[54:57]
	v_mfma_f32_16x16x32_bf16 v[46:49], v[194:197], v[210:213], v[46:49]
	v_mfma_f32_16x16x32_bf16 v[30:33], v[186:189], v[218:221], v[30:33]
	v_mfma_f32_16x16x32_bf16 v[26:29], v[194:197], v[218:221], v[26:29]
	v_mfma_f32_16x16x32_bf16 v[14:17], v[186:189], v[230:233], v[14:17]
	v_mfma_f32_16x16x32_bf16 v[10:13], v[194:197], v[230:233], v[10:13]
	s_setprio 0
	s_barrier
	s_add_i32 s64, 0, 0x18000
	v_add_u32_e32 v132, s64, v154
	s_add_i32 s65, 0, 0x1c000
	ds_read_b128 v[166:169], v132
	ds_read_b128 v[170:173], v132 offset:1024
	ds_read_b128 v[174:177], v132 offset:2048
	ds_read_b128 v[178:181], v132 offset:3072
	v_add_u32_e32 v132, s65, v154
	ds_read_b128 v[182:185], v132
	ds_read_b128 v[186:189], v132 offset:1024
	ds_read_b128 v[190:193], v132 offset:2048
	ds_read_b128 v[194:197], v132 offset:3072
	s_mov_b32 m0, s51
	v_cndmask_b32_e32 v132, v142, v162, vcc
	ds_read_b128 v[198:201], v160 offset:32768
	ds_read_b128 v[202:205], v160 offset:33792
	ds_read_b128 v[206:209], v160 offset:34816
	ds_read_b128 v[210:213], v160 offset:35840
	ds_read_b128 v[214:217], v160 offset:36864
	ds_read_b128 v[218:221], v160 offset:37888
	ds_read_b128 v[222:225], v160 offset:38912
	ds_read_b128 v[230:233], v160 offset:39936
	v_cndmask_b32_e32 v141, v140, v161, vcc
	global_load_lds_dwordx4 v132, s[44:45]
	s_mov_b32 m0, s52
	s_nop 0
	global_load_lds_dwordx4 v141, s[44:45]
	s_waitcnt vmcnt(8)
	s_waitcnt lgkmcnt(0)
	s_barrier
	s_setprio 3
	s_waitcnt lgkmcnt(0)
	v_mfma_f32_16x16x32_bf16 v[126:129], v[166:169], v[198:201], v[126:129]
	v_mfma_f32_16x16x32_bf16 v[122:125], v[174:177], v[198:201], v[122:125]
	v_mfma_f32_16x16x32_bf16 v[110:113], v[166:169], v[206:209], v[110:113]
	v_mfma_f32_16x16x32_bf16 v[106:109], v[174:177], v[206:209], v[106:109]
	v_mfma_f32_16x16x32_bf16 v[94:97], v[166:169], v[214:217], v[94:97]
	v_mfma_f32_16x16x32_bf16 v[90:93], v[174:177], v[214:217], v[90:93]
	v_mfma_f32_16x16x32_bf16 v[78:81], v[166:169], v[222:225], v[78:81]
	v_mfma_f32_16x16x32_bf16 v[74:77], v[174:177], v[222:225], v[74:77]
	v_mfma_f32_16x16x32_bf16 v[126:129], v[170:173], v[202:205], v[126:129]
	v_mfma_f32_16x16x32_bf16 v[122:125], v[178:181], v[202:205], v[122:125]
	v_mfma_f32_16x16x32_bf16 v[110:113], v[170:173], v[210:213], v[110:113]
	v_mfma_f32_16x16x32_bf16 v[106:109], v[178:181], v[210:213], v[106:109]
	v_mfma_f32_16x16x32_bf16 v[94:97], v[170:173], v[218:221], v[94:97]
	v_mfma_f32_16x16x32_bf16 v[90:93], v[178:181], v[218:221], v[90:93]
	v_mfma_f32_16x16x32_bf16 v[78:81], v[170:173], v[230:233], v[78:81]
	v_mfma_f32_16x16x32_bf16 v[74:77], v[178:181], v[230:233], v[74:77]
	v_mfma_f32_16x16x32_bf16 v[118:121], v[182:185], v[198:201], v[118:121]
	v_mfma_f32_16x16x32_bf16 v[114:117], v[190:193], v[198:201], v[114:117]
	v_mfma_f32_16x16x32_bf16 v[102:105], v[182:185], v[206:209], v[102:105]
	v_mfma_f32_16x16x32_bf16 v[98:101], v[190:193], v[206:209], v[98:101]
	v_mfma_f32_16x16x32_bf16 v[86:89], v[182:185], v[214:217], v[86:89]
	v_mfma_f32_16x16x32_bf16 v[82:85], v[190:193], v[214:217], v[82:85]
	v_mfma_f32_16x16x32_bf16 v[70:73], v[182:185], v[222:225], v[70:73]
	v_mfma_f32_16x16x32_bf16 v[66:69], v[190:193], v[222:225], v[66:69]
	v_mfma_f32_16x16x32_bf16 v[118:121], v[186:189], v[202:205], v[118:121]
	v_mfma_f32_16x16x32_bf16 v[114:117], v[194:197], v[202:205], v[114:117]
	v_mfma_f32_16x16x32_bf16 v[102:105], v[186:189], v[210:213], v[102:105]
	v_mfma_f32_16x16x32_bf16 v[98:101], v[194:197], v[210:213], v[98:101]
	v_mfma_f32_16x16x32_bf16 v[86:89], v[186:189], v[218:221], v[86:89]
	v_mfma_f32_16x16x32_bf16 v[82:85], v[194:197], v[218:221], v[82:85]
	v_mfma_f32_16x16x32_bf16 v[70:73], v[186:189], v[230:233], v[70:73]
	v_mfma_f32_16x16x32_bf16 v[66:69], v[194:197], v[230:233], v[66:69]
	s_setprio 0
	s_barrier
; #define PG8_GIDX(G_, PM_) do { if constexpr (Sched::GATHER) { _Pragma("unroll") for (int h_ = 0; h_ < 2; ++h_) _Pragma("unroll") for (int i_ = 0; i_ < 2; ++i_) { int R_, C_; stage_rc(tid * 16 + i_ * 8192, R_, C_); \
;         const int src_ = S.rowsrc[(PM_) * BM + h_ * HALF + R_]; G_[h_][i_] = (unsigned)(src_ * K + C_) * 2u; } } } while (0)
; #define PG8_STAGE_A(b, h, ptr, NX) do { if constexpr (Sched::GATHER) { unsigned gs_[2]; gs_[0] = ((NX) && last_) ? gN[h][0] : gA[h][0]; gs_[1] = ((NX) && last_) ? gN[h][1] : gA[h][1]; PG8_STAGE(PG8_SA(b, h), ptr, gs_); } \
;         else PG8_STAGE(PG8_SA(b, h), (ptr) + ((h) ? hstep : (size_t)0), voffA); } while (0)
; #define PG8_STAGE(bufoff, gbase, voff) do { _Pragma("unroll") for (int _i = 0; _i < 2; ++_i) \
;         __builtin_amdgcn_global_load_lds((const unsigned*)((const char*)(gbase) + (voff)[_i]), (PG8_LAS unsigned*)(lds + (bufoff) + ldsw + _i * 8192), 16, 0, 0); } while (0)
; #define PG8_LDA(dst, b, h) do { _Pragma("unroll") for (int m = 0; m < 4; ++m) _Pragma("unroll") for (int k = 0; k < 2; ++k) dst[m][k] = *(const PG8_LAS bf16x8*)(lds + PG8_SA(b, h) + aoff + m * 2048 + k * 1024); } while (0)
; #define PG8_LDB(dst, b, h) do { _Pragma("unroll") for (int n = 0; n < 2; ++n) _Pragma("unroll") for (int k = 0; k < 2; ++k) dst[n][k] = *(const PG8_LAS bf16x8*)(lds + PG8_SB(b, h) + boff + n * 2048 + k * 1024); } while (0)
; template <class Epi, class Sched, bool ALIGN_EPI = false, bool SP2 = false>
; __device__ __forceinline__ void gemm_phase(PG8_LAS unsigned char* lds, const Gemm g, const Sched& S, const Epi& E, const bool skip_epi = false) {
;     ...
;         const bool has_next = S.next(ui + 1, nxt);
;         if (has_next) PG8_GIDX(gN, nxt.pm);
;         const char* nA = has_next ? (const char*)g.A + (size_t)nxt.pm * pmstepA + nxt.ko : cA; const char* nB = has_next ? (const char*)g.Bt + (size_t)nxt.pn * tstep + nxt.ko : cB;
;     ...
;             PG8_LDB(B0, 0, 0); PG8_LDB(B1, 0, 1); PG8_SCHED; PG8_LDA(At, 0, 0); PG8_STAGE_A(1, 1, a1, false);
;             PG8_WAIT_V(8); PG8_WAIT_L(0); PG8_BAR; PG8_MMA(0, 0, At, B0); PG8_MMA(0, 1, At, B1); PG8_BAR; PG8_SCHED;
;     ...
;             PG8_LDA(At, 1, 1); PG8_STAGE(PG8_SB(1, 0), b3, voffB); PG8_STAGE(PG8_SB(1, 1), b3 + hstep, voffB); PG8_STAGE_A(1, 0, a3, true);
;             PG8_WAIT_V(8); PG8_WAIT_L(0); PG8_BAR; PG8_MMA(1, 0, At, B0); PG8_MMA(1, 1, At, B1); PG8_BAR; PG8_SCHED;
	s_add_i32 s44, s64, s50
	s_add_i32 m0, s44, 0xffffff80
	ds_read_b128 v[198:201], v160 offset:49152
	ds_read_b128 v[202:205], v160 offset:50176
	ds_read_b128 v[206:209], v160 offset:51200
	ds_read_b128 v[210:213], v160 offset:52224
	ds_read_b128 v[214:217], v160 offset:53248
	ds_read_b128 v[218:221], v160 offset:54272
	ds_read_b128 v[222:225], v160 offset:55296
	ds_read_b128 v[230:233], v160 offset:56320
	global_load_lds_dwordx4 v134, s[42:43] offset:128
	s_add_i32 m0, s44, 0x1f80
	s_add_i32 s44, s65, s50
	global_load_lds_dwordx4 v136, s[42:43] offset:128
	s_add_u32 s42, s42, 0x40080
	s_addc_u32 s43, s43, 0
	s_mov_b32 m0, s44
	s_nop 0
	global_load_lds_dwordx4 v134, s[42:43]
	s_add_i32 m0, s44, 0x2000
	s_nop 0
	global_load_lds_dwordx4 v136, s[42:43]
	s_add_i32 m0, s55, 0xffffff80
	s_nop 0
	global_load_lds_dwordx4 v[238:239], off offset:128
	s_add_i32 m0, s56, 0xffffff80
	s_nop 0
	global_load_lds_dwordx4 v[236:237], off offset:128
	s_waitcnt vmcnt(8)
	s_waitcnt lgkmcnt(0)
	s_barrier
	s_setprio 3
	s_waitcnt lgkmcnt(0)
	v_mfma_f32_16x16x32_bf16 v[62:65], v[166:169], v[198:201], v[62:65]
	v_mfma_f32_16x16x32_bf16 v[58:61], v[174:177], v[198:201], v[58:61]
	v_mfma_f32_16x16x32_bf16 v[38:41], v[166:169], v[206:209], v[38:41]
	v_mfma_f32_16x16x32_bf16 v[34:37], v[174:177], v[206:209], v[34:37]
	v_mfma_f32_16x16x32_bf16 v[22:25], v[166:169], v[214:217], v[22:25]
	v_mfma_f32_16x16x32_bf16 v[18:21], v[174:177], v[214:217], v[18:21]
	v_mfma_f32_16x16x32_bf16 v[6:9], v[166:169], v[222:225], v[6:9]
	v_mfma_f32_16x16x32_bf16 v[2:5], v[174:177], v[222:225], v[2:5]
	v_mfma_f32_16x16x32_bf16 v[62:65], v[170:173], v[202:205], v[62:65]
	v_mfma_f32_16x16x32_bf16 v[58:61], v[178:181], v[202:205], v[58:61]
	v_mfma_f32_16x16x32_bf16 v[38:41], v[170:173], v[210:213], v[38:41]
	v_mfma_f32_16x16x32_bf16 v[34:37], v[178:181], v[210:213], v[34:37]
	v_mfma_f32_16x16x32_bf16 v[22:25], v[170:173], v[218:221], v[22:25]
	v_mfma_f32_16x16x32_bf16 v[18:21], v[178:181], v[218:221], v[18:21]
	v_mfma_f32_16x16x32_bf16 v[6:9], v[170:173], v[230:233], v[6:9]
	v_mfma_f32_16x16x32_bf16 v[2:5], v[178:181], v[230:233], v[2:5]
	v_mfma_f32_16x16x32_bf16 v[50:53], v[182:185], v[198:201], v[50:53]
	v_mfma_f32_16x16x32_bf16 v[42:45], v[190:193], v[198:201], v[42:45]
	v_mfma_f32_16x16x32_bf16 v[54:57], v[182:185], v[206:209], v[54:57]
	v_mfma_f32_16x16x32_bf16 v[46:49], v[190:193], v[206:209], v[46:49]
	v_mfma_f32_16x16x32_bf16 v[30:33], v[182:185], v[214:217], v[30:33]
	v_mfma_f32_16x16x32_bf16 v[26:29], v[190:193], v[214:217], v[26:29]
	v_mfma_f32_16x16x32_bf16 v[14:17], v[182:185], v[222:225], v[14:17]
	v_mfma_f32_16x16x32_bf16 v[10:13], v[190:193], v[222:225], v[10:13]
	v_mfma_f32_16x16x32_bf16 v[50:53], v[186:189], v[202:205], v[50:53]
	v_mfma_f32_16x16x32_bf16 v[42:45], v[194:197], v[202:205], v[42:45]
	v_mfma_f32_16x16x32_bf16 v[54:57], v[186:189], v[210:213], v[54:57]
	v_mfma_f32_16x16x32_bf16 v[46:49], v[194:197], v[210:213], v[46:49]
	v_mfma_f32_16x16x32_bf16 v[30:33], v[186:189], v[218:221], v[30:33]
	v_mfma_f32_16x16x32_bf16 v[26:29], v[194:197], v[218:221], v[26:29]
	v_mfma_f32_16x16x32_bf16 v[14:17], v[186:189], v[230:233], v[14:17]
	v_mfma_f32_16x16x32_bf16 v[10:13], v[194:197], v[230:233], v[10:13]
	s_setprio 0
	s_barrier
	s_add_i32 s63, s63, 2
	s_add_u32 s40, s40, 0x100
	s_addc_u32 s41, s41, 0
	s_cmp_gt_u32 s63, 13
	s_andn2_b64 vcc, exec, s[6:7]
	s_cbranch_vccnz .Lg5_nonext
	s_waitcnt vmcnt(8)
	v_readfirstlane_b32 s34, v250
	v_lshl_add_u32 v164, v229, 11, v152
	v_lshl_add_u32 v163, v251, 11, v153
	v_lshl_add_u32 v162, v252, 11, v152
	v_lshl_add_u32 v161, v253, 11, v153
	s_mul_i32 s34, s34, 28
	s_add_i32 s30, s34, s30
	s_ashr_i32 s31, s30, 31
	s_lshl_b64 s[34:35], s[30:31], 19
	v_readlane_b32 s42, v254, 29
	v_readlane_b32 s43, v254, 30
	s_add_u32 s34, s42, s34
	s_addc_u32 s35, s43, s35
	s_mov_b32 s29, s35
	s_mov_b32 s31, s34
.Lg5_nonext:
.LBB0_1728:
	ds_read_b128 v[166:169], v158
	ds_read_b128 v[170:173], v158 offset:1024
	ds_read_b128 v[174:177], v158 offset:2048
	ds_read_b128 v[178:181], v158 offset:3072
	ds_read_b128 v[182:185], v159
	ds_read_b128 v[186:189], v159 offset:1024
	ds_read_b128 v[190:193], v159 offset:2048
	ds_read_b128 v[194:197], v159 offset:3072
	s_add_u32 s42, s78, s40
	s_addc_u32 s43, s79, s41
	s_add_u32 s44, s42, 0x1aa00100
	s_addc_u32 s45, s43, 0
	s_add_u32 s66, s61, s40
	s_addc_u32 s67, s62, s41
	s_cmpk_eq_i32 s40, 0x700
	s_cselect_b64 s[64:65], -1, 0
	s_and_b64 s[42:43], s[64:65], exec
	s_cselect_b32 s45, s87, s45
	s_cselect_b32 s44, s86, s44
	s_cselect_b32 s42, s31, s66
	s_cselect_b32 s43, s29, s67
	s_and_b64 vcc, s[6:7], s[64:65]
	v_lshl_add_u64 v[226:227], v[148:149], 0, s[40:41]
	s_add_i32 m0, s37, 0xc000
	ds_read_b128 v[198:201], v160
	ds_read_b128 v[202:205], v160 offset:1024
	ds_read_b128 v[206:209], v160 offset:2048
	ds_read_b128 v[210:213], v160 offset:3072
	ds_read_b128 v[214:217], v160 offset:4096
	ds_read_b128 v[218:221], v160 offset:5120
	ds_read_b128 v[222:225], v160 offset:6144
	ds_read_b128 v[230:233], v160 offset:7168
	global_load_lds_dwordx4 v[226:227], off
	v_lshl_add_u64 v[226:227], v[146:147], 0, s[40:41]
	s_add_i32 m0, s37, 0xe000
	s_nop 0
	global_load_lds_dwordx4 v[226:227], off
	s_waitcnt vmcnt(8)
	s_waitcnt lgkmcnt(0)
	s_barrier
; #define PG8_STAGE_A(b, h, ptr, NX) do { if constexpr (Sched::GATHER) { unsigned gs_[2]; gs_[0] = ((NX) && last_) ? gN[h][0] : gA[h][0]; gs_[1] = ((NX) && last_) ? gN[h][1] : gA[h][1]; PG8_STAGE(PG8_SA(b, h), ptr, gs_); } \
;         else PG8_STAGE(PG8_SA(b, h), (ptr) + ((h) ? hstep : (size_t)0), voffA); } while (0)
; #define PG8_STAGE(bufoff, gbase, voff) do { _Pragma("unroll") for (int _i = 0; _i < 2; ++_i) \
;         __builtin_amdgcn_global_load_lds((const unsigned*)((const char*)(gbase) + (voff)[_i]), (PG8_LAS unsigned*)(lds + (bufoff) + ldsw + _i * 8192), 16, 0, 0); } while (0)
; #define PG8_LDA(dst, b, h) do { _Pragma("unroll") for (int m = 0; m < 4; ++m) _Pragma("unroll") for (int k = 0; k < 2; ++k) dst[m][k] = *(const PG8_LAS bf16x8*)(lds + PG8_SA(b, h) + aoff + m * 2048 + k * 1024); } while (0)
; #define PG8_LDB(dst, b, h) do { _Pragma("unroll") for (int n = 0; n < 2; ++n) _Pragma("unroll") for (int k = 0; k < 2; ++k) dst[n][k] = *(const PG8_LAS bf16x8*)(lds + PG8_SB(b, h) + boff + n * 2048 + k * 1024); } while (0)
; #define PG8_MMA(ai, bj, At, Bt) do { __builtin_amdgcn_s_setprio(1); _Pragma("unroll") for (int m = 0; m < 4; ++m) _Pragma("unroll") for (int n = 0; n < 2; ++n) _Pragma("unroll") for (int k = 0; k < 2; ++k) \
;         acc[ai][bj][m][n] = __builtin_amdgcn_mfma_f32_16x16x32_bf16(Bt[n][k], At[m][k], acc[ai][bj][m][n], 0, 0, 0); __builtin_amdgcn_s_setprio(0); } while (0)
; template <class Epi, class Sched, bool ALIGN_EPI = false, bool SP2 = false>
; __device__ __forceinline__ void gemm_phase(PG8_LAS unsigned char* lds, const Gemm g, const Sched& S, const Epi& E, const bool skip_epi = false) {
;     ...
;             PG8_LDB(B0, 0, 0); PG8_LDB(B1, 0, 1); PG8_SCHED; PG8_LDA(At, 0, 0); PG8_STAGE_A(1, 1, a1, false);
;             PG8_WAIT_V(8); PG8_WAIT_L(0); PG8_BAR; PG8_MMA(0, 0, At, B0); PG8_MMA(0, 1, At, B1); PG8_BAR; PG8_SCHED;
;             PG8_LDA(At, 0, 1); PG8_STAGE(PG8_SB(0, 0), b2, voffB); PG8_STAGE(PG8_SB(0, 1), b2 + hstep, voffB); PG8_STAGE_A(0, 0, a2, true);
;             PG8_WAIT_V(8); PG8_WAIT_L(0); PG8_BAR; PG8_MMA(1, 0, At, B0); PG8_MMA(1, 1, At, B1); PG8_BAR; PG8_SCHED;
;             PG8_LDB(B0, 1, 0); PG8_LDB(B1, 1, 1); PG8_SCHED; PG8_LDA(At, 1, 0); PG8_STAGE_A(0, 1, a2, true);
;             PG8_WAIT_V(8); PG8_WAIT_L(0); PG8_BAR; PG8_MMA(0, 0, At, B0); PG8_MMA(0, 1, At, B1); PG8_BAR; PG8_SCHED;
	s_setprio 3
	s_waitcnt lgkmcnt(0)
	v_mfma_f32_16x16x32_bf16 v[126:129], v[166:169], v[198:201], v[126:129]
	v_mfma_f32_16x16x32_bf16 v[122:125], v[174:177], v[198:201], v[122:125]
	v_mfma_f32_16x16x32_bf16 v[110:113], v[166:169], v[206:209], v[110:113]
	v_mfma_f32_16x16x32_bf16 v[106:109], v[174:177], v[206:209], v[106:109]
	v_mfma_f32_16x16x32_bf16 v[94:97], v[166:169], v[214:217], v[94:97]
	v_mfma_f32_16x16x32_bf16 v[90:93], v[174:177], v[214:217], v[90:93]
	v_mfma_f32_16x16x32_bf16 v[78:81], v[166:169], v[222:225], v[78:81]
	v_mfma_f32_16x16x32_bf16 v[74:77], v[174:177], v[222:225], v[74:77]
	v_mfma_f32_16x16x32_bf16 v[126:129], v[170:173], v[202:205], v[126:129]
	v_mfma_f32_16x16x32_bf16 v[122:125], v[178:181], v[202:205], v[122:125]
	v_mfma_f32_16x16x32_bf16 v[110:113], v[170:173], v[210:213], v[110:113]
	v_mfma_f32_16x16x32_bf16 v[106:109], v[178:181], v[210:213], v[106:109]
	v_mfma_f32_16x16x32_bf16 v[94:97], v[170:173], v[218:221], v[94:97]
	v_mfma_f32_16x16x32_bf16 v[90:93], v[178:181], v[218:221], v[90:93]
	v_mfma_f32_16x16x32_bf16 v[78:81], v[170:173], v[230:233], v[78:81]
	v_mfma_f32_16x16x32_bf16 v[74:77], v[178:181], v[230:233], v[74:77]
	v_mfma_f32_16x16x32_bf16 v[118:121], v[182:185], v[198:201], v[118:121]
	v_mfma_f32_16x16x32_bf16 v[114:117], v[190:193], v[198:201], v[114:117]
	v_mfma_f32_16x16x32_bf16 v[102:105], v[182:185], v[206:209], v[102:105]
	v_mfma_f32_16x16x32_bf16 v[98:101], v[190:193], v[206:209], v[98:101]
	v_mfma_f32_16x16x32_bf16 v[86:89], v[182:185], v[214:217], v[86:89]
	v_mfma_f32_16x16x32_bf16 v[82:85], v[190:193], v[214:217], v[82:85]
	v_mfma_f32_16x16x32_bf16 v[70:73], v[182:185], v[222:225], v[70:73]
	v_mfma_f32_16x16x32_bf16 v[66:69], v[190:193], v[222:225], v[66:69]
	v_mfma_f32_16x16x32_bf16 v[118:121], v[186:189], v[202:205], v[118:121]
	v_mfma_f32_16x16x32_bf16 v[114:117], v[194:197], v[202:205], v[114:117]
	v_mfma_f32_16x16x32_bf16 v[102:105], v[186:189], v[210:213], v[102:105]
	v_mfma_f32_16x16x32_bf16 v[98:101], v[194:197], v[210:213], v[98:101]
	v_mfma_f32_16x16x32_bf16 v[86:89], v[186:189], v[218:221], v[86:89]
	v_mfma_f32_16x16x32_bf16 v[82:85], v[194:197], v[218:221], v[82:85]
	v_mfma_f32_16x16x32_bf16 v[70:73], v[186:189], v[230:233], v[70:73]
	v_mfma_f32_16x16x32_bf16 v[66:69], v[194:197], v[230:233], v[66:69]
	s_setprio 0
	s_barrier
	s_add_i32 s64, s58, s50
	s_mov_b32 m0, s64
	ds_read_b128 v[198:201], v160 offset:16384
	ds_read_b128 v[202:205], v160 offset:17408
	ds_read_b128 v[206:209], v160 offset:18432
	ds_read_b128 v[210:213], v160 offset:19456
	ds_read_b128 v[214:217], v160 offset:20480
	ds_read_b128 v[218:221], v160 offset:21504
	ds_read_b128 v[222:225], v160 offset:22528
	ds_read_b128 v[230:233], v160 offset:23552
	global_load_lds_dwordx4 v134, s[42:43]
	s_add_i32 m0, s64, 0x2000
	s_add_u32 s64, s42, 0x40000
	s_addc_u32 s65, s43, 0
	s_add_i32 s66, s59, s50
	global_load_lds_dwordx4 v136, s[42:43]
	s_mov_b32 m0, s66
	v_cndmask_b32_e32 v132, v130, v164, vcc
	global_load_lds_dwordx4 v134, s[64:65]
	s_add_i32 m0, s66, 0x2000
	v_lshl_add_u64 v[238:239], s[44:45], 0, v[132:133]
	global_load_lds_dwordx4 v136, s[64:65]
	s_mov_b32 m0, s37
	v_cndmask_b32_e32 v236, v144, v163, vcc
	global_load_lds_dwordx4 v132, s[44:45]
	s_mov_b32 m0, s39
	v_mov_b32_e32 v237, v133
	global_load_lds_dwordx4 v236, s[44:45]
	s_waitcnt vmcnt(8)
	s_waitcnt lgkmcnt(0)
	v_lshl_add_u64 v[236:237], s[44:45], 0, v[236:237]
	s_barrier
	s_setprio 3
	s_waitcnt lgkmcnt(0)
	v_mfma_f32_16x16x32_bf16 v[62:65], v[166:169], v[198:201], v[62:65]
	v_mfma_f32_16x16x32_bf16 v[58:61], v[174:177], v[198:201], v[58:61]
	v_mfma_f32_16x16x32_bf16 v[38:41], v[166:169], v[206:209], v[38:41]
	v_mfma_f32_16x16x32_bf16 v[34:37], v[174:177], v[206:209], v[34:37]
	v_mfma_f32_16x16x32_bf16 v[22:25], v[166:169], v[214:217], v[22:25]
	v_mfma_f32_16x16x32_bf16 v[18:21], v[174:177], v[214:217], v[18:21]
	v_mfma_f32_16x16x32_bf16 v[6:9], v[166:169], v[222:225], v[6:9]
	v_mfma_f32_16x16x32_bf16 v[2:5], v[174:177], v[222:225], v[2:5]
	v_mfma_f32_16x16x32_bf16 v[62:65], v[170:173], v[202:205], v[62:65]
	v_mfma_f32_16x16x32_bf16 v[58:61], v[178:181], v[202:205], v[58:61]
	v_mfma_f32_16x16x32_bf16 v[38:41], v[170:173], v[210:213], v[38:41]
	v_mfma_f32_16x16x32_bf16 v[34:37], v[178:181], v[210:213], v[34:37]
	v_mfma_f32_16x16x32_bf16 v[22:25], v[170:173], v[218:221], v[22:25]
	v_mfma_f32_16x16x32_bf16 v[18:21], v[178:181], v[218:221], v[18:21]
	v_mfma_f32_16x16x32_bf16 v[6:9], v[170:173], v[230:233], v[6:9]
	v_mfma_f32_16x16x32_bf16 v[2:5], v[178:181], v[230:233], v[2:5]
	v_mfma_f32_16x16x32_bf16 v[50:53], v[182:185], v[198:201], v[50:53]
	v_mfma_f32_16x16x32_bf16 v[42:45], v[190:193], v[198:201], v[42:45]
	v_mfma_f32_16x16x32_bf16 v[54:57], v[182:185], v[206:209], v[54:57]
	v_mfma_f32_16x16x32_bf16 v[46:49], v[190:193], v[206:209], v[46:49]
	v_mfma_f32_16x16x32_bf16 v[30:33], v[182:185], v[214:217], v[30:33]
	v_mfma_f32_16x16x32_bf16 v[26:29], v[190:193], v[214:217], v[26:29]
	v_mfma_f32_16x16x32_bf16 v[14:17], v[182:185], v[222:225], v[14:17]
	v_mfma_f32_16x16x32_bf16 v[10:13], v[190:193], v[222:225], v[10:13]
	v_mfma_f32_16x16x32_bf16 v[50:53], v[186:189], v[202:205], v[50:53]
	v_mfma_f32_16x16x32_bf16 v[42:45], v[194:197], v[202:205], v[42:45]
	v_mfma_f32_16x16x32_bf16 v[54:57], v[186:189], v[210:213], v[54:57]
	v_mfma_f32_16x16x32_bf16 v[46:49], v[194:197], v[210:213], v[46:49]
	v_mfma_f32_16x16x32_bf16 v[30:33], v[186:189], v[218:221], v[30:33]
	v_mfma_f32_16x16x32_bf16 v[26:29], v[194:197], v[218:221], v[26:29]
	v_mfma_f32_16x16x32_bf16 v[14:17], v[186:189], v[230:233], v[14:17]
	v_mfma_f32_16x16x32_bf16 v[10:13], v[194:197], v[230:233], v[10:13]
	s_setprio 0
	s_barrier
; #define PG8_STAGE_A(b, h, ptr, NX) do { if constexpr (Sched::GATHER) { unsigned gs_[2]; gs_[0] = ((NX) && last_) ? gN[h][0] : gA[h][0]; gs_[1] = ((NX) && last_) ? gN[h][1] : gA[h][1]; PG8_STAGE(PG8_SA(b, h), ptr, gs_); } \
;         else PG8_STAGE(PG8_SA(b, h), (ptr) + ((h) ? hstep : (size_t)0), voffA); } while (0)
; #define PG8_STAGE(bufoff, gbase, voff) do { _Pragma("unroll") for (int _i = 0; _i < 2; ++_i) \
;         __builtin_amdgcn_global_load_lds((const unsigned*)((const char*)(gbase) + (voff)[_i]), (PG8_LAS unsigned*)(lds + (bufoff) + ldsw + _i * 8192), 16, 0, 0); } while (0)
; #define PG8_LDA(dst, b, h) do { _Pragma("unroll") for (int m = 0; m < 4; ++m) _Pragma("unroll") for (int k = 0; k < 2; ++k) dst[m][k] = *(const PG8_LAS bf16x8*)(lds + PG8_SA(b, h) + aoff + m * 2048 + k * 1024); } while (0)
; #define PG8_LDB(dst, b, h) do { _Pragma("unroll") for (int n = 0; n < 2; ++n) _Pragma("unroll") for (int k = 0; k < 2; ++k) dst[n][k] = *(const PG8_LAS bf16x8*)(lds + PG8_SB(b, h) + boff + n * 2048 + k * 1024); } while (0)
; #define PG8_MMA(ai, bj, At, Bt) do { __builtin_amdgcn_s_setprio(1); _Pragma("unroll") for (int m = 0; m < 4; ++m) _Pragma("unroll") for (int n = 0; n < 2; ++n) _Pragma("unroll") for (int k = 0; k < 2; ++k) \
;         acc[ai][bj][m][n] = __builtin_amdgcn_mfma_f32_16x16x32_bf16(Bt[n][k], At[m][k], acc[ai][bj][m][n], 0, 0, 0); __builtin_amdgcn_s_setprio(0); } while (0)
; #define PG8_WAIT_V(n) asm volatile("s_waitcnt vmcnt(" #n ")" ::: "memory")
; #define PG8_WAIT_L(n) asm volatile("s_waitcnt lgkmcnt(" #n ")" ::: "memory")
; #define PG8_BAR __builtin_amdgcn_s_barrier()
; #define PG8_SCHED __builtin_amdgcn_sched_barrier(0)
; template <class Epi, class Sched, bool ALIGN_EPI = false, bool SP2 = false>
; __device__ __forceinline__ void gemm_phase(PG8_LAS unsigned char* lds, const Gemm g, const Sched& S, const Epi& E, const bool skip_epi = false) {
;     ...
;             PG8_LDB(B0, 1, 0); PG8_LDB(B1, 1, 1); PG8_SCHED; PG8_LDA(At, 1, 0); PG8_STAGE_A(0, 1, a2, true);
;             PG8_WAIT_V(8); PG8_WAIT_L(0); PG8_BAR; PG8_MMA(0, 0, At, B0); PG8_MMA(0, 1, At, B1); PG8_BAR; PG8_SCHED;
;             PG8_LDA(At, 1, 1); PG8_STAGE(PG8_SB(1, 0), b3, voffB); PG8_STAGE(PG8_SB(1, 1), b3 + hstep, voffB); PG8_STAGE_A(1, 0, a3, true);
;             PG8_WAIT_V(8); PG8_WAIT_L(0); PG8_BAR; PG8_MMA(1, 0, At, B0); PG8_MMA(1, 1, At, B1); PG8_BAR; PG8_SCHED;
	s_add_i32 s64, 0, 0x18000
	v_add_u32_e32 v132, s64, v154
	s_add_i32 s65, 0, 0x1c000
	ds_read_b128 v[166:169], v132
	ds_read_b128 v[170:173], v132 offset:1024
	ds_read_b128 v[174:177], v132 offset:2048
	ds_read_b128 v[178:181], v132 offset:3072
	v_add_u32_e32 v132, s65, v154
	ds_read_b128 v[182:185], v132
	ds_read_b128 v[186:189], v132 offset:1024
	ds_read_b128 v[190:193], v132 offset:2048
	ds_read_b128 v[194:197], v132 offset:3072
	s_mov_b32 m0, s51
	v_cndmask_b32_e32 v132, v142, v162, vcc
	ds_read_b128 v[198:201], v160 offset:32768
	ds_read_b128 v[202:205], v160 offset:33792
	ds_read_b128 v[206:209], v160 offset:34816
	ds_read_b128 v[210:213], v160 offset:35840
	ds_read_b128 v[214:217], v160 offset:36864
	ds_read_b128 v[218:221], v160 offset:37888
	ds_read_b128 v[222:225], v160 offset:38912
	ds_read_b128 v[230:233], v160 offset:39936
	v_cndmask_b32_e32 v141, v140, v161, vcc
	global_load_lds_dwordx4 v132, s[44:45]
	s_mov_b32 m0, s52
	s_nop 0
	global_load_lds_dwordx4 v141, s[44:45]
	s_waitcnt vmcnt(8)
	s_waitcnt lgkmcnt(0)
	s_barrier
	s_setprio 3
	s_waitcnt lgkmcnt(0)
	v_mfma_f32_16x16x32_bf16 v[126:129], v[166:169], v[198:201], v[126:129]
	v_mfma_f32_16x16x32_bf16 v[122:125], v[174:177], v[198:201], v[122:125]
	v_mfma_f32_16x16x32_bf16 v[110:113], v[166:169], v[206:209], v[110:113]
	v_mfma_f32_16x16x32_bf16 v[106:109], v[174:177], v[206:209], v[106:109]
	v_mfma_f32_16x16x32_bf16 v[94:97], v[166:169], v[214:217], v[94:97]
	v_mfma_f32_16x16x32_bf16 v[90:93], v[174:177], v[214:217], v[90:93]
	v_mfma_f32_16x16x32_bf16 v[78:81], v[166:169], v[222:225], v[78:81]
	v_mfma_f32_16x16x32_bf16 v[74:77], v[174:177], v[222:225], v[74:77]
	v_mfma_f32_16x16x32_bf16 v[126:129], v[170:173], v[202:205], v[126:129]
	v_mfma_f32_16x16x32_bf16 v[122:125], v[178:181], v[202:205], v[122:125]
	v_mfma_f32_16x16x32_bf16 v[110:113], v[170:173], v[210:213], v[110:113]
	v_mfma_f32_16x16x32_bf16 v[106:109], v[178:181], v[210:213], v[106:109]
	v_mfma_f32_16x16x32_bf16 v[94:97], v[170:173], v[218:221], v[94:97]
	v_mfma_f32_16x16x32_bf16 v[90:93], v[178:181], v[218:221], v[90:93]
	v_mfma_f32_16x16x32_bf16 v[78:81], v[170:173], v[230:233], v[78:81]
	v_mfma_f32_16x16x32_bf16 v[74:77], v[178:181], v[230:233], v[74:77]
	v_mfma_f32_16x16x32_bf16 v[118:121], v[182:185], v[198:201], v[118:121]
	v_mfma_f32_16x16x32_bf16 v[114:117], v[190:193], v[198:201], v[114:117]
	v_mfma_f32_16x16x32_bf16 v[102:105], v[182:185], v[206:209], v[102:105]
	v_mfma_f32_16x16x32_bf16 v[98:101], v[190:193], v[206:209], v[98:101]
	v_mfma_f32_16x16x32_bf16 v[86:89], v[182:185], v[214:217], v[86:89]
	v_mfma_f32_16x16x32_bf16 v[82:85], v[190:193], v[214:217], v[82:85]
	v_mfma_f32_16x16x32_bf16 v[70:73], v[182:185], v[222:225], v[70:73]
	v_mfma_f32_16x16x32_bf16 v[66:69], v[190:193], v[222:225], v[66:69]
	v_mfma_f32_16x16x32_bf16 v[118:121], v[186:189], v[202:205], v[118:121]
	v_mfma_f32_16x16x32_bf16 v[114:117], v[194:197], v[202:205], v[114:117]
	v_mfma_f32_16x16x32_bf16 v[102:105], v[186:189], v[210:213], v[102:105]
	v_mfma_f32_16x16x32_bf16 v[98:101], v[194:197], v[210:213], v[98:101]
	v_mfma_f32_16x16x32_bf16 v[86:89], v[186:189], v[218:221], v[86:89]
	v_mfma_f32_16x16x32_bf16 v[82:85], v[194:197], v[218:221], v[82:85]
	v_mfma_f32_16x16x32_bf16 v[70:73], v[186:189], v[230:233], v[70:73]
	v_mfma_f32_16x16x32_bf16 v[66:69], v[194:197], v[230:233], v[66:69]
	s_setprio 0
	s_barrier
	s_add_i32 s44, s64, s50
	s_add_i32 m0, s44, 0xffffff80
	ds_read_b128 v[198:201], v160 offset:49152
	ds_read_b128 v[202:205], v160 offset:50176
	ds_read_b128 v[206:209], v160 offset:51200
	ds_read_b128 v[210:213], v160 offset:52224
	ds_read_b128 v[214:217], v160 offset:53248
	ds_read_b128 v[218:221], v160 offset:54272
	ds_read_b128 v[222:225], v160 offset:55296
	ds_read_b128 v[230:233], v160 offset:56320
	global_load_lds_dwordx4 v134, s[42:43] offset:128
	s_add_i32 m0, s44, 0x1f80
	s_add_i32 s44, s65, s50
	global_load_lds_dwordx4 v136, s[42:43] offset:128
	s_add_u32 s42, s42, 0x40080
	s_addc_u32 s43, s43, 0
	s_mov_b32 m0, s44
	s_nop 0
	global_load_lds_dwordx4 v134, s[42:43]
	s_add_i32 m0, s44, 0x2000
	s_nop 0
	global_load_lds_dwordx4 v136, s[42:43]
	s_add_i32 m0, s55, 0xffffff80
	s_nop 0
	global_load_lds_dwordx4 v[238:239], off offset:128
	s_add_i32 m0, s56, 0xffffff80
	s_nop 0
	global_load_lds_dwordx4 v[236:237], off offset:128
	s_waitcnt vmcnt(8)
	s_waitcnt lgkmcnt(0)
	s_barrier
	s_setprio 3
	s_waitcnt lgkmcnt(0)
	v_mfma_f32_16x16x32_bf16 v[62:65], v[166:169], v[198:201], v[62:65]
	v_mfma_f32_16x16x32_bf16 v[58:61], v[174:177], v[198:201], v[58:61]
	v_mfma_f32_16x16x32_bf16 v[38:41], v[166:169], v[206:209], v[38:41]
	v_mfma_f32_16x16x32_bf16 v[34:37], v[174:177], v[206:209], v[34:37]
	v_mfma_f32_16x16x32_bf16 v[22:25], v[166:169], v[214:217], v[22:25]
	v_mfma_f32_16x16x32_bf16 v[18:21], v[174:177], v[214:217], v[18:21]
	v_mfma_f32_16x16x32_bf16 v[6:9], v[166:169], v[222:225], v[6:9]
	v_mfma_f32_16x16x32_bf16 v[2:5], v[174:177], v[222:225], v[2:5]
	v_mfma_f32_16x16x32_bf16 v[62:65], v[170:173], v[202:205], v[62:65]
	v_mfma_f32_16x16x32_bf16 v[58:61], v[178:181], v[202:205], v[58:61]
	v_mfma_f32_16x16x32_bf16 v[38:41], v[170:173], v[210:213], v[38:41]
	v_mfma_f32_16x16x32_bf16 v[34:37], v[178:181], v[210:213], v[34:37]
	v_mfma_f32_16x16x32_bf16 v[22:25], v[170:173], v[218:221], v[22:25]
	v_mfma_f32_16x16x32_bf16 v[18:21], v[178:181], v[218:221], v[18:21]
	v_mfma_f32_16x16x32_bf16 v[6:9], v[170:173], v[230:233], v[6:9]
	v_mfma_f32_16x16x32_bf16 v[2:5], v[178:181], v[230:233], v[2:5]
	v_mfma_f32_16x16x32_bf16 v[50:53], v[182:185], v[198:201], v[50:53]
	v_mfma_f32_16x16x32_bf16 v[42:45], v[190:193], v[198:201], v[42:45]
	v_mfma_f32_16x16x32_bf16 v[54:57], v[182:185], v[206:209], v[54:57]
	v_mfma_f32_16x16x32_bf16 v[46:49], v[190:193], v[206:209], v[46:49]
	v_mfma_f32_16x16x32_bf16 v[30:33], v[182:185], v[214:217], v[30:33]
	v_mfma_f32_16x16x32_bf16 v[26:29], v[190:193], v[214:217], v[26:29]
	v_mfma_f32_16x16x32_bf16 v[14:17], v[182:185], v[222:225], v[14:17]
	v_mfma_f32_16x16x32_bf16 v[10:13], v[190:193], v[222:225], v[10:13]
	v_mfma_f32_16x16x32_bf16 v[50:53], v[186:189], v[202:205], v[50:53]
	v_mfma_f32_16x16x32_bf16 v[42:45], v[194:197], v[202:205], v[42:45]
	v_mfma_f32_16x16x32_bf16 v[54:57], v[186:189], v[210:213], v[54:57]
	v_mfma_f32_16x16x32_bf16 v[46:49], v[194:197], v[210:213], v[46:49]
	v_mfma_f32_16x16x32_bf16 v[30:33], v[186:189], v[218:221], v[30:33]
	v_mfma_f32_16x16x32_bf16 v[26:29], v[194:197], v[218:221], v[26:29]
	v_mfma_f32_16x16x32_bf16 v[14:17], v[186:189], v[230:233], v[14:17]
	v_mfma_f32_16x16x32_bf16 v[10:13], v[194:197], v[230:233], v[10:13]
	s_setprio 0
	s_barrier
	s_add_i32 s63, s63, 2
	s_add_u32 s40, s40, 0x100
	s_addc_u32 s41, s41, 0
	s_cmp_gt_u32 s63, 13
	s_cbranch_scc0 .LBB0_1728
	s_and_b64 vcc, exec, s[26:27]
	s_cbranch_vccz .LBB0_1731
	s_barrier

; #define PG8_STAGE_A(b, h, ptr, NX) do { if constexpr (Sched::GATHER) { unsigned gs_[2]; gs_[0] = ((NX) && last_) ? gN[h][0] : gA[h][0]; gs_[1] = ((NX) && last_) ? gN[h][1] : gA[h][1]; PG8_STAGE(PG8_SA(b, h), ptr, gs_); } \
;         else PG8_STAGE(PG8_SA(b, h), (ptr) + ((h) ? hstep : (size_t)0), voffA); } while (0)
; #define PG8_STAGE(bufoff, gbase, voff) do { _Pragma("unroll") for (int _i = 0; _i < 2; ++_i) \
;         __builtin_amdgcn_global_load_lds((const unsigned*)((const char*)(gbase) + (voff)[_i]), (PG8_LAS unsigned*)(lds + (bufoff) + ldsw + _i * 8192), 16, 0, 0); } while (0)
; #define PG8_LDA(dst, b, h) do { _Pragma("unroll") for (int m = 0; m < 4; ++m) _Pragma("unroll") for (int k = 0; k < 2; ++k) dst[m][k] = *(const PG8_LAS bf16x8*)(lds + PG8_SA(b, h) + aoff + m * 2048 + k * 1024); } while (0)
; #define PG8_LDB(dst, b, h) do { _Pragma("unroll") for (int n = 0; n < 2; ++n) _Pragma("unroll") for (int k = 0; k < 2; ++k) dst[n][k] = *(const PG8_LAS bf16x8*)(lds + PG8_SB(b, h) + boff + n * 2048 + k * 1024); } while (0)
; #define PG8_WAIT_V(n) asm volatile("s_waitcnt vmcnt(" #n ")" ::: "memory")
; #define PG8_WAIT_L(n) asm volatile("s_waitcnt lgkmcnt(" #n ")" ::: "memory")
; template <class Epi, class Sched, bool ALIGN_EPI = false, bool SP2 = false>
; __device__ __forceinline__ void gemm_phase(PG8_LAS unsigned char* lds, const Gemm g, const Sched& S, const Epi& E, const bool skip_epi = false) {
;     ...
;         const char* nA = has_next ? (const char*)g.A + (size_t)nxt.pm * pmstepA + nxt.ko : cA; const char* nB = has_next ? (const char*)g.Bt + (size_t)nxt.pn * tstep + nxt.ko : cB;
;     ...
;             const char* a2 = last ? nA : cA + (size_t)(t + 2) * kstep; const char* b2 = last ? nB : cB + (size_t)(t + 2) * kstep;
;             const char* a3 = a2 + kstep; const char* b3 = b2 + kstep;
;             if (last && has_next) S.a_ready(nxt);
;             if constexpr (SP2) {
;             PG8_LDB(B0, 0, 0); PG8_LDB(B1, 0, 1); PG8_SCHED; PG8_LDA(At, 0, 0); PG8_STAGE_A(1, 1, a1, false);
;             PG8_WAIT_V(8); PG8_WAIT_L(0); PG8_BAR; PG8_MMA(0, 0, At, B0); PG8_MMA(0, 1, At, B1); PG8_BAR; PG8_SCHED;
;             PG8_LDA(At, 0, 1); PG8_STAGE(PG8_SB(0, 0), b2, voffB); PG8_STAGE(PG8_SB(0, 1), b2 + hstep, voffB); PG8_STAGE_A(0, 0, a2, true);
;             PG8_WAIT_V(8); PG8_WAIT_L(0); PG8_BAR; PG8_MMA(1, 0, At, B0); PG8_MMA(1, 1, At, B1); PG8_BAR; PG8_SCHED;
.LBB0_1822:
	s_add_u32 s67, s40, 0x100
	s_addc_u32 s68, s41, 0
	s_mov_b32 s69, -2
	ds_read_b128 v[160:163], v157
	ds_read_b128 v[164:167], v157 offset:1024
	ds_read_b128 v[168:171], v157 offset:2048
	ds_read_b128 v[172:175], v157 offset:3072
	ds_read_b128 v[176:179], v158
	ds_read_b128 v[180:183], v158 offset:1024
	ds_read_b128 v[184:187], v158 offset:2048
	ds_read_b128 v[188:191], v158 offset:3072
	s_add_u32 s40, s38, 0x100
	s_addc_u32 s41, s39, 0
	s_cmp_eq_u32 s69, 52
	s_cselect_b32 s45, s7, s41
	s_cselect_b32 s44, s6, s40
	s_cselect_b32 s43, s35, s68
	s_cselect_b32 s42, s34, s67
	v_lshl_add_u64 v[152:153], s[38:39], 0, v[140:141]
	s_add_i32 m0, s37, 0xc000
	ds_read_b128 v[192:195], v159
	ds_read_b128 v[196:199], v159 offset:1024
	ds_read_b128 v[200:203], v159 offset:2048
	ds_read_b128 v[204:207], v159 offset:3072
	ds_read_b128 v[208:211], v159 offset:4096
	ds_read_b128 v[212:215], v159 offset:5120
	ds_read_b128 v[216:219], v159 offset:6144
	ds_read_b128 v[220:223], v159 offset:7168
	global_load_lds_dwordx4 v[152:153], off
	v_lshl_add_u64 v[152:153], s[38:39], 0, v[142:143]
	s_add_i32 m0, s37, 0xe000
	s_nop 0
	global_load_lds_dwordx4 v[152:153], off
	s_waitcnt vmcnt(8)
	s_waitcnt lgkmcnt(0)
	s_barrier
	s_setprio 3
	s_waitcnt lgkmcnt(0)
	v_mfma_f32_16x16x32_bf16 v[126:129], v[160:163], v[192:195], 0
	v_mfma_f32_16x16x32_bf16 v[122:125], v[168:171], v[192:195], 0
	v_mfma_f32_16x16x32_bf16 v[118:121], v[160:163], v[200:203], 0
	v_mfma_f32_16x16x32_bf16 v[114:117], v[168:171], v[200:203], 0
	v_mfma_f32_16x16x32_bf16 v[106:109], v[160:163], v[208:211], 0
	v_mfma_f32_16x16x32_bf16 v[98:101], v[168:171], v[208:211], 0
	v_mfma_f32_16x16x32_bf16 v[78:81], v[160:163], v[216:219], 0
	v_mfma_f32_16x16x32_bf16 v[74:77], v[168:171], v[216:219], 0
	v_mfma_f32_16x16x32_bf16 v[126:129], v[164:167], v[196:199], v[126:129]
	v_mfma_f32_16x16x32_bf16 v[122:125], v[172:175], v[196:199], v[122:125]
	v_mfma_f32_16x16x32_bf16 v[118:121], v[164:167], v[204:207], v[118:121]
	v_mfma_f32_16x16x32_bf16 v[114:117], v[172:175], v[204:207], v[114:117]
	v_mfma_f32_16x16x32_bf16 v[106:109], v[164:167], v[212:215], v[106:109]
	v_mfma_f32_16x16x32_bf16 v[98:101], v[172:175], v[212:215], v[98:101]
	v_mfma_f32_16x16x32_bf16 v[78:81], v[164:167], v[220:223], v[78:81]
	v_mfma_f32_16x16x32_bf16 v[74:77], v[172:175], v[220:223], v[74:77]
	v_mfma_f32_16x16x32_bf16 v[110:113], v[176:179], v[192:195], 0
	v_mfma_f32_16x16x32_bf16 v[102:105], v[184:187], v[192:195], 0
	v_mfma_f32_16x16x32_bf16 v[94:97], v[176:179], v[200:203], 0
	v_mfma_f32_16x16x32_bf16 v[90:93], v[184:187], v[200:203], 0
	v_mfma_f32_16x16x32_bf16 v[86:89], v[176:179], v[208:211], 0
	v_mfma_f32_16x16x32_bf16 v[82:85], v[184:187], v[208:211], 0
	v_mfma_f32_16x16x32_bf16 v[70:73], v[176:179], v[216:219], 0
	v_mfma_f32_16x16x32_bf16 v[66:69], v[184:187], v[216:219], 0
	v_mfma_f32_16x16x32_bf16 v[110:113], v[180:183], v[196:199], v[110:113]
	v_mfma_f32_16x16x32_bf16 v[102:105], v[188:191], v[196:199], v[102:105]
	v_mfma_f32_16x16x32_bf16 v[94:97], v[180:183], v[204:207], v[94:97]
	v_mfma_f32_16x16x32_bf16 v[90:93], v[188:191], v[204:207], v[90:93]
	v_mfma_f32_16x16x32_bf16 v[86:89], v[180:183], v[212:215], v[86:89]
	v_mfma_f32_16x16x32_bf16 v[82:85], v[188:191], v[212:215], v[82:85]
	v_mfma_f32_16x16x32_bf16 v[70:73], v[180:183], v[220:223], v[70:73]
	v_mfma_f32_16x16x32_bf16 v[66:69], v[188:191], v[220:223], v[66:69]
	s_setprio 0
	s_barrier
	s_add_i32 s38, s60, s51
	s_mov_b64 s[98:99], s[42:43]
	s_mov_b32 m0, s38
	ds_read_b128 v[192:195], v159 offset:16384
	ds_read_b128 v[196:199], v159 offset:17408
	ds_read_b128 v[200:203], v159 offset:18432
	ds_read_b128 v[204:207], v159 offset:19456
	ds_read_b128 v[208:211], v159 offset:20480
	ds_read_b128 v[212:215], v159 offset:21504
	ds_read_b128 v[216:219], v159 offset:22528
	ds_read_b128 v[220:223], v159 offset:23552
	global_load_lds_dwordx4 v134, s[42:43]
	s_add_i32 m0, s38, 0x2000
	s_add_u32 s38, s42, 0xe0000
	s_addc_u32 s39, s43, 0
	s_add_i32 s70, s61, s51
	global_load_lds_dwordx4 v138, s[42:43]
	s_mov_b32 m0, s70
	s_nop 0
	global_load_lds_dwordx4 v134, s[38:39]
	s_add_i32 m0, s70, 0x2000
	s_nop 0
	global_load_lds_dwordx4 v138, s[38:39]
	s_mov_b32 m0, s37
	s_nop 0
	global_load_lds_dwordx4 v132, s[44:45]
	s_mov_b32 m0, s52
	s_nop 0
	global_load_lds_dwordx4 v136, s[44:45]
	s_waitcnt vmcnt(8)
	s_waitcnt lgkmcnt(0)
	s_barrier
	s_setprio 3
	s_waitcnt lgkmcnt(0)
	v_mfma_f32_16x16x32_bf16 v[62:65], v[160:163], v[192:195], 0
	v_mfma_f32_16x16x32_bf16 v[58:61], v[168:171], v[192:195], 0
	v_mfma_f32_16x16x32_bf16 v[50:53], v[160:163], v[200:203], 0
	v_mfma_f32_16x16x32_bf16 v[42:45], v[168:171], v[200:203], 0
	v_mfma_f32_16x16x32_bf16 v[34:37], v[160:163], v[208:211], 0
	v_mfma_f32_16x16x32_bf16 v[26:29], v[168:171], v[208:211], 0
	v_mfma_f32_16x16x32_bf16 v[18:21], v[160:163], v[216:219], 0
	v_mfma_f32_16x16x32_bf16 v[10:13], v[168:171], v[216:219], 0
	v_mfma_f32_16x16x32_bf16 v[62:65], v[164:167], v[196:199], v[62:65]
	v_mfma_f32_16x16x32_bf16 v[58:61], v[172:175], v[196:199], v[58:61]
	v_mfma_f32_16x16x32_bf16 v[50:53], v[164:167], v[204:207], v[50:53]
	v_mfma_f32_16x16x32_bf16 v[42:45], v[172:175], v[204:207], v[42:45]
	v_mfma_f32_16x16x32_bf16 v[34:37], v[164:167], v[212:215], v[34:37]
	v_mfma_f32_16x16x32_bf16 v[26:29], v[172:175], v[212:215], v[26:29]
	v_mfma_f32_16x16x32_bf16 v[18:21], v[164:167], v[220:223], v[18:21]
	v_mfma_f32_16x16x32_bf16 v[10:13], v[172:175], v[220:223], v[10:13]
	v_mfma_f32_16x16x32_bf16 v[54:57], v[176:179], v[192:195], 0
	v_mfma_f32_16x16x32_bf16 v[46:49], v[184:187], v[192:195], 0
	v_mfma_f32_16x16x32_bf16 v[38:41], v[176:179], v[200:203], 0
	v_mfma_f32_16x16x32_bf16 v[30:33], v[184:187], v[200:203], 0
	v_mfma_f32_16x16x32_bf16 v[22:25], v[176:179], v[208:211], 0
	v_mfma_f32_16x16x32_bf16 v[14:17], v[184:187], v[208:211], 0
	v_mfma_f32_16x16x32_bf16 v[6:9], v[176:179], v[216:219], 0
	v_mfma_f32_16x16x32_bf16 v[2:5], v[184:187], v[216:219], 0
	v_mfma_f32_16x16x32_bf16 v[54:57], v[180:183], v[196:199], v[54:57]
	v_mfma_f32_16x16x32_bf16 v[46:49], v[188:191], v[196:199], v[46:49]
	v_mfma_f32_16x16x32_bf16 v[38:41], v[180:183], v[204:207], v[38:41]
	v_mfma_f32_16x16x32_bf16 v[30:33], v[188:191], v[204:207], v[30:33]
	v_mfma_f32_16x16x32_bf16 v[22:25], v[180:183], v[212:215], v[22:25]
	v_mfma_f32_16x16x32_bf16 v[14:17], v[188:191], v[212:215], v[14:17]
	v_mfma_f32_16x16x32_bf16 v[6:9], v[180:183], v[220:223], v[6:9]
	v_mfma_f32_16x16x32_bf16 v[2:5], v[188:191], v[220:223], v[2:5]
	s_setprio 0
	s_barrier
; #define PG8_STAGE_A(b, h, ptr, NX) do { if constexpr (Sched::GATHER) { unsigned gs_[2]; gs_[0] = ((NX) && last_) ? gN[h][0] : gA[h][0]; gs_[1] = ((NX) && last_) ? gN[h][1] : gA[h][1]; PG8_STAGE(PG8_SA(b, h), ptr, gs_); } \
;         else PG8_STAGE(PG8_SA(b, h), (ptr) + ((h) ? hstep : (size_t)0), voffA); } while (0)
; #define PG8_STAGE(bufoff, gbase, voff) do { _Pragma("unroll") for (int _i = 0; _i < 2; ++_i) \
;         __builtin_amdgcn_global_load_lds((const unsigned*)((const char*)(gbase) + (voff)[_i]), (PG8_LAS unsigned*)(lds + (bufoff) + ldsw + _i * 8192), 16, 0, 0); } while (0)
; #define PG8_LDA(dst, b, h) do { _Pragma("unroll") for (int m = 0; m < 4; ++m) _Pragma("unroll") for (int k = 0; k < 2; ++k) dst[m][k] = *(const PG8_LAS bf16x8*)(lds + PG8_SA(b, h) + aoff + m * 2048 + k * 1024); } while (0)
; #define PG8_LDB(dst, b, h) do { _Pragma("unroll") for (int n = 0; n < 2; ++n) _Pragma("unroll") for (int k = 0; k < 2; ++k) dst[n][k] = *(const PG8_LAS bf16x8*)(lds + PG8_SB(b, h) + boff + n * 2048 + k * 1024); } while (0)
; #define PG8_MMA(ai, bj, At, Bt) do { __builtin_amdgcn_s_setprio(1); _Pragma("unroll") for (int m = 0; m < 4; ++m) _Pragma("unroll") for (int n = 0; n < 2; ++n) _Pragma("unroll") for (int k = 0; k < 2; ++k) \
;         acc[ai][bj][m][n] = __builtin_amdgcn_mfma_f32_16x16x32_bf16(Bt[n][k], At[m][k], acc[ai][bj][m][n], 0, 0, 0); __builtin_amdgcn_s_setprio(0); } while (0)
; #define PG8_WAIT_V(n) asm volatile("s_waitcnt vmcnt(" #n ")" ::: "memory")
; #define PG8_WAIT_L(n) asm volatile("s_waitcnt lgkmcnt(" #n ")" ::: "memory")
; #define PG8_BAR __builtin_amdgcn_s_barrier()
; #define PG8_SCHED __builtin_amdgcn_sched_barrier(0)
; template <class Epi, class Sched, bool ALIGN_EPI = false, bool SP2 = false>
; __device__ __forceinline__ void gemm_phase(PG8_LAS unsigned char* lds, const Gemm g, const Sched& S, const Epi& E, const bool skip_epi = false) {
;     ...
;             PG8_LDB(B0, 1, 0); PG8_LDB(B1, 1, 1); PG8_SCHED; PG8_LDA(At, 1, 0); PG8_STAGE_A(0, 1, a2, true);
;             PG8_WAIT_V(8); PG8_WAIT_L(0); PG8_BAR; PG8_MMA(0, 0, At, B0); PG8_MMA(0, 1, At, B1); PG8_BAR; PG8_SCHED;
;             PG8_LDA(At, 1, 1); PG8_STAGE(PG8_SB(1, 0), b3, voffB); PG8_STAGE(PG8_SB(1, 1), b3 + hstep, voffB); PG8_STAGE_A(1, 0, a3, true);
;             PG8_WAIT_V(8); PG8_WAIT_L(0); PG8_BAR; PG8_MMA(1, 0, At, B0); PG8_MMA(1, 1, At, B1); PG8_BAR; PG8_SCHED;
	s_add_i32 s70, 0, 0x18000
	v_add_u32_e32 v130, s70, v147
	s_add_i32 s71, 0, 0x1c000
	ds_read_b128 v[160:163], v130
	ds_read_b128 v[164:167], v130 offset:1024
	ds_read_b128 v[168:171], v130 offset:2048
	ds_read_b128 v[172:175], v130 offset:3072
	v_add_u32_e32 v130, s71, v147
	ds_read_b128 v[176:179], v130
	ds_read_b128 v[180:183], v130 offset:1024
	ds_read_b128 v[184:187], v130 offset:2048
	ds_read_b128 v[188:191], v130 offset:3072
	s_add_u32 s38, s44, 0xe0000
	s_addc_u32 s39, s45, 0
	s_mov_b32 m0, s53
	ds_read_b128 v[192:195], v159 offset:32768
	ds_read_b128 v[196:199], v159 offset:33792
	ds_read_b128 v[200:203], v159 offset:34816
	ds_read_b128 v[204:207], v159 offset:35840
	ds_read_b128 v[208:211], v159 offset:36864
	ds_read_b128 v[212:215], v159 offset:37888
	ds_read_b128 v[216:219], v159 offset:38912
	ds_read_b128 v[220:223], v159 offset:39936
	global_load_lds_dwordx4 v132, s[38:39]
	s_mov_b32 m0, s54
	s_nop 0
	global_load_lds_dwordx4 v136, s[38:39]
	s_waitcnt vmcnt(8)
	s_waitcnt lgkmcnt(0)
	s_barrier
	s_setprio 3
	s_waitcnt lgkmcnt(0)
	v_mfma_f32_16x16x32_bf16 v[126:129], v[160:163], v[192:195], v[126:129]
	v_mfma_f32_16x16x32_bf16 v[122:125], v[168:171], v[192:195], v[122:125]
	v_mfma_f32_16x16x32_bf16 v[118:121], v[160:163], v[200:203], v[118:121]
	v_mfma_f32_16x16x32_bf16 v[114:117], v[168:171], v[200:203], v[114:117]
	v_mfma_f32_16x16x32_bf16 v[106:109], v[160:163], v[208:211], v[106:109]
	v_mfma_f32_16x16x32_bf16 v[98:101], v[168:171], v[208:211], v[98:101]
	v_mfma_f32_16x16x32_bf16 v[78:81], v[160:163], v[216:219], v[78:81]
	v_mfma_f32_16x16x32_bf16 v[74:77], v[168:171], v[216:219], v[74:77]
	v_mfma_f32_16x16x32_bf16 v[126:129], v[164:167], v[196:199], v[126:129]
	v_mfma_f32_16x16x32_bf16 v[122:125], v[172:175], v[196:199], v[122:125]
	v_mfma_f32_16x16x32_bf16 v[118:121], v[164:167], v[204:207], v[118:121]
	v_mfma_f32_16x16x32_bf16 v[114:117], v[172:175], v[204:207], v[114:117]
	v_mfma_f32_16x16x32_bf16 v[106:109], v[164:167], v[212:215], v[106:109]
	v_mfma_f32_16x16x32_bf16 v[98:101], v[172:175], v[212:215], v[98:101]
	v_mfma_f32_16x16x32_bf16 v[78:81], v[164:167], v[220:223], v[78:81]
	v_mfma_f32_16x16x32_bf16 v[74:77], v[172:175], v[220:223], v[74:77]
	v_mfma_f32_16x16x32_bf16 v[110:113], v[176:179], v[192:195], v[110:113]
	v_mfma_f32_16x16x32_bf16 v[102:105], v[184:187], v[192:195], v[102:105]
	v_mfma_f32_16x16x32_bf16 v[94:97], v[176:179], v[200:203], v[94:97]
	v_mfma_f32_16x16x32_bf16 v[90:93], v[184:187], v[200:203], v[90:93]
	v_mfma_f32_16x16x32_bf16 v[86:89], v[176:179], v[208:211], v[86:89]
	v_mfma_f32_16x16x32_bf16 v[82:85], v[184:187], v[208:211], v[82:85]
	v_mfma_f32_16x16x32_bf16 v[70:73], v[176:179], v[216:219], v[70:73]
	v_mfma_f32_16x16x32_bf16 v[66:69], v[184:187], v[216:219], v[66:69]
	v_mfma_f32_16x16x32_bf16 v[110:113], v[180:183], v[196:199], v[110:113]
	v_mfma_f32_16x16x32_bf16 v[102:105], v[188:191], v[196:199], v[102:105]
	v_mfma_f32_16x16x32_bf16 v[94:97], v[180:183], v[204:207], v[94:97]
	v_mfma_f32_16x16x32_bf16 v[90:93], v[188:191], v[204:207], v[90:93]
	v_mfma_f32_16x16x32_bf16 v[86:89], v[180:183], v[212:215], v[86:89]
	v_mfma_f32_16x16x32_bf16 v[82:85], v[188:191], v[212:215], v[82:85]
	v_mfma_f32_16x16x32_bf16 v[70:73], v[180:183], v[220:223], v[70:73]
	v_mfma_f32_16x16x32_bf16 v[66:69], v[188:191], v[220:223], v[66:69]
	s_setprio 0
	s_barrier
	s_add_i32 s38, s70, s51
	s_add_i32 m0, s38, 0xffffff80
	ds_read_b128 v[192:195], v159 offset:49152
	ds_read_b128 v[196:199], v159 offset:50176
	ds_read_b128 v[200:203], v159 offset:51200
	ds_read_b128 v[204:207], v159 offset:52224
	ds_read_b128 v[208:211], v159 offset:53248
	ds_read_b128 v[212:215], v159 offset:54272
	ds_read_b128 v[216:219], v159 offset:55296
	ds_read_b128 v[220:223], v159 offset:56320
	global_load_lds_dwordx4 v134, s[42:43] offset:128
	s_add_i32 m0, s38, 0x1f80
	s_add_u32 s38, s42, 0xe0080
	s_addc_u32 s39, s43, 0
	s_add_i32 s42, s71, s51
	global_load_lds_dwordx4 v138, s[98:99] offset:128
	s_mov_b32 m0, s42
	s_nop 0
	global_load_lds_dwordx4 v134, s[38:39]
	s_add_i32 m0, s42, 0x2000
	s_nop 0
	global_load_lds_dwordx4 v138, s[38:39]
	s_add_i32 m0, s57, 0xffffff80
	s_nop 0
	global_load_lds_dwordx4 v132, s[44:45] offset:128
	s_add_i32 m0, s58, 0xffffff80
	s_nop 0
	global_load_lds_dwordx4 v136, s[44:45] offset:128
	s_waitcnt vmcnt(8)
	s_waitcnt lgkmcnt(0)
	s_barrier
	s_setprio 3
	s_waitcnt lgkmcnt(0)
	v_mfma_f32_16x16x32_bf16 v[62:65], v[160:163], v[192:195], v[62:65]
	v_mfma_f32_16x16x32_bf16 v[58:61], v[168:171], v[192:195], v[58:61]
	v_mfma_f32_16x16x32_bf16 v[50:53], v[160:163], v[200:203], v[50:53]
	v_mfma_f32_16x16x32_bf16 v[42:45], v[168:171], v[200:203], v[42:45]
	v_mfma_f32_16x16x32_bf16 v[34:37], v[160:163], v[208:211], v[34:37]
	v_mfma_f32_16x16x32_bf16 v[26:29], v[168:171], v[208:211], v[26:29]
	v_mfma_f32_16x16x32_bf16 v[18:21], v[160:163], v[216:219], v[18:21]
	v_mfma_f32_16x16x32_bf16 v[10:13], v[168:171], v[216:219], v[10:13]
	v_mfma_f32_16x16x32_bf16 v[62:65], v[164:167], v[196:199], v[62:65]
	v_mfma_f32_16x16x32_bf16 v[58:61], v[172:175], v[196:199], v[58:61]
	v_mfma_f32_16x16x32_bf16 v[50:53], v[164:167], v[204:207], v[50:53]
	v_mfma_f32_16x16x32_bf16 v[42:45], v[172:175], v[204:207], v[42:45]
	v_mfma_f32_16x16x32_bf16 v[34:37], v[164:167], v[212:215], v[34:37]
	v_mfma_f32_16x16x32_bf16 v[26:29], v[172:175], v[212:215], v[26:29]
	v_mfma_f32_16x16x32_bf16 v[18:21], v[164:167], v[220:223], v[18:21]
	v_mfma_f32_16x16x32_bf16 v[10:13], v[172:175], v[220:223], v[10:13]
	v_mfma_f32_16x16x32_bf16 v[54:57], v[176:179], v[192:195], v[54:57]
	v_mfma_f32_16x16x32_bf16 v[46:49], v[184:187], v[192:195], v[46:49]
	v_mfma_f32_16x16x32_bf16 v[38:41], v[176:179], v[200:203], v[38:41]
	v_mfma_f32_16x16x32_bf16 v[30:33], v[184:187], v[200:203], v[30:33]
	v_mfma_f32_16x16x32_bf16 v[22:25], v[176:179], v[208:211], v[22:25]
	v_mfma_f32_16x16x32_bf16 v[14:17], v[184:187], v[208:211], v[14:17]
	v_mfma_f32_16x16x32_bf16 v[6:9], v[176:179], v[216:219], v[6:9]
	v_mfma_f32_16x16x32_bf16 v[2:5], v[184:187], v[216:219], v[2:5]
	v_mfma_f32_16x16x32_bf16 v[54:57], v[180:183], v[196:199], v[54:57]
	v_mfma_f32_16x16x32_bf16 v[46:49], v[188:191], v[196:199], v[46:49]
	v_mfma_f32_16x16x32_bf16 v[38:41], v[180:183], v[204:207], v[38:41]
	v_mfma_f32_16x16x32_bf16 v[30:33], v[188:191], v[204:207], v[30:33]
	v_mfma_f32_16x16x32_bf16 v[22:25], v[180:183], v[212:215], v[22:25]
	v_mfma_f32_16x16x32_bf16 v[14:17], v[188:191], v[212:215], v[14:17]
	v_mfma_f32_16x16x32_bf16 v[6:9], v[180:183], v[220:223], v[6:9]
	v_mfma_f32_16x16x32_bf16 v[2:5], v[188:191], v[220:223], v[2:5]
	s_setprio 0
	s_barrier
	s_add_i32 s69, s69, 2
	s_add_u32 s67, s67, 0x100
	s_addc_u32 s68, s68, 0
	s_cmp_gt_u32 s69, 53
	s_mov_b64 s[38:39], s[40:41]
; #define PG8_STAGE_A(b, h, ptr, NX) do { if constexpr (Sched::GATHER) { unsigned gs_[2]; gs_[0] = ((NX) && last_) ? gN[h][0] : gA[h][0]; gs_[1] = ((NX) && last_) ? gN[h][1] : gA[h][1]; PG8_STAGE(PG8_SA(b, h), ptr, gs_); } \
;         else PG8_STAGE(PG8_SA(b, h), (ptr) + ((h) ? hstep : (size_t)0), voffA); } while (0)
; #define PG8_STAGE(bufoff, gbase, voff) do { _Pragma("unroll") for (int _i = 0; _i < 2; ++_i) \
;         __builtin_amdgcn_global_load_lds((const unsigned*)((const char*)(gbase) + (voff)[_i]), (PG8_LAS unsigned*)(lds + (bufoff) + ldsw + _i * 8192), 16, 0, 0); } while (0)
; #define PG8_LDA(dst, b, h) do { _Pragma("unroll") for (int m = 0; m < 4; ++m) _Pragma("unroll") for (int k = 0; k < 2; ++k) dst[m][k] = *(const PG8_LAS bf16x8*)(lds + PG8_SA(b, h) + aoff + m * 2048 + k * 1024); } while (0)
; #define PG8_LDB(dst, b, h) do { _Pragma("unroll") for (int n = 0; n < 2; ++n) _Pragma("unroll") for (int k = 0; k < 2; ++k) dst[n][k] = *(const PG8_LAS bf16x8*)(lds + PG8_SB(b, h) + boff + n * 2048 + k * 1024); } while (0)
; #define PG8_MMA(ai, bj, At, Bt) do { __builtin_amdgcn_s_setprio(1); _Pragma("unroll") for (int m = 0; m < 4; ++m) _Pragma("unroll") for (int n = 0; n < 2; ++n) _Pragma("unroll") for (int k = 0; k < 2; ++k) \
;         acc[ai][bj][m][n] = __builtin_amdgcn_mfma_f32_16x16x32_bf16(Bt[n][k], At[m][k], acc[ai][bj][m][n], 0, 0, 0); __builtin_amdgcn_s_setprio(0); } while (0)
; #define PG8_WAIT_V(n) asm volatile("s_waitcnt vmcnt(" #n ")" ::: "memory")
; #define PG8_WAIT_L(n) asm volatile("s_waitcnt lgkmcnt(" #n ")" ::: "memory")
; #define PG8_BAR __builtin_amdgcn_s_barrier()
; #define PG8_SCHED __builtin_amdgcn_sched_barrier(0)
; template <class Epi, class Sched, bool ALIGN_EPI = false, bool SP2 = false>
; __device__ __forceinline__ void gemm_phase(PG8_LAS unsigned char* lds, const Gemm g, const Sched& S, const Epi& E, const bool skip_epi = false) {
;     ...
;             PG8_LDB(B0, 0, 0); PG8_LDB(B1, 0, 1); PG8_SCHED; PG8_LDA(At, 0, 0); PG8_STAGE_A(1, 1, a1, false);
;             PG8_WAIT_V(8); PG8_WAIT_L(0); PG8_BAR; PG8_MMA(0, 0, At, B0); PG8_MMA(0, 1, At, B1); PG8_BAR; PG8_SCHED;
;             PG8_LDA(At, 0, 1); PG8_STAGE(PG8_SB(0, 0), b2, voffB); PG8_STAGE(PG8_SB(0, 1), b2 + hstep, voffB); PG8_STAGE_A(0, 0, a2, true);
;             PG8_WAIT_V(8); PG8_WAIT_L(0); PG8_BAR; PG8_MMA(1, 0, At, B0); PG8_MMA(1, 1, At, B1); PG8_BAR; PG8_SCHED;
.LBB0_1823:
	ds_read_b128 v[160:163], v157
	ds_read_b128 v[164:167], v157 offset:1024
	ds_read_b128 v[168:171], v157 offset:2048
	ds_read_b128 v[172:175], v157 offset:3072
	ds_read_b128 v[176:179], v158
	ds_read_b128 v[180:183], v158 offset:1024
	ds_read_b128 v[184:187], v158 offset:2048
	ds_read_b128 v[188:191], v158 offset:3072
	s_add_u32 s40, s38, 0x100
	s_addc_u32 s41, s39, 0
	s_cmp_eq_u32 s69, 52
	s_cselect_b32 s45, s7, s41
	s_cselect_b32 s44, s6, s40
	s_cselect_b32 s43, s35, s68
	s_cselect_b32 s42, s34, s67
	v_lshl_add_u64 v[152:153], s[38:39], 0, v[140:141]
	s_add_i32 m0, s37, 0xc000
	ds_read_b128 v[192:195], v159
	ds_read_b128 v[196:199], v159 offset:1024
	ds_read_b128 v[200:203], v159 offset:2048
	ds_read_b128 v[204:207], v159 offset:3072
	ds_read_b128 v[208:211], v159 offset:4096
	ds_read_b128 v[212:215], v159 offset:5120
	ds_read_b128 v[216:219], v159 offset:6144
	ds_read_b128 v[220:223], v159 offset:7168
	global_load_lds_dwordx4 v[152:153], off
	v_lshl_add_u64 v[152:153], s[38:39], 0, v[142:143]
	s_add_i32 m0, s37, 0xe000
	s_nop 0
	global_load_lds_dwordx4 v[152:153], off
	s_waitcnt vmcnt(8)
	s_waitcnt lgkmcnt(0)
	s_barrier
	s_setprio 3
	s_waitcnt lgkmcnt(0)
	v_mfma_f32_16x16x32_bf16 v[126:129], v[160:163], v[192:195], v[126:129]
	v_mfma_f32_16x16x32_bf16 v[122:125], v[168:171], v[192:195], v[122:125]
	v_mfma_f32_16x16x32_bf16 v[118:121], v[160:163], v[200:203], v[118:121]
	v_mfma_f32_16x16x32_bf16 v[114:117], v[168:171], v[200:203], v[114:117]
	v_mfma_f32_16x16x32_bf16 v[106:109], v[160:163], v[208:211], v[106:109]
	v_mfma_f32_16x16x32_bf16 v[98:101], v[168:171], v[208:211], v[98:101]
	v_mfma_f32_16x16x32_bf16 v[78:81], v[160:163], v[216:219], v[78:81]
	v_mfma_f32_16x16x32_bf16 v[74:77], v[168:171], v[216:219], v[74:77]
	v_mfma_f32_16x16x32_bf16 v[126:129], v[164:167], v[196:199], v[126:129]
	v_mfma_f32_16x16x32_bf16 v[122:125], v[172:175], v[196:199], v[122:125]
	v_mfma_f32_16x16x32_bf16 v[118:121], v[164:167], v[204:207], v[118:121]
	v_mfma_f32_16x16x32_bf16 v[114:117], v[172:175], v[204:207], v[114:117]
	v_mfma_f32_16x16x32_bf16 v[106:109], v[164:167], v[212:215], v[106:109]
	v_mfma_f32_16x16x32_bf16 v[98:101], v[172:175], v[212:215], v[98:101]
	v_mfma_f32_16x16x32_bf16 v[78:81], v[164:167], v[220:223], v[78:81]
	v_mfma_f32_16x16x32_bf16 v[74:77], v[172:175], v[220:223], v[74:77]
	v_mfma_f32_16x16x32_bf16 v[110:113], v[176:179], v[192:195], v[110:113]
	v_mfma_f32_16x16x32_bf16 v[102:105], v[184:187], v[192:195], v[102:105]
	v_mfma_f32_16x16x32_bf16 v[94:97], v[176:179], v[200:203], v[94:97]
	v_mfma_f32_16x16x32_bf16 v[90:93], v[184:187], v[200:203], v[90:93]
	v_mfma_f32_16x16x32_bf16 v[86:89], v[176:179], v[208:211], v[86:89]
	v_mfma_f32_16x16x32_bf16 v[82:85], v[184:187], v[208:211], v[82:85]
	v_mfma_f32_16x16x32_bf16 v[70:73], v[176:179], v[216:219], v[70:73]
	v_mfma_f32_16x16x32_bf16 v[66:69], v[184:187], v[216:219], v[66:69]
	v_mfma_f32_16x16x32_bf16 v[110:113], v[180:183], v[196:199], v[110:113]
	v_mfma_f32_16x16x32_bf16 v[102:105], v[188:191], v[196:199], v[102:105]
	v_mfma_f32_16x16x32_bf16 v[94:97], v[180:183], v[204:207], v[94:97]
	v_mfma_f32_16x16x32_bf16 v[90:93], v[188:191], v[204:207], v[90:93]
	v_mfma_f32_16x16x32_bf16 v[86:89], v[180:183], v[212:215], v[86:89]
	v_mfma_f32_16x16x32_bf16 v[82:85], v[188:191], v[212:215], v[82:85]
	v_mfma_f32_16x16x32_bf16 v[70:73], v[180:183], v[220:223], v[70:73]
	v_mfma_f32_16x16x32_bf16 v[66:69], v[188:191], v[220:223], v[66:69]
	s_setprio 0
	s_barrier
	s_add_i32 s38, s60, s51
	s_mov_b64 s[98:99], s[42:43]
	s_mov_b32 m0, s38
	ds_read_b128 v[192:195], v159 offset:16384
	ds_read_b128 v[196:199], v159 offset:17408
	ds_read_b128 v[200:203], v159 offset:18432
	ds_read_b128 v[204:207], v159 offset:19456
	ds_read_b128 v[208:211], v159 offset:20480
	ds_read_b128 v[212:215], v159 offset:21504
	ds_read_b128 v[216:219], v159 offset:22528
	ds_read_b128 v[220:223], v159 offset:23552
	global_load_lds_dwordx4 v134, s[42:43]
	s_add_i32 m0, s38, 0x2000
	s_add_u32 s38, s42, 0xe0000
	s_addc_u32 s39, s43, 0
	s_add_i32 s70, s61, s51
	global_load_lds_dwordx4 v138, s[42:43]
	s_mov_b32 m0, s70
	s_nop 0
	global_load_lds_dwordx4 v134, s[38:39]
	s_add_i32 m0, s70, 0x2000
	s_nop 0
	global_load_lds_dwordx4 v138, s[38:39]
	s_mov_b32 m0, s37
	s_nop 0
	global_load_lds_dwordx4 v132, s[44:45]
	s_mov_b32 m0, s52
	s_nop 0
	global_load_lds_dwordx4 v136, s[44:45]
	s_waitcnt vmcnt(8)
	s_waitcnt lgkmcnt(0)
	s_barrier
	s_setprio 3
	s_waitcnt lgkmcnt(0)
	v_mfma_f32_16x16x32_bf16 v[62:65], v[160:163], v[192:195], v[62:65]
	v_mfma_f32_16x16x32_bf16 v[58:61], v[168:171], v[192:195], v[58:61]
	v_mfma_f32_16x16x32_bf16 v[50:53], v[160:163], v[200:203], v[50:53]
	v_mfma_f32_16x16x32_bf16 v[42:45], v[168:171], v[200:203], v[42:45]
	v_mfma_f32_16x16x32_bf16 v[34:37], v[160:163], v[208:211], v[34:37]
	v_mfma_f32_16x16x32_bf16 v[26:29], v[168:171], v[208:211], v[26:29]
	v_mfma_f32_16x16x32_bf16 v[18:21], v[160:163], v[216:219], v[18:21]
	v_mfma_f32_16x16x32_bf16 v[10:13], v[168:171], v[216:219], v[10:13]
	v_mfma_f32_16x16x32_bf16 v[62:65], v[164:167], v[196:199], v[62:65]
	v_mfma_f32_16x16x32_bf16 v[58:61], v[172:175], v[196:199], v[58:61]
	v_mfma_f32_16x16x32_bf16 v[50:53], v[164:167], v[204:207], v[50:53]
	v_mfma_f32_16x16x32_bf16 v[42:45], v[172:175], v[204:207], v[42:45]
	v_mfma_f32_16x16x32_bf16 v[34:37], v[164:167], v[212:215], v[34:37]
	v_mfma_f32_16x16x32_bf16 v[26:29], v[172:175], v[212:215], v[26:29]
	v_mfma_f32_16x16x32_bf16 v[18:21], v[164:167], v[220:223], v[18:21]
	v_mfma_f32_16x16x32_bf16 v[10:13], v[172:175], v[220:223], v[10:13]
	v_mfma_f32_16x16x32_bf16 v[54:57], v[176:179], v[192:195], v[54:57]
	v_mfma_f32_16x16x32_bf16 v[46:49], v[184:187], v[192:195], v[46:49]
	v_mfma_f32_16x16x32_bf16 v[38:41], v[176:179], v[200:203], v[38:41]
	v_mfma_f32_16x16x32_bf16 v[30:33], v[184:187], v[200:203], v[30:33]
	v_mfma_f32_16x16x32_bf16 v[22:25], v[176:179], v[208:211], v[22:25]
	v_mfma_f32_16x16x32_bf16 v[14:17], v[184:187], v[208:211], v[14:17]
	v_mfma_f32_16x16x32_bf16 v[6:9], v[176:179], v[216:219], v[6:9]
	v_mfma_f32_16x16x32_bf16 v[2:5], v[184:187], v[216:219], v[2:5]
	v_mfma_f32_16x16x32_bf16 v[54:57], v[180:183], v[196:199], v[54:57]
	v_mfma_f32_16x16x32_bf16 v[46:49], v[188:191], v[196:199], v[46:49]
	v_mfma_f32_16x16x32_bf16 v[38:41], v[180:183], v[204:207], v[38:41]
	v_mfma_f32_16x16x32_bf16 v[30:33], v[188:191], v[204:207], v[30:33]
	v_mfma_f32_16x16x32_bf16 v[22:25], v[180:183], v[212:215], v[22:25]
	v_mfma_f32_16x16x32_bf16 v[14:17], v[188:191], v[212:215], v[14:17]
	v_mfma_f32_16x16x32_bf16 v[6:9], v[180:183], v[220:223], v[6:9]
	v_mfma_f32_16x16x32_bf16 v[2:5], v[188:191], v[220:223], v[2:5]
	s_setprio 0
	s_barrier
; #define PG8_STAGE_A(b, h, ptr, NX) do { if constexpr (Sched::GATHER) { unsigned gs_[2]; gs_[0] = ((NX) && last_) ? gN[h][0] : gA[h][0]; gs_[1] = ((NX) && last_) ? gN[h][1] : gA[h][1]; PG8_STAGE(PG8_SA(b, h), ptr, gs_); } \
;         else PG8_STAGE(PG8_SA(b, h), (ptr) + ((h) ? hstep : (size_t)0), voffA); } while (0)
; #define PG8_STAGE(bufoff, gbase, voff) do { _Pragma("unroll") for (int _i = 0; _i < 2; ++_i) \
;         __builtin_amdgcn_global_load_lds((const unsigned*)((const char*)(gbase) + (voff)[_i]), (PG8_LAS unsigned*)(lds + (bufoff) + ldsw + _i * 8192), 16, 0, 0); } while (0)
; #define PG8_LDA(dst, b, h) do { _Pragma("unroll") for (int m = 0; m < 4; ++m) _Pragma("unroll") for (int k = 0; k < 2; ++k) dst[m][k] = *(const PG8_LAS bf16x8*)(lds + PG8_SA(b, h) + aoff + m * 2048 + k * 1024); } while (0)
; #define PG8_LDB(dst, b, h) do { _Pragma("unroll") for (int n = 0; n < 2; ++n) _Pragma("unroll") for (int k = 0; k < 2; ++k) dst[n][k] = *(const PG8_LAS bf16x8*)(lds + PG8_SB(b, h) + boff + n * 2048 + k * 1024); } while (0)
; #define PG8_MMA(ai, bj, At, Bt) do { __builtin_amdgcn_s_setprio(1); _Pragma("unroll") for (int m = 0; m < 4; ++m) _Pragma("unroll") for (int n = 0; n < 2; ++n) _Pragma("unroll") for (int k = 0; k < 2; ++k) \
;         acc[ai][bj][m][n] = __builtin_amdgcn_mfma_f32_16x16x32_bf16(Bt[n][k], At[m][k], acc[ai][bj][m][n], 0, 0, 0); __builtin_amdgcn_s_setprio(0); } while (0)
; #define PG8_WAIT_V(n) asm volatile("s_waitcnt vmcnt(" #n ")" ::: "memory")
; #define PG8_WAIT_L(n) asm volatile("s_waitcnt lgkmcnt(" #n ")" ::: "memory")
; #define PG8_BAR __builtin_amdgcn_s_barrier()
; #define PG8_SCHED __builtin_amdgcn_sched_barrier(0)
; template <class Epi, class Sched, bool ALIGN_EPI = false, bool SP2 = false>
; __device__ __forceinline__ void gemm_phase(PG8_LAS unsigned char* lds, const Gemm g, const Sched& S, const Epi& E, const bool skip_epi = false) {
;     ...
;             PG8_LDB(B0, 1, 0); PG8_LDB(B1, 1, 1); PG8_SCHED; PG8_LDA(At, 1, 0); PG8_STAGE_A(0, 1, a2, true);
;             PG8_WAIT_V(8); PG8_WAIT_L(0); PG8_BAR; PG8_MMA(0, 0, At, B0); PG8_MMA(0, 1, At, B1); PG8_BAR; PG8_SCHED;
;             PG8_LDA(At, 1, 1); PG8_STAGE(PG8_SB(1, 0), b3, voffB); PG8_STAGE(PG8_SB(1, 1), b3 + hstep, voffB); PG8_STAGE_A(1, 0, a3, true);
;             PG8_WAIT_V(8); PG8_WAIT_L(0); PG8_BAR; PG8_MMA(1, 0, At, B0); PG8_MMA(1, 1, At, B1); PG8_BAR; PG8_SCHED;
	s_add_i32 s70, 0, 0x18000
	v_add_u32_e32 v130, s70, v147
	s_add_i32 s71, 0, 0x1c000
	ds_read_b128 v[160:163], v130
	ds_read_b128 v[164:167], v130 offset:1024
	ds_read_b128 v[168:171], v130 offset:2048
	ds_read_b128 v[172:175], v130 offset:3072
	v_add_u32_e32 v130, s71, v147
	ds_read_b128 v[176:179], v130
	ds_read_b128 v[180:183], v130 offset:1024
	ds_read_b128 v[184:187], v130 offset:2048
	ds_read_b128 v[188:191], v130 offset:3072
	s_add_u32 s38, s44, 0xe0000
	s_addc_u32 s39, s45, 0
	s_mov_b32 m0, s53
	ds_read_b128 v[192:195], v159 offset:32768
	ds_read_b128 v[196:199], v159 offset:33792
	ds_read_b128 v[200:203], v159 offset:34816
	ds_read_b128 v[204:207], v159 offset:35840
	ds_read_b128 v[208:211], v159 offset:36864
	ds_read_b128 v[212:215], v159 offset:37888
	ds_read_b128 v[216:219], v159 offset:38912
	ds_read_b128 v[220:223], v159 offset:39936
	global_load_lds_dwordx4 v132, s[38:39]
	s_mov_b32 m0, s54
	s_nop 0
	global_load_lds_dwordx4 v136, s[38:39]
	s_waitcnt vmcnt(8)
	s_waitcnt lgkmcnt(0)
	s_barrier
	s_setprio 3
	s_waitcnt lgkmcnt(0)
	v_mfma_f32_16x16x32_bf16 v[126:129], v[160:163], v[192:195], v[126:129]
	v_mfma_f32_16x16x32_bf16 v[122:125], v[168:171], v[192:195], v[122:125]
	v_mfma_f32_16x16x32_bf16 v[118:121], v[160:163], v[200:203], v[118:121]
	v_mfma_f32_16x16x32_bf16 v[114:117], v[168:171], v[200:203], v[114:117]
	v_mfma_f32_16x16x32_bf16 v[106:109], v[160:163], v[208:211], v[106:109]
	v_mfma_f32_16x16x32_bf16 v[98:101], v[168:171], v[208:211], v[98:101]
	v_mfma_f32_16x16x32_bf16 v[78:81], v[160:163], v[216:219], v[78:81]
	v_mfma_f32_16x16x32_bf16 v[74:77], v[168:171], v[216:219], v[74:77]
	v_mfma_f32_16x16x32_bf16 v[126:129], v[164:167], v[196:199], v[126:129]
	v_mfma_f32_16x16x32_bf16 v[122:125], v[172:175], v[196:199], v[122:125]
	v_mfma_f32_16x16x32_bf16 v[118:121], v[164:167], v[204:207], v[118:121]
	v_mfma_f32_16x16x32_bf16 v[114:117], v[172:175], v[204:207], v[114:117]
	v_mfma_f32_16x16x32_bf16 v[106:109], v[164:167], v[212:215], v[106:109]
	v_mfma_f32_16x16x32_bf16 v[98:101], v[172:175], v[212:215], v[98:101]
	v_mfma_f32_16x16x32_bf16 v[78:81], v[164:167], v[220:223], v[78:81]
	v_mfma_f32_16x16x32_bf16 v[74:77], v[172:175], v[220:223], v[74:77]
	v_mfma_f32_16x16x32_bf16 v[110:113], v[176:179], v[192:195], v[110:113]
	v_mfma_f32_16x16x32_bf16 v[102:105], v[184:187], v[192:195], v[102:105]
	v_mfma_f32_16x16x32_bf16 v[94:97], v[176:179], v[200:203], v[94:97]
	v_mfma_f32_16x16x32_bf16 v[90:93], v[184:187], v[200:203], v[90:93]
	v_mfma_f32_16x16x32_bf16 v[86:89], v[176:179], v[208:211], v[86:89]
	v_mfma_f32_16x16x32_bf16 v[82:85], v[184:187], v[208:211], v[82:85]
	v_mfma_f32_16x16x32_bf16 v[70:73], v[176:179], v[216:219], v[70:73]
	v_mfma_f32_16x16x32_bf16 v[66:69], v[184:187], v[216:219], v[66:69]
	v_mfma_f32_16x16x32_bf16 v[110:113], v[180:183], v[196:199], v[110:113]
	v_mfma_f32_16x16x32_bf16 v[102:105], v[188:191], v[196:199], v[102:105]
	v_mfma_f32_16x16x32_bf16 v[94:97], v[180:183], v[204:207], v[94:97]
	v_mfma_f32_16x16x32_bf16 v[90:93], v[188:191], v[204:207], v[90:93]
	v_mfma_f32_16x16x32_bf16 v[86:89], v[180:183], v[212:215], v[86:89]
	v_mfma_f32_16x16x32_bf16 v[82:85], v[188:191], v[212:215], v[82:85]
	v_mfma_f32_16x16x32_bf16 v[70:73], v[180:183], v[220:223], v[70:73]
	v_mfma_f32_16x16x32_bf16 v[66:69], v[188:191], v[220:223], v[66:69]
	s_setprio 0
	s_barrier
	s_add_i32 s38, s70, s51
	s_add_i32 m0, s38, 0xffffff80
	ds_read_b128 v[192:195], v159 offset:49152
	ds_read_b128 v[196:199], v159 offset:50176
	ds_read_b128 v[200:203], v159 offset:51200
	ds_read_b128 v[204:207], v159 offset:52224
	ds_read_b128 v[208:211], v159 offset:53248
	ds_read_b128 v[212:215], v159 offset:54272
	ds_read_b128 v[216:219], v159 offset:55296
	ds_read_b128 v[220:223], v159 offset:56320
	global_load_lds_dwordx4 v134, s[42:43] offset:128
	s_add_i32 m0, s38, 0x1f80
	s_add_u32 s38, s42, 0xe0080
	s_addc_u32 s39, s43, 0
	s_add_i32 s42, s71, s51
	global_load_lds_dwordx4 v138, s[98:99] offset:128
	s_mov_b32 m0, s42
	s_nop 0
	global_load_lds_dwordx4 v134, s[38:39]
	s_add_i32 m0, s42, 0x2000
	s_nop 0
	global_load_lds_dwordx4 v138, s[38:39]
	s_add_i32 m0, s57, 0xffffff80
	s_nop 0
	global_load_lds_dwordx4 v132, s[44:45] offset:128
	s_add_i32 m0, s58, 0xffffff80
	s_nop 0
	global_load_lds_dwordx4 v136, s[44:45] offset:128
	s_waitcnt vmcnt(8)
	s_waitcnt lgkmcnt(0)
	s_barrier
	s_setprio 3
	s_waitcnt lgkmcnt(0)
	v_mfma_f32_16x16x32_bf16 v[62:65], v[160:163], v[192:195], v[62:65]
	v_mfma_f32_16x16x32_bf16 v[58:61], v[168:171], v[192:195], v[58:61]
	v_mfma_f32_16x16x32_bf16 v[50:53], v[160:163], v[200:203], v[50:53]
	v_mfma_f32_16x16x32_bf16 v[42:45], v[168:171], v[200:203], v[42:45]
	v_mfma_f32_16x16x32_bf16 v[34:37], v[160:163], v[208:211], v[34:37]
	v_mfma_f32_16x16x32_bf16 v[26:29], v[168:171], v[208:211], v[26:29]
	v_mfma_f32_16x16x32_bf16 v[18:21], v[160:163], v[216:219], v[18:21]
	v_mfma_f32_16x16x32_bf16 v[10:13], v[168:171], v[216:219], v[10:13]
	v_mfma_f32_16x16x32_bf16 v[62:65], v[164:167], v[196:199], v[62:65]
	v_mfma_f32_16x16x32_bf16 v[58:61], v[172:175], v[196:199], v[58:61]
	v_mfma_f32_16x16x32_bf16 v[50:53], v[164:167], v[204:207], v[50:53]
	v_mfma_f32_16x16x32_bf16 v[42:45], v[172:175], v[204:207], v[42:45]
	v_mfma_f32_16x16x32_bf16 v[34:37], v[164:167], v[212:215], v[34:37]
	v_mfma_f32_16x16x32_bf16 v[26:29], v[172:175], v[212:215], v[26:29]
	v_mfma_f32_16x16x32_bf16 v[18:21], v[164:167], v[220:223], v[18:21]
	v_mfma_f32_16x16x32_bf16 v[10:13], v[172:175], v[220:223], v[10:13]
	v_mfma_f32_16x16x32_bf16 v[54:57], v[176:179], v[192:195], v[54:57]
	v_mfma_f32_16x16x32_bf16 v[46:49], v[184:187], v[192:195], v[46:49]
	v_mfma_f32_16x16x32_bf16 v[38:41], v[176:179], v[200:203], v[38:41]
	v_mfma_f32_16x16x32_bf16 v[30:33], v[184:187], v[200:203], v[30:33]
	v_mfma_f32_16x16x32_bf16 v[22:25], v[176:179], v[208:211], v[22:25]
	v_mfma_f32_16x16x32_bf16 v[14:17], v[184:187], v[208:211], v[14:17]
	v_mfma_f32_16x16x32_bf16 v[6:9], v[176:179], v[216:219], v[6:9]
	v_mfma_f32_16x16x32_bf16 v[2:5], v[184:187], v[216:219], v[2:5]
	v_mfma_f32_16x16x32_bf16 v[54:57], v[180:183], v[196:199], v[54:57]
	v_mfma_f32_16x16x32_bf16 v[46:49], v[188:191], v[196:199], v[46:49]
	v_mfma_f32_16x16x32_bf16 v[38:41], v[180:183], v[204:207], v[38:41]
	v_mfma_f32_16x16x32_bf16 v[30:33], v[188:191], v[204:207], v[30:33]
	v_mfma_f32_16x16x32_bf16 v[22:25], v[180:183], v[212:215], v[22:25]
	v_mfma_f32_16x16x32_bf16 v[14:17], v[188:191], v[212:215], v[14:17]
	v_mfma_f32_16x16x32_bf16 v[6:9], v[180:183], v[220:223], v[6:9]
	v_mfma_f32_16x16x32_bf16 v[2:5], v[188:191], v[220:223], v[2:5]
	s_setprio 0
	s_barrier
	s_add_i32 s69, s69, 2
	s_add_u32 s67, s67, 0x100
	s_addc_u32 s68, s68, 0
	s_cmp_gt_u32 s69, 53
	s_mov_b64 s[38:39], s[40:41]
	s_cbranch_scc0 .LBB0_1823
	s_and_b64 vcc, exec, s[20:21]
	s_cbranch_vccz .LBB0_1826
	s_barrier

; #define PG8_STAGE_A(b, h, ptr, NX) do { if constexpr (Sched::GATHER) { unsigned gs_[2]; gs_[0] = ((NX) && last_) ? gN[h][0] : gA[h][0]; gs_[1] = ((NX) && last_) ? gN[h][1] : gA[h][1]; PG8_STAGE(PG8_SA(b, h), ptr, gs_); } \
;         else PG8_STAGE(PG8_SA(b, h), (ptr) + ((h) ? hstep : (size_t)0), voffA); } while (0)
; #define PG8_STAGE(bufoff, gbase, voff) do { _Pragma("unroll") for (int _i = 0; _i < 2; ++_i) \
;         __builtin_amdgcn_global_load_lds((const unsigned*)((const char*)(gbase) + (voff)[_i]), (PG8_LAS unsigned*)(lds + (bufoff) + ldsw + _i * 8192), 16, 0, 0); } while (0)
; #define PG8_LDA(dst, b, h) do { _Pragma("unroll") for (int m = 0; m < 4; ++m) _Pragma("unroll") for (int k = 0; k < 2; ++k) dst[m][k] = *(const PG8_LAS bf16x8*)(lds + PG8_SA(b, h) + aoff + m * 2048 + k * 1024); } while (0)
; #define PG8_LDB(dst, b, h) do { _Pragma("unroll") for (int n = 0; n < 2; ++n) _Pragma("unroll") for (int k = 0; k < 2; ++k) dst[n][k] = *(const PG8_LAS bf16x8*)(lds + PG8_SB(b, h) + boff + n * 2048 + k * 1024); } while (0)
; #define PG8_WAIT_V(n) asm volatile("s_waitcnt vmcnt(" #n ")" ::: "memory")
; #define PG8_WAIT_L(n) asm volatile("s_waitcnt lgkmcnt(" #n ")" ::: "memory")
; template <class Epi, class Sched, bool ALIGN_EPI = false, bool SP2 = false>
; __device__ __forceinline__ void gemm_phase(PG8_LAS unsigned char* lds, const Gemm g, const Sched& S, const Epi& E, const bool skip_epi = false) {
;     ...
;         const char* nA = has_next ? (const char*)g.A + (size_t)nxt.pm * pmstepA + nxt.ko : cA; const char* nB = has_next ? (const char*)g.Bt + (size_t)nxt.pn * tstep + nxt.ko : cB;
;     ...
;             const char* a2 = last ? nA : cA + (size_t)(t + 2) * kstep; const char* b2 = last ? nB : cB + (size_t)(t + 2) * kstep;
;             const char* a3 = a2 + kstep; const char* b3 = b2 + kstep;
;             if (last && has_next) S.a_ready(nxt);
;             if constexpr (SP2) {
;             PG8_LDB(B0, 0, 0); PG8_LDB(B1, 0, 1); PG8_SCHED; PG8_LDA(At, 0, 0); PG8_STAGE_A(1, 1, a1, false);
;             PG8_WAIT_V(8); PG8_WAIT_L(0); PG8_BAR; PG8_MMA(0, 0, At, B0); PG8_MMA(0, 1, At, B1); PG8_BAR; PG8_SCHED;
;             PG8_LDA(At, 0, 1); PG8_STAGE(PG8_SB(0, 0), b2, voffB); PG8_STAGE(PG8_SB(0, 1), b2 + hstep, voffB); PG8_STAGE_A(0, 0, a2, true);
;             PG8_WAIT_V(8); PG8_WAIT_L(0); PG8_BAR; PG8_MMA(1, 0, At, B0); PG8_MMA(1, 1, At, B1); PG8_BAR; PG8_SCHED;
.LBB0_1843:
	s_add_u32 s54, s30, 0x100
	s_addc_u32 s55, s31, 0
	s_mov_b32 s56, -2
	ds_read_b128 v[142:145], v150
	ds_read_b128 v[154:157], v150 offset:1024
	ds_read_b128 v[158:161], v150 offset:2048
	ds_read_b128 v[162:165], v150 offset:3072
	ds_read_b128 v[166:169], v151
	ds_read_b128 v[170:173], v151 offset:1024
	ds_read_b128 v[174:177], v151 offset:2048
	ds_read_b128 v[178:181], v151 offset:3072
	s_add_u32 s30, s28, 0x100
	s_addc_u32 s31, s29, 0
	s_cmp_eq_u32 s56, 10
	s_cselect_b32 s37, s7, s31
	s_cselect_b32 s36, s6, s30
	s_cselect_b32 s35, s25, s55
	s_cselect_b32 s34, s24, s54
	v_lshl_add_u64 v[214:215], s[28:29], 0, v[136:137]
	s_add_i32 m0, s38, 0xc000
	ds_read_b128 v[182:185], v152
	ds_read_b128 v[186:189], v152 offset:1024
	ds_read_b128 v[190:193], v152 offset:2048
	ds_read_b128 v[194:197], v152 offset:3072
	ds_read_b128 v[198:201], v152 offset:4096
	ds_read_b128 v[202:205], v152 offset:5120
	ds_read_b128 v[206:209], v152 offset:6144
	ds_read_b128 v[210:213], v152 offset:7168
	global_load_lds_dwordx4 v[214:215], off
	v_lshl_add_u64 v[214:215], s[28:29], 0, v[138:139]
	s_add_i32 m0, s38, 0xe000
	s_nop 0
	global_load_lds_dwordx4 v[214:215], off
	s_waitcnt vmcnt(8)
	s_waitcnt lgkmcnt(0)
	s_barrier
	s_setprio 3
	s_waitcnt lgkmcnt(0)
	v_mfma_f32_16x16x32_bf16 v[126:129], v[142:145], v[182:185], 0
	v_mfma_f32_16x16x32_bf16 v[122:125], v[158:161], v[182:185], 0
	v_mfma_f32_16x16x32_bf16 v[110:113], v[142:145], v[190:193], 0
	v_mfma_f32_16x16x32_bf16 v[106:109], v[158:161], v[190:193], 0
	v_mfma_f32_16x16x32_bf16 v[94:97], v[142:145], v[198:201], 0
	v_mfma_f32_16x16x32_bf16 v[90:93], v[158:161], v[198:201], 0
	v_mfma_f32_16x16x32_bf16 v[78:81], v[142:145], v[206:209], 0
	v_mfma_f32_16x16x32_bf16 v[74:77], v[158:161], v[206:209], 0
	v_mfma_f32_16x16x32_bf16 v[126:129], v[154:157], v[186:189], v[126:129]
	v_mfma_f32_16x16x32_bf16 v[122:125], v[162:165], v[186:189], v[122:125]
	v_mfma_f32_16x16x32_bf16 v[110:113], v[154:157], v[194:197], v[110:113]
	v_mfma_f32_16x16x32_bf16 v[106:109], v[162:165], v[194:197], v[106:109]
	v_mfma_f32_16x16x32_bf16 v[94:97], v[154:157], v[202:205], v[94:97]
	v_mfma_f32_16x16x32_bf16 v[90:93], v[162:165], v[202:205], v[90:93]
	v_mfma_f32_16x16x32_bf16 v[78:81], v[154:157], v[210:213], v[78:81]
	v_mfma_f32_16x16x32_bf16 v[74:77], v[162:165], v[210:213], v[74:77]
	v_mfma_f32_16x16x32_bf16 v[118:121], v[166:169], v[182:185], 0
	v_mfma_f32_16x16x32_bf16 v[114:117], v[174:177], v[182:185], 0
	v_mfma_f32_16x16x32_bf16 v[102:105], v[166:169], v[190:193], 0
	v_mfma_f32_16x16x32_bf16 v[98:101], v[174:177], v[190:193], 0
	v_mfma_f32_16x16x32_bf16 v[86:89], v[166:169], v[198:201], 0
	v_mfma_f32_16x16x32_bf16 v[82:85], v[174:177], v[198:201], 0
	v_mfma_f32_16x16x32_bf16 v[70:73], v[166:169], v[206:209], 0
	v_mfma_f32_16x16x32_bf16 v[66:69], v[174:177], v[206:209], 0
	v_mfma_f32_16x16x32_bf16 v[118:121], v[170:173], v[186:189], v[118:121]
	v_mfma_f32_16x16x32_bf16 v[114:117], v[178:181], v[186:189], v[114:117]
	v_mfma_f32_16x16x32_bf16 v[102:105], v[170:173], v[194:197], v[102:105]
	v_mfma_f32_16x16x32_bf16 v[98:101], v[178:181], v[194:197], v[98:101]
	v_mfma_f32_16x16x32_bf16 v[86:89], v[170:173], v[202:205], v[86:89]
	v_mfma_f32_16x16x32_bf16 v[82:85], v[178:181], v[202:205], v[82:85]
	v_mfma_f32_16x16x32_bf16 v[70:73], v[170:173], v[210:213], v[70:73]
	v_mfma_f32_16x16x32_bf16 v[66:69], v[178:181], v[210:213], v[66:69]
	s_setprio 0
	s_barrier
	s_add_i32 s28, s50, s3
	s_mov_b64 s[98:99], s[34:35]
	s_mov_b32 m0, s28
	ds_read_b128 v[182:185], v152 offset:16384
	ds_read_b128 v[186:189], v152 offset:17408
	ds_read_b128 v[190:193], v152 offset:18432
	ds_read_b128 v[194:197], v152 offset:19456
	ds_read_b128 v[198:201], v152 offset:20480
	ds_read_b128 v[202:205], v152 offset:21504
	ds_read_b128 v[206:209], v152 offset:22528
	ds_read_b128 v[210:213], v152 offset:23552
	global_load_lds_dwordx4 v132, s[34:35]
	s_add_i32 m0, s28, 0x2000
	s_add_u32 s28, s34, 0xe0000
	s_addc_u32 s29, s35, 0
	s_add_i32 s57, s51, s3
	global_load_lds_dwordx4 v134, s[34:35]
	s_mov_b32 m0, s57
	s_nop 0
	global_load_lds_dwordx4 v132, s[28:29]
	s_add_i32 m0, s57, 0x2000
	s_nop 0
	global_load_lds_dwordx4 v134, s[28:29]
	s_mov_b32 m0, s38
	s_nop 0
	global_load_lds_dwordx4 v132, s[36:37]
	s_mov_b32 m0, s39
	s_nop 0
	global_load_lds_dwordx4 v134, s[36:37]
	s_waitcnt vmcnt(8)
	s_waitcnt lgkmcnt(0)
	s_barrier
	s_setprio 3
	s_waitcnt lgkmcnt(0)
	v_mfma_f32_16x16x32_bf16 v[62:65], v[142:145], v[182:185], 0
	v_mfma_f32_16x16x32_bf16 v[58:61], v[158:161], v[182:185], 0
	v_mfma_f32_16x16x32_bf16 v[46:49], v[142:145], v[190:193], 0
	v_mfma_f32_16x16x32_bf16 v[42:45], v[158:161], v[190:193], 0
	v_mfma_f32_16x16x32_bf16 v[30:33], v[142:145], v[198:201], 0
	v_mfma_f32_16x16x32_bf16 v[26:29], v[158:161], v[198:201], 0
	v_mfma_f32_16x16x32_bf16 v[14:17], v[142:145], v[206:209], 0
	v_mfma_f32_16x16x32_bf16 v[10:13], v[158:161], v[206:209], 0
	v_mfma_f32_16x16x32_bf16 v[62:65], v[154:157], v[186:189], v[62:65]
	v_mfma_f32_16x16x32_bf16 v[58:61], v[162:165], v[186:189], v[58:61]
	v_mfma_f32_16x16x32_bf16 v[46:49], v[154:157], v[194:197], v[46:49]
	v_mfma_f32_16x16x32_bf16 v[42:45], v[162:165], v[194:197], v[42:45]
	v_mfma_f32_16x16x32_bf16 v[30:33], v[154:157], v[202:205], v[30:33]
	v_mfma_f32_16x16x32_bf16 v[26:29], v[162:165], v[202:205], v[26:29]
	v_mfma_f32_16x16x32_bf16 v[14:17], v[154:157], v[210:213], v[14:17]
	v_mfma_f32_16x16x32_bf16 v[10:13], v[162:165], v[210:213], v[10:13]
	v_mfma_f32_16x16x32_bf16 v[54:57], v[166:169], v[182:185], 0
	v_mfma_f32_16x16x32_bf16 v[50:53], v[174:177], v[182:185], 0
	v_mfma_f32_16x16x32_bf16 v[38:41], v[166:169], v[190:193], 0
	v_mfma_f32_16x16x32_bf16 v[34:37], v[174:177], v[190:193], 0
	v_mfma_f32_16x16x32_bf16 v[22:25], v[166:169], v[198:201], 0
	v_mfma_f32_16x16x32_bf16 v[18:21], v[174:177], v[198:201], 0
	v_mfma_f32_16x16x32_bf16 v[6:9], v[166:169], v[206:209], 0
	v_mfma_f32_16x16x32_bf16 v[2:5], v[174:177], v[206:209], 0
	v_mfma_f32_16x16x32_bf16 v[54:57], v[170:173], v[186:189], v[54:57]
	v_mfma_f32_16x16x32_bf16 v[50:53], v[178:181], v[186:189], v[50:53]
	v_mfma_f32_16x16x32_bf16 v[38:41], v[170:173], v[194:197], v[38:41]
	v_mfma_f32_16x16x32_bf16 v[34:37], v[178:181], v[194:197], v[34:37]
	v_mfma_f32_16x16x32_bf16 v[22:25], v[170:173], v[202:205], v[22:25]
	v_mfma_f32_16x16x32_bf16 v[18:21], v[178:181], v[202:205], v[18:21]
	v_mfma_f32_16x16x32_bf16 v[6:9], v[170:173], v[210:213], v[6:9]
	v_mfma_f32_16x16x32_bf16 v[2:5], v[178:181], v[210:213], v[2:5]
	s_setprio 0
	s_barrier
; #define PG8_STAGE_A(b, h, ptr, NX) do { if constexpr (Sched::GATHER) { unsigned gs_[2]; gs_[0] = ((NX) && last_) ? gN[h][0] : gA[h][0]; gs_[1] = ((NX) && last_) ? gN[h][1] : gA[h][1]; PG8_STAGE(PG8_SA(b, h), ptr, gs_); } \
;         else PG8_STAGE(PG8_SA(b, h), (ptr) + ((h) ? hstep : (size_t)0), voffA); } while (0)
; #define PG8_STAGE(bufoff, gbase, voff) do { _Pragma("unroll") for (int _i = 0; _i < 2; ++_i) \
;         __builtin_amdgcn_global_load_lds((const unsigned*)((const char*)(gbase) + (voff)[_i]), (PG8_LAS unsigned*)(lds + (bufoff) + ldsw + _i * 8192), 16, 0, 0); } while (0)
; #define PG8_LDA(dst, b, h) do { _Pragma("unroll") for (int m = 0; m < 4; ++m) _Pragma("unroll") for (int k = 0; k < 2; ++k) dst[m][k] = *(const PG8_LAS bf16x8*)(lds + PG8_SA(b, h) + aoff + m * 2048 + k * 1024); } while (0)
; #define PG8_LDB(dst, b, h) do { _Pragma("unroll") for (int n = 0; n < 2; ++n) _Pragma("unroll") for (int k = 0; k < 2; ++k) dst[n][k] = *(const PG8_LAS bf16x8*)(lds + PG8_SB(b, h) + boff + n * 2048 + k * 1024); } while (0)
; #define PG8_MMA(ai, bj, At, Bt) do { __builtin_amdgcn_s_setprio(1); _Pragma("unroll") for (int m = 0; m < 4; ++m) _Pragma("unroll") for (int n = 0; n < 2; ++n) _Pragma("unroll") for (int k = 0; k < 2; ++k) \
;         acc[ai][bj][m][n] = __builtin_amdgcn_mfma_f32_16x16x32_bf16(Bt[n][k], At[m][k], acc[ai][bj][m][n], 0, 0, 0); __builtin_amdgcn_s_setprio(0); } while (0)
; #define PG8_WAIT_V(n) asm volatile("s_waitcnt vmcnt(" #n ")" ::: "memory")
; #define PG8_WAIT_L(n) asm volatile("s_waitcnt lgkmcnt(" #n ")" ::: "memory")
; #define PG8_BAR __builtin_amdgcn_s_barrier()
; #define PG8_SCHED __builtin_amdgcn_sched_barrier(0)
; template <class Epi, class Sched, bool ALIGN_EPI = false, bool SP2 = false>
; __device__ __forceinline__ void gemm_phase(PG8_LAS unsigned char* lds, const Gemm g, const Sched& S, const Epi& E, const bool skip_epi = false) {
;     ...
;             PG8_LDB(B0, 1, 0); PG8_LDB(B1, 1, 1); PG8_SCHED; PG8_LDA(At, 1, 0); PG8_STAGE_A(0, 1, a2, true);
;             PG8_WAIT_V(8); PG8_WAIT_L(0); PG8_BAR; PG8_MMA(0, 0, At, B0); PG8_MMA(0, 1, At, B1); PG8_BAR; PG8_SCHED;
;             PG8_LDA(At, 1, 1); PG8_STAGE(PG8_SB(1, 0), b3, voffB); PG8_STAGE(PG8_SB(1, 1), b3 + hstep, voffB); PG8_STAGE_A(1, 0, a3, true);
;             PG8_WAIT_V(8); PG8_WAIT_L(0); PG8_BAR; PG8_MMA(1, 0, At, B0); PG8_MMA(1, 1, At, B1); PG8_BAR; PG8_SCHED;
	s_add_i32 s57, 0, 0x18000
	v_add_u32_e32 v130, s57, v146
	s_add_i32 s58, 0, 0x1c000
	ds_read_b128 v[142:145], v130
	ds_read_b128 v[154:157], v130 offset:1024
	ds_read_b128 v[158:161], v130 offset:2048
	ds_read_b128 v[162:165], v130 offset:3072
	v_add_u32_e32 v130, s58, v146
	ds_read_b128 v[166:169], v130
	ds_read_b128 v[170:173], v130 offset:1024
	ds_read_b128 v[174:177], v130 offset:2048
	ds_read_b128 v[178:181], v130 offset:3072
	s_add_u32 s28, s36, 0xe0000
	s_addc_u32 s29, s37, 0
	s_mov_b32 m0, s40
	ds_read_b128 v[182:185], v152 offset:32768
	ds_read_b128 v[186:189], v152 offset:33792
	ds_read_b128 v[190:193], v152 offset:34816
	ds_read_b128 v[194:197], v152 offset:35840
	ds_read_b128 v[198:201], v152 offset:36864
	ds_read_b128 v[202:205], v152 offset:37888
	ds_read_b128 v[206:209], v152 offset:38912
	ds_read_b128 v[210:213], v152 offset:39936
	global_load_lds_dwordx4 v132, s[28:29]
	s_mov_b32 m0, s41
	s_nop 0
	global_load_lds_dwordx4 v134, s[28:29]
	s_waitcnt vmcnt(8)
	s_waitcnt lgkmcnt(0)
	s_barrier
	s_setprio 3
	s_waitcnt lgkmcnt(0)
	v_mfma_f32_16x16x32_bf16 v[126:129], v[142:145], v[182:185], v[126:129]
	v_mfma_f32_16x16x32_bf16 v[122:125], v[158:161], v[182:185], v[122:125]
	v_mfma_f32_16x16x32_bf16 v[110:113], v[142:145], v[190:193], v[110:113]
	v_mfma_f32_16x16x32_bf16 v[106:109], v[158:161], v[190:193], v[106:109]
	v_mfma_f32_16x16x32_bf16 v[94:97], v[142:145], v[198:201], v[94:97]
	v_mfma_f32_16x16x32_bf16 v[90:93], v[158:161], v[198:201], v[90:93]
	v_mfma_f32_16x16x32_bf16 v[78:81], v[142:145], v[206:209], v[78:81]
	v_mfma_f32_16x16x32_bf16 v[74:77], v[158:161], v[206:209], v[74:77]
	v_mfma_f32_16x16x32_bf16 v[126:129], v[154:157], v[186:189], v[126:129]
	v_mfma_f32_16x16x32_bf16 v[122:125], v[162:165], v[186:189], v[122:125]
	v_mfma_f32_16x16x32_bf16 v[110:113], v[154:157], v[194:197], v[110:113]
	v_mfma_f32_16x16x32_bf16 v[106:109], v[162:165], v[194:197], v[106:109]
	v_mfma_f32_16x16x32_bf16 v[94:97], v[154:157], v[202:205], v[94:97]
	v_mfma_f32_16x16x32_bf16 v[90:93], v[162:165], v[202:205], v[90:93]
	v_mfma_f32_16x16x32_bf16 v[78:81], v[154:157], v[210:213], v[78:81]
	v_mfma_f32_16x16x32_bf16 v[74:77], v[162:165], v[210:213], v[74:77]
	v_mfma_f32_16x16x32_bf16 v[118:121], v[166:169], v[182:185], v[118:121]
	v_mfma_f32_16x16x32_bf16 v[114:117], v[174:177], v[182:185], v[114:117]
	v_mfma_f32_16x16x32_bf16 v[102:105], v[166:169], v[190:193], v[102:105]
	v_mfma_f32_16x16x32_bf16 v[98:101], v[174:177], v[190:193], v[98:101]
	v_mfma_f32_16x16x32_bf16 v[86:89], v[166:169], v[198:201], v[86:89]
	v_mfma_f32_16x16x32_bf16 v[82:85], v[174:177], v[198:201], v[82:85]
	v_mfma_f32_16x16x32_bf16 v[70:73], v[166:169], v[206:209], v[70:73]
	v_mfma_f32_16x16x32_bf16 v[66:69], v[174:177], v[206:209], v[66:69]
	v_mfma_f32_16x16x32_bf16 v[118:121], v[170:173], v[186:189], v[118:121]
	v_mfma_f32_16x16x32_bf16 v[114:117], v[178:181], v[186:189], v[114:117]
	v_mfma_f32_16x16x32_bf16 v[102:105], v[170:173], v[194:197], v[102:105]
	v_mfma_f32_16x16x32_bf16 v[98:101], v[178:181], v[194:197], v[98:101]
	v_mfma_f32_16x16x32_bf16 v[86:89], v[170:173], v[202:205], v[86:89]
	v_mfma_f32_16x16x32_bf16 v[82:85], v[178:181], v[202:205], v[82:85]
	v_mfma_f32_16x16x32_bf16 v[70:73], v[170:173], v[210:213], v[70:73]
	v_mfma_f32_16x16x32_bf16 v[66:69], v[178:181], v[210:213], v[66:69]
	s_setprio 0
	s_barrier
	s_add_i32 s28, s57, s3
	s_add_i32 m0, s28, 0xffffff80
	ds_read_b128 v[182:185], v152 offset:49152
	ds_read_b128 v[186:189], v152 offset:50176
	ds_read_b128 v[190:193], v152 offset:51200
	ds_read_b128 v[194:197], v152 offset:52224
	ds_read_b128 v[198:201], v152 offset:53248
	ds_read_b128 v[202:205], v152 offset:54272
	ds_read_b128 v[206:209], v152 offset:55296
	ds_read_b128 v[210:213], v152 offset:56320
	global_load_lds_dwordx4 v132, s[34:35] offset:128
	s_add_i32 m0, s28, 0x1f80
	s_add_u32 s28, s34, 0xe0080
	s_addc_u32 s29, s35, 0
	s_add_i32 s34, s58, s3
	global_load_lds_dwordx4 v134, s[98:99] offset:128
	s_mov_b32 m0, s34
	s_nop 0
	global_load_lds_dwordx4 v132, s[28:29]
	s_add_i32 m0, s34, 0x2000
	s_nop 0
	global_load_lds_dwordx4 v134, s[28:29]
	s_add_i32 m0, s46, 0xffffff80
	s_nop 0
	global_load_lds_dwordx4 v132, s[36:37] offset:128
	s_add_i32 m0, s47, 0xffffff80
	s_nop 0
	global_load_lds_dwordx4 v134, s[36:37] offset:128
	s_waitcnt vmcnt(8)
	s_waitcnt lgkmcnt(0)
	s_barrier
	s_setprio 3
	s_waitcnt lgkmcnt(0)
	v_mfma_f32_16x16x32_bf16 v[62:65], v[142:145], v[182:185], v[62:65]
	v_mfma_f32_16x16x32_bf16 v[58:61], v[158:161], v[182:185], v[58:61]
	v_mfma_f32_16x16x32_bf16 v[46:49], v[142:145], v[190:193], v[46:49]
	v_mfma_f32_16x16x32_bf16 v[42:45], v[158:161], v[190:193], v[42:45]
	v_mfma_f32_16x16x32_bf16 v[30:33], v[142:145], v[198:201], v[30:33]
	v_mfma_f32_16x16x32_bf16 v[26:29], v[158:161], v[198:201], v[26:29]
	v_mfma_f32_16x16x32_bf16 v[14:17], v[142:145], v[206:209], v[14:17]
	v_mfma_f32_16x16x32_bf16 v[10:13], v[158:161], v[206:209], v[10:13]
	v_mfma_f32_16x16x32_bf16 v[62:65], v[154:157], v[186:189], v[62:65]
	v_mfma_f32_16x16x32_bf16 v[58:61], v[162:165], v[186:189], v[58:61]
	v_mfma_f32_16x16x32_bf16 v[46:49], v[154:157], v[194:197], v[46:49]
	v_mfma_f32_16x16x32_bf16 v[42:45], v[162:165], v[194:197], v[42:45]
	v_mfma_f32_16x16x32_bf16 v[30:33], v[154:157], v[202:205], v[30:33]
	v_mfma_f32_16x16x32_bf16 v[26:29], v[162:165], v[202:205], v[26:29]
	v_mfma_f32_16x16x32_bf16 v[14:17], v[154:157], v[210:213], v[14:17]
	v_mfma_f32_16x16x32_bf16 v[10:13], v[162:165], v[210:213], v[10:13]
	v_mfma_f32_16x16x32_bf16 v[54:57], v[166:169], v[182:185], v[54:57]
	v_mfma_f32_16x16x32_bf16 v[50:53], v[174:177], v[182:185], v[50:53]
	v_mfma_f32_16x16x32_bf16 v[38:41], v[166:169], v[190:193], v[38:41]
	v_mfma_f32_16x16x32_bf16 v[34:37], v[174:177], v[190:193], v[34:37]
	v_mfma_f32_16x16x32_bf16 v[22:25], v[166:169], v[198:201], v[22:25]
	v_mfma_f32_16x16x32_bf16 v[18:21], v[174:177], v[198:201], v[18:21]
	v_mfma_f32_16x16x32_bf16 v[6:9], v[166:169], v[206:209], v[6:9]
	v_mfma_f32_16x16x32_bf16 v[2:5], v[174:177], v[206:209], v[2:5]
	v_mfma_f32_16x16x32_bf16 v[54:57], v[170:173], v[186:189], v[54:57]
	v_mfma_f32_16x16x32_bf16 v[50:53], v[178:181], v[186:189], v[50:53]
	v_mfma_f32_16x16x32_bf16 v[38:41], v[170:173], v[194:197], v[38:41]
	v_mfma_f32_16x16x32_bf16 v[34:37], v[178:181], v[194:197], v[34:37]
	v_mfma_f32_16x16x32_bf16 v[22:25], v[170:173], v[202:205], v[22:25]
	v_mfma_f32_16x16x32_bf16 v[18:21], v[178:181], v[202:205], v[18:21]
	v_mfma_f32_16x16x32_bf16 v[6:9], v[170:173], v[210:213], v[6:9]
	v_mfma_f32_16x16x32_bf16 v[2:5], v[178:181], v[210:213], v[2:5]
	s_setprio 0
	s_barrier
	s_add_i32 s56, s56, 2
	s_add_u32 s54, s54, 0x100
	s_addc_u32 s55, s55, 0
	s_cmp_gt_u32 s56, 11
	s_mov_b64 s[28:29], s[30:31]
; #define PG8_STAGE_A(b, h, ptr, NX) do { if constexpr (Sched::GATHER) { unsigned gs_[2]; gs_[0] = ((NX) && last_) ? gN[h][0] : gA[h][0]; gs_[1] = ((NX) && last_) ? gN[h][1] : gA[h][1]; PG8_STAGE(PG8_SA(b, h), ptr, gs_); } \
;         else PG8_STAGE(PG8_SA(b, h), (ptr) + ((h) ? hstep : (size_t)0), voffA); } while (0)
; #define PG8_STAGE(bufoff, gbase, voff) do { _Pragma("unroll") for (int _i = 0; _i < 2; ++_i) \
;         __builtin_amdgcn_global_load_lds((const unsigned*)((const char*)(gbase) + (voff)[_i]), (PG8_LAS unsigned*)(lds + (bufoff) + ldsw + _i * 8192), 16, 0, 0); } while (0)
; #define PG8_LDA(dst, b, h) do { _Pragma("unroll") for (int m = 0; m < 4; ++m) _Pragma("unroll") for (int k = 0; k < 2; ++k) dst[m][k] = *(const PG8_LAS bf16x8*)(lds + PG8_SA(b, h) + aoff + m * 2048 + k * 1024); } while (0)
; #define PG8_LDB(dst, b, h) do { _Pragma("unroll") for (int n = 0; n < 2; ++n) _Pragma("unroll") for (int k = 0; k < 2; ++k) dst[n][k] = *(const PG8_LAS bf16x8*)(lds + PG8_SB(b, h) + boff + n * 2048 + k * 1024); } while (0)
; #define PG8_WAIT_V(n) asm volatile("s_waitcnt vmcnt(" #n ")" ::: "memory")
; #define PG8_WAIT_L(n) asm volatile("s_waitcnt lgkmcnt(" #n ")" ::: "memory")
; #define PG8_BAR __builtin_amdgcn_s_barrier()
; template <class Epi, class Sched, bool ALIGN_EPI = false, bool SP2 = false>
; __device__ __forceinline__ void gemm_phase(PG8_LAS unsigned char* lds, const Gemm g, const Sched& S, const Epi& E, const bool skip_epi = false) {
;     ...
;             const bool last = (t == nt - 2); last_ = last && has_next;
;             const char* a1 = cA + (size_t)(t + 1) * kstep;
;             const char* a2 = last ? nA : cA + (size_t)(t + 2) * kstep; const char* b2 = last ? nB : cB + (size_t)(t + 2) * kstep;
;             const char* a3 = a2 + kstep; const char* b3 = b2 + kstep;
;             if (last && has_next) S.a_ready(nxt);
;             if constexpr (SP2) {
;             PG8_LDB(B0, 0, 0); PG8_LDB(B1, 0, 1); PG8_SCHED; PG8_LDA(At, 0, 0); PG8_STAGE_A(1, 1, a1, false);
;             PG8_WAIT_V(8); PG8_WAIT_L(0); PG8_BAR; PG8_MMA(0, 0, At, B0); PG8_MMA(0, 1, At, B1); PG8_BAR; PG8_SCHED;
;             PG8_LDA(At, 0, 1); PG8_STAGE(PG8_SB(0, 0), b2, voffB); PG8_STAGE(PG8_SB(0, 1), b2 + hstep, voffB); PG8_STAGE_A(0, 0, a2, true);
;             PG8_WAIT_V(8); PG8_WAIT_L(0); PG8_BAR; PG8_MMA(1, 0, At, B0); PG8_MMA(1, 1, At, B1); PG8_BAR; PG8_SCHED;
.LBB0_1844:
	ds_read_b128 v[142:145], v150
	ds_read_b128 v[154:157], v150 offset:1024
	ds_read_b128 v[158:161], v150 offset:2048
	ds_read_b128 v[162:165], v150 offset:3072
	ds_read_b128 v[166:169], v151
	ds_read_b128 v[170:173], v151 offset:1024
	ds_read_b128 v[174:177], v151 offset:2048
	ds_read_b128 v[178:181], v151 offset:3072
	s_add_u32 s30, s28, 0x100
	s_addc_u32 s31, s29, 0
	s_cmp_eq_u32 s56, 10
	s_cselect_b32 s37, s7, s31
	s_cselect_b32 s36, s6, s30
	s_cselect_b32 s35, s25, s55
	s_cselect_b32 s34, s24, s54
	v_lshl_add_u64 v[214:215], s[28:29], 0, v[136:137]
	s_add_i32 m0, s38, 0xc000
	ds_read_b128 v[182:185], v152
	ds_read_b128 v[186:189], v152 offset:1024
	ds_read_b128 v[190:193], v152 offset:2048
	ds_read_b128 v[194:197], v152 offset:3072
	ds_read_b128 v[198:201], v152 offset:4096
	ds_read_b128 v[202:205], v152 offset:5120
	ds_read_b128 v[206:209], v152 offset:6144
	ds_read_b128 v[210:213], v152 offset:7168
	global_load_lds_dwordx4 v[214:215], off
	v_lshl_add_u64 v[214:215], s[28:29], 0, v[138:139]
	s_add_i32 m0, s38, 0xe000
	s_nop 0
	global_load_lds_dwordx4 v[214:215], off
	s_waitcnt vmcnt(8)
	s_waitcnt lgkmcnt(0)
	s_barrier
	s_setprio 3
	s_waitcnt lgkmcnt(0)
	v_mfma_f32_16x16x32_bf16 v[126:129], v[142:145], v[182:185], v[126:129]
	v_mfma_f32_16x16x32_bf16 v[122:125], v[158:161], v[182:185], v[122:125]
	v_mfma_f32_16x16x32_bf16 v[110:113], v[142:145], v[190:193], v[110:113]
	v_mfma_f32_16x16x32_bf16 v[106:109], v[158:161], v[190:193], v[106:109]
	v_mfma_f32_16x16x32_bf16 v[94:97], v[142:145], v[198:201], v[94:97]
	v_mfma_f32_16x16x32_bf16 v[90:93], v[158:161], v[198:201], v[90:93]
	v_mfma_f32_16x16x32_bf16 v[78:81], v[142:145], v[206:209], v[78:81]
	v_mfma_f32_16x16x32_bf16 v[74:77], v[158:161], v[206:209], v[74:77]
	v_mfma_f32_16x16x32_bf16 v[126:129], v[154:157], v[186:189], v[126:129]
	v_mfma_f32_16x16x32_bf16 v[122:125], v[162:165], v[186:189], v[122:125]
	v_mfma_f32_16x16x32_bf16 v[110:113], v[154:157], v[194:197], v[110:113]
	v_mfma_f32_16x16x32_bf16 v[106:109], v[162:165], v[194:197], v[106:109]
	v_mfma_f32_16x16x32_bf16 v[94:97], v[154:157], v[202:205], v[94:97]
	v_mfma_f32_16x16x32_bf16 v[90:93], v[162:165], v[202:205], v[90:93]
	v_mfma_f32_16x16x32_bf16 v[78:81], v[154:157], v[210:213], v[78:81]
	v_mfma_f32_16x16x32_bf16 v[74:77], v[162:165], v[210:213], v[74:77]
	v_mfma_f32_16x16x32_bf16 v[118:121], v[166:169], v[182:185], v[118:121]
	v_mfma_f32_16x16x32_bf16 v[114:117], v[174:177], v[182:185], v[114:117]
	v_mfma_f32_16x16x32_bf16 v[102:105], v[166:169], v[190:193], v[102:105]
	v_mfma_f32_16x16x32_bf16 v[98:101], v[174:177], v[190:193], v[98:101]
	v_mfma_f32_16x16x32_bf16 v[86:89], v[166:169], v[198:201], v[86:89]
	v_mfma_f32_16x16x32_bf16 v[82:85], v[174:177], v[198:201], v[82:85]
	v_mfma_f32_16x16x32_bf16 v[70:73], v[166:169], v[206:209], v[70:73]
	v_mfma_f32_16x16x32_bf16 v[66:69], v[174:177], v[206:209], v[66:69]
	v_mfma_f32_16x16x32_bf16 v[118:121], v[170:173], v[186:189], v[118:121]
	v_mfma_f32_16x16x32_bf16 v[114:117], v[178:181], v[186:189], v[114:117]
	v_mfma_f32_16x16x32_bf16 v[102:105], v[170:173], v[194:197], v[102:105]
	v_mfma_f32_16x16x32_bf16 v[98:101], v[178:181], v[194:197], v[98:101]
	v_mfma_f32_16x16x32_bf16 v[86:89], v[170:173], v[202:205], v[86:89]
	v_mfma_f32_16x16x32_bf16 v[82:85], v[178:181], v[202:205], v[82:85]
	v_mfma_f32_16x16x32_bf16 v[70:73], v[170:173], v[210:213], v[70:73]
	v_mfma_f32_16x16x32_bf16 v[66:69], v[178:181], v[210:213], v[66:69]
	s_setprio 0
	s_barrier
	s_add_i32 s28, s50, s3
	s_mov_b64 s[98:99], s[34:35]
	s_mov_b32 m0, s28
	ds_read_b128 v[182:185], v152 offset:16384
	ds_read_b128 v[186:189], v152 offset:17408
	ds_read_b128 v[190:193], v152 offset:18432
	ds_read_b128 v[194:197], v152 offset:19456
	ds_read_b128 v[198:201], v152 offset:20480
	ds_read_b128 v[202:205], v152 offset:21504
	ds_read_b128 v[206:209], v152 offset:22528
	ds_read_b128 v[210:213], v152 offset:23552
	global_load_lds_dwordx4 v132, s[34:35]
	s_add_i32 m0, s28, 0x2000
	s_add_u32 s28, s34, 0xe0000
	s_addc_u32 s29, s35, 0
	s_add_i32 s57, s51, s3
	global_load_lds_dwordx4 v134, s[34:35]
	s_mov_b32 m0, s57
	s_nop 0
	global_load_lds_dwordx4 v132, s[28:29]
	s_add_i32 m0, s57, 0x2000
	s_nop 0
	global_load_lds_dwordx4 v134, s[28:29]
	s_mov_b32 m0, s38
	s_nop 0
	global_load_lds_dwordx4 v132, s[36:37]
	s_mov_b32 m0, s39
	s_nop 0
	global_load_lds_dwordx4 v134, s[36:37]
	s_waitcnt vmcnt(8)
	s_waitcnt lgkmcnt(0)
	s_barrier
	s_setprio 3
	s_waitcnt lgkmcnt(0)
	v_mfma_f32_16x16x32_bf16 v[62:65], v[142:145], v[182:185], v[62:65]
	v_mfma_f32_16x16x32_bf16 v[58:61], v[158:161], v[182:185], v[58:61]
	v_mfma_f32_16x16x32_bf16 v[46:49], v[142:145], v[190:193], v[46:49]
	v_mfma_f32_16x16x32_bf16 v[42:45], v[158:161], v[190:193], v[42:45]
	v_mfma_f32_16x16x32_bf16 v[30:33], v[142:145], v[198:201], v[30:33]
	v_mfma_f32_16x16x32_bf16 v[26:29], v[158:161], v[198:201], v[26:29]
	v_mfma_f32_16x16x32_bf16 v[14:17], v[142:145], v[206:209], v[14:17]
	v_mfma_f32_16x16x32_bf16 v[10:13], v[158:161], v[206:209], v[10:13]
	v_mfma_f32_16x16x32_bf16 v[62:65], v[154:157], v[186:189], v[62:65]
	v_mfma_f32_16x16x32_bf16 v[58:61], v[162:165], v[186:189], v[58:61]
	v_mfma_f32_16x16x32_bf16 v[46:49], v[154:157], v[194:197], v[46:49]
	v_mfma_f32_16x16x32_bf16 v[42:45], v[162:165], v[194:197], v[42:45]
	v_mfma_f32_16x16x32_bf16 v[30:33], v[154:157], v[202:205], v[30:33]
	v_mfma_f32_16x16x32_bf16 v[26:29], v[162:165], v[202:205], v[26:29]
	v_mfma_f32_16x16x32_bf16 v[14:17], v[154:157], v[210:213], v[14:17]
	v_mfma_f32_16x16x32_bf16 v[10:13], v[162:165], v[210:213], v[10:13]
	v_mfma_f32_16x16x32_bf16 v[54:57], v[166:169], v[182:185], v[54:57]
	v_mfma_f32_16x16x32_bf16 v[50:53], v[174:177], v[182:185], v[50:53]
	v_mfma_f32_16x16x32_bf16 v[38:41], v[166:169], v[190:193], v[38:41]
	v_mfma_f32_16x16x32_bf16 v[34:37], v[174:177], v[190:193], v[34:37]
	v_mfma_f32_16x16x32_bf16 v[22:25], v[166:169], v[198:201], v[22:25]
	v_mfma_f32_16x16x32_bf16 v[18:21], v[174:177], v[198:201], v[18:21]
	v_mfma_f32_16x16x32_bf16 v[6:9], v[166:169], v[206:209], v[6:9]
	v_mfma_f32_16x16x32_bf16 v[2:5], v[174:177], v[206:209], v[2:5]
	v_mfma_f32_16x16x32_bf16 v[54:57], v[170:173], v[186:189], v[54:57]
	v_mfma_f32_16x16x32_bf16 v[50:53], v[178:181], v[186:189], v[50:53]
	v_mfma_f32_16x16x32_bf16 v[38:41], v[170:173], v[194:197], v[38:41]
	v_mfma_f32_16x16x32_bf16 v[34:37], v[178:181], v[194:197], v[34:37]
	v_mfma_f32_16x16x32_bf16 v[22:25], v[170:173], v[202:205], v[22:25]
	v_mfma_f32_16x16x32_bf16 v[18:21], v[178:181], v[202:205], v[18:21]
	v_mfma_f32_16x16x32_bf16 v[6:9], v[170:173], v[210:213], v[6:9]
	v_mfma_f32_16x16x32_bf16 v[2:5], v[178:181], v[210:213], v[2:5]
	s_setprio 0
	s_barrier
; #define PG8_STAGE_A(b, h, ptr, NX) do { if constexpr (Sched::GATHER) { unsigned gs_[2]; gs_[0] = ((NX) && last_) ? gN[h][0] : gA[h][0]; gs_[1] = ((NX) && last_) ? gN[h][1] : gA[h][1]; PG8_STAGE(PG8_SA(b, h), ptr, gs_); } \
;         else PG8_STAGE(PG8_SA(b, h), (ptr) + ((h) ? hstep : (size_t)0), voffA); } while (0)
; #define PG8_STAGE(bufoff, gbase, voff) do { _Pragma("unroll") for (int _i = 0; _i < 2; ++_i) \
;         __builtin_amdgcn_global_load_lds((const unsigned*)((const char*)(gbase) + (voff)[_i]), (PG8_LAS unsigned*)(lds + (bufoff) + ldsw + _i * 8192), 16, 0, 0); } while (0)
; #define PG8_LDA(dst, b, h) do { _Pragma("unroll") for (int m = 0; m < 4; ++m) _Pragma("unroll") for (int k = 0; k < 2; ++k) dst[m][k] = *(const PG8_LAS bf16x8*)(lds + PG8_SA(b, h) + aoff + m * 2048 + k * 1024); } while (0)
; #define PG8_LDB(dst, b, h) do { _Pragma("unroll") for (int n = 0; n < 2; ++n) _Pragma("unroll") for (int k = 0; k < 2; ++k) dst[n][k] = *(const PG8_LAS bf16x8*)(lds + PG8_SB(b, h) + boff + n * 2048 + k * 1024); } while (0)
; #define PG8_MMA(ai, bj, At, Bt) do { __builtin_amdgcn_s_setprio(1); _Pragma("unroll") for (int m = 0; m < 4; ++m) _Pragma("unroll") for (int n = 0; n < 2; ++n) _Pragma("unroll") for (int k = 0; k < 2; ++k) \
;         acc[ai][bj][m][n] = __builtin_amdgcn_mfma_f32_16x16x32_bf16(Bt[n][k], At[m][k], acc[ai][bj][m][n], 0, 0, 0); __builtin_amdgcn_s_setprio(0); } while (0)
; #define PG8_WAIT_V(n) asm volatile("s_waitcnt vmcnt(" #n ")" ::: "memory")
; #define PG8_WAIT_L(n) asm volatile("s_waitcnt lgkmcnt(" #n ")" ::: "memory")
; #define PG8_BAR __builtin_amdgcn_s_barrier()
; #define PG8_SCHED __builtin_amdgcn_sched_barrier(0)
; template <class Epi, class Sched, bool ALIGN_EPI = false, bool SP2 = false>
; __device__ __forceinline__ void gemm_phase(PG8_LAS unsigned char* lds, const Gemm g, const Sched& S, const Epi& E, const bool skip_epi = false) {
;     ...
;             PG8_LDB(B0, 1, 0); PG8_LDB(B1, 1, 1); PG8_SCHED; PG8_LDA(At, 1, 0); PG8_STAGE_A(0, 1, a2, true);
;             PG8_WAIT_V(8); PG8_WAIT_L(0); PG8_BAR; PG8_MMA(0, 0, At, B0); PG8_MMA(0, 1, At, B1); PG8_BAR; PG8_SCHED;
;             PG8_LDA(At, 1, 1); PG8_STAGE(PG8_SB(1, 0), b3, voffB); PG8_STAGE(PG8_SB(1, 1), b3 + hstep, voffB); PG8_STAGE_A(1, 0, a3, true);
;             PG8_WAIT_V(8); PG8_WAIT_L(0); PG8_BAR; PG8_MMA(1, 0, At, B0); PG8_MMA(1, 1, At, B1); PG8_BAR; PG8_SCHED;
	s_add_i32 s57, 0, 0x18000
	v_add_u32_e32 v130, s57, v146
	s_add_i32 s58, 0, 0x1c000
	ds_read_b128 v[142:145], v130
	ds_read_b128 v[154:157], v130 offset:1024
	ds_read_b128 v[158:161], v130 offset:2048
	ds_read_b128 v[162:165], v130 offset:3072
	v_add_u32_e32 v130, s58, v146
	ds_read_b128 v[166:169], v130
	ds_read_b128 v[170:173], v130 offset:1024
	ds_read_b128 v[174:177], v130 offset:2048
	ds_read_b128 v[178:181], v130 offset:3072
	s_add_u32 s28, s36, 0xe0000
	s_addc_u32 s29, s37, 0
	s_mov_b32 m0, s40
	ds_read_b128 v[182:185], v152 offset:32768
	ds_read_b128 v[186:189], v152 offset:33792
	ds_read_b128 v[190:193], v152 offset:34816
	ds_read_b128 v[194:197], v152 offset:35840
	ds_read_b128 v[198:201], v152 offset:36864
	ds_read_b128 v[202:205], v152 offset:37888
	ds_read_b128 v[206:209], v152 offset:38912
	ds_read_b128 v[210:213], v152 offset:39936
	global_load_lds_dwordx4 v132, s[28:29]
	s_mov_b32 m0, s41
	s_nop 0
	global_load_lds_dwordx4 v134, s[28:29]
	s_waitcnt vmcnt(8)
	s_waitcnt lgkmcnt(0)
	s_barrier
	s_setprio 3
	s_waitcnt lgkmcnt(0)
	v_mfma_f32_16x16x32_bf16 v[126:129], v[142:145], v[182:185], v[126:129]
	v_mfma_f32_16x16x32_bf16 v[122:125], v[158:161], v[182:185], v[122:125]
	v_mfma_f32_16x16x32_bf16 v[110:113], v[142:145], v[190:193], v[110:113]
	v_mfma_f32_16x16x32_bf16 v[106:109], v[158:161], v[190:193], v[106:109]
	v_mfma_f32_16x16x32_bf16 v[94:97], v[142:145], v[198:201], v[94:97]
	v_mfma_f32_16x16x32_bf16 v[90:93], v[158:161], v[198:201], v[90:93]
	v_mfma_f32_16x16x32_bf16 v[78:81], v[142:145], v[206:209], v[78:81]
	v_mfma_f32_16x16x32_bf16 v[74:77], v[158:161], v[206:209], v[74:77]
	v_mfma_f32_16x16x32_bf16 v[126:129], v[154:157], v[186:189], v[126:129]
	v_mfma_f32_16x16x32_bf16 v[122:125], v[162:165], v[186:189], v[122:125]
	v_mfma_f32_16x16x32_bf16 v[110:113], v[154:157], v[194:197], v[110:113]
	v_mfma_f32_16x16x32_bf16 v[106:109], v[162:165], v[194:197], v[106:109]
	v_mfma_f32_16x16x32_bf16 v[94:97], v[154:157], v[202:205], v[94:97]
	v_mfma_f32_16x16x32_bf16 v[90:93], v[162:165], v[202:205], v[90:93]
	v_mfma_f32_16x16x32_bf16 v[78:81], v[154:157], v[210:213], v[78:81]
	v_mfma_f32_16x16x32_bf16 v[74:77], v[162:165], v[210:213], v[74:77]
	v_mfma_f32_16x16x32_bf16 v[118:121], v[166:169], v[182:185], v[118:121]
	v_mfma_f32_16x16x32_bf16 v[114:117], v[174:177], v[182:185], v[114:117]
	v_mfma_f32_16x16x32_bf16 v[102:105], v[166:169], v[190:193], v[102:105]
	v_mfma_f32_16x16x32_bf16 v[98:101], v[174:177], v[190:193], v[98:101]
	v_mfma_f32_16x16x32_bf16 v[86:89], v[166:169], v[198:201], v[86:89]
	v_mfma_f32_16x16x32_bf16 v[82:85], v[174:177], v[198:201], v[82:85]
	v_mfma_f32_16x16x32_bf16 v[70:73], v[166:169], v[206:209], v[70:73]
	v_mfma_f32_16x16x32_bf16 v[66:69], v[174:177], v[206:209], v[66:69]
	v_mfma_f32_16x16x32_bf16 v[118:121], v[170:173], v[186:189], v[118:121]
	v_mfma_f32_16x16x32_bf16 v[114:117], v[178:181], v[186:189], v[114:117]
	v_mfma_f32_16x16x32_bf16 v[102:105], v[170:173], v[194:197], v[102:105]
	v_mfma_f32_16x16x32_bf16 v[98:101], v[178:181], v[194:197], v[98:101]
	v_mfma_f32_16x16x32_bf16 v[86:89], v[170:173], v[202:205], v[86:89]
	v_mfma_f32_16x16x32_bf16 v[82:85], v[178:181], v[202:205], v[82:85]
	v_mfma_f32_16x16x32_bf16 v[70:73], v[170:173], v[210:213], v[70:73]
	v_mfma_f32_16x16x32_bf16 v[66:69], v[178:181], v[210:213], v[66:69]
	s_setprio 0
	s_barrier
	s_add_i32 s28, s57, s3
	s_add_i32 m0, s28, 0xffffff80
	ds_read_b128 v[182:185], v152 offset:49152
	ds_read_b128 v[186:189], v152 offset:50176
	ds_read_b128 v[190:193], v152 offset:51200
	ds_read_b128 v[194:197], v152 offset:52224
	ds_read_b128 v[198:201], v152 offset:53248
	ds_read_b128 v[202:205], v152 offset:54272
	ds_read_b128 v[206:209], v152 offset:55296
	ds_read_b128 v[210:213], v152 offset:56320
	global_load_lds_dwordx4 v132, s[34:35] offset:128
	s_add_i32 m0, s28, 0x1f80
	s_add_u32 s28, s34, 0xe0080
	s_addc_u32 s29, s35, 0
	s_add_i32 s34, s58, s3
	global_load_lds_dwordx4 v134, s[98:99] offset:128
	s_mov_b32 m0, s34
	s_nop 0
	global_load_lds_dwordx4 v132, s[28:29]
	s_add_i32 m0, s34, 0x2000
	s_nop 0
	global_load_lds_dwordx4 v134, s[28:29]
	s_add_i32 m0, s46, 0xffffff80
	s_nop 0
	global_load_lds_dwordx4 v132, s[36:37] offset:128
	s_add_i32 m0, s47, 0xffffff80
	s_nop 0
	global_load_lds_dwordx4 v134, s[36:37] offset:128
	s_waitcnt vmcnt(8)
	s_waitcnt lgkmcnt(0)
	s_barrier
	s_setprio 3
	s_waitcnt lgkmcnt(0)
	v_mfma_f32_16x16x32_bf16 v[62:65], v[142:145], v[182:185], v[62:65]
	v_mfma_f32_16x16x32_bf16 v[58:61], v[158:161], v[182:185], v[58:61]
	v_mfma_f32_16x16x32_bf16 v[46:49], v[142:145], v[190:193], v[46:49]
	v_mfma_f32_16x16x32_bf16 v[42:45], v[158:161], v[190:193], v[42:45]
	v_mfma_f32_16x16x32_bf16 v[30:33], v[142:145], v[198:201], v[30:33]
	v_mfma_f32_16x16x32_bf16 v[26:29], v[158:161], v[198:201], v[26:29]
	v_mfma_f32_16x16x32_bf16 v[14:17], v[142:145], v[206:209], v[14:17]
	v_mfma_f32_16x16x32_bf16 v[10:13], v[158:161], v[206:209], v[10:13]
	v_mfma_f32_16x16x32_bf16 v[62:65], v[154:157], v[186:189], v[62:65]
	v_mfma_f32_16x16x32_bf16 v[58:61], v[162:165], v[186:189], v[58:61]
	v_mfma_f32_16x16x32_bf16 v[46:49], v[154:157], v[194:197], v[46:49]
	v_mfma_f32_16x16x32_bf16 v[42:45], v[162:165], v[194:197], v[42:45]
	v_mfma_f32_16x16x32_bf16 v[30:33], v[154:157], v[202:205], v[30:33]
	v_mfma_f32_16x16x32_bf16 v[26:29], v[162:165], v[202:205], v[26:29]
	v_mfma_f32_16x16x32_bf16 v[14:17], v[154:157], v[210:213], v[14:17]
	v_mfma_f32_16x16x32_bf16 v[10:13], v[162:165], v[210:213], v[10:13]
	v_mfma_f32_16x16x32_bf16 v[54:57], v[166:169], v[182:185], v[54:57]
	v_mfma_f32_16x16x32_bf16 v[50:53], v[174:177], v[182:185], v[50:53]
	v_mfma_f32_16x16x32_bf16 v[38:41], v[166:169], v[190:193], v[38:41]
	v_mfma_f32_16x16x32_bf16 v[34:37], v[174:177], v[190:193], v[34:37]
	v_mfma_f32_16x16x32_bf16 v[22:25], v[166:169], v[198:201], v[22:25]
	v_mfma_f32_16x16x32_bf16 v[18:21], v[174:177], v[198:201], v[18:21]
	v_mfma_f32_16x16x32_bf16 v[6:9], v[166:169], v[206:209], v[6:9]
	v_mfma_f32_16x16x32_bf16 v[2:5], v[174:177], v[206:209], v[2:5]
	v_mfma_f32_16x16x32_bf16 v[54:57], v[170:173], v[186:189], v[54:57]
	v_mfma_f32_16x16x32_bf16 v[50:53], v[178:181], v[186:189], v[50:53]
	v_mfma_f32_16x16x32_bf16 v[38:41], v[170:173], v[194:197], v[38:41]
	v_mfma_f32_16x16x32_bf16 v[34:37], v[178:181], v[194:197], v[34:37]
	v_mfma_f32_16x16x32_bf16 v[22:25], v[170:173], v[202:205], v[22:25]
	v_mfma_f32_16x16x32_bf16 v[18:21], v[178:181], v[202:205], v[18:21]
	v_mfma_f32_16x16x32_bf16 v[6:9], v[170:173], v[210:213], v[6:9]
	v_mfma_f32_16x16x32_bf16 v[2:5], v[178:181], v[210:213], v[2:5]
	s_setprio 0
	s_barrier
	s_add_i32 s56, s56, 2
	s_add_u32 s54, s54, 0x100
	s_addc_u32 s55, s55, 0
	s_cmp_gt_u32 s56, 11
	s_mov_b64 s[28:29], s[30:31]
	s_cbranch_scc0 .LBB0_1844
	s_and_b64 vcc, exec, s[20:21]
	s_cbranch_vccz .LBB0_1847
	s_barrier
